# v79 + the s_nop 3 between the two 8-MFMA blocks of each fused fp8 compute segment removed
# speedup vs baseline: 1.0018x; 1.0004x over previous
; #define PG8_STAGE(bufoff, gbase, voff) do { _Pragma("unroll") for (int _i = 0; _i < 2; ++_i) \
;         __builtin_amdgcn_global_load_lds((const unsigned*)((const char*)(gbase) + (voff)[_i]), (PG8_LAS unsigned*)(lds + (bufoff) + ldsw + _i * 8192), 16, 0, 0); } while (0)
; #define PG8_WAIT_V(n) asm volatile("s_waitcnt vmcnt(" #n ")" ::: "memory")
; #define PG8_WAIT_L(n) asm volatile("s_waitcnt lgkmcnt(" #n ")" ::: "memory")
; template <class Epi, class Sched, bool ALIGN_EPI = true, bool F8 = false>
; __device__ __forceinline__ void gemm_phase(PG8_LAS unsigned char* lds, const Sched& S, const Epi& E) {
;     ...
;         for (int t = 0; t < nt; t += 2) {
;             const bool last = (t == nt - 2);
;             if constexpr (Sched::GATHER) { if (last && has_next) S.a_off(nxt, Rs, Cs, voffAn); }
;             const char* a1 = cA + (size_t)(t + 1) * kstep;
;             const char* a2 = last ? nA : cA + (size_t)(t + 2) * kstep; const char* b2 = last ? nB : cB + (size_t)(t + 2) * kstepB;
;             const char* a3 = a2 + kstep; const char* b3 = b2 + kstepB;
;             unsigned vA2[2][2];
; #pragma unroll
;             for (int h = 0; h < 2; ++h)
; #pragma unroll
;                 for (int i = 0; i < 2; ++i) { if constexpr (Sched::GATHER) vA2[h][i] = (last && has_next) ? voffAn[h][i] : voffA[h][i]; else vA2[h][i] = voffA[h][i]; }
;             PG8_LDB(B0, 0, 0); PG8_LDB(B1, 0, 1); PG8_SCHED; PG8_LDA(At, 0, 0); PG8_STAGE(PG8_SA(1, 1), a1, voffA[1]);
;             PG8_WAIT_V(8); PG8_WAIT_L(0); PG8_BAR; PG8_MMA(0, 0, At, B0); PG8_MMA(0, 1, At, B1); PG8_BAR; PG8_SCHED;
;             PG8_LDA(At, 0, 1); PG8_STAGE(PG8_SB(0, 0), b2, voffB[0]); PG8_STAGE(PG8_SB(0, 1), b2, voffB[1]); PG8_STAGE(PG8_SA(0, 0), a2, vA2[0]);
;             PG8_WAIT_V(8); PG8_WAIT_L(0); PG8_BAR; PG8_MMA(1, 0, At, B0); PG8_MMA(1, 1, At, B1); PG8_BAR; PG8_SCHED;
;             PG8_LDB(B0, 1, 0); PG8_LDB(B1, 1, 1); PG8_SCHED; PG8_LDA(At, 1, 0); PG8_STAGE(PG8_SA(0, 1), a2, vA2[1]);
;             PG8_WAIT_V(8); PG8_WAIT_L(0); PG8_BAR; PG8_MMA(0, 0, At, B0); PG8_MMA(0, 1, At, B1); PG8_BAR; PG8_SCHED;
;             PG8_LDA(At, 1, 1); PG8_STAGE(PG8_SB(1, 0), b3, voffB[0]); PG8_STAGE(PG8_SB(1, 1), b3, voffB[1]); PG8_STAGE(PG8_SA(1, 0), a3, vA2[0]);
;             PG8_WAIT_V(8); PG8_WAIT_L(0); PG8_BAR; PG8_MMA(1, 0, At, B0); PG8_MMA(1, 1, At, B1); PG8_BAR; PG8_SCHED;
.Lpk0_372:
	ds_read_b128 v[18:21], v207
	ds_read_b128 v[22:25], v207 offset:1024
	ds_read_b128 v[26:29], v207 offset:2048
	ds_read_b128 v[30:33], v207 offset:3072
	ds_read_b128 v[2:5], v208
	ds_read_b128 v[6:9], v208 offset:1024
	ds_read_b128 v[10:13], v208 offset:2048
	ds_read_b128 v[14:17], v208 offset:3072
	s_add_u32 s28, s26, 0x8000
	s_addc_u32 s29, s27, 0
	s_cmp_eq_u32 s21, 12
	s_cselect_b32 s40, s22, s28
	s_cselect_b32 s41, s23, s29
	s_cselect_b32 s30, s24, s5
	s_cselect_b32 s31, s25, s19
	s_add_u32 s28, s40, 0x8000
	s_addc_u32 s29, s41, 0
	s_add_i32 m0, s46, 0xc000
	ds_read_b128 v[212:215], v209
	ds_read_b128 v[216:219], v209 offset:1024
	ds_read_b128 v[220:223], v209 offset:2048
	ds_read_b128 v[224:227], v209 offset:3072
	ds_read_b128 v[228:231], v209 offset:4096
	ds_read_b128 v[232:235], v209 offset:5120
	ds_read_b128 v[236:239], v209 offset:6144
	ds_read_b128 v[240:243], v209 offset:7168
	global_load_lds_dwordx4 v190, s[26:27]
	s_add_i32 m0, s46, 0xe000
	s_nop 0
	global_load_lds_dwordx4 v188, s[26:27]
	s_waitcnt vmcnt(8)
	s_waitcnt lgkmcnt(0)
	s_setprio 1
	v_mfma_f32_16x16x128_f8f6f4 v[158:161], v[18:25], v[212:219], 0
	v_mfma_f32_16x16x128_f8f6f4 v[154:157], v[26:33], v[212:219], 0
	v_mfma_f32_16x16x128_f8f6f4 v[142:145], v[18:25], v[220:227], 0
	v_mfma_f32_16x16x128_f8f6f4 v[138:141], v[26:33], v[220:227], 0
	v_mfma_f32_16x16x128_f8f6f4 v[126:129], v[18:25], v[228:235], 0
	v_mfma_f32_16x16x128_f8f6f4 v[122:125], v[26:33], v[228:235], 0
	v_mfma_f32_16x16x128_f8f6f4 v[110:113], v[18:25], v[236:243], 0
	v_mfma_f32_16x16x128_f8f6f4 v[106:109], v[26:33], v[236:243], 0
	s_setprio 0
	s_setprio 1
	v_mfma_f32_16x16x128_f8f6f4 v[150:153], v[2:9], v[212:219], 0
	v_mfma_f32_16x16x128_f8f6f4 v[146:149], v[10:17], v[212:219], 0
	v_mfma_f32_16x16x128_f8f6f4 v[134:137], v[2:9], v[220:227], 0
	v_mfma_f32_16x16x128_f8f6f4 v[130:133], v[10:17], v[220:227], 0
	v_mfma_f32_16x16x128_f8f6f4 v[118:121], v[2:9], v[228:235], 0
	v_mfma_f32_16x16x128_f8f6f4 v[114:117], v[10:17], v[228:235], 0
	v_mfma_f32_16x16x128_f8f6f4 v[102:105], v[2:9], v[236:243], 0
	v_mfma_f32_16x16x128_f8f6f4 v[98:101], v[10:17], v[236:243], 0
	s_setprio 0
	s_barrier
	s_add_i32 s67, s62, s45
	s_mov_b32 m0, s67
	ds_read_b128 v[212:215], v209 offset:16384
	ds_read_b128 v[216:219], v209 offset:17408
	ds_read_b128 v[220:223], v209 offset:18432
	ds_read_b128 v[224:227], v209 offset:19456
	ds_read_b128 v[228:231], v209 offset:20480
	ds_read_b128 v[232:235], v209 offset:21504
	ds_read_b128 v[236:239], v209 offset:22528
	ds_read_b128 v[240:243], v209 offset:23552
	global_load_lds_dwordx4 v164, s[30:31]
	s_add_i32 m0, s67, 0x2000
	s_add_i32 s67, s63, s45
	global_load_lds_dwordx4 v166, s[30:31]
	s_add_u32 s98, s30, s8
	s_addc_u32 s99, s31, s9
	s_mov_b32 m0, s67
	s_nop 0
	global_load_lds_dwordx4 v164, s[98:99]
	s_add_u32 s100, s30, s8
	s_addc_u32 s101, s31, s9
	s_add_i32 m0, s67, 0x2000
	s_nop 0
	global_load_lds_dwordx4 v166, s[100:101]
	s_mov_b32 m0, s46
	s_nop 0
	global_load_lds_dwordx4 v174, s[40:41]
	s_mov_b32 m0, s47
	s_nop 0
	global_load_lds_dwordx4 v176, s[40:41]
	s_waitcnt vmcnt(8)
	s_waitcnt lgkmcnt(0)
	s_setprio 1
	v_mfma_f32_16x16x128_f8f6f4 v[94:97], v[18:25], v[212:219], 0
	v_mfma_f32_16x16x128_f8f6f4 v[90:93], v[26:33], v[212:219], 0
	v_mfma_f32_16x16x128_f8f6f4 v[78:81], v[18:25], v[220:227], 0
	v_mfma_f32_16x16x128_f8f6f4 v[74:77], v[26:33], v[220:227], 0
	v_mfma_f32_16x16x128_f8f6f4 v[62:65], v[18:25], v[228:235], 0
	v_mfma_f32_16x16x128_f8f6f4 v[58:61], v[26:33], v[228:235], 0
	v_mfma_f32_16x16x128_f8f6f4 v[46:49], v[18:25], v[236:243], 0
	v_mfma_f32_16x16x128_f8f6f4 v[42:45], v[26:33], v[236:243], 0
	s_setprio 0
	s_setprio 1
	v_mfma_f32_16x16x128_f8f6f4 v[86:89], v[2:9], v[212:219], 0
	v_mfma_f32_16x16x128_f8f6f4 v[82:85], v[10:17], v[212:219], 0
	v_mfma_f32_16x16x128_f8f6f4 v[70:73], v[2:9], v[220:227], 0
	v_mfma_f32_16x16x128_f8f6f4 v[66:69], v[10:17], v[220:227], 0
	v_mfma_f32_16x16x128_f8f6f4 v[54:57], v[2:9], v[228:235], 0
	v_mfma_f32_16x16x128_f8f6f4 v[50:53], v[10:17], v[228:235], 0
	v_mfma_f32_16x16x128_f8f6f4 v[38:41], v[2:9], v[236:243], 0
	v_mfma_f32_16x16x128_f8f6f4 v[34:37], v[10:17], v[236:243], 0
	s_setprio 0
	s_barrier
	s_add_i32 s67, 0, 0x18000
	s_add_i32 s68, 0, 0x1c000
	v_add_u32_e32 v14, s67, v202
	v_add_u32_e32 v30, s68, v202
	ds_read_b128 v[2:5], v14
	ds_read_b128 v[6:9], v14 offset:1024
	ds_read_b128 v[10:13], v14 offset:2048
	ds_read_b128 v[14:17], v14 offset:3072
	ds_read_b128 v[18:21], v30
	ds_read_b128 v[22:25], v30 offset:1024
	ds_read_b128 v[26:29], v30 offset:2048
	ds_read_b128 v[30:33], v30 offset:3072
	s_mov_b32 m0, s48
	ds_read_b128 v[212:215], v209 offset:32768
	ds_read_b128 v[216:219], v209 offset:33792
	ds_read_b128 v[220:223], v209 offset:34816
	ds_read_b128 v[224:227], v209 offset:35840
	ds_read_b128 v[228:231], v209 offset:36864
	ds_read_b128 v[232:235], v209 offset:37888
	ds_read_b128 v[236:239], v209 offset:38912
	ds_read_b128 v[240:243], v209 offset:39936
	global_load_lds_dwordx4 v178, s[40:41]
	s_mov_b32 m0, s49
	s_nop 0
	global_load_lds_dwordx4 v180, s[40:41]
	s_waitcnt vmcnt(8)
	s_waitcnt lgkmcnt(0)
	s_setprio 1
	v_mfma_f32_16x16x128_f8f6f4 v[158:161], v[2:9], v[212:219], v[158:161]
	v_mfma_f32_16x16x128_f8f6f4 v[154:157], v[10:17], v[212:219], v[154:157]
	v_mfma_f32_16x16x128_f8f6f4 v[142:145], v[2:9], v[220:227], v[142:145]
	v_mfma_f32_16x16x128_f8f6f4 v[138:141], v[10:17], v[220:227], v[138:141]
	v_mfma_f32_16x16x128_f8f6f4 v[126:129], v[2:9], v[228:235], v[126:129]
	v_mfma_f32_16x16x128_f8f6f4 v[122:125], v[10:17], v[228:235], v[122:125]
	v_mfma_f32_16x16x128_f8f6f4 v[110:113], v[2:9], v[236:243], v[110:113]
	v_mfma_f32_16x16x128_f8f6f4 v[106:109], v[10:17], v[236:243], v[106:109]
	s_setprio 0
	s_setprio 1
	v_mfma_f32_16x16x128_f8f6f4 v[150:153], v[18:25], v[212:219], v[150:153]
	v_mfma_f32_16x16x128_f8f6f4 v[146:149], v[26:33], v[212:219], v[146:149]
	v_mfma_f32_16x16x128_f8f6f4 v[134:137], v[18:25], v[220:227], v[134:137]
	v_mfma_f32_16x16x128_f8f6f4 v[130:133], v[26:33], v[220:227], v[130:133]
	v_mfma_f32_16x16x128_f8f6f4 v[118:121], v[18:25], v[228:235], v[118:121]
	v_mfma_f32_16x16x128_f8f6f4 v[114:117], v[26:33], v[228:235], v[114:117]
	v_mfma_f32_16x16x128_f8f6f4 v[102:105], v[18:25], v[236:243], v[102:105]
	v_mfma_f32_16x16x128_f8f6f4 v[98:101], v[26:33], v[236:243], v[98:101]
	s_setprio 0
	s_barrier
; #define PG8_STAGE(bufoff, gbase, voff) do { _Pragma("unroll") for (int _i = 0; _i < 2; ++_i) \
;         __builtin_amdgcn_global_load_lds((const unsigned*)((const char*)(gbase) + (voff)[_i]), (PG8_LAS unsigned*)(lds + (bufoff) + ldsw + _i * 8192), 16, 0, 0); } while (0)
; #define PG8_WAIT_V(n) asm volatile("s_waitcnt vmcnt(" #n ")" ::: "memory")
; #define PG8_WAIT_L(n) asm volatile("s_waitcnt lgkmcnt(" #n ")" ::: "memory")
; template <class Epi, class Sched, bool ALIGN_EPI = true, bool F8 = false>
; __device__ __forceinline__ void gemm_phase(PG8_LAS unsigned char* lds, const Sched& S, const Epi& E) {
;     ...
;         for (int t = 0; t < nt; t += 2) {
;             const bool last = (t == nt - 2);
;             if constexpr (Sched::GATHER) { if (last && has_next) S.a_off(nxt, Rs, Cs, voffAn); }
;             const char* a1 = cA + (size_t)(t + 1) * kstep;
;             const char* a2 = last ? nA : cA + (size_t)(t + 2) * kstep; const char* b2 = last ? nB : cB + (size_t)(t + 2) * kstepB;
;             const char* a3 = a2 + kstep; const char* b3 = b2 + kstepB;
;             unsigned vA2[2][2];
; #pragma unroll
;             for (int h = 0; h < 2; ++h)
; #pragma unroll
;                 for (int i = 0; i < 2; ++i) { if constexpr (Sched::GATHER) vA2[h][i] = (last && has_next) ? voffAn[h][i] : voffA[h][i]; else vA2[h][i] = voffA[h][i]; }
;             PG8_LDB(B0, 0, 0); PG8_LDB(B1, 0, 1); PG8_SCHED; PG8_LDA(At, 0, 0); PG8_STAGE(PG8_SA(1, 1), a1, voffA[1]);
;             PG8_WAIT_V(8); PG8_WAIT_L(0); PG8_BAR; PG8_MMA(0, 0, At, B0); PG8_MMA(0, 1, At, B1); PG8_BAR; PG8_SCHED;
;             PG8_LDA(At, 0, 1); PG8_STAGE(PG8_SB(0, 0), b2, voffB[0]); PG8_STAGE(PG8_SB(0, 1), b2, voffB[1]); PG8_STAGE(PG8_SA(0, 0), a2, vA2[0]);
;             PG8_WAIT_V(8); PG8_WAIT_L(0); PG8_BAR; PG8_MMA(1, 0, At, B0); PG8_MMA(1, 1, At, B1); PG8_BAR; PG8_SCHED;
;             PG8_LDB(B0, 1, 0); PG8_LDB(B1, 1, 1); PG8_SCHED; PG8_LDA(At, 1, 0); PG8_STAGE(PG8_SA(0, 1), a2, vA2[1]);
;             PG8_WAIT_V(8); PG8_WAIT_L(0); PG8_BAR; PG8_MMA(0, 0, At, B0); PG8_MMA(0, 1, At, B1); PG8_BAR; PG8_SCHED;
;             PG8_LDA(At, 1, 1); PG8_STAGE(PG8_SB(1, 0), b3, voffB[0]); PG8_STAGE(PG8_SB(1, 1), b3, voffB[1]); PG8_STAGE(PG8_SA(1, 0), a3, vA2[0]);
;             PG8_WAIT_V(8); PG8_WAIT_L(0); PG8_BAR; PG8_MMA(1, 0, At, B0); PG8_MMA(1, 1, At, B1); PG8_BAR; PG8_SCHED;
	s_add_u32 s30, s30, 0x8000
	s_addc_u32 s31, s31, 0
	s_add_i32 s40, s67, s45
	s_mov_b32 m0, s40
	ds_read_b128 v[212:215], v209 offset:49152
	ds_read_b128 v[216:219], v209 offset:50176
	ds_read_b128 v[220:223], v209 offset:51200
	ds_read_b128 v[224:227], v209 offset:52224
	ds_read_b128 v[228:231], v209 offset:53248
	ds_read_b128 v[232:235], v209 offset:54272
	ds_read_b128 v[236:239], v209 offset:55296
	ds_read_b128 v[240:243], v209 offset:56320
	global_load_lds_dwordx4 v164, s[30:31]
	s_add_i32 m0, s40, 0x2000
	s_add_i32 s40, s68, s45
	global_load_lds_dwordx4 v166, s[30:31]
	s_mov_b32 m0, s40
	s_nop 0
	global_load_lds_dwordx4 v168, s[30:31]
	s_add_i32 m0, s40, 0x2000
	s_nop 0
	global_load_lds_dwordx4 v172, s[30:31]
	s_mov_b32 m0, s52
	s_nop 0
	global_load_lds_dwordx4 v174, s[28:29]
	s_mov_b32 m0, s53
	s_nop 0
	global_load_lds_dwordx4 v176, s[28:29]
	s_waitcnt vmcnt(8)
	s_waitcnt lgkmcnt(0)
	s_setprio 1
	v_mfma_f32_16x16x128_f8f6f4 v[94:97], v[2:9], v[212:219], v[94:97]
	v_mfma_f32_16x16x128_f8f6f4 v[90:93], v[10:17], v[212:219], v[90:93]
	v_mfma_f32_16x16x128_f8f6f4 v[78:81], v[2:9], v[220:227], v[78:81]
	v_mfma_f32_16x16x128_f8f6f4 v[74:77], v[10:17], v[220:227], v[74:77]
	v_mfma_f32_16x16x128_f8f6f4 v[62:65], v[2:9], v[228:235], v[62:65]
	v_mfma_f32_16x16x128_f8f6f4 v[58:61], v[10:17], v[228:235], v[58:61]
	v_mfma_f32_16x16x128_f8f6f4 v[46:49], v[2:9], v[236:243], v[46:49]
	v_mfma_f32_16x16x128_f8f6f4 v[42:45], v[10:17], v[236:243], v[42:45]
	s_setprio 0
	s_setprio 1
	v_mfma_f32_16x16x128_f8f6f4 v[86:89], v[18:25], v[212:219], v[86:89]
	v_mfma_f32_16x16x128_f8f6f4 v[82:85], v[26:33], v[212:219], v[82:85]
	v_mfma_f32_16x16x128_f8f6f4 v[70:73], v[18:25], v[220:227], v[70:73]
	v_mfma_f32_16x16x128_f8f6f4 v[66:69], v[26:33], v[220:227], v[66:69]
	v_mfma_f32_16x16x128_f8f6f4 v[54:57], v[18:25], v[228:235], v[54:57]
	v_mfma_f32_16x16x128_f8f6f4 v[50:53], v[26:33], v[228:235], v[50:53]
	v_mfma_f32_16x16x128_f8f6f4 v[38:41], v[18:25], v[236:243], v[38:41]
	v_mfma_f32_16x16x128_f8f6f4 v[34:37], v[26:33], v[236:243], v[34:37]
	s_setprio 0
	s_barrier
	s_add_i32 s21, s21, 2
	s_add_u32 s5, s5, 0x10000
	s_addc_u32 s19, s19, 0
	s_add_u32 s26, s26, 0x10000
	s_addc_u32 s27, s27, 0
	s_cmp_gt_u32 s21, 13
	s_cbranch_scc0 .LBB0_372
	s_branch .Lfx_9967
.LBB0_372:
	ds_read_b128 v[18:21], v207
	ds_read_b128 v[22:25], v207 offset:1024
	ds_read_b128 v[26:29], v207 offset:2048
	ds_read_b128 v[30:33], v207 offset:3072
	ds_read_b128 v[2:5], v208
	ds_read_b128 v[6:9], v208 offset:1024
	ds_read_b128 v[10:13], v208 offset:2048
	ds_read_b128 v[14:17], v208 offset:3072
	s_add_u32 s28, s26, 0x8000
	s_addc_u32 s29, s27, 0
	s_cmp_eq_u32 s21, 12
	s_cselect_b32 s40, s22, s28
	s_cselect_b32 s41, s23, s29
	s_cselect_b32 s30, s24, s5
	s_cselect_b32 s31, s25, s19
	s_add_u32 s28, s40, 0x8000
	s_addc_u32 s29, s41, 0
	s_add_i32 m0, s46, 0xc000
	ds_read_b128 v[212:215], v209
	ds_read_b128 v[216:219], v209 offset:1024
	ds_read_b128 v[220:223], v209 offset:2048
	ds_read_b128 v[224:227], v209 offset:3072
	ds_read_b128 v[228:231], v209 offset:4096
	ds_read_b128 v[232:235], v209 offset:5120
	ds_read_b128 v[236:239], v209 offset:6144
	ds_read_b128 v[240:243], v209 offset:7168
	global_load_lds_dwordx4 v190, s[26:27]
	s_add_i32 m0, s46, 0xe000
	s_nop 0
	global_load_lds_dwordx4 v188, s[26:27]
	s_waitcnt vmcnt(8)
	s_waitcnt lgkmcnt(0)
	s_setprio 1
	v_mfma_f32_16x16x128_f8f6f4 v[158:161], v[18:25], v[212:219], v[158:161]
	v_mfma_f32_16x16x128_f8f6f4 v[154:157], v[26:33], v[212:219], v[154:157]
	v_mfma_f32_16x16x128_f8f6f4 v[142:145], v[18:25], v[220:227], v[142:145]
	v_mfma_f32_16x16x128_f8f6f4 v[138:141], v[26:33], v[220:227], v[138:141]
	v_mfma_f32_16x16x128_f8f6f4 v[126:129], v[18:25], v[228:235], v[126:129]
	v_mfma_f32_16x16x128_f8f6f4 v[122:125], v[26:33], v[228:235], v[122:125]
	v_mfma_f32_16x16x128_f8f6f4 v[110:113], v[18:25], v[236:243], v[110:113]
	v_mfma_f32_16x16x128_f8f6f4 v[106:109], v[26:33], v[236:243], v[106:109]
	s_setprio 0
	s_setprio 1
	v_mfma_f32_16x16x128_f8f6f4 v[150:153], v[2:9], v[212:219], v[150:153]
	v_mfma_f32_16x16x128_f8f6f4 v[146:149], v[10:17], v[212:219], v[146:149]
	v_mfma_f32_16x16x128_f8f6f4 v[134:137], v[2:9], v[220:227], v[134:137]
	v_mfma_f32_16x16x128_f8f6f4 v[130:133], v[10:17], v[220:227], v[130:133]
	v_mfma_f32_16x16x128_f8f6f4 v[118:121], v[2:9], v[228:235], v[118:121]
	v_mfma_f32_16x16x128_f8f6f4 v[114:117], v[10:17], v[228:235], v[114:117]
	v_mfma_f32_16x16x128_f8f6f4 v[102:105], v[2:9], v[236:243], v[102:105]
	v_mfma_f32_16x16x128_f8f6f4 v[98:101], v[10:17], v[236:243], v[98:101]
	s_setprio 0
	s_barrier
; #define PG8_STAGE(bufoff, gbase, voff) do { _Pragma("unroll") for (int _i = 0; _i < 2; ++_i) \
;         __builtin_amdgcn_global_load_lds((const unsigned*)((const char*)(gbase) + (voff)[_i]), (PG8_LAS unsigned*)(lds + (bufoff) + ldsw + _i * 8192), 16, 0, 0); } while (0)
; #define PG8_WAIT_V(n) asm volatile("s_waitcnt vmcnt(" #n ")" ::: "memory")
; #define PG8_WAIT_L(n) asm volatile("s_waitcnt lgkmcnt(" #n ")" ::: "memory")
; template <class Epi, class Sched, bool ALIGN_EPI = true, bool F8 = false>
; __device__ __forceinline__ void gemm_phase(PG8_LAS unsigned char* lds, const Sched& S, const Epi& E) {
;     ...
;         for (int t = 0; t < nt; t += 2) {
;             const bool last = (t == nt - 2);
;             if constexpr (Sched::GATHER) { if (last && has_next) S.a_off(nxt, Rs, Cs, voffAn); }
;             const char* a1 = cA + (size_t)(t + 1) * kstep;
;             const char* a2 = last ? nA : cA + (size_t)(t + 2) * kstep; const char* b2 = last ? nB : cB + (size_t)(t + 2) * kstepB;
;             const char* a3 = a2 + kstep; const char* b3 = b2 + kstepB;
;             unsigned vA2[2][2];
; #pragma unroll
;             for (int h = 0; h < 2; ++h)
; #pragma unroll
;                 for (int i = 0; i < 2; ++i) { if constexpr (Sched::GATHER) vA2[h][i] = (last && has_next) ? voffAn[h][i] : voffA[h][i]; else vA2[h][i] = voffA[h][i]; }
;             PG8_LDB(B0, 0, 0); PG8_LDB(B1, 0, 1); PG8_SCHED; PG8_LDA(At, 0, 0); PG8_STAGE(PG8_SA(1, 1), a1, voffA[1]);
;             PG8_WAIT_V(8); PG8_WAIT_L(0); PG8_BAR; PG8_MMA(0, 0, At, B0); PG8_MMA(0, 1, At, B1); PG8_BAR; PG8_SCHED;
;             PG8_LDA(At, 0, 1); PG8_STAGE(PG8_SB(0, 0), b2, voffB[0]); PG8_STAGE(PG8_SB(0, 1), b2, voffB[1]); PG8_STAGE(PG8_SA(0, 0), a2, vA2[0]);
;             PG8_WAIT_V(8); PG8_WAIT_L(0); PG8_BAR; PG8_MMA(1, 0, At, B0); PG8_MMA(1, 1, At, B1); PG8_BAR; PG8_SCHED;
;             PG8_LDB(B0, 1, 0); PG8_LDB(B1, 1, 1); PG8_SCHED; PG8_LDA(At, 1, 0); PG8_STAGE(PG8_SA(0, 1), a2, vA2[1]);
;             PG8_WAIT_V(8); PG8_WAIT_L(0); PG8_BAR; PG8_MMA(0, 0, At, B0); PG8_MMA(0, 1, At, B1); PG8_BAR; PG8_SCHED;
;             PG8_LDA(At, 1, 1); PG8_STAGE(PG8_SB(1, 0), b3, voffB[0]); PG8_STAGE(PG8_SB(1, 1), b3, voffB[1]); PG8_STAGE(PG8_SA(1, 0), a3, vA2[0]);
;             PG8_WAIT_V(8); PG8_WAIT_L(0); PG8_BAR; PG8_MMA(1, 0, At, B0); PG8_MMA(1, 1, At, B1); PG8_BAR; PG8_SCHED;
	s_add_i32 s67, s62, s45
	s_mov_b32 m0, s67
	ds_read_b128 v[212:215], v209 offset:16384
	ds_read_b128 v[216:219], v209 offset:17408
	ds_read_b128 v[220:223], v209 offset:18432
	ds_read_b128 v[224:227], v209 offset:19456
	ds_read_b128 v[228:231], v209 offset:20480
	ds_read_b128 v[232:235], v209 offset:21504
	ds_read_b128 v[236:239], v209 offset:22528
	ds_read_b128 v[240:243], v209 offset:23552
	global_load_lds_dwordx4 v164, s[30:31]
	s_add_i32 m0, s67, 0x2000
	s_add_i32 s67, s63, s45
	global_load_lds_dwordx4 v166, s[30:31]
	s_add_u32 s98, s30, s8
	s_addc_u32 s99, s31, s9
	s_mov_b32 m0, s67
	s_nop 0
	global_load_lds_dwordx4 v164, s[98:99]
	s_add_u32 s100, s30, s8
	s_addc_u32 s101, s31, s9
	s_add_i32 m0, s67, 0x2000
	s_nop 0
	global_load_lds_dwordx4 v166, s[100:101]
	s_mov_b32 m0, s46
	s_nop 0
	global_load_lds_dwordx4 v174, s[40:41]
	s_mov_b32 m0, s47
	s_nop 0
	global_load_lds_dwordx4 v176, s[40:41]
	s_waitcnt vmcnt(8)
	s_waitcnt lgkmcnt(0)
	s_setprio 1
	v_mfma_f32_16x16x128_f8f6f4 v[94:97], v[18:25], v[212:219], v[94:97]
	v_mfma_f32_16x16x128_f8f6f4 v[90:93], v[26:33], v[212:219], v[90:93]
	v_mfma_f32_16x16x128_f8f6f4 v[78:81], v[18:25], v[220:227], v[78:81]
	v_mfma_f32_16x16x128_f8f6f4 v[74:77], v[26:33], v[220:227], v[74:77]
	v_mfma_f32_16x16x128_f8f6f4 v[62:65], v[18:25], v[228:235], v[62:65]
	v_mfma_f32_16x16x128_f8f6f4 v[58:61], v[26:33], v[228:235], v[58:61]
	v_mfma_f32_16x16x128_f8f6f4 v[46:49], v[18:25], v[236:243], v[46:49]
	v_mfma_f32_16x16x128_f8f6f4 v[42:45], v[26:33], v[236:243], v[42:45]
	s_setprio 0
	s_setprio 1
	v_mfma_f32_16x16x128_f8f6f4 v[86:89], v[2:9], v[212:219], v[86:89]
	v_mfma_f32_16x16x128_f8f6f4 v[82:85], v[10:17], v[212:219], v[82:85]
	v_mfma_f32_16x16x128_f8f6f4 v[70:73], v[2:9], v[220:227], v[70:73]
	v_mfma_f32_16x16x128_f8f6f4 v[66:69], v[10:17], v[220:227], v[66:69]
	v_mfma_f32_16x16x128_f8f6f4 v[54:57], v[2:9], v[228:235], v[54:57]
	v_mfma_f32_16x16x128_f8f6f4 v[50:53], v[10:17], v[228:235], v[50:53]
	v_mfma_f32_16x16x128_f8f6f4 v[38:41], v[2:9], v[236:243], v[38:41]
	v_mfma_f32_16x16x128_f8f6f4 v[34:37], v[10:17], v[236:243], v[34:37]
	s_setprio 0
	s_barrier
	s_add_i32 s67, 0, 0x18000
	s_add_i32 s68, 0, 0x1c000
	v_add_u32_e32 v14, s67, v202
	v_add_u32_e32 v30, s68, v202
	ds_read_b128 v[2:5], v14
	ds_read_b128 v[6:9], v14 offset:1024
	ds_read_b128 v[10:13], v14 offset:2048
	ds_read_b128 v[14:17], v14 offset:3072
	ds_read_b128 v[18:21], v30
	ds_read_b128 v[22:25], v30 offset:1024
	ds_read_b128 v[26:29], v30 offset:2048
	ds_read_b128 v[30:33], v30 offset:3072
	s_mov_b32 m0, s48
	ds_read_b128 v[212:215], v209 offset:32768
	ds_read_b128 v[216:219], v209 offset:33792
	ds_read_b128 v[220:223], v209 offset:34816
	ds_read_b128 v[224:227], v209 offset:35840
	ds_read_b128 v[228:231], v209 offset:36864
	ds_read_b128 v[232:235], v209 offset:37888
	ds_read_b128 v[236:239], v209 offset:38912
	ds_read_b128 v[240:243], v209 offset:39936
	global_load_lds_dwordx4 v178, s[40:41]
	s_mov_b32 m0, s49
	s_nop 0
	global_load_lds_dwordx4 v180, s[40:41]
	s_waitcnt vmcnt(8)
	s_waitcnt lgkmcnt(0)
	s_setprio 1
	v_mfma_f32_16x16x128_f8f6f4 v[158:161], v[2:9], v[212:219], v[158:161]
	v_mfma_f32_16x16x128_f8f6f4 v[154:157], v[10:17], v[212:219], v[154:157]
	v_mfma_f32_16x16x128_f8f6f4 v[142:145], v[2:9], v[220:227], v[142:145]
	v_mfma_f32_16x16x128_f8f6f4 v[138:141], v[10:17], v[220:227], v[138:141]
	v_mfma_f32_16x16x128_f8f6f4 v[126:129], v[2:9], v[228:235], v[126:129]
	v_mfma_f32_16x16x128_f8f6f4 v[122:125], v[10:17], v[228:235], v[122:125]
	v_mfma_f32_16x16x128_f8f6f4 v[110:113], v[2:9], v[236:243], v[110:113]
	v_mfma_f32_16x16x128_f8f6f4 v[106:109], v[10:17], v[236:243], v[106:109]
	s_setprio 0
	s_setprio 1
	v_mfma_f32_16x16x128_f8f6f4 v[150:153], v[18:25], v[212:219], v[150:153]
	v_mfma_f32_16x16x128_f8f6f4 v[146:149], v[26:33], v[212:219], v[146:149]
	v_mfma_f32_16x16x128_f8f6f4 v[134:137], v[18:25], v[220:227], v[134:137]
	v_mfma_f32_16x16x128_f8f6f4 v[130:133], v[26:33], v[220:227], v[130:133]
	v_mfma_f32_16x16x128_f8f6f4 v[118:121], v[18:25], v[228:235], v[118:121]
	v_mfma_f32_16x16x128_f8f6f4 v[114:117], v[26:33], v[228:235], v[114:117]
	v_mfma_f32_16x16x128_f8f6f4 v[102:105], v[18:25], v[236:243], v[102:105]
	v_mfma_f32_16x16x128_f8f6f4 v[98:101], v[26:33], v[236:243], v[98:101]
	s_setprio 0
	s_barrier
	s_add_u32 s30, s30, 0x8000
	s_addc_u32 s31, s31, 0
	s_add_i32 s40, s67, s45
	s_mov_b32 m0, s40
	ds_read_b128 v[212:215], v209 offset:49152
	ds_read_b128 v[216:219], v209 offset:50176
	ds_read_b128 v[220:223], v209 offset:51200
	ds_read_b128 v[224:227], v209 offset:52224
	ds_read_b128 v[228:231], v209 offset:53248
	ds_read_b128 v[232:235], v209 offset:54272
	ds_read_b128 v[236:239], v209 offset:55296
	ds_read_b128 v[240:243], v209 offset:56320
	global_load_lds_dwordx4 v164, s[30:31]
	s_add_i32 m0, s40, 0x2000
	s_add_i32 s40, s68, s45
	global_load_lds_dwordx4 v166, s[30:31]
	s_mov_b32 m0, s40
	s_nop 0
	global_load_lds_dwordx4 v168, s[30:31]
	s_add_i32 m0, s40, 0x2000
	s_nop 0
	global_load_lds_dwordx4 v172, s[30:31]
	s_mov_b32 m0, s52
	s_nop 0
	global_load_lds_dwordx4 v174, s[28:29]
	s_mov_b32 m0, s53
	s_nop 0
	global_load_lds_dwordx4 v176, s[28:29]
	s_waitcnt vmcnt(8)
	s_waitcnt lgkmcnt(0)
	s_setprio 1
	v_mfma_f32_16x16x128_f8f6f4 v[94:97], v[2:9], v[212:219], v[94:97]
	v_mfma_f32_16x16x128_f8f6f4 v[90:93], v[10:17], v[212:219], v[90:93]
	v_mfma_f32_16x16x128_f8f6f4 v[78:81], v[2:9], v[220:227], v[78:81]
	v_mfma_f32_16x16x128_f8f6f4 v[74:77], v[10:17], v[220:227], v[74:77]
	v_mfma_f32_16x16x128_f8f6f4 v[62:65], v[2:9], v[228:235], v[62:65]
	v_mfma_f32_16x16x128_f8f6f4 v[58:61], v[10:17], v[228:235], v[58:61]
	v_mfma_f32_16x16x128_f8f6f4 v[46:49], v[2:9], v[236:243], v[46:49]
	v_mfma_f32_16x16x128_f8f6f4 v[42:45], v[10:17], v[236:243], v[42:45]
	s_setprio 0
	s_setprio 1
	v_mfma_f32_16x16x128_f8f6f4 v[86:89], v[18:25], v[212:219], v[86:89]
	v_mfma_f32_16x16x128_f8f6f4 v[82:85], v[26:33], v[212:219], v[82:85]
	v_mfma_f32_16x16x128_f8f6f4 v[70:73], v[18:25], v[220:227], v[70:73]
	v_mfma_f32_16x16x128_f8f6f4 v[66:69], v[26:33], v[220:227], v[66:69]
	v_mfma_f32_16x16x128_f8f6f4 v[54:57], v[18:25], v[228:235], v[54:57]
	v_mfma_f32_16x16x128_f8f6f4 v[50:53], v[26:33], v[228:235], v[50:53]
	v_mfma_f32_16x16x128_f8f6f4 v[38:41], v[18:25], v[236:243], v[38:41]
	v_mfma_f32_16x16x128_f8f6f4 v[34:37], v[26:33], v[236:243], v[34:37]
	s_setprio 0
	s_barrier
	s_add_i32 s21, s21, 2
	s_add_u32 s5, s5, 0x10000
	s_addc_u32 s19, s19, 0
	s_add_u32 s26, s26, 0x10000
	s_addc_u32 s27, s27, 0
	s_cmp_gt_u32 s21, 13
	s_cbranch_scc0 .LBB0_372
	s_branch .Lfx_9967
; #define PG8_WAIT_V(n) asm volatile("s_waitcnt vmcnt(" #n ")" ::: "memory")
; #define PG8_WAIT_L(n) asm volatile("s_waitcnt lgkmcnt(" #n ")" ::: "memory")
; template <class Epi, class Sched, bool ALIGN_EPI = true, bool F8 = false>
; __device__ __forceinline__ void gemm_phase(PG8_LAS unsigned char* lds, const Sched& S, const Epi& E) {
;     ...
;         for (int t = 0; t < nt; t += 2) {
;             const bool last = (t == nt - 2);
;             if constexpr (Sched::GATHER) { if (last && has_next) S.a_off(nxt, Rs, Cs, voffAn); }
;             const char* a1 = cA + (size_t)(t + 1) * kstep;
;             const char* a2 = last ? nA : cA + (size_t)(t + 2) * kstep; const char* b2 = last ? nB : cB + (size_t)(t + 2) * kstepB;
;             const char* a3 = a2 + kstep; const char* b3 = b2 + kstepB;
;             unsigned vA2[2][2];
; #pragma unroll
;             for (int h = 0; h < 2; ++h)
; #pragma unroll
;                 for (int i = 0; i < 2; ++i) { if constexpr (Sched::GATHER) vA2[h][i] = (last && has_next) ? voffAn[h][i] : voffA[h][i]; else vA2[h][i] = voffA[h][i]; }
;             PG8_LDB(B0, 0, 0); PG8_LDB(B1, 0, 1); PG8_SCHED; PG8_LDA(At, 0, 0); PG8_STAGE(PG8_SA(1, 1), a1, voffA[1]);
;             PG8_WAIT_V(8); PG8_WAIT_L(0); PG8_BAR; PG8_MMA(0, 0, At, B0); PG8_MMA(0, 1, At, B1); PG8_BAR; PG8_SCHED;
;             PG8_LDA(At, 0, 1); PG8_STAGE(PG8_SB(0, 0), b2, voffB[0]); PG8_STAGE(PG8_SB(0, 1), b2, voffB[1]); PG8_STAGE(PG8_SA(0, 0), a2, vA2[0]);
;             PG8_WAIT_V(8); PG8_WAIT_L(0); PG8_BAR; PG8_MMA(1, 0, At, B0); PG8_MMA(1, 1, At, B1); PG8_BAR; PG8_SCHED;
;             PG8_LDB(B0, 1, 0); PG8_LDB(B1, 1, 1); PG8_SCHED; PG8_LDA(At, 1, 0); PG8_STAGE(PG8_SA(0, 1), a2, vA2[1]);
;             PG8_WAIT_V(8); PG8_WAIT_L(0); PG8_BAR; PG8_MMA(0, 0, At, B0); PG8_MMA(0, 1, At, B1); PG8_BAR; PG8_SCHED;
;             PG8_LDA(At, 1, 1); PG8_STAGE(PG8_SB(1, 0), b3, voffB[0]); PG8_STAGE(PG8_SB(1, 1), b3, voffB[1]); PG8_STAGE(PG8_SA(1, 0), a3, vA2[0]);
;             PG8_WAIT_V(8); PG8_WAIT_L(0); PG8_BAR; PG8_MMA(1, 0, At, B0); PG8_MMA(1, 1, At, B1); PG8_BAR; PG8_SCHED;
;     ...
;         for (int a = 0; a < 2; ++a)
; #pragma unroll
;             for (int b = 0; b < 2; ++b)
; #pragma unroll
;                 for (int m = 0; m < 4; ++m)
; #pragma unroll
;                     for (int n = 0; n < 2; ++n) acc[a][b][m][n] = (f32x4){0.f, 0.f, 0.f, 0.f};
.Lh1e_9967:
.Lpk1_372:
	ds_read_b128 v[18:21], v207
	ds_read_b128 v[22:25], v207 offset:1024
	ds_read_b128 v[26:29], v207 offset:2048
	ds_read_b128 v[30:33], v207 offset:3072
	ds_read_b128 v[2:5], v208
	ds_read_b128 v[6:9], v208 offset:1024
	ds_read_b128 v[10:13], v208 offset:2048
	ds_read_b128 v[14:17], v208 offset:3072
	s_add_u32 s28, s26, 0x8000
	s_addc_u32 s29, s27, 0
	s_cmp_eq_u32 s21, 12
	s_cselect_b32 s40, s22, s28
	s_cselect_b32 s41, s23, s29
	s_cselect_b32 s30, s24, s5
	s_cselect_b32 s31, s25, s19
	s_add_u32 s28, s40, 0x8000
	s_addc_u32 s29, s41, 0
	s_add_i32 m0, s46, 0xc000
	ds_read_b128 v[212:215], v209
	ds_read_b128 v[216:219], v209 offset:1024
	ds_read_b128 v[220:223], v209 offset:2048
	ds_read_b128 v[224:227], v209 offset:3072
	ds_read_b128 v[228:231], v209 offset:4096
	ds_read_b128 v[232:235], v209 offset:5120
	ds_read_b128 v[236:239], v209 offset:6144
	ds_read_b128 v[240:243], v209 offset:7168
	global_load_lds_dwordx4 v190, s[26:27]
	s_add_i32 m0, s46, 0xe000
	s_nop 0
	global_load_lds_dwordx4 v188, s[26:27]
	s_waitcnt vmcnt(8)
	s_waitcnt lgkmcnt(0)
	s_barrier
	s_setprio 2
	v_mfma_f32_16x16x128_f8f6f4 v[158:161], v[18:25], v[212:219], 0
	v_mfma_f32_16x16x128_f8f6f4 v[154:157], v[26:33], v[212:219], 0
	v_mfma_f32_16x16x128_f8f6f4 v[142:145], v[18:25], v[220:227], 0
	v_mfma_f32_16x16x128_f8f6f4 v[138:141], v[26:33], v[220:227], 0
	v_mfma_f32_16x16x128_f8f6f4 v[126:129], v[18:25], v[228:235], 0
	v_mfma_f32_16x16x128_f8f6f4 v[122:125], v[26:33], v[228:235], 0
	v_mfma_f32_16x16x128_f8f6f4 v[110:113], v[18:25], v[236:243], 0
	v_mfma_f32_16x16x128_f8f6f4 v[106:109], v[26:33], v[236:243], 0
	s_setprio 0
	s_setprio 2
	v_mfma_f32_16x16x128_f8f6f4 v[150:153], v[2:9], v[212:219], 0
	v_mfma_f32_16x16x128_f8f6f4 v[146:149], v[10:17], v[212:219], 0
	v_mfma_f32_16x16x128_f8f6f4 v[134:137], v[2:9], v[220:227], 0
	v_mfma_f32_16x16x128_f8f6f4 v[130:133], v[10:17], v[220:227], 0
	v_mfma_f32_16x16x128_f8f6f4 v[118:121], v[2:9], v[228:235], 0
	v_mfma_f32_16x16x128_f8f6f4 v[114:117], v[10:17], v[228:235], 0
	v_mfma_f32_16x16x128_f8f6f4 v[102:105], v[2:9], v[236:243], 0
	v_mfma_f32_16x16x128_f8f6f4 v[98:101], v[10:17], v[236:243], 0
	s_setprio 0
	s_add_i32 s67, s62, s45
	s_mov_b32 m0, s67
	ds_read_b128 v[212:215], v209 offset:16384
	ds_read_b128 v[216:219], v209 offset:17408
	ds_read_b128 v[220:223], v209 offset:18432
	ds_read_b128 v[224:227], v209 offset:19456
	ds_read_b128 v[228:231], v209 offset:20480
	ds_read_b128 v[232:235], v209 offset:21504
	ds_read_b128 v[236:239], v209 offset:22528
	ds_read_b128 v[240:243], v209 offset:23552
	global_load_lds_dwordx4 v164, s[30:31]
	s_add_i32 m0, s67, 0x2000
	s_add_i32 s67, s63, s45
	global_load_lds_dwordx4 v166, s[30:31]
	s_add_u32 s98, s30, s8
	s_addc_u32 s99, s31, s9
	s_mov_b32 m0, s67
	s_nop 0
	global_load_lds_dwordx4 v164, s[98:99]
	s_add_u32 s100, s30, s8
	s_addc_u32 s101, s31, s9
	s_add_i32 m0, s67, 0x2000
	s_nop 0
	global_load_lds_dwordx4 v166, s[100:101]
	s_mov_b32 m0, s46
	s_nop 0
	global_load_lds_dwordx4 v174, s[40:41]
	s_mov_b32 m0, s47
	s_nop 0
	global_load_lds_dwordx4 v176, s[40:41]
	s_waitcnt vmcnt(8)
	s_waitcnt lgkmcnt(0)
	s_barrier
	s_setprio 2
	v_mfma_f32_16x16x128_f8f6f4 v[94:97], v[18:25], v[212:219], 0
	v_mfma_f32_16x16x128_f8f6f4 v[90:93], v[26:33], v[212:219], 0
	v_mfma_f32_16x16x128_f8f6f4 v[78:81], v[18:25], v[220:227], 0
	v_mfma_f32_16x16x128_f8f6f4 v[74:77], v[26:33], v[220:227], 0
	v_mfma_f32_16x16x128_f8f6f4 v[62:65], v[18:25], v[228:235], 0
	v_mfma_f32_16x16x128_f8f6f4 v[58:61], v[26:33], v[228:235], 0
	v_mfma_f32_16x16x128_f8f6f4 v[46:49], v[18:25], v[236:243], 0
	v_mfma_f32_16x16x128_f8f6f4 v[42:45], v[26:33], v[236:243], 0
	s_setprio 0
	s_setprio 2
	v_mfma_f32_16x16x128_f8f6f4 v[86:89], v[2:9], v[212:219], 0
	v_mfma_f32_16x16x128_f8f6f4 v[82:85], v[10:17], v[212:219], 0
	v_mfma_f32_16x16x128_f8f6f4 v[70:73], v[2:9], v[220:227], 0
	v_mfma_f32_16x16x128_f8f6f4 v[66:69], v[10:17], v[220:227], 0
	v_mfma_f32_16x16x128_f8f6f4 v[54:57], v[2:9], v[228:235], 0
	v_mfma_f32_16x16x128_f8f6f4 v[50:53], v[10:17], v[228:235], 0
	v_mfma_f32_16x16x128_f8f6f4 v[38:41], v[2:9], v[236:243], 0
	v_mfma_f32_16x16x128_f8f6f4 v[34:37], v[10:17], v[236:243], 0
	s_setprio 0
	s_add_i32 s67, 0, 0x18000
	s_add_i32 s68, 0, 0x1c000
	v_add_u32_e32 v14, s67, v202
	v_add_u32_e32 v30, s68, v202
	ds_read_b128 v[2:5], v14
	ds_read_b128 v[6:9], v14 offset:1024
	ds_read_b128 v[10:13], v14 offset:2048
	ds_read_b128 v[14:17], v14 offset:3072
	ds_read_b128 v[18:21], v30
	ds_read_b128 v[22:25], v30 offset:1024
	ds_read_b128 v[26:29], v30 offset:2048
	ds_read_b128 v[30:33], v30 offset:3072
	s_mov_b32 m0, s48
	ds_read_b128 v[212:215], v209 offset:32768
	ds_read_b128 v[216:219], v209 offset:33792
	ds_read_b128 v[220:223], v209 offset:34816
	ds_read_b128 v[224:227], v209 offset:35840
	ds_read_b128 v[228:231], v209 offset:36864
	ds_read_b128 v[232:235], v209 offset:37888
	ds_read_b128 v[236:239], v209 offset:38912
	ds_read_b128 v[240:243], v209 offset:39936
	global_load_lds_dwordx4 v178, s[40:41]
	s_mov_b32 m0, s49
	s_nop 0
	global_load_lds_dwordx4 v180, s[40:41]
	s_waitcnt vmcnt(8)
	s_waitcnt lgkmcnt(0)
	s_barrier
; #define PG8_STAGE(bufoff, gbase, voff) do { _Pragma("unroll") for (int _i = 0; _i < 2; ++_i) \
;         __builtin_amdgcn_global_load_lds((const unsigned*)((const char*)(gbase) + (voff)[_i]), (PG8_LAS unsigned*)(lds + (bufoff) + ldsw + _i * 8192), 16, 0, 0); } while (0)
; #define PG8_WAIT_V(n) asm volatile("s_waitcnt vmcnt(" #n ")" ::: "memory")
; #define PG8_WAIT_L(n) asm volatile("s_waitcnt lgkmcnt(" #n ")" ::: "memory")
; template <class Epi, class Sched, bool ALIGN_EPI = true, bool F8 = false>
; __device__ __forceinline__ void gemm_phase(PG8_LAS unsigned char* lds, const Sched& S, const Epi& E) {
;     ...
;         for (int t = 0; t < nt; t += 2) {
;             const bool last = (t == nt - 2);
;             if constexpr (Sched::GATHER) { if (last && has_next) S.a_off(nxt, Rs, Cs, voffAn); }
;             const char* a1 = cA + (size_t)(t + 1) * kstep;
;             const char* a2 = last ? nA : cA + (size_t)(t + 2) * kstep; const char* b2 = last ? nB : cB + (size_t)(t + 2) * kstepB;
;             const char* a3 = a2 + kstep; const char* b3 = b2 + kstepB;
;             unsigned vA2[2][2];
; #pragma unroll
;             for (int h = 0; h < 2; ++h)
; #pragma unroll
;                 for (int i = 0; i < 2; ++i) { if constexpr (Sched::GATHER) vA2[h][i] = (last && has_next) ? voffAn[h][i] : voffA[h][i]; else vA2[h][i] = voffA[h][i]; }
;             PG8_LDB(B0, 0, 0); PG8_LDB(B1, 0, 1); PG8_SCHED; PG8_LDA(At, 0, 0); PG8_STAGE(PG8_SA(1, 1), a1, voffA[1]);
;             PG8_WAIT_V(8); PG8_WAIT_L(0); PG8_BAR; PG8_MMA(0, 0, At, B0); PG8_MMA(0, 1, At, B1); PG8_BAR; PG8_SCHED;
;             PG8_LDA(At, 0, 1); PG8_STAGE(PG8_SB(0, 0), b2, voffB[0]); PG8_STAGE(PG8_SB(0, 1), b2, voffB[1]); PG8_STAGE(PG8_SA(0, 0), a2, vA2[0]);
;             PG8_WAIT_V(8); PG8_WAIT_L(0); PG8_BAR; PG8_MMA(1, 0, At, B0); PG8_MMA(1, 1, At, B1); PG8_BAR; PG8_SCHED;
;             PG8_LDB(B0, 1, 0); PG8_LDB(B1, 1, 1); PG8_SCHED; PG8_LDA(At, 1, 0); PG8_STAGE(PG8_SA(0, 1), a2, vA2[1]);
;             PG8_WAIT_V(8); PG8_WAIT_L(0); PG8_BAR; PG8_MMA(0, 0, At, B0); PG8_MMA(0, 1, At, B1); PG8_BAR; PG8_SCHED;
;             PG8_LDA(At, 1, 1); PG8_STAGE(PG8_SB(1, 0), b3, voffB[0]); PG8_STAGE(PG8_SB(1, 1), b3, voffB[1]); PG8_STAGE(PG8_SA(1, 0), a3, vA2[0]);
;             PG8_WAIT_V(8); PG8_WAIT_L(0); PG8_BAR; PG8_MMA(1, 0, At, B0); PG8_MMA(1, 1, At, B1); PG8_BAR; PG8_SCHED;
	s_setprio 2
	v_mfma_f32_16x16x128_f8f6f4 v[158:161], v[2:9], v[212:219], v[158:161]
	v_mfma_f32_16x16x128_f8f6f4 v[154:157], v[10:17], v[212:219], v[154:157]
	v_mfma_f32_16x16x128_f8f6f4 v[142:145], v[2:9], v[220:227], v[142:145]
	v_mfma_f32_16x16x128_f8f6f4 v[138:141], v[10:17], v[220:227], v[138:141]
	v_mfma_f32_16x16x128_f8f6f4 v[126:129], v[2:9], v[228:235], v[126:129]
	v_mfma_f32_16x16x128_f8f6f4 v[122:125], v[10:17], v[228:235], v[122:125]
	v_mfma_f32_16x16x128_f8f6f4 v[110:113], v[2:9], v[236:243], v[110:113]
	v_mfma_f32_16x16x128_f8f6f4 v[106:109], v[10:17], v[236:243], v[106:109]
	s_setprio 0
	s_setprio 2
	v_mfma_f32_16x16x128_f8f6f4 v[150:153], v[18:25], v[212:219], v[150:153]
	v_mfma_f32_16x16x128_f8f6f4 v[146:149], v[26:33], v[212:219], v[146:149]
	v_mfma_f32_16x16x128_f8f6f4 v[134:137], v[18:25], v[220:227], v[134:137]
	v_mfma_f32_16x16x128_f8f6f4 v[130:133], v[26:33], v[220:227], v[130:133]
	v_mfma_f32_16x16x128_f8f6f4 v[118:121], v[18:25], v[228:235], v[118:121]
	v_mfma_f32_16x16x128_f8f6f4 v[114:117], v[26:33], v[228:235], v[114:117]
	v_mfma_f32_16x16x128_f8f6f4 v[102:105], v[18:25], v[236:243], v[102:105]
	v_mfma_f32_16x16x128_f8f6f4 v[98:101], v[26:33], v[236:243], v[98:101]
	s_setprio 0
	s_add_u32 s30, s30, 0x8000
	s_addc_u32 s31, s31, 0
	s_add_i32 s40, s67, s45
	s_mov_b32 m0, s40
	ds_read_b128 v[212:215], v209 offset:49152
	ds_read_b128 v[216:219], v209 offset:50176
	ds_read_b128 v[220:223], v209 offset:51200
	ds_read_b128 v[224:227], v209 offset:52224
	ds_read_b128 v[228:231], v209 offset:53248
	ds_read_b128 v[232:235], v209 offset:54272
	ds_read_b128 v[236:239], v209 offset:55296
	ds_read_b128 v[240:243], v209 offset:56320
	global_load_lds_dwordx4 v164, s[30:31]
	s_add_i32 m0, s40, 0x2000
	s_add_i32 s40, s68, s45
	global_load_lds_dwordx4 v166, s[30:31]
	s_mov_b32 m0, s40
	s_nop 0
	global_load_lds_dwordx4 v168, s[30:31]
	s_add_i32 m0, s40, 0x2000
	s_nop 0
	global_load_lds_dwordx4 v172, s[30:31]
	s_mov_b32 m0, s52
	s_nop 0
	global_load_lds_dwordx4 v174, s[28:29]
	s_mov_b32 m0, s53
	s_nop 0
	global_load_lds_dwordx4 v176, s[28:29]
	s_waitcnt vmcnt(8)
	s_waitcnt lgkmcnt(0)
	s_barrier
	s_setprio 2
	v_mfma_f32_16x16x128_f8f6f4 v[94:97], v[2:9], v[212:219], v[94:97]
	v_mfma_f32_16x16x128_f8f6f4 v[90:93], v[10:17], v[212:219], v[90:93]
	v_mfma_f32_16x16x128_f8f6f4 v[78:81], v[2:9], v[220:227], v[78:81]
	v_mfma_f32_16x16x128_f8f6f4 v[74:77], v[10:17], v[220:227], v[74:77]
	v_mfma_f32_16x16x128_f8f6f4 v[62:65], v[2:9], v[228:235], v[62:65]
	v_mfma_f32_16x16x128_f8f6f4 v[58:61], v[10:17], v[228:235], v[58:61]
	v_mfma_f32_16x16x128_f8f6f4 v[46:49], v[2:9], v[236:243], v[46:49]
	v_mfma_f32_16x16x128_f8f6f4 v[42:45], v[10:17], v[236:243], v[42:45]
	s_setprio 0
	s_setprio 2
	v_mfma_f32_16x16x128_f8f6f4 v[86:89], v[18:25], v[212:219], v[86:89]
	v_mfma_f32_16x16x128_f8f6f4 v[82:85], v[26:33], v[212:219], v[82:85]
	v_mfma_f32_16x16x128_f8f6f4 v[70:73], v[18:25], v[220:227], v[70:73]
	v_mfma_f32_16x16x128_f8f6f4 v[66:69], v[26:33], v[220:227], v[66:69]
	v_mfma_f32_16x16x128_f8f6f4 v[54:57], v[18:25], v[228:235], v[54:57]
	v_mfma_f32_16x16x128_f8f6f4 v[50:53], v[26:33], v[228:235], v[50:53]
	v_mfma_f32_16x16x128_f8f6f4 v[38:41], v[18:25], v[236:243], v[38:41]
	v_mfma_f32_16x16x128_f8f6f4 v[34:37], v[26:33], v[236:243], v[34:37]
	s_setprio 0
	s_add_i32 s21, s21, 2
	s_add_u32 s5, s5, 0x10000
	s_addc_u32 s19, s19, 0
	s_add_u32 s26, s26, 0x10000
	s_addc_u32 s27, s27, 0
	s_cmp_gt_u32 s21, 13
	s_cbranch_scc0 .Lh1_372
	s_branch .Lfx_9967
.Lh1_372:
	ds_read_b128 v[18:21], v207
	ds_read_b128 v[22:25], v207 offset:1024
	ds_read_b128 v[26:29], v207 offset:2048
	ds_read_b128 v[30:33], v207 offset:3072
	ds_read_b128 v[2:5], v208
	ds_read_b128 v[6:9], v208 offset:1024
	ds_read_b128 v[10:13], v208 offset:2048
	ds_read_b128 v[14:17], v208 offset:3072
	s_add_u32 s28, s26, 0x8000
	s_addc_u32 s29, s27, 0
	s_cmp_eq_u32 s21, 12
	s_cselect_b32 s40, s22, s28
	s_cselect_b32 s41, s23, s29
	s_cselect_b32 s30, s24, s5
	s_cselect_b32 s31, s25, s19
	s_add_u32 s28, s40, 0x8000
	s_addc_u32 s29, s41, 0
	s_add_i32 m0, s46, 0xc000
	ds_read_b128 v[212:215], v209
	ds_read_b128 v[216:219], v209 offset:1024
	ds_read_b128 v[220:223], v209 offset:2048
	ds_read_b128 v[224:227], v209 offset:3072
	ds_read_b128 v[228:231], v209 offset:4096
	ds_read_b128 v[232:235], v209 offset:5120
	ds_read_b128 v[236:239], v209 offset:6144
	ds_read_b128 v[240:243], v209 offset:7168
	global_load_lds_dwordx4 v190, s[26:27]
	s_add_i32 m0, s46, 0xe000
	s_nop 0
	global_load_lds_dwordx4 v188, s[26:27]
	s_waitcnt vmcnt(8)
	s_waitcnt lgkmcnt(0)
	s_barrier
; #define PG8_STAGE(bufoff, gbase, voff) do { _Pragma("unroll") for (int _i = 0; _i < 2; ++_i) \
;         __builtin_amdgcn_global_load_lds((const unsigned*)((const char*)(gbase) + (voff)[_i]), (PG8_LAS unsigned*)(lds + (bufoff) + ldsw + _i * 8192), 16, 0, 0); } while (0)
; #define PG8_WAIT_V(n) asm volatile("s_waitcnt vmcnt(" #n ")" ::: "memory")
; #define PG8_WAIT_L(n) asm volatile("s_waitcnt lgkmcnt(" #n ")" ::: "memory")
; template <class Epi, class Sched, bool ALIGN_EPI = true, bool F8 = false>
; __device__ __forceinline__ void gemm_phase(PG8_LAS unsigned char* lds, const Sched& S, const Epi& E) {
;     ...
;         for (int t = 0; t < nt; t += 2) {
;             const bool last = (t == nt - 2);
;             if constexpr (Sched::GATHER) { if (last && has_next) S.a_off(nxt, Rs, Cs, voffAn); }
;             const char* a1 = cA + (size_t)(t + 1) * kstep;
;             const char* a2 = last ? nA : cA + (size_t)(t + 2) * kstep; const char* b2 = last ? nB : cB + (size_t)(t + 2) * kstepB;
;             const char* a3 = a2 + kstep; const char* b3 = b2 + kstepB;
;             unsigned vA2[2][2];
; #pragma unroll
;             for (int h = 0; h < 2; ++h)
; #pragma unroll
;                 for (int i = 0; i < 2; ++i) { if constexpr (Sched::GATHER) vA2[h][i] = (last && has_next) ? voffAn[h][i] : voffA[h][i]; else vA2[h][i] = voffA[h][i]; }
;             PG8_LDB(B0, 0, 0); PG8_LDB(B1, 0, 1); PG8_SCHED; PG8_LDA(At, 0, 0); PG8_STAGE(PG8_SA(1, 1), a1, voffA[1]);
;             PG8_WAIT_V(8); PG8_WAIT_L(0); PG8_BAR; PG8_MMA(0, 0, At, B0); PG8_MMA(0, 1, At, B1); PG8_BAR; PG8_SCHED;
;             PG8_LDA(At, 0, 1); PG8_STAGE(PG8_SB(0, 0), b2, voffB[0]); PG8_STAGE(PG8_SB(0, 1), b2, voffB[1]); PG8_STAGE(PG8_SA(0, 0), a2, vA2[0]);
;             PG8_WAIT_V(8); PG8_WAIT_L(0); PG8_BAR; PG8_MMA(1, 0, At, B0); PG8_MMA(1, 1, At, B1); PG8_BAR; PG8_SCHED;
;             PG8_LDB(B0, 1, 0); PG8_LDB(B1, 1, 1); PG8_SCHED; PG8_LDA(At, 1, 0); PG8_STAGE(PG8_SA(0, 1), a2, vA2[1]);
;             PG8_WAIT_V(8); PG8_WAIT_L(0); PG8_BAR; PG8_MMA(0, 0, At, B0); PG8_MMA(0, 1, At, B1); PG8_BAR; PG8_SCHED;
;             PG8_LDA(At, 1, 1); PG8_STAGE(PG8_SB(1, 0), b3, voffB[0]); PG8_STAGE(PG8_SB(1, 1), b3, voffB[1]); PG8_STAGE(PG8_SA(1, 0), a3, vA2[0]);
;             PG8_WAIT_V(8); PG8_WAIT_L(0); PG8_BAR; PG8_MMA(1, 0, At, B0); PG8_MMA(1, 1, At, B1); PG8_BAR; PG8_SCHED;
	s_setprio 2
	v_mfma_f32_16x16x128_f8f6f4 v[158:161], v[18:25], v[212:219], v[158:161]
	v_mfma_f32_16x16x128_f8f6f4 v[154:157], v[26:33], v[212:219], v[154:157]
	v_mfma_f32_16x16x128_f8f6f4 v[142:145], v[18:25], v[220:227], v[142:145]
	v_mfma_f32_16x16x128_f8f6f4 v[138:141], v[26:33], v[220:227], v[138:141]
	v_mfma_f32_16x16x128_f8f6f4 v[126:129], v[18:25], v[228:235], v[126:129]
	v_mfma_f32_16x16x128_f8f6f4 v[122:125], v[26:33], v[228:235], v[122:125]
	v_mfma_f32_16x16x128_f8f6f4 v[110:113], v[18:25], v[236:243], v[110:113]
	v_mfma_f32_16x16x128_f8f6f4 v[106:109], v[26:33], v[236:243], v[106:109]
	s_setprio 0
	s_setprio 2
	v_mfma_f32_16x16x128_f8f6f4 v[150:153], v[2:9], v[212:219], v[150:153]
	v_mfma_f32_16x16x128_f8f6f4 v[146:149], v[10:17], v[212:219], v[146:149]
	v_mfma_f32_16x16x128_f8f6f4 v[134:137], v[2:9], v[220:227], v[134:137]
	v_mfma_f32_16x16x128_f8f6f4 v[130:133], v[10:17], v[220:227], v[130:133]
	v_mfma_f32_16x16x128_f8f6f4 v[118:121], v[2:9], v[228:235], v[118:121]
	v_mfma_f32_16x16x128_f8f6f4 v[114:117], v[10:17], v[228:235], v[114:117]
	v_mfma_f32_16x16x128_f8f6f4 v[102:105], v[2:9], v[236:243], v[102:105]
	v_mfma_f32_16x16x128_f8f6f4 v[98:101], v[10:17], v[236:243], v[98:101]
	s_setprio 0
	s_add_i32 s67, s62, s45
	s_mov_b32 m0, s67
	ds_read_b128 v[212:215], v209 offset:16384
	ds_read_b128 v[216:219], v209 offset:17408
	ds_read_b128 v[220:223], v209 offset:18432
	ds_read_b128 v[224:227], v209 offset:19456
	ds_read_b128 v[228:231], v209 offset:20480
	ds_read_b128 v[232:235], v209 offset:21504
	ds_read_b128 v[236:239], v209 offset:22528
	ds_read_b128 v[240:243], v209 offset:23552
	global_load_lds_dwordx4 v164, s[30:31]
	s_add_i32 m0, s67, 0x2000
	s_add_i32 s67, s63, s45
	global_load_lds_dwordx4 v166, s[30:31]
	s_add_u32 s98, s30, s8
	s_addc_u32 s99, s31, s9
	s_mov_b32 m0, s67
	s_nop 0
	global_load_lds_dwordx4 v164, s[98:99]
	s_add_u32 s100, s30, s8
	s_addc_u32 s101, s31, s9
	s_add_i32 m0, s67, 0x2000
	s_nop 0
	global_load_lds_dwordx4 v166, s[100:101]
	s_mov_b32 m0, s46
	s_nop 0
	global_load_lds_dwordx4 v174, s[40:41]
	s_mov_b32 m0, s47
	s_nop 0
	global_load_lds_dwordx4 v176, s[40:41]
	s_waitcnt vmcnt(8)
	s_waitcnt lgkmcnt(0)
	s_barrier
	s_setprio 2
	v_mfma_f32_16x16x128_f8f6f4 v[94:97], v[18:25], v[212:219], v[94:97]
	v_mfma_f32_16x16x128_f8f6f4 v[90:93], v[26:33], v[212:219], v[90:93]
	v_mfma_f32_16x16x128_f8f6f4 v[78:81], v[18:25], v[220:227], v[78:81]
	v_mfma_f32_16x16x128_f8f6f4 v[74:77], v[26:33], v[220:227], v[74:77]
	v_mfma_f32_16x16x128_f8f6f4 v[62:65], v[18:25], v[228:235], v[62:65]
	v_mfma_f32_16x16x128_f8f6f4 v[58:61], v[26:33], v[228:235], v[58:61]
	v_mfma_f32_16x16x128_f8f6f4 v[46:49], v[18:25], v[236:243], v[46:49]
	v_mfma_f32_16x16x128_f8f6f4 v[42:45], v[26:33], v[236:243], v[42:45]
	s_setprio 0
	s_setprio 2
	v_mfma_f32_16x16x128_f8f6f4 v[86:89], v[2:9], v[212:219], v[86:89]
	v_mfma_f32_16x16x128_f8f6f4 v[82:85], v[10:17], v[212:219], v[82:85]
	v_mfma_f32_16x16x128_f8f6f4 v[70:73], v[2:9], v[220:227], v[70:73]
	v_mfma_f32_16x16x128_f8f6f4 v[66:69], v[10:17], v[220:227], v[66:69]
	v_mfma_f32_16x16x128_f8f6f4 v[54:57], v[2:9], v[228:235], v[54:57]
	v_mfma_f32_16x16x128_f8f6f4 v[50:53], v[10:17], v[228:235], v[50:53]
	v_mfma_f32_16x16x128_f8f6f4 v[38:41], v[2:9], v[236:243], v[38:41]
	v_mfma_f32_16x16x128_f8f6f4 v[34:37], v[10:17], v[236:243], v[34:37]
	s_setprio 0
	s_add_i32 s67, 0, 0x18000
	s_add_i32 s68, 0, 0x1c000
	v_add_u32_e32 v14, s67, v202
	v_add_u32_e32 v30, s68, v202
	ds_read_b128 v[2:5], v14
	ds_read_b128 v[6:9], v14 offset:1024
	ds_read_b128 v[10:13], v14 offset:2048
	ds_read_b128 v[14:17], v14 offset:3072
	ds_read_b128 v[18:21], v30
	ds_read_b128 v[22:25], v30 offset:1024
	ds_read_b128 v[26:29], v30 offset:2048
	ds_read_b128 v[30:33], v30 offset:3072
	s_mov_b32 m0, s48
	ds_read_b128 v[212:215], v209 offset:32768
	ds_read_b128 v[216:219], v209 offset:33792
	ds_read_b128 v[220:223], v209 offset:34816
	ds_read_b128 v[224:227], v209 offset:35840
	ds_read_b128 v[228:231], v209 offset:36864
	ds_read_b128 v[232:235], v209 offset:37888
	ds_read_b128 v[236:239], v209 offset:38912
	ds_read_b128 v[240:243], v209 offset:39936
	global_load_lds_dwordx4 v178, s[40:41]
	s_mov_b32 m0, s49
	s_nop 0
	global_load_lds_dwordx4 v180, s[40:41]
	s_waitcnt vmcnt(8)
	s_waitcnt lgkmcnt(0)
	s_barrier
; #define PG8_STAGE(bufoff, gbase, voff) do { _Pragma("unroll") for (int _i = 0; _i < 2; ++_i) \
;         __builtin_amdgcn_global_load_lds((const unsigned*)((const char*)(gbase) + (voff)[_i]), (PG8_LAS unsigned*)(lds + (bufoff) + ldsw + _i * 8192), 16, 0, 0); } while (0)
; #define PG8_WAIT_V(n) asm volatile("s_waitcnt vmcnt(" #n ")" ::: "memory")
; #define PG8_WAIT_L(n) asm volatile("s_waitcnt lgkmcnt(" #n ")" ::: "memory")
; template <class Epi, class Sched, bool ALIGN_EPI = true, bool F8 = false>
; __device__ __forceinline__ void gemm_phase(PG8_LAS unsigned char* lds, const Sched& S, const Epi& E) {
;     ...
;         for (int t = 0; t < nt; t += 2) {
;             const bool last = (t == nt - 2);
;             if constexpr (Sched::GATHER) { if (last && has_next) S.a_off(nxt, Rs, Cs, voffAn); }
;             const char* a1 = cA + (size_t)(t + 1) * kstep;
;             const char* a2 = last ? nA : cA + (size_t)(t + 2) * kstep; const char* b2 = last ? nB : cB + (size_t)(t + 2) * kstepB;
;             const char* a3 = a2 + kstep; const char* b3 = b2 + kstepB;
;             unsigned vA2[2][2];
; #pragma unroll
;             for (int h = 0; h < 2; ++h)
; #pragma unroll
;                 for (int i = 0; i < 2; ++i) { if constexpr (Sched::GATHER) vA2[h][i] = (last && has_next) ? voffAn[h][i] : voffA[h][i]; else vA2[h][i] = voffA[h][i]; }
;             PG8_LDB(B0, 0, 0); PG8_LDB(B1, 0, 1); PG8_SCHED; PG8_LDA(At, 0, 0); PG8_STAGE(PG8_SA(1, 1), a1, voffA[1]);
;             PG8_WAIT_V(8); PG8_WAIT_L(0); PG8_BAR; PG8_MMA(0, 0, At, B0); PG8_MMA(0, 1, At, B1); PG8_BAR; PG8_SCHED;
;             PG8_LDA(At, 0, 1); PG8_STAGE(PG8_SB(0, 0), b2, voffB[0]); PG8_STAGE(PG8_SB(0, 1), b2, voffB[1]); PG8_STAGE(PG8_SA(0, 0), a2, vA2[0]);
;             PG8_WAIT_V(8); PG8_WAIT_L(0); PG8_BAR; PG8_MMA(1, 0, At, B0); PG8_MMA(1, 1, At, B1); PG8_BAR; PG8_SCHED;
;             PG8_LDB(B0, 1, 0); PG8_LDB(B1, 1, 1); PG8_SCHED; PG8_LDA(At, 1, 0); PG8_STAGE(PG8_SA(0, 1), a2, vA2[1]);
;             PG8_WAIT_V(8); PG8_WAIT_L(0); PG8_BAR; PG8_MMA(0, 0, At, B0); PG8_MMA(0, 1, At, B1); PG8_BAR; PG8_SCHED;
;             PG8_LDA(At, 1, 1); PG8_STAGE(PG8_SB(1, 0), b3, voffB[0]); PG8_STAGE(PG8_SB(1, 1), b3, voffB[1]); PG8_STAGE(PG8_SA(1, 0), a3, vA2[0]);
;             PG8_WAIT_V(8); PG8_WAIT_L(0); PG8_BAR; PG8_MMA(1, 0, At, B0); PG8_MMA(1, 1, At, B1); PG8_BAR; PG8_SCHED;
	s_setprio 2
	v_mfma_f32_16x16x128_f8f6f4 v[158:161], v[2:9], v[212:219], v[158:161]
	v_mfma_f32_16x16x128_f8f6f4 v[154:157], v[10:17], v[212:219], v[154:157]
	v_mfma_f32_16x16x128_f8f6f4 v[142:145], v[2:9], v[220:227], v[142:145]
	v_mfma_f32_16x16x128_f8f6f4 v[138:141], v[10:17], v[220:227], v[138:141]
	v_mfma_f32_16x16x128_f8f6f4 v[126:129], v[2:9], v[228:235], v[126:129]
	v_mfma_f32_16x16x128_f8f6f4 v[122:125], v[10:17], v[228:235], v[122:125]
	v_mfma_f32_16x16x128_f8f6f4 v[110:113], v[2:9], v[236:243], v[110:113]
	v_mfma_f32_16x16x128_f8f6f4 v[106:109], v[10:17], v[236:243], v[106:109]
	s_setprio 0
	s_setprio 2
	v_mfma_f32_16x16x128_f8f6f4 v[150:153], v[18:25], v[212:219], v[150:153]
	v_mfma_f32_16x16x128_f8f6f4 v[146:149], v[26:33], v[212:219], v[146:149]
	v_mfma_f32_16x16x128_f8f6f4 v[134:137], v[18:25], v[220:227], v[134:137]
	v_mfma_f32_16x16x128_f8f6f4 v[130:133], v[26:33], v[220:227], v[130:133]
	v_mfma_f32_16x16x128_f8f6f4 v[118:121], v[18:25], v[228:235], v[118:121]
	v_mfma_f32_16x16x128_f8f6f4 v[114:117], v[26:33], v[228:235], v[114:117]
	v_mfma_f32_16x16x128_f8f6f4 v[102:105], v[18:25], v[236:243], v[102:105]
	v_mfma_f32_16x16x128_f8f6f4 v[98:101], v[26:33], v[236:243], v[98:101]
	s_setprio 0
	s_add_u32 s30, s30, 0x8000
	s_addc_u32 s31, s31, 0
	s_add_i32 s40, s67, s45
	s_mov_b32 m0, s40
	ds_read_b128 v[212:215], v209 offset:49152
	ds_read_b128 v[216:219], v209 offset:50176
	ds_read_b128 v[220:223], v209 offset:51200
	ds_read_b128 v[224:227], v209 offset:52224
	ds_read_b128 v[228:231], v209 offset:53248
	ds_read_b128 v[232:235], v209 offset:54272
	ds_read_b128 v[236:239], v209 offset:55296
	ds_read_b128 v[240:243], v209 offset:56320
	global_load_lds_dwordx4 v164, s[30:31]
	s_add_i32 m0, s40, 0x2000
	s_add_i32 s40, s68, s45
	global_load_lds_dwordx4 v166, s[30:31]
	s_mov_b32 m0, s40
	s_nop 0
	global_load_lds_dwordx4 v168, s[30:31]
	s_add_i32 m0, s40, 0x2000
	s_nop 0
	global_load_lds_dwordx4 v172, s[30:31]
	s_mov_b32 m0, s52
	s_nop 0
	global_load_lds_dwordx4 v174, s[28:29]
	s_mov_b32 m0, s53
	s_nop 0
	global_load_lds_dwordx4 v176, s[28:29]
	s_waitcnt vmcnt(8)
	s_waitcnt lgkmcnt(0)
	s_barrier
	s_setprio 2
	v_mfma_f32_16x16x128_f8f6f4 v[94:97], v[2:9], v[212:219], v[94:97]
	v_mfma_f32_16x16x128_f8f6f4 v[90:93], v[10:17], v[212:219], v[90:93]
	v_mfma_f32_16x16x128_f8f6f4 v[78:81], v[2:9], v[220:227], v[78:81]
	v_mfma_f32_16x16x128_f8f6f4 v[74:77], v[10:17], v[220:227], v[74:77]
	v_mfma_f32_16x16x128_f8f6f4 v[62:65], v[2:9], v[228:235], v[62:65]
	v_mfma_f32_16x16x128_f8f6f4 v[58:61], v[10:17], v[228:235], v[58:61]
	v_mfma_f32_16x16x128_f8f6f4 v[46:49], v[2:9], v[236:243], v[46:49]
	v_mfma_f32_16x16x128_f8f6f4 v[42:45], v[10:17], v[236:243], v[42:45]
	s_setprio 0
	s_setprio 2
	v_mfma_f32_16x16x128_f8f6f4 v[86:89], v[18:25], v[212:219], v[86:89]
	v_mfma_f32_16x16x128_f8f6f4 v[82:85], v[26:33], v[212:219], v[82:85]
	v_mfma_f32_16x16x128_f8f6f4 v[70:73], v[18:25], v[220:227], v[70:73]
	v_mfma_f32_16x16x128_f8f6f4 v[66:69], v[26:33], v[220:227], v[66:69]
	v_mfma_f32_16x16x128_f8f6f4 v[54:57], v[18:25], v[228:235], v[54:57]
	v_mfma_f32_16x16x128_f8f6f4 v[50:53], v[26:33], v[228:235], v[50:53]
	v_mfma_f32_16x16x128_f8f6f4 v[38:41], v[18:25], v[236:243], v[38:41]
	v_mfma_f32_16x16x128_f8f6f4 v[34:37], v[26:33], v[236:243], v[34:37]
	s_setprio 0
	s_add_i32 s21, s21, 2
	s_add_u32 s5, s5, 0x10000
	s_addc_u32 s19, s19, 0
	s_add_u32 s26, s26, 0x10000
	s_addc_u32 s27, s27, 0
	s_cmp_gt_u32 s21, 13
	s_cbranch_scc0 .Lh1_372

; #define PG8_WAIT_V(n) asm volatile("s_waitcnt vmcnt(" #n ")" ::: "memory")
; #define PG8_WAIT_L(n) asm volatile("s_waitcnt lgkmcnt(" #n ")" ::: "memory")
; template <class Epi, class Sched, bool ALIGN_EPI = true, bool F8 = false>
; __device__ __forceinline__ void gemm_phase(PG8_LAS unsigned char* lds, const Sched& S, const Epi& E) {
;     ...
;         for (int t = 0; t < nt; t += 2) {
;             const bool last = (t == nt - 2);
;             if constexpr (Sched::GATHER) { if (last && has_next) S.a_off(nxt, Rs, Cs, voffAn); }
;             const char* a1 = cA + (size_t)(t + 1) * kstep;
;             const char* a2 = last ? nA : cA + (size_t)(t + 2) * kstep; const char* b2 = last ? nB : cB + (size_t)(t + 2) * kstepB;
;             const char* a3 = a2 + kstep; const char* b3 = b2 + kstepB;
;             unsigned vA2[2][2];
; #pragma unroll
;             for (int h = 0; h < 2; ++h)
; #pragma unroll
;                 for (int i = 0; i < 2; ++i) { if constexpr (Sched::GATHER) vA2[h][i] = (last && has_next) ? voffAn[h][i] : voffA[h][i]; else vA2[h][i] = voffA[h][i]; }
;             PG8_LDB(B0, 0, 0); PG8_LDB(B1, 0, 1); PG8_SCHED; PG8_LDA(At, 0, 0); PG8_STAGE(PG8_SA(1, 1), a1, voffA[1]);
;             PG8_WAIT_V(8); PG8_WAIT_L(0); PG8_BAR; PG8_MMA(0, 0, At, B0); PG8_MMA(0, 1, At, B1); PG8_BAR; PG8_SCHED;
;             PG8_LDA(At, 0, 1); PG8_STAGE(PG8_SB(0, 0), b2, voffB[0]); PG8_STAGE(PG8_SB(0, 1), b2, voffB[1]); PG8_STAGE(PG8_SA(0, 0), a2, vA2[0]);
;             PG8_WAIT_V(8); PG8_WAIT_L(0); PG8_BAR; PG8_MMA(1, 0, At, B0); PG8_MMA(1, 1, At, B1); PG8_BAR; PG8_SCHED;
;             PG8_LDB(B0, 1, 0); PG8_LDB(B1, 1, 1); PG8_SCHED; PG8_LDA(At, 1, 0); PG8_STAGE(PG8_SA(0, 1), a2, vA2[1]);
;             PG8_WAIT_V(8); PG8_WAIT_L(0); PG8_BAR; PG8_MMA(0, 0, At, B0); PG8_MMA(0, 1, At, B1); PG8_BAR; PG8_SCHED;
;             PG8_LDA(At, 1, 1); PG8_STAGE(PG8_SB(1, 0), b3, voffB[0]); PG8_STAGE(PG8_SB(1, 1), b3, voffB[1]); PG8_STAGE(PG8_SA(1, 0), a3, vA2[0]);
;             PG8_WAIT_V(8); PG8_WAIT_L(0); PG8_BAR; PG8_MMA(1, 0, At, B0); PG8_MMA(1, 1, At, B1); PG8_BAR; PG8_SCHED;
;     ...
;         for (int a = 0; a < 2; ++a)
; #pragma unroll
;             for (int b = 0; b < 2; ++b)
; #pragma unroll
;                 for (int m = 0; m < 4; ++m)
; #pragma unroll
;                     for (int n = 0; n < 2; ++n) acc[a][b][m][n] = (f32x4){0.f, 0.f, 0.f, 0.f};
.Lpk0_428:
	ds_read_b128 v[18:21], v192
	ds_read_b128 v[22:25], v192 offset:1024
	ds_read_b128 v[26:29], v192 offset:2048
	ds_read_b128 v[30:33], v192 offset:3072
	ds_read_b128 v[2:5], v193
	ds_read_b128 v[6:9], v193 offset:1024
	ds_read_b128 v[10:13], v193 offset:2048
	ds_read_b128 v[14:17], v193 offset:3072
	s_add_u32 s26, s24, 0x8000
	s_addc_u32 s27, s25, 0
	s_cmp_eq_u32 s74, 12
	s_cselect_b32 s30, s20, s26
	s_cselect_b32 s31, s21, s27
	s_cselect_b32 s28, s22, s17
	s_cselect_b32 s29, s23, s19
	s_add_u32 s26, s30, 0x8000
	s_addc_u32 s27, s31, 0
	s_add_i32 m0, s48, 0xc000
	ds_read_b128 v[198:201], v194
	ds_read_b128 v[202:205], v194 offset:1024
	ds_read_b128 v[206:209], v194 offset:2048
	ds_read_b128 v[210:213], v194 offset:3072
	ds_read_b128 v[214:217], v194 offset:4096
	ds_read_b128 v[218:221], v194 offset:5120
	ds_read_b128 v[222:225], v194 offset:6144
	ds_read_b128 v[226:229], v194 offset:7168
	global_load_lds_dwordx4 v184, s[24:25]
	s_add_i32 m0, s48, 0xe000
	s_nop 0
	global_load_lds_dwordx4 v182, s[24:25]
	s_waitcnt vmcnt(8)
	s_waitcnt lgkmcnt(0)
	s_setprio 1
	v_mfma_f32_16x16x128_f8f6f4 v[158:161], v[18:25], v[198:205], 0
	v_mfma_f32_16x16x128_f8f6f4 v[154:157], v[26:33], v[198:205], 0
	v_mfma_f32_16x16x128_f8f6f4 v[142:145], v[18:25], v[206:213], 0
	v_mfma_f32_16x16x128_f8f6f4 v[138:141], v[26:33], v[206:213], 0
	v_mfma_f32_16x16x128_f8f6f4 v[126:129], v[18:25], v[214:221], 0
	v_mfma_f32_16x16x128_f8f6f4 v[122:125], v[26:33], v[214:221], 0
	v_mfma_f32_16x16x128_f8f6f4 v[110:113], v[18:25], v[222:229], 0
	v_mfma_f32_16x16x128_f8f6f4 v[106:109], v[26:33], v[222:229], 0
	s_setprio 0
	s_setprio 1
	v_mfma_f32_16x16x128_f8f6f4 v[150:153], v[2:9], v[198:205], 0
	v_mfma_f32_16x16x128_f8f6f4 v[146:149], v[10:17], v[198:205], 0
	v_mfma_f32_16x16x128_f8f6f4 v[134:137], v[2:9], v[206:213], 0
	v_mfma_f32_16x16x128_f8f6f4 v[130:133], v[10:17], v[206:213], 0
	v_mfma_f32_16x16x128_f8f6f4 v[118:121], v[2:9], v[214:221], 0
	v_mfma_f32_16x16x128_f8f6f4 v[114:117], v[10:17], v[214:221], 0
	v_mfma_f32_16x16x128_f8f6f4 v[102:105], v[2:9], v[222:229], 0
	v_mfma_f32_16x16x128_f8f6f4 v[98:101], v[10:17], v[222:229], 0
	s_setprio 0
	s_barrier
	s_add_i32 s75, s65, s47
	s_mov_b32 m0, s75
	ds_read_b128 v[198:201], v194 offset:16384
	ds_read_b128 v[202:205], v194 offset:17408
	ds_read_b128 v[206:209], v194 offset:18432
	ds_read_b128 v[210:213], v194 offset:19456
	ds_read_b128 v[214:217], v194 offset:20480
	ds_read_b128 v[218:221], v194 offset:21504
	ds_read_b128 v[222:225], v194 offset:22528
	ds_read_b128 v[226:229], v194 offset:23552
	global_load_lds_dwordx4 v164, s[28:29]
	s_add_i32 m0, s75, 0x2000
	s_add_i32 s75, s66, s47
	global_load_lds_dwordx4 v166, s[28:29]
	s_add_u32 s98, s28, s4
	s_addc_u32 s99, s29, s5
	s_mov_b32 m0, s75
	s_nop 0
	global_load_lds_dwordx4 v164, s[98:99]
	s_add_u32 s100, s28, s4
	s_addc_u32 s101, s29, s5
	s_add_i32 m0, s75, 0x2000
	s_nop 0
	global_load_lds_dwordx4 v166, s[100:101]
	s_mov_b32 m0, s48
	s_nop 0
	global_load_lds_dwordx4 v174, s[30:31]
	s_mov_b32 m0, s49
	s_nop 0
	global_load_lds_dwordx4 v176, s[30:31]
	s_waitcnt vmcnt(8)
	s_waitcnt lgkmcnt(0)
	s_setprio 1
	v_mfma_f32_16x16x128_f8f6f4 v[94:97], v[18:25], v[198:205], 0
	v_mfma_f32_16x16x128_f8f6f4 v[90:93], v[26:33], v[198:205], 0
	v_mfma_f32_16x16x128_f8f6f4 v[78:81], v[18:25], v[206:213], 0
	v_mfma_f32_16x16x128_f8f6f4 v[74:77], v[26:33], v[206:213], 0
	v_mfma_f32_16x16x128_f8f6f4 v[62:65], v[18:25], v[214:221], 0
	v_mfma_f32_16x16x128_f8f6f4 v[58:61], v[26:33], v[214:221], 0
	v_mfma_f32_16x16x128_f8f6f4 v[46:49], v[18:25], v[222:229], 0
	v_mfma_f32_16x16x128_f8f6f4 v[42:45], v[26:33], v[222:229], 0
	s_setprio 0
	s_setprio 1
	v_mfma_f32_16x16x128_f8f6f4 v[86:89], v[2:9], v[198:205], 0
	v_mfma_f32_16x16x128_f8f6f4 v[82:85], v[10:17], v[198:205], 0
	v_mfma_f32_16x16x128_f8f6f4 v[70:73], v[2:9], v[206:213], 0
	v_mfma_f32_16x16x128_f8f6f4 v[66:69], v[10:17], v[206:213], 0
	v_mfma_f32_16x16x128_f8f6f4 v[54:57], v[2:9], v[214:221], 0
	v_mfma_f32_16x16x128_f8f6f4 v[50:53], v[10:17], v[214:221], 0
	v_mfma_f32_16x16x128_f8f6f4 v[38:41], v[2:9], v[222:229], 0
	v_mfma_f32_16x16x128_f8f6f4 v[34:37], v[10:17], v[222:229], 0
	s_setprio 0
	s_barrier
	s_add_i32 s75, 0, 0x18000
	s_add_i32 s76, 0, 0x1c000
	v_add_u32_e32 v14, s75, v191
	v_add_u32_e32 v30, s76, v191
	ds_read_b128 v[2:5], v14
	ds_read_b128 v[6:9], v14 offset:1024
	ds_read_b128 v[10:13], v14 offset:2048
	ds_read_b128 v[14:17], v14 offset:3072
	ds_read_b128 v[18:21], v30
	ds_read_b128 v[22:25], v30 offset:1024
	ds_read_b128 v[26:29], v30 offset:2048
	ds_read_b128 v[30:33], v30 offset:3072
	s_mov_b32 m0, s50
	ds_read_b128 v[198:201], v194 offset:32768
	ds_read_b128 v[202:205], v194 offset:33792
	ds_read_b128 v[206:209], v194 offset:34816
	ds_read_b128 v[210:213], v194 offset:35840
	ds_read_b128 v[214:217], v194 offset:36864
	ds_read_b128 v[218:221], v194 offset:37888
	ds_read_b128 v[222:225], v194 offset:38912
	ds_read_b128 v[226:229], v194 offset:39936
	global_load_lds_dwordx4 v178, s[30:31]
	s_mov_b32 m0, s51
	s_nop 0
	global_load_lds_dwordx4 v180, s[30:31]
	s_waitcnt vmcnt(8)
	s_waitcnt lgkmcnt(0)
	s_setprio 1
	v_mfma_f32_16x16x128_f8f6f4 v[158:161], v[2:9], v[198:205], v[158:161]
	v_mfma_f32_16x16x128_f8f6f4 v[154:157], v[10:17], v[198:205], v[154:157]
	v_mfma_f32_16x16x128_f8f6f4 v[142:145], v[2:9], v[206:213], v[142:145]
	v_mfma_f32_16x16x128_f8f6f4 v[138:141], v[10:17], v[206:213], v[138:141]
	v_mfma_f32_16x16x128_f8f6f4 v[126:129], v[2:9], v[214:221], v[126:129]
	v_mfma_f32_16x16x128_f8f6f4 v[122:125], v[10:17], v[214:221], v[122:125]
	v_mfma_f32_16x16x128_f8f6f4 v[110:113], v[2:9], v[222:229], v[110:113]
	v_mfma_f32_16x16x128_f8f6f4 v[106:109], v[10:17], v[222:229], v[106:109]
	s_setprio 0
	s_setprio 1
	v_mfma_f32_16x16x128_f8f6f4 v[150:153], v[18:25], v[198:205], v[150:153]
	v_mfma_f32_16x16x128_f8f6f4 v[146:149], v[26:33], v[198:205], v[146:149]
	v_mfma_f32_16x16x128_f8f6f4 v[134:137], v[18:25], v[206:213], v[134:137]
	v_mfma_f32_16x16x128_f8f6f4 v[130:133], v[26:33], v[206:213], v[130:133]
	v_mfma_f32_16x16x128_f8f6f4 v[118:121], v[18:25], v[214:221], v[118:121]
	v_mfma_f32_16x16x128_f8f6f4 v[114:117], v[26:33], v[214:221], v[114:117]
	v_mfma_f32_16x16x128_f8f6f4 v[102:105], v[18:25], v[222:229], v[102:105]
	v_mfma_f32_16x16x128_f8f6f4 v[98:101], v[26:33], v[222:229], v[98:101]
	s_setprio 0
	s_barrier
; #define PG8_STAGE(bufoff, gbase, voff) do { _Pragma("unroll") for (int _i = 0; _i < 2; ++_i) \
;         __builtin_amdgcn_global_load_lds((const unsigned*)((const char*)(gbase) + (voff)[_i]), (PG8_LAS unsigned*)(lds + (bufoff) + ldsw + _i * 8192), 16, 0, 0); } while (0)
; #define PG8_WAIT_V(n) asm volatile("s_waitcnt vmcnt(" #n ")" ::: "memory")
; #define PG8_WAIT_L(n) asm volatile("s_waitcnt lgkmcnt(" #n ")" ::: "memory")
; template <class Epi, class Sched, bool ALIGN_EPI = true, bool F8 = false>
; __device__ __forceinline__ void gemm_phase(PG8_LAS unsigned char* lds, const Sched& S, const Epi& E) {
;     ...
;         for (int t = 0; t < nt; t += 2) {
;             const bool last = (t == nt - 2);
;             if constexpr (Sched::GATHER) { if (last && has_next) S.a_off(nxt, Rs, Cs, voffAn); }
;             const char* a1 = cA + (size_t)(t + 1) * kstep;
;             const char* a2 = last ? nA : cA + (size_t)(t + 2) * kstep; const char* b2 = last ? nB : cB + (size_t)(t + 2) * kstepB;
;             const char* a3 = a2 + kstep; const char* b3 = b2 + kstepB;
;             unsigned vA2[2][2];
; #pragma unroll
;             for (int h = 0; h < 2; ++h)
; #pragma unroll
;                 for (int i = 0; i < 2; ++i) { if constexpr (Sched::GATHER) vA2[h][i] = (last && has_next) ? voffAn[h][i] : voffA[h][i]; else vA2[h][i] = voffA[h][i]; }
;             PG8_LDB(B0, 0, 0); PG8_LDB(B1, 0, 1); PG8_SCHED; PG8_LDA(At, 0, 0); PG8_STAGE(PG8_SA(1, 1), a1, voffA[1]);
;             PG8_WAIT_V(8); PG8_WAIT_L(0); PG8_BAR; PG8_MMA(0, 0, At, B0); PG8_MMA(0, 1, At, B1); PG8_BAR; PG8_SCHED;
;             PG8_LDA(At, 0, 1); PG8_STAGE(PG8_SB(0, 0), b2, voffB[0]); PG8_STAGE(PG8_SB(0, 1), b2, voffB[1]); PG8_STAGE(PG8_SA(0, 0), a2, vA2[0]);
;             PG8_WAIT_V(8); PG8_WAIT_L(0); PG8_BAR; PG8_MMA(1, 0, At, B0); PG8_MMA(1, 1, At, B1); PG8_BAR; PG8_SCHED;
;             PG8_LDB(B0, 1, 0); PG8_LDB(B1, 1, 1); PG8_SCHED; PG8_LDA(At, 1, 0); PG8_STAGE(PG8_SA(0, 1), a2, vA2[1]);
;             PG8_WAIT_V(8); PG8_WAIT_L(0); PG8_BAR; PG8_MMA(0, 0, At, B0); PG8_MMA(0, 1, At, B1); PG8_BAR; PG8_SCHED;
;             PG8_LDA(At, 1, 1); PG8_STAGE(PG8_SB(1, 0), b3, voffB[0]); PG8_STAGE(PG8_SB(1, 1), b3, voffB[1]); PG8_STAGE(PG8_SA(1, 0), a3, vA2[0]);
;             PG8_WAIT_V(8); PG8_WAIT_L(0); PG8_BAR; PG8_MMA(1, 0, At, B0); PG8_MMA(1, 1, At, B1); PG8_BAR; PG8_SCHED;
	s_add_u32 s28, s28, 0x8000
	s_addc_u32 s29, s29, 0
	s_add_i32 s30, s75, s47
	s_mov_b32 m0, s30
	ds_read_b128 v[198:201], v194 offset:49152
	ds_read_b128 v[202:205], v194 offset:50176
	ds_read_b128 v[206:209], v194 offset:51200
	ds_read_b128 v[210:213], v194 offset:52224
	ds_read_b128 v[214:217], v194 offset:53248
	ds_read_b128 v[218:221], v194 offset:54272
	ds_read_b128 v[222:225], v194 offset:55296
	ds_read_b128 v[226:229], v194 offset:56320
	global_load_lds_dwordx4 v164, s[28:29]
	s_add_i32 m0, s30, 0x2000
	s_add_i32 s30, s76, s47
	global_load_lds_dwordx4 v166, s[28:29]
	s_mov_b32 m0, s30
	s_nop 0
	global_load_lds_dwordx4 v168, s[28:29]
	s_add_i32 m0, s30, 0x2000
	s_nop 0
	global_load_lds_dwordx4 v172, s[28:29]
	s_mov_b32 m0, s60
	s_nop 0
	global_load_lds_dwordx4 v174, s[26:27]
	s_mov_b32 m0, s61
	s_nop 0
	global_load_lds_dwordx4 v176, s[26:27]
	s_waitcnt vmcnt(8)
	s_waitcnt lgkmcnt(0)
	s_setprio 1
	v_mfma_f32_16x16x128_f8f6f4 v[94:97], v[2:9], v[198:205], v[94:97]
	v_mfma_f32_16x16x128_f8f6f4 v[90:93], v[10:17], v[198:205], v[90:93]
	v_mfma_f32_16x16x128_f8f6f4 v[78:81], v[2:9], v[206:213], v[78:81]
	v_mfma_f32_16x16x128_f8f6f4 v[74:77], v[10:17], v[206:213], v[74:77]
	v_mfma_f32_16x16x128_f8f6f4 v[62:65], v[2:9], v[214:221], v[62:65]
	v_mfma_f32_16x16x128_f8f6f4 v[58:61], v[10:17], v[214:221], v[58:61]
	v_mfma_f32_16x16x128_f8f6f4 v[46:49], v[2:9], v[222:229], v[46:49]
	v_mfma_f32_16x16x128_f8f6f4 v[42:45], v[10:17], v[222:229], v[42:45]
	s_setprio 0
	s_setprio 1
	v_mfma_f32_16x16x128_f8f6f4 v[86:89], v[18:25], v[198:205], v[86:89]
	v_mfma_f32_16x16x128_f8f6f4 v[82:85], v[26:33], v[198:205], v[82:85]
	v_mfma_f32_16x16x128_f8f6f4 v[70:73], v[18:25], v[206:213], v[70:73]
	v_mfma_f32_16x16x128_f8f6f4 v[66:69], v[26:33], v[206:213], v[66:69]
	v_mfma_f32_16x16x128_f8f6f4 v[54:57], v[18:25], v[214:221], v[54:57]
	v_mfma_f32_16x16x128_f8f6f4 v[50:53], v[26:33], v[214:221], v[50:53]
	v_mfma_f32_16x16x128_f8f6f4 v[38:41], v[18:25], v[222:229], v[38:41]
	v_mfma_f32_16x16x128_f8f6f4 v[34:37], v[26:33], v[222:229], v[34:37]
	s_setprio 0
	s_barrier
	s_add_i32 s74, s74, 2
	s_add_u32 s17, s17, 0x10000
	s_addc_u32 s19, s19, 0
	s_add_u32 s24, s24, 0x10000
	s_addc_u32 s25, s25, 0
	s_cmp_gt_u32 s74, 13
	s_cbranch_scc0 .LBB0_428
	s_branch .Lfx_11141
.LBB0_428:
	ds_read_b128 v[18:21], v192
	ds_read_b128 v[22:25], v192 offset:1024
	ds_read_b128 v[26:29], v192 offset:2048
	ds_read_b128 v[30:33], v192 offset:3072
	ds_read_b128 v[2:5], v193
	ds_read_b128 v[6:9], v193 offset:1024
	ds_read_b128 v[10:13], v193 offset:2048
	ds_read_b128 v[14:17], v193 offset:3072
	s_add_u32 s26, s24, 0x8000
	s_addc_u32 s27, s25, 0
	s_cmp_eq_u32 s74, 12
	s_cselect_b32 s30, s20, s26
	s_cselect_b32 s31, s21, s27
	s_cselect_b32 s28, s22, s17
	s_cselect_b32 s29, s23, s19
	s_add_u32 s26, s30, 0x8000
	s_addc_u32 s27, s31, 0
	s_add_i32 m0, s48, 0xc000
	ds_read_b128 v[198:201], v194
	ds_read_b128 v[202:205], v194 offset:1024
	ds_read_b128 v[206:209], v194 offset:2048
	ds_read_b128 v[210:213], v194 offset:3072
	ds_read_b128 v[214:217], v194 offset:4096
	ds_read_b128 v[218:221], v194 offset:5120
	ds_read_b128 v[222:225], v194 offset:6144
	ds_read_b128 v[226:229], v194 offset:7168
	global_load_lds_dwordx4 v184, s[24:25]
	s_add_i32 m0, s48, 0xe000
	s_nop 0
	global_load_lds_dwordx4 v182, s[24:25]
	s_waitcnt vmcnt(8)
	s_waitcnt lgkmcnt(0)
	s_setprio 1
	v_mfma_f32_16x16x128_f8f6f4 v[158:161], v[18:25], v[198:205], v[158:161]
	v_mfma_f32_16x16x128_f8f6f4 v[154:157], v[26:33], v[198:205], v[154:157]
	v_mfma_f32_16x16x128_f8f6f4 v[142:145], v[18:25], v[206:213], v[142:145]
	v_mfma_f32_16x16x128_f8f6f4 v[138:141], v[26:33], v[206:213], v[138:141]
	v_mfma_f32_16x16x128_f8f6f4 v[126:129], v[18:25], v[214:221], v[126:129]
	v_mfma_f32_16x16x128_f8f6f4 v[122:125], v[26:33], v[214:221], v[122:125]
	v_mfma_f32_16x16x128_f8f6f4 v[110:113], v[18:25], v[222:229], v[110:113]
	v_mfma_f32_16x16x128_f8f6f4 v[106:109], v[26:33], v[222:229], v[106:109]
	s_setprio 0
	s_setprio 1
	v_mfma_f32_16x16x128_f8f6f4 v[150:153], v[2:9], v[198:205], v[150:153]
	v_mfma_f32_16x16x128_f8f6f4 v[146:149], v[10:17], v[198:205], v[146:149]
	v_mfma_f32_16x16x128_f8f6f4 v[134:137], v[2:9], v[206:213], v[134:137]
	v_mfma_f32_16x16x128_f8f6f4 v[130:133], v[10:17], v[206:213], v[130:133]
	v_mfma_f32_16x16x128_f8f6f4 v[118:121], v[2:9], v[214:221], v[118:121]
	v_mfma_f32_16x16x128_f8f6f4 v[114:117], v[10:17], v[214:221], v[114:117]
	v_mfma_f32_16x16x128_f8f6f4 v[102:105], v[2:9], v[222:229], v[102:105]
	v_mfma_f32_16x16x128_f8f6f4 v[98:101], v[10:17], v[222:229], v[98:101]
	s_setprio 0
	s_barrier
; #define PG8_STAGE(bufoff, gbase, voff) do { _Pragma("unroll") for (int _i = 0; _i < 2; ++_i) \
;         __builtin_amdgcn_global_load_lds((const unsigned*)((const char*)(gbase) + (voff)[_i]), (PG8_LAS unsigned*)(lds + (bufoff) + ldsw + _i * 8192), 16, 0, 0); } while (0)
; #define PG8_WAIT_V(n) asm volatile("s_waitcnt vmcnt(" #n ")" ::: "memory")
; #define PG8_WAIT_L(n) asm volatile("s_waitcnt lgkmcnt(" #n ")" ::: "memory")
; template <class Epi, class Sched, bool ALIGN_EPI = true, bool F8 = false>
; __device__ __forceinline__ void gemm_phase(PG8_LAS unsigned char* lds, const Sched& S, const Epi& E) {
;     ...
;         for (int t = 0; t < nt; t += 2) {
;             const bool last = (t == nt - 2);
;             if constexpr (Sched::GATHER) { if (last && has_next) S.a_off(nxt, Rs, Cs, voffAn); }
;             const char* a1 = cA + (size_t)(t + 1) * kstep;
;             const char* a2 = last ? nA : cA + (size_t)(t + 2) * kstep; const char* b2 = last ? nB : cB + (size_t)(t + 2) * kstepB;
;             const char* a3 = a2 + kstep; const char* b3 = b2 + kstepB;
;             unsigned vA2[2][2];
; #pragma unroll
;             for (int h = 0; h < 2; ++h)
; #pragma unroll
;                 for (int i = 0; i < 2; ++i) { if constexpr (Sched::GATHER) vA2[h][i] = (last && has_next) ? voffAn[h][i] : voffA[h][i]; else vA2[h][i] = voffA[h][i]; }
;             PG8_LDB(B0, 0, 0); PG8_LDB(B1, 0, 1); PG8_SCHED; PG8_LDA(At, 0, 0); PG8_STAGE(PG8_SA(1, 1), a1, voffA[1]);
;             PG8_WAIT_V(8); PG8_WAIT_L(0); PG8_BAR; PG8_MMA(0, 0, At, B0); PG8_MMA(0, 1, At, B1); PG8_BAR; PG8_SCHED;
;             PG8_LDA(At, 0, 1); PG8_STAGE(PG8_SB(0, 0), b2, voffB[0]); PG8_STAGE(PG8_SB(0, 1), b2, voffB[1]); PG8_STAGE(PG8_SA(0, 0), a2, vA2[0]);
;             PG8_WAIT_V(8); PG8_WAIT_L(0); PG8_BAR; PG8_MMA(1, 0, At, B0); PG8_MMA(1, 1, At, B1); PG8_BAR; PG8_SCHED;
;             PG8_LDB(B0, 1, 0); PG8_LDB(B1, 1, 1); PG8_SCHED; PG8_LDA(At, 1, 0); PG8_STAGE(PG8_SA(0, 1), a2, vA2[1]);
;             PG8_WAIT_V(8); PG8_WAIT_L(0); PG8_BAR; PG8_MMA(0, 0, At, B0); PG8_MMA(0, 1, At, B1); PG8_BAR; PG8_SCHED;
;             PG8_LDA(At, 1, 1); PG8_STAGE(PG8_SB(1, 0), b3, voffB[0]); PG8_STAGE(PG8_SB(1, 1), b3, voffB[1]); PG8_STAGE(PG8_SA(1, 0), a3, vA2[0]);
;             PG8_WAIT_V(8); PG8_WAIT_L(0); PG8_BAR; PG8_MMA(1, 0, At, B0); PG8_MMA(1, 1, At, B1); PG8_BAR; PG8_SCHED;
	s_add_i32 s75, s65, s47
	s_mov_b32 m0, s75
	ds_read_b128 v[198:201], v194 offset:16384
	ds_read_b128 v[202:205], v194 offset:17408
	ds_read_b128 v[206:209], v194 offset:18432
	ds_read_b128 v[210:213], v194 offset:19456
	ds_read_b128 v[214:217], v194 offset:20480
	ds_read_b128 v[218:221], v194 offset:21504
	ds_read_b128 v[222:225], v194 offset:22528
	ds_read_b128 v[226:229], v194 offset:23552
	global_load_lds_dwordx4 v164, s[28:29]
	s_add_i32 m0, s75, 0x2000
	s_add_i32 s75, s66, s47
	global_load_lds_dwordx4 v166, s[28:29]
	s_add_u32 s98, s28, s4
	s_addc_u32 s99, s29, s5
	s_mov_b32 m0, s75
	s_nop 0
	global_load_lds_dwordx4 v164, s[98:99]
	s_add_u32 s100, s28, s4
	s_addc_u32 s101, s29, s5
	s_add_i32 m0, s75, 0x2000
	s_nop 0
	global_load_lds_dwordx4 v166, s[100:101]
	s_mov_b32 m0, s48
	s_nop 0
	global_load_lds_dwordx4 v174, s[30:31]
	s_mov_b32 m0, s49
	s_nop 0
	global_load_lds_dwordx4 v176, s[30:31]
	s_waitcnt vmcnt(8)
	s_waitcnt lgkmcnt(0)
	s_setprio 1
	v_mfma_f32_16x16x128_f8f6f4 v[94:97], v[18:25], v[198:205], v[94:97]
	v_mfma_f32_16x16x128_f8f6f4 v[90:93], v[26:33], v[198:205], v[90:93]
	v_mfma_f32_16x16x128_f8f6f4 v[78:81], v[18:25], v[206:213], v[78:81]
	v_mfma_f32_16x16x128_f8f6f4 v[74:77], v[26:33], v[206:213], v[74:77]
	v_mfma_f32_16x16x128_f8f6f4 v[62:65], v[18:25], v[214:221], v[62:65]
	v_mfma_f32_16x16x128_f8f6f4 v[58:61], v[26:33], v[214:221], v[58:61]
	v_mfma_f32_16x16x128_f8f6f4 v[46:49], v[18:25], v[222:229], v[46:49]
	v_mfma_f32_16x16x128_f8f6f4 v[42:45], v[26:33], v[222:229], v[42:45]
	s_setprio 0
	s_setprio 1
	v_mfma_f32_16x16x128_f8f6f4 v[86:89], v[2:9], v[198:205], v[86:89]
	v_mfma_f32_16x16x128_f8f6f4 v[82:85], v[10:17], v[198:205], v[82:85]
	v_mfma_f32_16x16x128_f8f6f4 v[70:73], v[2:9], v[206:213], v[70:73]
	v_mfma_f32_16x16x128_f8f6f4 v[66:69], v[10:17], v[206:213], v[66:69]
	v_mfma_f32_16x16x128_f8f6f4 v[54:57], v[2:9], v[214:221], v[54:57]
	v_mfma_f32_16x16x128_f8f6f4 v[50:53], v[10:17], v[214:221], v[50:53]
	v_mfma_f32_16x16x128_f8f6f4 v[38:41], v[2:9], v[222:229], v[38:41]
	v_mfma_f32_16x16x128_f8f6f4 v[34:37], v[10:17], v[222:229], v[34:37]
	s_setprio 0
	s_barrier
	s_add_i32 s75, 0, 0x18000
	s_add_i32 s76, 0, 0x1c000
	v_add_u32_e32 v14, s75, v191
	v_add_u32_e32 v30, s76, v191
	ds_read_b128 v[2:5], v14
	ds_read_b128 v[6:9], v14 offset:1024
	ds_read_b128 v[10:13], v14 offset:2048
	ds_read_b128 v[14:17], v14 offset:3072
	ds_read_b128 v[18:21], v30
	ds_read_b128 v[22:25], v30 offset:1024
	ds_read_b128 v[26:29], v30 offset:2048
	ds_read_b128 v[30:33], v30 offset:3072
	s_mov_b32 m0, s50
	ds_read_b128 v[198:201], v194 offset:32768
	ds_read_b128 v[202:205], v194 offset:33792
	ds_read_b128 v[206:209], v194 offset:34816
	ds_read_b128 v[210:213], v194 offset:35840
	ds_read_b128 v[214:217], v194 offset:36864
	ds_read_b128 v[218:221], v194 offset:37888
	ds_read_b128 v[222:225], v194 offset:38912
	ds_read_b128 v[226:229], v194 offset:39936
	global_load_lds_dwordx4 v178, s[30:31]
	s_mov_b32 m0, s51
	s_nop 0
	global_load_lds_dwordx4 v180, s[30:31]
	s_waitcnt vmcnt(8)
	s_waitcnt lgkmcnt(0)
	s_setprio 1
	v_mfma_f32_16x16x128_f8f6f4 v[158:161], v[2:9], v[198:205], v[158:161]
	v_mfma_f32_16x16x128_f8f6f4 v[154:157], v[10:17], v[198:205], v[154:157]
	v_mfma_f32_16x16x128_f8f6f4 v[142:145], v[2:9], v[206:213], v[142:145]
	v_mfma_f32_16x16x128_f8f6f4 v[138:141], v[10:17], v[206:213], v[138:141]
	v_mfma_f32_16x16x128_f8f6f4 v[126:129], v[2:9], v[214:221], v[126:129]
	v_mfma_f32_16x16x128_f8f6f4 v[122:125], v[10:17], v[214:221], v[122:125]
	v_mfma_f32_16x16x128_f8f6f4 v[110:113], v[2:9], v[222:229], v[110:113]
	v_mfma_f32_16x16x128_f8f6f4 v[106:109], v[10:17], v[222:229], v[106:109]
	s_setprio 0
	s_setprio 1
	v_mfma_f32_16x16x128_f8f6f4 v[150:153], v[18:25], v[198:205], v[150:153]
	v_mfma_f32_16x16x128_f8f6f4 v[146:149], v[26:33], v[198:205], v[146:149]
	v_mfma_f32_16x16x128_f8f6f4 v[134:137], v[18:25], v[206:213], v[134:137]
	v_mfma_f32_16x16x128_f8f6f4 v[130:133], v[26:33], v[206:213], v[130:133]
	v_mfma_f32_16x16x128_f8f6f4 v[118:121], v[18:25], v[214:221], v[118:121]
	v_mfma_f32_16x16x128_f8f6f4 v[114:117], v[26:33], v[214:221], v[114:117]
	v_mfma_f32_16x16x128_f8f6f4 v[102:105], v[18:25], v[222:229], v[102:105]
	v_mfma_f32_16x16x128_f8f6f4 v[98:101], v[26:33], v[222:229], v[98:101]
	s_setprio 0
	s_barrier
	s_add_u32 s28, s28, 0x8000
	s_addc_u32 s29, s29, 0
	s_add_i32 s30, s75, s47
	s_mov_b32 m0, s30
	ds_read_b128 v[198:201], v194 offset:49152
	ds_read_b128 v[202:205], v194 offset:50176
	ds_read_b128 v[206:209], v194 offset:51200
	ds_read_b128 v[210:213], v194 offset:52224
	ds_read_b128 v[214:217], v194 offset:53248
	ds_read_b128 v[218:221], v194 offset:54272
	ds_read_b128 v[222:225], v194 offset:55296
	ds_read_b128 v[226:229], v194 offset:56320
	global_load_lds_dwordx4 v164, s[28:29]
	s_add_i32 m0, s30, 0x2000
	s_add_i32 s30, s76, s47
	global_load_lds_dwordx4 v166, s[28:29]
	s_mov_b32 m0, s30
	s_nop 0
	global_load_lds_dwordx4 v168, s[28:29]
	s_add_i32 m0, s30, 0x2000
	s_nop 0
	global_load_lds_dwordx4 v172, s[28:29]
	s_mov_b32 m0, s60
	s_nop 0
	global_load_lds_dwordx4 v174, s[26:27]
	s_mov_b32 m0, s61
	s_nop 0
	global_load_lds_dwordx4 v176, s[26:27]
	s_waitcnt vmcnt(8)
	s_waitcnt lgkmcnt(0)
	s_setprio 1
	v_mfma_f32_16x16x128_f8f6f4 v[94:97], v[2:9], v[198:205], v[94:97]
	v_mfma_f32_16x16x128_f8f6f4 v[90:93], v[10:17], v[198:205], v[90:93]
	v_mfma_f32_16x16x128_f8f6f4 v[78:81], v[2:9], v[206:213], v[78:81]
	v_mfma_f32_16x16x128_f8f6f4 v[74:77], v[10:17], v[206:213], v[74:77]
	v_mfma_f32_16x16x128_f8f6f4 v[62:65], v[2:9], v[214:221], v[62:65]
	v_mfma_f32_16x16x128_f8f6f4 v[58:61], v[10:17], v[214:221], v[58:61]
	v_mfma_f32_16x16x128_f8f6f4 v[46:49], v[2:9], v[222:229], v[46:49]
	v_mfma_f32_16x16x128_f8f6f4 v[42:45], v[10:17], v[222:229], v[42:45]
	s_setprio 0
	s_setprio 1
	v_mfma_f32_16x16x128_f8f6f4 v[86:89], v[18:25], v[198:205], v[86:89]
	v_mfma_f32_16x16x128_f8f6f4 v[82:85], v[26:33], v[198:205], v[82:85]
	v_mfma_f32_16x16x128_f8f6f4 v[70:73], v[18:25], v[206:213], v[70:73]
	v_mfma_f32_16x16x128_f8f6f4 v[66:69], v[26:33], v[206:213], v[66:69]
	v_mfma_f32_16x16x128_f8f6f4 v[54:57], v[18:25], v[214:221], v[54:57]
	v_mfma_f32_16x16x128_f8f6f4 v[50:53], v[26:33], v[214:221], v[50:53]
	v_mfma_f32_16x16x128_f8f6f4 v[38:41], v[18:25], v[222:229], v[38:41]
	v_mfma_f32_16x16x128_f8f6f4 v[34:37], v[26:33], v[222:229], v[34:37]
	s_setprio 0
	s_barrier
	s_add_i32 s74, s74, 2
	s_add_u32 s17, s17, 0x10000
	s_addc_u32 s19, s19, 0
	s_add_u32 s24, s24, 0x10000
	s_addc_u32 s25, s25, 0
	s_cmp_gt_u32 s74, 13
	s_cbranch_scc0 .LBB0_428
	s_branch .Lfx_11141
; #define PG8_WAIT_V(n) asm volatile("s_waitcnt vmcnt(" #n ")" ::: "memory")
; #define PG8_WAIT_L(n) asm volatile("s_waitcnt lgkmcnt(" #n ")" ::: "memory")
; template <class Epi, class Sched, bool ALIGN_EPI = true, bool F8 = false>
; __device__ __forceinline__ void gemm_phase(PG8_LAS unsigned char* lds, const Sched& S, const Epi& E) {
;     ...
;         for (int t = 0; t < nt; t += 2) {
;             const bool last = (t == nt - 2);
;             if constexpr (Sched::GATHER) { if (last && has_next) S.a_off(nxt, Rs, Cs, voffAn); }
;             const char* a1 = cA + (size_t)(t + 1) * kstep;
;             const char* a2 = last ? nA : cA + (size_t)(t + 2) * kstep; const char* b2 = last ? nB : cB + (size_t)(t + 2) * kstepB;
;             const char* a3 = a2 + kstep; const char* b3 = b2 + kstepB;
;             unsigned vA2[2][2];
; #pragma unroll
;             for (int h = 0; h < 2; ++h)
; #pragma unroll
;                 for (int i = 0; i < 2; ++i) { if constexpr (Sched::GATHER) vA2[h][i] = (last && has_next) ? voffAn[h][i] : voffA[h][i]; else vA2[h][i] = voffA[h][i]; }
;             PG8_LDB(B0, 0, 0); PG8_LDB(B1, 0, 1); PG8_SCHED; PG8_LDA(At, 0, 0); PG8_STAGE(PG8_SA(1, 1), a1, voffA[1]);
;             PG8_WAIT_V(8); PG8_WAIT_L(0); PG8_BAR; PG8_MMA(0, 0, At, B0); PG8_MMA(0, 1, At, B1); PG8_BAR; PG8_SCHED;
;             PG8_LDA(At, 0, 1); PG8_STAGE(PG8_SB(0, 0), b2, voffB[0]); PG8_STAGE(PG8_SB(0, 1), b2, voffB[1]); PG8_STAGE(PG8_SA(0, 0), a2, vA2[0]);
;             PG8_WAIT_V(8); PG8_WAIT_L(0); PG8_BAR; PG8_MMA(1, 0, At, B0); PG8_MMA(1, 1, At, B1); PG8_BAR; PG8_SCHED;
;             PG8_LDB(B0, 1, 0); PG8_LDB(B1, 1, 1); PG8_SCHED; PG8_LDA(At, 1, 0); PG8_STAGE(PG8_SA(0, 1), a2, vA2[1]);
;             PG8_WAIT_V(8); PG8_WAIT_L(0); PG8_BAR; PG8_MMA(0, 0, At, B0); PG8_MMA(0, 1, At, B1); PG8_BAR; PG8_SCHED;
;             PG8_LDA(At, 1, 1); PG8_STAGE(PG8_SB(1, 0), b3, voffB[0]); PG8_STAGE(PG8_SB(1, 1), b3, voffB[1]); PG8_STAGE(PG8_SA(1, 0), a3, vA2[0]);
;             PG8_WAIT_V(8); PG8_WAIT_L(0); PG8_BAR; PG8_MMA(1, 0, At, B0); PG8_MMA(1, 1, At, B1); PG8_BAR; PG8_SCHED;
;     ...
;         for (int a = 0; a < 2; ++a)
; #pragma unroll
;             for (int b = 0; b < 2; ++b)
; #pragma unroll
;                 for (int m = 0; m < 4; ++m)
; #pragma unroll
;                     for (int n = 0; n < 2; ++n) acc[a][b][m][n] = (f32x4){0.f, 0.f, 0.f, 0.f};
.Lh1e_11141:
.Lpk1_428:
	ds_read_b128 v[18:21], v192
	ds_read_b128 v[22:25], v192 offset:1024
	ds_read_b128 v[26:29], v192 offset:2048
	ds_read_b128 v[30:33], v192 offset:3072
	ds_read_b128 v[2:5], v193
	ds_read_b128 v[6:9], v193 offset:1024
	ds_read_b128 v[10:13], v193 offset:2048
	ds_read_b128 v[14:17], v193 offset:3072
	s_add_u32 s26, s24, 0x8000
	s_addc_u32 s27, s25, 0
	s_cmp_eq_u32 s74, 12
	s_cselect_b32 s30, s20, s26
	s_cselect_b32 s31, s21, s27
	s_cselect_b32 s28, s22, s17
	s_cselect_b32 s29, s23, s19
	s_add_u32 s26, s30, 0x8000
	s_addc_u32 s27, s31, 0
	s_add_i32 m0, s48, 0xc000
	ds_read_b128 v[198:201], v194
	ds_read_b128 v[202:205], v194 offset:1024
	ds_read_b128 v[206:209], v194 offset:2048
	ds_read_b128 v[210:213], v194 offset:3072
	ds_read_b128 v[214:217], v194 offset:4096
	ds_read_b128 v[218:221], v194 offset:5120
	ds_read_b128 v[222:225], v194 offset:6144
	ds_read_b128 v[226:229], v194 offset:7168
	global_load_lds_dwordx4 v184, s[24:25]
	s_add_i32 m0, s48, 0xe000
	s_nop 0
	global_load_lds_dwordx4 v182, s[24:25]
	s_waitcnt vmcnt(8)
	s_waitcnt lgkmcnt(0)
	s_barrier
	s_setprio 2
	v_mfma_f32_16x16x128_f8f6f4 v[158:161], v[18:25], v[198:205], 0
	v_mfma_f32_16x16x128_f8f6f4 v[154:157], v[26:33], v[198:205], 0
	v_mfma_f32_16x16x128_f8f6f4 v[142:145], v[18:25], v[206:213], 0
	v_mfma_f32_16x16x128_f8f6f4 v[138:141], v[26:33], v[206:213], 0
	v_mfma_f32_16x16x128_f8f6f4 v[126:129], v[18:25], v[214:221], 0
	v_mfma_f32_16x16x128_f8f6f4 v[122:125], v[26:33], v[214:221], 0
	v_mfma_f32_16x16x128_f8f6f4 v[110:113], v[18:25], v[222:229], 0
	v_mfma_f32_16x16x128_f8f6f4 v[106:109], v[26:33], v[222:229], 0
	s_setprio 0
	s_setprio 2
	v_mfma_f32_16x16x128_f8f6f4 v[150:153], v[2:9], v[198:205], 0
	v_mfma_f32_16x16x128_f8f6f4 v[146:149], v[10:17], v[198:205], 0
	v_mfma_f32_16x16x128_f8f6f4 v[134:137], v[2:9], v[206:213], 0
	v_mfma_f32_16x16x128_f8f6f4 v[130:133], v[10:17], v[206:213], 0
	v_mfma_f32_16x16x128_f8f6f4 v[118:121], v[2:9], v[214:221], 0
	v_mfma_f32_16x16x128_f8f6f4 v[114:117], v[10:17], v[214:221], 0
	v_mfma_f32_16x16x128_f8f6f4 v[102:105], v[2:9], v[222:229], 0
	v_mfma_f32_16x16x128_f8f6f4 v[98:101], v[10:17], v[222:229], 0
	s_setprio 0
	s_add_i32 s75, s65, s47
	s_mov_b32 m0, s75
	ds_read_b128 v[198:201], v194 offset:16384
	ds_read_b128 v[202:205], v194 offset:17408
	ds_read_b128 v[206:209], v194 offset:18432
	ds_read_b128 v[210:213], v194 offset:19456
	ds_read_b128 v[214:217], v194 offset:20480
	ds_read_b128 v[218:221], v194 offset:21504
	ds_read_b128 v[222:225], v194 offset:22528
	ds_read_b128 v[226:229], v194 offset:23552
	global_load_lds_dwordx4 v164, s[28:29]
	s_add_i32 m0, s75, 0x2000
	s_add_i32 s75, s66, s47
	global_load_lds_dwordx4 v166, s[28:29]
	s_add_u32 s98, s28, s4
	s_addc_u32 s99, s29, s5
	s_mov_b32 m0, s75
	s_nop 0
	global_load_lds_dwordx4 v164, s[98:99]
	s_add_u32 s100, s28, s4
	s_addc_u32 s101, s29, s5
	s_add_i32 m0, s75, 0x2000
	s_nop 0
	global_load_lds_dwordx4 v166, s[100:101]
	s_mov_b32 m0, s48
	s_nop 0
	global_load_lds_dwordx4 v174, s[30:31]
	s_mov_b32 m0, s49
	s_nop 0
	global_load_lds_dwordx4 v176, s[30:31]
	s_waitcnt vmcnt(8)
	s_waitcnt lgkmcnt(0)
	s_barrier
	s_setprio 2
	v_mfma_f32_16x16x128_f8f6f4 v[94:97], v[18:25], v[198:205], 0
	v_mfma_f32_16x16x128_f8f6f4 v[90:93], v[26:33], v[198:205], 0
	v_mfma_f32_16x16x128_f8f6f4 v[78:81], v[18:25], v[206:213], 0
	v_mfma_f32_16x16x128_f8f6f4 v[74:77], v[26:33], v[206:213], 0
	v_mfma_f32_16x16x128_f8f6f4 v[62:65], v[18:25], v[214:221], 0
	v_mfma_f32_16x16x128_f8f6f4 v[58:61], v[26:33], v[214:221], 0
	v_mfma_f32_16x16x128_f8f6f4 v[46:49], v[18:25], v[222:229], 0
	v_mfma_f32_16x16x128_f8f6f4 v[42:45], v[26:33], v[222:229], 0
	s_setprio 0
	s_setprio 2
	v_mfma_f32_16x16x128_f8f6f4 v[86:89], v[2:9], v[198:205], 0
	v_mfma_f32_16x16x128_f8f6f4 v[82:85], v[10:17], v[198:205], 0
	v_mfma_f32_16x16x128_f8f6f4 v[70:73], v[2:9], v[206:213], 0
	v_mfma_f32_16x16x128_f8f6f4 v[66:69], v[10:17], v[206:213], 0
	v_mfma_f32_16x16x128_f8f6f4 v[54:57], v[2:9], v[214:221], 0
	v_mfma_f32_16x16x128_f8f6f4 v[50:53], v[10:17], v[214:221], 0
	v_mfma_f32_16x16x128_f8f6f4 v[38:41], v[2:9], v[222:229], 0
	v_mfma_f32_16x16x128_f8f6f4 v[34:37], v[10:17], v[222:229], 0
	s_setprio 0
	s_add_i32 s75, 0, 0x18000
	s_add_i32 s76, 0, 0x1c000
	v_add_u32_e32 v14, s75, v191
	v_add_u32_e32 v30, s76, v191
	ds_read_b128 v[2:5], v14
	ds_read_b128 v[6:9], v14 offset:1024
	ds_read_b128 v[10:13], v14 offset:2048
	ds_read_b128 v[14:17], v14 offset:3072
	ds_read_b128 v[18:21], v30
	ds_read_b128 v[22:25], v30 offset:1024
	ds_read_b128 v[26:29], v30 offset:2048
	ds_read_b128 v[30:33], v30 offset:3072
	s_mov_b32 m0, s50
	ds_read_b128 v[198:201], v194 offset:32768
	ds_read_b128 v[202:205], v194 offset:33792
	ds_read_b128 v[206:209], v194 offset:34816
	ds_read_b128 v[210:213], v194 offset:35840
	ds_read_b128 v[214:217], v194 offset:36864
	ds_read_b128 v[218:221], v194 offset:37888
	ds_read_b128 v[222:225], v194 offset:38912
	ds_read_b128 v[226:229], v194 offset:39936
	global_load_lds_dwordx4 v178, s[30:31]
	s_mov_b32 m0, s51
	s_nop 0
	global_load_lds_dwordx4 v180, s[30:31]
	s_waitcnt vmcnt(8)
	s_waitcnt lgkmcnt(0)
	s_barrier
; #define PG8_STAGE(bufoff, gbase, voff) do { _Pragma("unroll") for (int _i = 0; _i < 2; ++_i) \
;         __builtin_amdgcn_global_load_lds((const unsigned*)((const char*)(gbase) + (voff)[_i]), (PG8_LAS unsigned*)(lds + (bufoff) + ldsw + _i * 8192), 16, 0, 0); } while (0)
; #define PG8_WAIT_V(n) asm volatile("s_waitcnt vmcnt(" #n ")" ::: "memory")
; #define PG8_WAIT_L(n) asm volatile("s_waitcnt lgkmcnt(" #n ")" ::: "memory")
; template <class Epi, class Sched, bool ALIGN_EPI = true, bool F8 = false>
; __device__ __forceinline__ void gemm_phase(PG8_LAS unsigned char* lds, const Sched& S, const Epi& E) {
;     ...
;         for (int t = 0; t < nt; t += 2) {
;             const bool last = (t == nt - 2);
;             if constexpr (Sched::GATHER) { if (last && has_next) S.a_off(nxt, Rs, Cs, voffAn); }
;             const char* a1 = cA + (size_t)(t + 1) * kstep;
;             const char* a2 = last ? nA : cA + (size_t)(t + 2) * kstep; const char* b2 = last ? nB : cB + (size_t)(t + 2) * kstepB;
;             const char* a3 = a2 + kstep; const char* b3 = b2 + kstepB;
;             unsigned vA2[2][2];
; #pragma unroll
;             for (int h = 0; h < 2; ++h)
; #pragma unroll
;                 for (int i = 0; i < 2; ++i) { if constexpr (Sched::GATHER) vA2[h][i] = (last && has_next) ? voffAn[h][i] : voffA[h][i]; else vA2[h][i] = voffA[h][i]; }
;             PG8_LDB(B0, 0, 0); PG8_LDB(B1, 0, 1); PG8_SCHED; PG8_LDA(At, 0, 0); PG8_STAGE(PG8_SA(1, 1), a1, voffA[1]);
;             PG8_WAIT_V(8); PG8_WAIT_L(0); PG8_BAR; PG8_MMA(0, 0, At, B0); PG8_MMA(0, 1, At, B1); PG8_BAR; PG8_SCHED;
;             PG8_LDA(At, 0, 1); PG8_STAGE(PG8_SB(0, 0), b2, voffB[0]); PG8_STAGE(PG8_SB(0, 1), b2, voffB[1]); PG8_STAGE(PG8_SA(0, 0), a2, vA2[0]);
;             PG8_WAIT_V(8); PG8_WAIT_L(0); PG8_BAR; PG8_MMA(1, 0, At, B0); PG8_MMA(1, 1, At, B1); PG8_BAR; PG8_SCHED;
;             PG8_LDB(B0, 1, 0); PG8_LDB(B1, 1, 1); PG8_SCHED; PG8_LDA(At, 1, 0); PG8_STAGE(PG8_SA(0, 1), a2, vA2[1]);
;             PG8_WAIT_V(8); PG8_WAIT_L(0); PG8_BAR; PG8_MMA(0, 0, At, B0); PG8_MMA(0, 1, At, B1); PG8_BAR; PG8_SCHED;
;             PG8_LDA(At, 1, 1); PG8_STAGE(PG8_SB(1, 0), b3, voffB[0]); PG8_STAGE(PG8_SB(1, 1), b3, voffB[1]); PG8_STAGE(PG8_SA(1, 0), a3, vA2[0]);
;             PG8_WAIT_V(8); PG8_WAIT_L(0); PG8_BAR; PG8_MMA(1, 0, At, B0); PG8_MMA(1, 1, At, B1); PG8_BAR; PG8_SCHED;
	s_setprio 2
	v_mfma_f32_16x16x128_f8f6f4 v[158:161], v[2:9], v[198:205], v[158:161]
	v_mfma_f32_16x16x128_f8f6f4 v[154:157], v[10:17], v[198:205], v[154:157]
	v_mfma_f32_16x16x128_f8f6f4 v[142:145], v[2:9], v[206:213], v[142:145]
	v_mfma_f32_16x16x128_f8f6f4 v[138:141], v[10:17], v[206:213], v[138:141]
	v_mfma_f32_16x16x128_f8f6f4 v[126:129], v[2:9], v[214:221], v[126:129]
	v_mfma_f32_16x16x128_f8f6f4 v[122:125], v[10:17], v[214:221], v[122:125]
	v_mfma_f32_16x16x128_f8f6f4 v[110:113], v[2:9], v[222:229], v[110:113]
	v_mfma_f32_16x16x128_f8f6f4 v[106:109], v[10:17], v[222:229], v[106:109]
	s_setprio 0
	s_setprio 2
	v_mfma_f32_16x16x128_f8f6f4 v[150:153], v[18:25], v[198:205], v[150:153]
	v_mfma_f32_16x16x128_f8f6f4 v[146:149], v[26:33], v[198:205], v[146:149]
	v_mfma_f32_16x16x128_f8f6f4 v[134:137], v[18:25], v[206:213], v[134:137]
	v_mfma_f32_16x16x128_f8f6f4 v[130:133], v[26:33], v[206:213], v[130:133]
	v_mfma_f32_16x16x128_f8f6f4 v[118:121], v[18:25], v[214:221], v[118:121]
	v_mfma_f32_16x16x128_f8f6f4 v[114:117], v[26:33], v[214:221], v[114:117]
	v_mfma_f32_16x16x128_f8f6f4 v[102:105], v[18:25], v[222:229], v[102:105]
	v_mfma_f32_16x16x128_f8f6f4 v[98:101], v[26:33], v[222:229], v[98:101]
	s_setprio 0
	s_add_u32 s28, s28, 0x8000
	s_addc_u32 s29, s29, 0
	s_add_i32 s30, s75, s47
	s_mov_b32 m0, s30
	ds_read_b128 v[198:201], v194 offset:49152
	ds_read_b128 v[202:205], v194 offset:50176
	ds_read_b128 v[206:209], v194 offset:51200
	ds_read_b128 v[210:213], v194 offset:52224
	ds_read_b128 v[214:217], v194 offset:53248
	ds_read_b128 v[218:221], v194 offset:54272
	ds_read_b128 v[222:225], v194 offset:55296
	ds_read_b128 v[226:229], v194 offset:56320
	global_load_lds_dwordx4 v164, s[28:29]
	s_add_i32 m0, s30, 0x2000
	s_add_i32 s30, s76, s47
	global_load_lds_dwordx4 v166, s[28:29]
	s_mov_b32 m0, s30
	s_nop 0
	global_load_lds_dwordx4 v168, s[28:29]
	s_add_i32 m0, s30, 0x2000
	s_nop 0
	global_load_lds_dwordx4 v172, s[28:29]
	s_mov_b32 m0, s60
	s_nop 0
	global_load_lds_dwordx4 v174, s[26:27]
	s_mov_b32 m0, s61
	s_nop 0
	global_load_lds_dwordx4 v176, s[26:27]
	s_waitcnt vmcnt(8)
	s_waitcnt lgkmcnt(0)
	s_barrier
	s_setprio 2
	v_mfma_f32_16x16x128_f8f6f4 v[94:97], v[2:9], v[198:205], v[94:97]
	v_mfma_f32_16x16x128_f8f6f4 v[90:93], v[10:17], v[198:205], v[90:93]
	v_mfma_f32_16x16x128_f8f6f4 v[78:81], v[2:9], v[206:213], v[78:81]
	v_mfma_f32_16x16x128_f8f6f4 v[74:77], v[10:17], v[206:213], v[74:77]
	v_mfma_f32_16x16x128_f8f6f4 v[62:65], v[2:9], v[214:221], v[62:65]
	v_mfma_f32_16x16x128_f8f6f4 v[58:61], v[10:17], v[214:221], v[58:61]
	v_mfma_f32_16x16x128_f8f6f4 v[46:49], v[2:9], v[222:229], v[46:49]
	v_mfma_f32_16x16x128_f8f6f4 v[42:45], v[10:17], v[222:229], v[42:45]
	s_setprio 0
	s_setprio 2
	v_mfma_f32_16x16x128_f8f6f4 v[86:89], v[18:25], v[198:205], v[86:89]
	v_mfma_f32_16x16x128_f8f6f4 v[82:85], v[26:33], v[198:205], v[82:85]
	v_mfma_f32_16x16x128_f8f6f4 v[70:73], v[18:25], v[206:213], v[70:73]
	v_mfma_f32_16x16x128_f8f6f4 v[66:69], v[26:33], v[206:213], v[66:69]
	v_mfma_f32_16x16x128_f8f6f4 v[54:57], v[18:25], v[214:221], v[54:57]
	v_mfma_f32_16x16x128_f8f6f4 v[50:53], v[26:33], v[214:221], v[50:53]
	v_mfma_f32_16x16x128_f8f6f4 v[38:41], v[18:25], v[222:229], v[38:41]
	v_mfma_f32_16x16x128_f8f6f4 v[34:37], v[26:33], v[222:229], v[34:37]
	s_setprio 0
	s_add_i32 s74, s74, 2
	s_add_u32 s17, s17, 0x10000
	s_addc_u32 s19, s19, 0
	s_add_u32 s24, s24, 0x10000
	s_addc_u32 s25, s25, 0
	s_cmp_gt_u32 s74, 13
	s_cbranch_scc0 .Lh1_428
	s_branch .Lfx_11141
.Lh1_428:
	ds_read_b128 v[18:21], v192
	ds_read_b128 v[22:25], v192 offset:1024
	ds_read_b128 v[26:29], v192 offset:2048
	ds_read_b128 v[30:33], v192 offset:3072
	ds_read_b128 v[2:5], v193
	ds_read_b128 v[6:9], v193 offset:1024
	ds_read_b128 v[10:13], v193 offset:2048
	ds_read_b128 v[14:17], v193 offset:3072
	s_add_u32 s26, s24, 0x8000
	s_addc_u32 s27, s25, 0
	s_cmp_eq_u32 s74, 12
	s_cselect_b32 s30, s20, s26
	s_cselect_b32 s31, s21, s27
	s_cselect_b32 s28, s22, s17
	s_cselect_b32 s29, s23, s19
	s_add_u32 s26, s30, 0x8000
	s_addc_u32 s27, s31, 0
	s_add_i32 m0, s48, 0xc000
	ds_read_b128 v[198:201], v194
	ds_read_b128 v[202:205], v194 offset:1024
	ds_read_b128 v[206:209], v194 offset:2048
	ds_read_b128 v[210:213], v194 offset:3072
	ds_read_b128 v[214:217], v194 offset:4096
	ds_read_b128 v[218:221], v194 offset:5120
	ds_read_b128 v[222:225], v194 offset:6144
	ds_read_b128 v[226:229], v194 offset:7168
	global_load_lds_dwordx4 v184, s[24:25]
	s_add_i32 m0, s48, 0xe000
	s_nop 0
	global_load_lds_dwordx4 v182, s[24:25]
	s_waitcnt vmcnt(8)
	s_waitcnt lgkmcnt(0)
	s_barrier
; #define PG8_STAGE(bufoff, gbase, voff) do { _Pragma("unroll") for (int _i = 0; _i < 2; ++_i) \
;         __builtin_amdgcn_global_load_lds((const unsigned*)((const char*)(gbase) + (voff)[_i]), (PG8_LAS unsigned*)(lds + (bufoff) + ldsw + _i * 8192), 16, 0, 0); } while (0)
; #define PG8_WAIT_V(n) asm volatile("s_waitcnt vmcnt(" #n ")" ::: "memory")
; #define PG8_WAIT_L(n) asm volatile("s_waitcnt lgkmcnt(" #n ")" ::: "memory")
; template <class Epi, class Sched, bool ALIGN_EPI = true, bool F8 = false>
; __device__ __forceinline__ void gemm_phase(PG8_LAS unsigned char* lds, const Sched& S, const Epi& E) {
;     ...
;         for (int t = 0; t < nt; t += 2) {
;             const bool last = (t == nt - 2);
;             if constexpr (Sched::GATHER) { if (last && has_next) S.a_off(nxt, Rs, Cs, voffAn); }
;             const char* a1 = cA + (size_t)(t + 1) * kstep;
;             const char* a2 = last ? nA : cA + (size_t)(t + 2) * kstep; const char* b2 = last ? nB : cB + (size_t)(t + 2) * kstepB;
;             const char* a3 = a2 + kstep; const char* b3 = b2 + kstepB;
;             unsigned vA2[2][2];
; #pragma unroll
;             for (int h = 0; h < 2; ++h)
; #pragma unroll
;                 for (int i = 0; i < 2; ++i) { if constexpr (Sched::GATHER) vA2[h][i] = (last && has_next) ? voffAn[h][i] : voffA[h][i]; else vA2[h][i] = voffA[h][i]; }
;             PG8_LDB(B0, 0, 0); PG8_LDB(B1, 0, 1); PG8_SCHED; PG8_LDA(At, 0, 0); PG8_STAGE(PG8_SA(1, 1), a1, voffA[1]);
;             PG8_WAIT_V(8); PG8_WAIT_L(0); PG8_BAR; PG8_MMA(0, 0, At, B0); PG8_MMA(0, 1, At, B1); PG8_BAR; PG8_SCHED;
;             PG8_LDA(At, 0, 1); PG8_STAGE(PG8_SB(0, 0), b2, voffB[0]); PG8_STAGE(PG8_SB(0, 1), b2, voffB[1]); PG8_STAGE(PG8_SA(0, 0), a2, vA2[0]);
;             PG8_WAIT_V(8); PG8_WAIT_L(0); PG8_BAR; PG8_MMA(1, 0, At, B0); PG8_MMA(1, 1, At, B1); PG8_BAR; PG8_SCHED;
;             PG8_LDB(B0, 1, 0); PG8_LDB(B1, 1, 1); PG8_SCHED; PG8_LDA(At, 1, 0); PG8_STAGE(PG8_SA(0, 1), a2, vA2[1]);
;             PG8_WAIT_V(8); PG8_WAIT_L(0); PG8_BAR; PG8_MMA(0, 0, At, B0); PG8_MMA(0, 1, At, B1); PG8_BAR; PG8_SCHED;
;             PG8_LDA(At, 1, 1); PG8_STAGE(PG8_SB(1, 0), b3, voffB[0]); PG8_STAGE(PG8_SB(1, 1), b3, voffB[1]); PG8_STAGE(PG8_SA(1, 0), a3, vA2[0]);
;             PG8_WAIT_V(8); PG8_WAIT_L(0); PG8_BAR; PG8_MMA(1, 0, At, B0); PG8_MMA(1, 1, At, B1); PG8_BAR; PG8_SCHED;
	s_setprio 2
	v_mfma_f32_16x16x128_f8f6f4 v[158:161], v[18:25], v[198:205], v[158:161]
	v_mfma_f32_16x16x128_f8f6f4 v[154:157], v[26:33], v[198:205], v[154:157]
	v_mfma_f32_16x16x128_f8f6f4 v[142:145], v[18:25], v[206:213], v[142:145]
	v_mfma_f32_16x16x128_f8f6f4 v[138:141], v[26:33], v[206:213], v[138:141]
	v_mfma_f32_16x16x128_f8f6f4 v[126:129], v[18:25], v[214:221], v[126:129]
	v_mfma_f32_16x16x128_f8f6f4 v[122:125], v[26:33], v[214:221], v[122:125]
	v_mfma_f32_16x16x128_f8f6f4 v[110:113], v[18:25], v[222:229], v[110:113]
	v_mfma_f32_16x16x128_f8f6f4 v[106:109], v[26:33], v[222:229], v[106:109]
	s_setprio 0
	s_setprio 2
	v_mfma_f32_16x16x128_f8f6f4 v[150:153], v[2:9], v[198:205], v[150:153]
	v_mfma_f32_16x16x128_f8f6f4 v[146:149], v[10:17], v[198:205], v[146:149]
	v_mfma_f32_16x16x128_f8f6f4 v[134:137], v[2:9], v[206:213], v[134:137]
	v_mfma_f32_16x16x128_f8f6f4 v[130:133], v[10:17], v[206:213], v[130:133]
	v_mfma_f32_16x16x128_f8f6f4 v[118:121], v[2:9], v[214:221], v[118:121]
	v_mfma_f32_16x16x128_f8f6f4 v[114:117], v[10:17], v[214:221], v[114:117]
	v_mfma_f32_16x16x128_f8f6f4 v[102:105], v[2:9], v[222:229], v[102:105]
	v_mfma_f32_16x16x128_f8f6f4 v[98:101], v[10:17], v[222:229], v[98:101]
	s_setprio 0
	s_add_i32 s75, s65, s47
	s_mov_b32 m0, s75
	ds_read_b128 v[198:201], v194 offset:16384
	ds_read_b128 v[202:205], v194 offset:17408
	ds_read_b128 v[206:209], v194 offset:18432
	ds_read_b128 v[210:213], v194 offset:19456
	ds_read_b128 v[214:217], v194 offset:20480
	ds_read_b128 v[218:221], v194 offset:21504
	ds_read_b128 v[222:225], v194 offset:22528
	ds_read_b128 v[226:229], v194 offset:23552
	global_load_lds_dwordx4 v164, s[28:29]
	s_add_i32 m0, s75, 0x2000
	s_add_i32 s75, s66, s47
	global_load_lds_dwordx4 v166, s[28:29]
	s_add_u32 s98, s28, s4
	s_addc_u32 s99, s29, s5
	s_mov_b32 m0, s75
	s_nop 0
	global_load_lds_dwordx4 v164, s[98:99]
	s_add_u32 s100, s28, s4
	s_addc_u32 s101, s29, s5
	s_add_i32 m0, s75, 0x2000
	s_nop 0
	global_load_lds_dwordx4 v166, s[100:101]
	s_mov_b32 m0, s48
	s_nop 0
	global_load_lds_dwordx4 v174, s[30:31]
	s_mov_b32 m0, s49
	s_nop 0
	global_load_lds_dwordx4 v176, s[30:31]
	s_waitcnt vmcnt(8)
	s_waitcnt lgkmcnt(0)
	s_barrier
	s_setprio 2
	v_mfma_f32_16x16x128_f8f6f4 v[94:97], v[18:25], v[198:205], v[94:97]
	v_mfma_f32_16x16x128_f8f6f4 v[90:93], v[26:33], v[198:205], v[90:93]
	v_mfma_f32_16x16x128_f8f6f4 v[78:81], v[18:25], v[206:213], v[78:81]
	v_mfma_f32_16x16x128_f8f6f4 v[74:77], v[26:33], v[206:213], v[74:77]
	v_mfma_f32_16x16x128_f8f6f4 v[62:65], v[18:25], v[214:221], v[62:65]
	v_mfma_f32_16x16x128_f8f6f4 v[58:61], v[26:33], v[214:221], v[58:61]
	v_mfma_f32_16x16x128_f8f6f4 v[46:49], v[18:25], v[222:229], v[46:49]
	v_mfma_f32_16x16x128_f8f6f4 v[42:45], v[26:33], v[222:229], v[42:45]
	s_setprio 0
	s_setprio 2
	v_mfma_f32_16x16x128_f8f6f4 v[86:89], v[2:9], v[198:205], v[86:89]
	v_mfma_f32_16x16x128_f8f6f4 v[82:85], v[10:17], v[198:205], v[82:85]
	v_mfma_f32_16x16x128_f8f6f4 v[70:73], v[2:9], v[206:213], v[70:73]
	v_mfma_f32_16x16x128_f8f6f4 v[66:69], v[10:17], v[206:213], v[66:69]
	v_mfma_f32_16x16x128_f8f6f4 v[54:57], v[2:9], v[214:221], v[54:57]
	v_mfma_f32_16x16x128_f8f6f4 v[50:53], v[10:17], v[214:221], v[50:53]
	v_mfma_f32_16x16x128_f8f6f4 v[38:41], v[2:9], v[222:229], v[38:41]
	v_mfma_f32_16x16x128_f8f6f4 v[34:37], v[10:17], v[222:229], v[34:37]
	s_setprio 0
	s_add_i32 s75, 0, 0x18000
	s_add_i32 s76, 0, 0x1c000
	v_add_u32_e32 v14, s75, v191
	v_add_u32_e32 v30, s76, v191
	ds_read_b128 v[2:5], v14
	ds_read_b128 v[6:9], v14 offset:1024
	ds_read_b128 v[10:13], v14 offset:2048
	ds_read_b128 v[14:17], v14 offset:3072
	ds_read_b128 v[18:21], v30
	ds_read_b128 v[22:25], v30 offset:1024
	ds_read_b128 v[26:29], v30 offset:2048
	ds_read_b128 v[30:33], v30 offset:3072
	s_mov_b32 m0, s50
	ds_read_b128 v[198:201], v194 offset:32768
	ds_read_b128 v[202:205], v194 offset:33792
	ds_read_b128 v[206:209], v194 offset:34816
	ds_read_b128 v[210:213], v194 offset:35840
	ds_read_b128 v[214:217], v194 offset:36864
	ds_read_b128 v[218:221], v194 offset:37888
	ds_read_b128 v[222:225], v194 offset:38912
	ds_read_b128 v[226:229], v194 offset:39936
	global_load_lds_dwordx4 v178, s[30:31]
	s_mov_b32 m0, s51
	s_nop 0
	global_load_lds_dwordx4 v180, s[30:31]
	s_waitcnt vmcnt(8)
	s_waitcnt lgkmcnt(0)
	s_barrier
; #define PG8_STAGE(bufoff, gbase, voff) do { _Pragma("unroll") for (int _i = 0; _i < 2; ++_i) \
;         __builtin_amdgcn_global_load_lds((const unsigned*)((const char*)(gbase) + (voff)[_i]), (PG8_LAS unsigned*)(lds + (bufoff) + ldsw + _i * 8192), 16, 0, 0); } while (0)
; #define PG8_WAIT_V(n) asm volatile("s_waitcnt vmcnt(" #n ")" ::: "memory")
; #define PG8_WAIT_L(n) asm volatile("s_waitcnt lgkmcnt(" #n ")" ::: "memory")
; template <class Epi, class Sched, bool ALIGN_EPI = true, bool F8 = false>
; __device__ __forceinline__ void gemm_phase(PG8_LAS unsigned char* lds, const Sched& S, const Epi& E) {
;     ...
;         for (int t = 0; t < nt; t += 2) {
;             const bool last = (t == nt - 2);
;             if constexpr (Sched::GATHER) { if (last && has_next) S.a_off(nxt, Rs, Cs, voffAn); }
;             const char* a1 = cA + (size_t)(t + 1) * kstep;
;             const char* a2 = last ? nA : cA + (size_t)(t + 2) * kstep; const char* b2 = last ? nB : cB + (size_t)(t + 2) * kstepB;
;             const char* a3 = a2 + kstep; const char* b3 = b2 + kstepB;
;             unsigned vA2[2][2];
; #pragma unroll
;             for (int h = 0; h < 2; ++h)
; #pragma unroll
;                 for (int i = 0; i < 2; ++i) { if constexpr (Sched::GATHER) vA2[h][i] = (last && has_next) ? voffAn[h][i] : voffA[h][i]; else vA2[h][i] = voffA[h][i]; }
;             PG8_LDB(B0, 0, 0); PG8_LDB(B1, 0, 1); PG8_SCHED; PG8_LDA(At, 0, 0); PG8_STAGE(PG8_SA(1, 1), a1, voffA[1]);
;             PG8_WAIT_V(8); PG8_WAIT_L(0); PG8_BAR; PG8_MMA(0, 0, At, B0); PG8_MMA(0, 1, At, B1); PG8_BAR; PG8_SCHED;
;             PG8_LDA(At, 0, 1); PG8_STAGE(PG8_SB(0, 0), b2, voffB[0]); PG8_STAGE(PG8_SB(0, 1), b2, voffB[1]); PG8_STAGE(PG8_SA(0, 0), a2, vA2[0]);
;             PG8_WAIT_V(8); PG8_WAIT_L(0); PG8_BAR; PG8_MMA(1, 0, At, B0); PG8_MMA(1, 1, At, B1); PG8_BAR; PG8_SCHED;
;             PG8_LDB(B0, 1, 0); PG8_LDB(B1, 1, 1); PG8_SCHED; PG8_LDA(At, 1, 0); PG8_STAGE(PG8_SA(0, 1), a2, vA2[1]);
;             PG8_WAIT_V(8); PG8_WAIT_L(0); PG8_BAR; PG8_MMA(0, 0, At, B0); PG8_MMA(0, 1, At, B1); PG8_BAR; PG8_SCHED;
;             PG8_LDA(At, 1, 1); PG8_STAGE(PG8_SB(1, 0), b3, voffB[0]); PG8_STAGE(PG8_SB(1, 1), b3, voffB[1]); PG8_STAGE(PG8_SA(1, 0), a3, vA2[0]);
;             PG8_WAIT_V(8); PG8_WAIT_L(0); PG8_BAR; PG8_MMA(1, 0, At, B0); PG8_MMA(1, 1, At, B1); PG8_BAR; PG8_SCHED;
	s_setprio 2
	v_mfma_f32_16x16x128_f8f6f4 v[158:161], v[2:9], v[198:205], v[158:161]
	v_mfma_f32_16x16x128_f8f6f4 v[154:157], v[10:17], v[198:205], v[154:157]
	v_mfma_f32_16x16x128_f8f6f4 v[142:145], v[2:9], v[206:213], v[142:145]
	v_mfma_f32_16x16x128_f8f6f4 v[138:141], v[10:17], v[206:213], v[138:141]
	v_mfma_f32_16x16x128_f8f6f4 v[126:129], v[2:9], v[214:221], v[126:129]
	v_mfma_f32_16x16x128_f8f6f4 v[122:125], v[10:17], v[214:221], v[122:125]
	v_mfma_f32_16x16x128_f8f6f4 v[110:113], v[2:9], v[222:229], v[110:113]
	v_mfma_f32_16x16x128_f8f6f4 v[106:109], v[10:17], v[222:229], v[106:109]
	s_setprio 0
	s_setprio 2
	v_mfma_f32_16x16x128_f8f6f4 v[150:153], v[18:25], v[198:205], v[150:153]
	v_mfma_f32_16x16x128_f8f6f4 v[146:149], v[26:33], v[198:205], v[146:149]
	v_mfma_f32_16x16x128_f8f6f4 v[134:137], v[18:25], v[206:213], v[134:137]
	v_mfma_f32_16x16x128_f8f6f4 v[130:133], v[26:33], v[206:213], v[130:133]
	v_mfma_f32_16x16x128_f8f6f4 v[118:121], v[18:25], v[214:221], v[118:121]
	v_mfma_f32_16x16x128_f8f6f4 v[114:117], v[26:33], v[214:221], v[114:117]
	v_mfma_f32_16x16x128_f8f6f4 v[102:105], v[18:25], v[222:229], v[102:105]
	v_mfma_f32_16x16x128_f8f6f4 v[98:101], v[26:33], v[222:229], v[98:101]
	s_setprio 0
	s_add_u32 s28, s28, 0x8000
	s_addc_u32 s29, s29, 0
	s_add_i32 s30, s75, s47
	s_mov_b32 m0, s30
	ds_read_b128 v[198:201], v194 offset:49152
	ds_read_b128 v[202:205], v194 offset:50176
	ds_read_b128 v[206:209], v194 offset:51200
	ds_read_b128 v[210:213], v194 offset:52224
	ds_read_b128 v[214:217], v194 offset:53248
	ds_read_b128 v[218:221], v194 offset:54272
	ds_read_b128 v[222:225], v194 offset:55296
	ds_read_b128 v[226:229], v194 offset:56320
	global_load_lds_dwordx4 v164, s[28:29]
	s_add_i32 m0, s30, 0x2000
	s_add_i32 s30, s76, s47
	global_load_lds_dwordx4 v166, s[28:29]
	s_mov_b32 m0, s30
	s_nop 0
	global_load_lds_dwordx4 v168, s[28:29]
	s_add_i32 m0, s30, 0x2000
	s_nop 0
	global_load_lds_dwordx4 v172, s[28:29]
	s_mov_b32 m0, s60
	s_nop 0
	global_load_lds_dwordx4 v174, s[26:27]
	s_mov_b32 m0, s61
	s_nop 0
	global_load_lds_dwordx4 v176, s[26:27]
	s_waitcnt vmcnt(8)
	s_waitcnt lgkmcnt(0)
	s_barrier
	s_setprio 2
	v_mfma_f32_16x16x128_f8f6f4 v[94:97], v[2:9], v[198:205], v[94:97]
	v_mfma_f32_16x16x128_f8f6f4 v[90:93], v[10:17], v[198:205], v[90:93]
	v_mfma_f32_16x16x128_f8f6f4 v[78:81], v[2:9], v[206:213], v[78:81]
	v_mfma_f32_16x16x128_f8f6f4 v[74:77], v[10:17], v[206:213], v[74:77]
	v_mfma_f32_16x16x128_f8f6f4 v[62:65], v[2:9], v[214:221], v[62:65]
	v_mfma_f32_16x16x128_f8f6f4 v[58:61], v[10:17], v[214:221], v[58:61]
	v_mfma_f32_16x16x128_f8f6f4 v[46:49], v[2:9], v[222:229], v[46:49]
	v_mfma_f32_16x16x128_f8f6f4 v[42:45], v[10:17], v[222:229], v[42:45]
	s_setprio 0
	s_setprio 2
	v_mfma_f32_16x16x128_f8f6f4 v[86:89], v[18:25], v[198:205], v[86:89]
	v_mfma_f32_16x16x128_f8f6f4 v[82:85], v[26:33], v[198:205], v[82:85]
	v_mfma_f32_16x16x128_f8f6f4 v[70:73], v[18:25], v[206:213], v[70:73]
	v_mfma_f32_16x16x128_f8f6f4 v[66:69], v[26:33], v[206:213], v[66:69]
	v_mfma_f32_16x16x128_f8f6f4 v[54:57], v[18:25], v[214:221], v[54:57]
	v_mfma_f32_16x16x128_f8f6f4 v[50:53], v[26:33], v[214:221], v[50:53]
	v_mfma_f32_16x16x128_f8f6f4 v[38:41], v[18:25], v[222:229], v[38:41]
	v_mfma_f32_16x16x128_f8f6f4 v[34:37], v[26:33], v[222:229], v[34:37]
	s_setprio 0
	s_add_i32 s74, s74, 2
	s_add_u32 s17, s17, 0x10000
	s_addc_u32 s19, s19, 0
	s_add_u32 s24, s24, 0x10000
	s_addc_u32 s25, s25, 0
	s_cmp_gt_u32 s74, 13
	s_cbranch_scc0 .Lh1_428

; #define PG8_STAGE(bufoff, gbase, voff) do { _Pragma("unroll") for (int _i = 0; _i < 2; ++_i) \
;         __builtin_amdgcn_global_load_lds((const unsigned*)((const char*)(gbase) + (voff)[_i]), (PG8_LAS unsigned*)(lds + (bufoff) + ldsw + _i * 8192), 16, 0, 0); } while (0)
; #define PG8_WAIT_V(n) asm volatile("s_waitcnt vmcnt(" #n ")" ::: "memory")
; #define PG8_WAIT_L(n) asm volatile("s_waitcnt lgkmcnt(" #n ")" ::: "memory")
; template <class Epi, class Sched, bool ALIGN_EPI = true, bool F8 = false>
; __device__ __forceinline__ void gemm_phase(PG8_LAS unsigned char* lds, const Sched& S, const Epi& E) {
;     ...
;         for (int t = 0; t < nt; t += 2) {
;             const bool last = (t == nt - 2);
;             if constexpr (Sched::GATHER) { if (last && has_next) S.a_off(nxt, Rs, Cs, voffAn); }
;             const char* a1 = cA + (size_t)(t + 1) * kstep;
;             const char* a2 = last ? nA : cA + (size_t)(t + 2) * kstep; const char* b2 = last ? nB : cB + (size_t)(t + 2) * kstepB;
;             const char* a3 = a2 + kstep; const char* b3 = b2 + kstepB;
;             unsigned vA2[2][2];
; #pragma unroll
;             for (int h = 0; h < 2; ++h)
; #pragma unroll
;                 for (int i = 0; i < 2; ++i) { if constexpr (Sched::GATHER) vA2[h][i] = (last && has_next) ? voffAn[h][i] : voffA[h][i]; else vA2[h][i] = voffA[h][i]; }
;             PG8_LDB(B0, 0, 0); PG8_LDB(B1, 0, 1); PG8_SCHED; PG8_LDA(At, 0, 0); PG8_STAGE(PG8_SA(1, 1), a1, voffA[1]);
;             PG8_WAIT_V(8); PG8_WAIT_L(0); PG8_BAR; PG8_MMA(0, 0, At, B0); PG8_MMA(0, 1, At, B1); PG8_BAR; PG8_SCHED;
;             PG8_LDA(At, 0, 1); PG8_STAGE(PG8_SB(0, 0), b2, voffB[0]); PG8_STAGE(PG8_SB(0, 1), b2, voffB[1]); PG8_STAGE(PG8_SA(0, 0), a2, vA2[0]);
;             PG8_WAIT_V(8); PG8_WAIT_L(0); PG8_BAR; PG8_MMA(1, 0, At, B0); PG8_MMA(1, 1, At, B1); PG8_BAR; PG8_SCHED;
;             PG8_LDB(B0, 1, 0); PG8_LDB(B1, 1, 1); PG8_SCHED; PG8_LDA(At, 1, 0); PG8_STAGE(PG8_SA(0, 1), a2, vA2[1]);
;             PG8_WAIT_V(8); PG8_WAIT_L(0); PG8_BAR; PG8_MMA(0, 0, At, B0); PG8_MMA(0, 1, At, B1); PG8_BAR; PG8_SCHED;
;             PG8_LDA(At, 1, 1); PG8_STAGE(PG8_SB(1, 0), b3, voffB[0]); PG8_STAGE(PG8_SB(1, 1), b3, voffB[1]); PG8_STAGE(PG8_SA(1, 0), a3, vA2[0]);
;             PG8_WAIT_V(8); PG8_WAIT_L(0); PG8_BAR; PG8_MMA(1, 0, At, B0); PG8_MMA(1, 1, At, B1); PG8_BAR; PG8_SCHED;
.LBB0_834:
	v_add_u32_e32 v10, s58, v190
	ds_read_b128 v[2:5], v10
	ds_read_b128 v[6:9], v10 offset:1024
	ds_read_b128 v[142:145], v10 offset:2048
	ds_read_b128 v[146:149], v10 offset:3072
	v_add_u32_e32 v10, s59, v190
	ds_read_b128 v[150:153], v10
	ds_read_b128 v[154:157], v10 offset:1024
	ds_read_b128 v[202:205], v10 offset:2048
	ds_read_b128 v[206:209], v10 offset:3072
	s_add_i32 s77, s26, 2
	s_add_u32 s27, s24, 0x8000
	s_addc_u32 s28, s25, 0
	s_cmp_eq_u32 s74, s26
	s_cselect_b32 s30, s20, s27
	s_cselect_b32 s31, s21, s28
	s_cselect_b32 s28, s22, s75
	s_cselect_b32 s29, s23, s76
	s_add_u32 s26, s30, 0x8000
	s_addc_u32 s27, s31, 0
	s_add_i32 m0, s45, 0xc000
	ds_read_b128 v[210:213], v198
	ds_read_b128 v[214:217], v198 offset:1024
	ds_read_b128 v[218:221], v198 offset:2048
	ds_read_b128 v[222:225], v198 offset:3072
	ds_read_b128 v[226:229], v198 offset:4096
	ds_read_b128 v[230:233], v198 offset:5120
	ds_read_b128 v[234:237], v198 offset:6144
	ds_read_b128 v[238:241], v198 offset:7168
	global_load_lds_dwordx4 v182, s[24:25]
	s_add_i32 m0, s45, 0xe000
	s_nop 0
	global_load_lds_dwordx4 v180, s[24:25]
	s_waitcnt vmcnt(8)
	s_waitcnt lgkmcnt(0)
	s_setprio 1
	v_mfma_f32_16x16x128_f8f6f4 v[138:141], v[2:9], v[210:217], v[138:141]
	v_mfma_f32_16x16x128_f8f6f4 v[134:137], v[142:149], v[210:217], v[134:137]
	v_mfma_f32_16x16x128_f8f6f4 v[130:133], v[2:9], v[218:225], v[130:133]
	v_mfma_f32_16x16x128_f8f6f4 v[126:129], v[142:149], v[218:225], v[126:129]
	v_mfma_f32_16x16x128_f8f6f4 v[122:125], v[2:9], v[226:233], v[122:125]
	v_mfma_f32_16x16x128_f8f6f4 v[118:121], v[142:149], v[226:233], v[118:121]
	v_mfma_f32_16x16x128_f8f6f4 v[114:117], v[2:9], v[234:241], v[114:117]
	v_mfma_f32_16x16x128_f8f6f4 v[110:113], v[142:149], v[234:241], v[110:113]
	s_setprio 0
	s_setprio 1
	v_mfma_f32_16x16x128_f8f6f4 v[106:109], v[150:157], v[210:217], v[106:109]
	v_mfma_f32_16x16x128_f8f6f4 v[102:105], v[202:209], v[210:217], v[102:105]
	v_mfma_f32_16x16x128_f8f6f4 v[98:101], v[150:157], v[218:225], v[98:101]
	v_mfma_f32_16x16x128_f8f6f4 v[94:97], v[202:209], v[218:225], v[94:97]
	v_mfma_f32_16x16x128_f8f6f4 v[90:93], v[150:157], v[226:233], v[90:93]
	v_mfma_f32_16x16x128_f8f6f4 v[86:89], v[202:209], v[226:233], v[86:89]
	v_mfma_f32_16x16x128_f8f6f4 v[82:85], v[150:157], v[234:241], v[82:85]
	v_mfma_f32_16x16x128_f8f6f4 v[78:81], v[202:209], v[234:241], v[78:81]
	s_setprio 0
	s_barrier
	s_add_i32 s78, s58, s44
	s_mov_b32 m0, s78
	ds_read_b128 v[210:213], v198 offset:16384
	ds_read_b128 v[214:217], v198 offset:17408
	ds_read_b128 v[218:221], v198 offset:18432
	ds_read_b128 v[222:225], v198 offset:19456
	ds_read_b128 v[226:229], v198 offset:20480
	ds_read_b128 v[230:233], v198 offset:21504
	ds_read_b128 v[234:237], v198 offset:22528
	ds_read_b128 v[238:241], v198 offset:23552
	global_load_lds_dwordx4 v158, s[28:29]
	s_add_i32 m0, s78, 0x2000
	s_add_i32 s78, s59, s44
	global_load_lds_dwordx4 v160, s[28:29]
	s_add_u32 s98, s28, s8
	s_addc_u32 s99, s29, s9
	s_mov_b32 m0, s78
	s_nop 0
	global_load_lds_dwordx4 v158, s[98:99]
	s_add_u32 s100, s28, s8
	s_addc_u32 s101, s29, s9
	s_add_i32 m0, s78, 0x2000
	s_nop 0
	global_load_lds_dwordx4 v160, s[100:101]
	s_mov_b32 m0, s45
	s_nop 0
	global_load_lds_dwordx4 v162, s[30:31]
	s_mov_b32 m0, s46
	s_nop 0
	global_load_lds_dwordx4 v164, s[30:31]
	s_waitcnt vmcnt(8)
	s_waitcnt lgkmcnt(0)
	s_setprio 1
	v_mfma_f32_16x16x128_f8f6f4 v[74:77], v[2:9], v[210:217], v[74:77]
	v_mfma_f32_16x16x128_f8f6f4 v[70:73], v[142:149], v[210:217], v[70:73]
	v_mfma_f32_16x16x128_f8f6f4 v[66:69], v[2:9], v[218:225], v[66:69]
	v_mfma_f32_16x16x128_f8f6f4 v[62:65], v[142:149], v[218:225], v[62:65]
	v_mfma_f32_16x16x128_f8f6f4 v[58:61], v[2:9], v[226:233], v[58:61]
	v_mfma_f32_16x16x128_f8f6f4 v[54:57], v[142:149], v[226:233], v[54:57]
	v_mfma_f32_16x16x128_f8f6f4 v[50:53], v[2:9], v[234:241], v[50:53]
	v_mfma_f32_16x16x128_f8f6f4 v[46:49], v[142:149], v[234:241], v[46:49]
	s_setprio 0
	s_setprio 1
	v_mfma_f32_16x16x128_f8f6f4 v[42:45], v[150:157], v[210:217], v[42:45]
	v_mfma_f32_16x16x128_f8f6f4 v[38:41], v[202:209], v[210:217], v[38:41]
	v_mfma_f32_16x16x128_f8f6f4 v[34:37], v[150:157], v[218:225], v[34:37]
	v_mfma_f32_16x16x128_f8f6f4 v[30:33], v[202:209], v[218:225], v[30:33]
	v_mfma_f32_16x16x128_f8f6f4 v[26:29], v[150:157], v[226:233], v[26:29]
	v_mfma_f32_16x16x128_f8f6f4 v[22:25], v[202:209], v[226:233], v[22:25]
	v_mfma_f32_16x16x128_f8f6f4 v[18:21], v[150:157], v[234:241], v[18:21]
	v_mfma_f32_16x16x128_f8f6f4 v[14:17], v[202:209], v[234:241], v[14:17]
	s_setprio 0
	s_barrier
	s_add_i32 s78, 0, 0x18000
	s_add_i32 s79, 0, 0x1c000
	v_add_u32_e32 v2, s78, v190
	v_add_u32_e32 v10, s79, v190
	ds_read_b128 v[142:145], v2
	ds_read_b128 v[146:149], v2 offset:1024
	ds_read_b128 v[150:153], v2 offset:2048
	ds_read_b128 v[154:157], v2 offset:3072
	ds_read_b128 v[2:5], v10
	ds_read_b128 v[6:9], v10 offset:1024
	ds_read_b128 v[202:205], v10 offset:2048
	ds_read_b128 v[206:209], v10 offset:3072
	s_mov_b32 m0, s47
	ds_read_b128 v[210:213], v198 offset:32768
	ds_read_b128 v[214:217], v198 offset:33792
	ds_read_b128 v[218:221], v198 offset:34816
	ds_read_b128 v[222:225], v198 offset:35840
	ds_read_b128 v[226:229], v198 offset:36864
	ds_read_b128 v[230:233], v198 offset:37888
	ds_read_b128 v[234:237], v198 offset:38912
	ds_read_b128 v[238:241], v198 offset:39936
	global_load_lds_dwordx4 v166, s[30:31]
	s_mov_b32 m0, s48
	s_nop 0
	global_load_lds_dwordx4 v168, s[30:31]
	s_waitcnt vmcnt(8)
	s_waitcnt lgkmcnt(0)
	s_setprio 1
	v_mfma_f32_16x16x128_f8f6f4 v[138:141], v[142:149], v[210:217], v[138:141]
	v_mfma_f32_16x16x128_f8f6f4 v[134:137], v[150:157], v[210:217], v[134:137]
	v_mfma_f32_16x16x128_f8f6f4 v[130:133], v[142:149], v[218:225], v[130:133]
	v_mfma_f32_16x16x128_f8f6f4 v[126:129], v[150:157], v[218:225], v[126:129]
	v_mfma_f32_16x16x128_f8f6f4 v[122:125], v[142:149], v[226:233], v[122:125]
	v_mfma_f32_16x16x128_f8f6f4 v[118:121], v[150:157], v[226:233], v[118:121]
	v_mfma_f32_16x16x128_f8f6f4 v[114:117], v[142:149], v[234:241], v[114:117]
	v_mfma_f32_16x16x128_f8f6f4 v[110:113], v[150:157], v[234:241], v[110:113]
	s_setprio 0
	s_setprio 1
	v_mfma_f32_16x16x128_f8f6f4 v[106:109], v[2:9], v[210:217], v[106:109]
	v_mfma_f32_16x16x128_f8f6f4 v[102:105], v[202:209], v[210:217], v[102:105]
	v_mfma_f32_16x16x128_f8f6f4 v[98:101], v[2:9], v[218:225], v[98:101]
	v_mfma_f32_16x16x128_f8f6f4 v[94:97], v[202:209], v[218:225], v[94:97]
	v_mfma_f32_16x16x128_f8f6f4 v[90:93], v[2:9], v[226:233], v[90:93]
	v_mfma_f32_16x16x128_f8f6f4 v[86:89], v[202:209], v[226:233], v[86:89]
	v_mfma_f32_16x16x128_f8f6f4 v[82:85], v[2:9], v[234:241], v[82:85]
	v_mfma_f32_16x16x128_f8f6f4 v[78:81], v[202:209], v[234:241], v[78:81]
	s_setprio 0
	s_barrier
; #define PG8_STAGE(bufoff, gbase, voff) do { _Pragma("unroll") for (int _i = 0; _i < 2; ++_i) \
;         __builtin_amdgcn_global_load_lds((const unsigned*)((const char*)(gbase) + (voff)[_i]), (PG8_LAS unsigned*)(lds + (bufoff) + ldsw + _i * 8192), 16, 0, 0); } while (0)
; #define PG8_WAIT_V(n) asm volatile("s_waitcnt vmcnt(" #n ")" ::: "memory")
; #define PG8_WAIT_L(n) asm volatile("s_waitcnt lgkmcnt(" #n ")" ::: "memory")
; template <class Epi, class Sched, bool ALIGN_EPI = true, bool F8 = false>
; __device__ __forceinline__ void gemm_phase(PG8_LAS unsigned char* lds, const Sched& S, const Epi& E) {
;     ...
;         for (int t = 0; t < nt; t += 2) {
;             const bool last = (t == nt - 2);
;             if constexpr (Sched::GATHER) { if (last && has_next) S.a_off(nxt, Rs, Cs, voffAn); }
;             const char* a1 = cA + (size_t)(t + 1) * kstep;
;             const char* a2 = last ? nA : cA + (size_t)(t + 2) * kstep; const char* b2 = last ? nB : cB + (size_t)(t + 2) * kstepB;
;             const char* a3 = a2 + kstep; const char* b3 = b2 + kstepB;
;             unsigned vA2[2][2];
; #pragma unroll
;             for (int h = 0; h < 2; ++h)
; #pragma unroll
;                 for (int i = 0; i < 2; ++i) { if constexpr (Sched::GATHER) vA2[h][i] = (last && has_next) ? voffAn[h][i] : voffA[h][i]; else vA2[h][i] = voffA[h][i]; }
;             PG8_LDB(B0, 0, 0); PG8_LDB(B1, 0, 1); PG8_SCHED; PG8_LDA(At, 0, 0); PG8_STAGE(PG8_SA(1, 1), a1, voffA[1]);
;             PG8_WAIT_V(8); PG8_WAIT_L(0); PG8_BAR; PG8_MMA(0, 0, At, B0); PG8_MMA(0, 1, At, B1); PG8_BAR; PG8_SCHED;
;             PG8_LDA(At, 0, 1); PG8_STAGE(PG8_SB(0, 0), b2, voffB[0]); PG8_STAGE(PG8_SB(0, 1), b2, voffB[1]); PG8_STAGE(PG8_SA(0, 0), a2, vA2[0]);
;             PG8_WAIT_V(8); PG8_WAIT_L(0); PG8_BAR; PG8_MMA(1, 0, At, B0); PG8_MMA(1, 1, At, B1); PG8_BAR; PG8_SCHED;
;             PG8_LDB(B0, 1, 0); PG8_LDB(B1, 1, 1); PG8_SCHED; PG8_LDA(At, 1, 0); PG8_STAGE(PG8_SA(0, 1), a2, vA2[1]);
;             PG8_WAIT_V(8); PG8_WAIT_L(0); PG8_BAR; PG8_MMA(0, 0, At, B0); PG8_MMA(0, 1, At, B1); PG8_BAR; PG8_SCHED;
;             PG8_LDA(At, 1, 1); PG8_STAGE(PG8_SB(1, 0), b3, voffB[0]); PG8_STAGE(PG8_SB(1, 1), b3, voffB[1]); PG8_STAGE(PG8_SA(1, 0), a3, vA2[0]);
;             PG8_WAIT_V(8); PG8_WAIT_L(0); PG8_BAR; PG8_MMA(1, 0, At, B0); PG8_MMA(1, 1, At, B1); PG8_BAR; PG8_SCHED;
;         }
	s_add_u32 s28, s28, 0x8000
	s_addc_u32 s29, s29, 0
	s_add_i32 s30, s78, s44
	s_mov_b32 m0, s30
	ds_read_b128 v[210:213], v198 offset:49152
	ds_read_b128 v[214:217], v198 offset:50176
	ds_read_b128 v[218:221], v198 offset:51200
	ds_read_b128 v[222:225], v198 offset:52224
	ds_read_b128 v[226:229], v198 offset:53248
	ds_read_b128 v[230:233], v198 offset:54272
	ds_read_b128 v[234:237], v198 offset:55296
	ds_read_b128 v[238:241], v198 offset:56320
	global_load_lds_dwordx4 v158, s[28:29]
	s_add_i32 m0, s30, 0x2000
	s_add_i32 s30, s79, s44
	global_load_lds_dwordx4 v160, s[28:29]
	s_mov_b32 m0, s30
	s_nop 0
	global_load_lds_dwordx4 v172, s[28:29]
	s_add_i32 m0, s30, 0x2000
	s_nop 0
	global_load_lds_dwordx4 v174, s[28:29]
	s_mov_b32 m0, s50
	s_nop 0
	global_load_lds_dwordx4 v162, s[26:27]
	s_mov_b32 m0, s51
	s_nop 0
	global_load_lds_dwordx4 v164, s[26:27]
	s_waitcnt vmcnt(8)
	s_waitcnt lgkmcnt(0)
	s_setprio 1
	v_mfma_f32_16x16x128_f8f6f4 v[74:77], v[142:149], v[210:217], v[74:77]
	v_mfma_f32_16x16x128_f8f6f4 v[70:73], v[150:157], v[210:217], v[70:73]
	v_mfma_f32_16x16x128_f8f6f4 v[66:69], v[142:149], v[218:225], v[66:69]
	v_mfma_f32_16x16x128_f8f6f4 v[62:65], v[150:157], v[218:225], v[62:65]
	v_mfma_f32_16x16x128_f8f6f4 v[58:61], v[142:149], v[226:233], v[58:61]
	v_mfma_f32_16x16x128_f8f6f4 v[54:57], v[150:157], v[226:233], v[54:57]
	v_mfma_f32_16x16x128_f8f6f4 v[50:53], v[142:149], v[234:241], v[50:53]
	v_mfma_f32_16x16x128_f8f6f4 v[46:49], v[150:157], v[234:241], v[46:49]
	s_setprio 0
	s_setprio 1
	v_mfma_f32_16x16x128_f8f6f4 v[42:45], v[2:9], v[210:217], v[42:45]
	v_mfma_f32_16x16x128_f8f6f4 v[38:41], v[202:209], v[210:217], v[38:41]
	v_mfma_f32_16x16x128_f8f6f4 v[34:37], v[2:9], v[218:225], v[34:37]
	v_mfma_f32_16x16x128_f8f6f4 v[30:33], v[202:209], v[218:225], v[30:33]
	v_mfma_f32_16x16x128_f8f6f4 v[26:29], v[2:9], v[226:233], v[26:29]
	v_mfma_f32_16x16x128_f8f6f4 v[22:25], v[202:209], v[226:233], v[22:25]
	v_mfma_f32_16x16x128_f8f6f4 v[18:21], v[2:9], v[234:241], v[18:21]
	v_mfma_f32_16x16x128_f8f6f4 v[14:17], v[202:209], v[234:241], v[14:17]
	s_setprio 0
	s_barrier
	s_add_u32 s75, s75, 0x10000
	s_addc_u32 s76, s76, 0
	s_add_u32 s24, s24, 0x10000
	s_addc_u32 s25, s25, 0
	s_cmp_ge_i32 s77, s72
	s_mov_b32 s26, s77
	s_cbranch_scc0 .LBB0_834
	s_branch .Lfx_23459
.Lh1e_23459:
.Lh1_834:
	v_add_u32_e32 v10, s58, v190
	ds_read_b128 v[2:5], v10
	ds_read_b128 v[6:9], v10 offset:1024
	ds_read_b128 v[142:145], v10 offset:2048
	ds_read_b128 v[146:149], v10 offset:3072
	v_add_u32_e32 v10, s59, v190
	ds_read_b128 v[150:153], v10
	ds_read_b128 v[154:157], v10 offset:1024
	ds_read_b128 v[202:205], v10 offset:2048
	ds_read_b128 v[206:209], v10 offset:3072
	s_add_i32 s77, s26, 2
	s_add_u32 s27, s24, 0x8000
	s_addc_u32 s28, s25, 0
	s_cmp_eq_u32 s74, s26
	s_cselect_b32 s30, s20, s27
	s_cselect_b32 s31, s21, s28
	s_cselect_b32 s28, s22, s75
	s_cselect_b32 s29, s23, s76
	s_add_u32 s26, s30, 0x8000
	s_addc_u32 s27, s31, 0
	s_add_i32 m0, s45, 0xc000
	ds_read_b128 v[210:213], v198
	ds_read_b128 v[214:217], v198 offset:1024
	ds_read_b128 v[218:221], v198 offset:2048
	ds_read_b128 v[222:225], v198 offset:3072
	ds_read_b128 v[226:229], v198 offset:4096
	ds_read_b128 v[230:233], v198 offset:5120
	ds_read_b128 v[234:237], v198 offset:6144
	ds_read_b128 v[238:241], v198 offset:7168
	global_load_lds_dwordx4 v182, s[24:25]
	s_add_i32 m0, s45, 0xe000
	s_nop 0
	global_load_lds_dwordx4 v180, s[24:25]
	s_waitcnt vmcnt(8)
	s_waitcnt lgkmcnt(0)
	s_barrier
	s_setprio 2
	v_mfma_f32_16x16x128_f8f6f4 v[138:141], v[2:9], v[210:217], v[138:141]
	v_mfma_f32_16x16x128_f8f6f4 v[134:137], v[142:149], v[210:217], v[134:137]
	v_mfma_f32_16x16x128_f8f6f4 v[130:133], v[2:9], v[218:225], v[130:133]
	v_mfma_f32_16x16x128_f8f6f4 v[126:129], v[142:149], v[218:225], v[126:129]
	v_mfma_f32_16x16x128_f8f6f4 v[122:125], v[2:9], v[226:233], v[122:125]
	v_mfma_f32_16x16x128_f8f6f4 v[118:121], v[142:149], v[226:233], v[118:121]
	v_mfma_f32_16x16x128_f8f6f4 v[114:117], v[2:9], v[234:241], v[114:117]
	v_mfma_f32_16x16x128_f8f6f4 v[110:113], v[142:149], v[234:241], v[110:113]
	s_setprio 0
	s_setprio 2
	v_mfma_f32_16x16x128_f8f6f4 v[106:109], v[150:157], v[210:217], v[106:109]
	v_mfma_f32_16x16x128_f8f6f4 v[102:105], v[202:209], v[210:217], v[102:105]
	v_mfma_f32_16x16x128_f8f6f4 v[98:101], v[150:157], v[218:225], v[98:101]
	v_mfma_f32_16x16x128_f8f6f4 v[94:97], v[202:209], v[218:225], v[94:97]
	v_mfma_f32_16x16x128_f8f6f4 v[90:93], v[150:157], v[226:233], v[90:93]
	v_mfma_f32_16x16x128_f8f6f4 v[86:89], v[202:209], v[226:233], v[86:89]
	v_mfma_f32_16x16x128_f8f6f4 v[82:85], v[150:157], v[234:241], v[82:85]
	v_mfma_f32_16x16x128_f8f6f4 v[78:81], v[202:209], v[234:241], v[78:81]
	s_setprio 0
	s_add_i32 s78, s58, s44
	s_mov_b32 m0, s78
	ds_read_b128 v[210:213], v198 offset:16384
	ds_read_b128 v[214:217], v198 offset:17408
	ds_read_b128 v[218:221], v198 offset:18432
	ds_read_b128 v[222:225], v198 offset:19456
	ds_read_b128 v[226:229], v198 offset:20480
	ds_read_b128 v[230:233], v198 offset:21504
	ds_read_b128 v[234:237], v198 offset:22528
	ds_read_b128 v[238:241], v198 offset:23552
	global_load_lds_dwordx4 v158, s[28:29]
	s_add_i32 m0, s78, 0x2000
	s_add_i32 s78, s59, s44
	global_load_lds_dwordx4 v160, s[28:29]
	s_add_u32 s98, s28, s8
	s_addc_u32 s99, s29, s9
	s_mov_b32 m0, s78
	s_nop 0
	global_load_lds_dwordx4 v158, s[98:99]
	s_add_u32 s100, s28, s8
	s_addc_u32 s101, s29, s9
	s_add_i32 m0, s78, 0x2000
	s_nop 0
	global_load_lds_dwordx4 v160, s[100:101]
	s_mov_b32 m0, s45
	s_nop 0
	global_load_lds_dwordx4 v162, s[30:31]
	s_mov_b32 m0, s46
	s_nop 0
	global_load_lds_dwordx4 v164, s[30:31]
	s_waitcnt vmcnt(8)
	s_waitcnt lgkmcnt(0)
	s_barrier
; #define PG8_STAGE(bufoff, gbase, voff) do { _Pragma("unroll") for (int _i = 0; _i < 2; ++_i) \
;         __builtin_amdgcn_global_load_lds((const unsigned*)((const char*)(gbase) + (voff)[_i]), (PG8_LAS unsigned*)(lds + (bufoff) + ldsw + _i * 8192), 16, 0, 0); } while (0)
; #define PG8_WAIT_V(n) asm volatile("s_waitcnt vmcnt(" #n ")" ::: "memory")
; #define PG8_WAIT_L(n) asm volatile("s_waitcnt lgkmcnt(" #n ")" ::: "memory")
; template <class Epi, class Sched, bool ALIGN_EPI = true, bool F8 = false>
; __device__ __forceinline__ void gemm_phase(PG8_LAS unsigned char* lds, const Sched& S, const Epi& E) {
;     ...
;         for (int t = 0; t < nt; t += 2) {
;             const bool last = (t == nt - 2);
;             if constexpr (Sched::GATHER) { if (last && has_next) S.a_off(nxt, Rs, Cs, voffAn); }
;             const char* a1 = cA + (size_t)(t + 1) * kstep;
;             const char* a2 = last ? nA : cA + (size_t)(t + 2) * kstep; const char* b2 = last ? nB : cB + (size_t)(t + 2) * kstepB;
;             const char* a3 = a2 + kstep; const char* b3 = b2 + kstepB;
;             unsigned vA2[2][2];
; #pragma unroll
;             for (int h = 0; h < 2; ++h)
; #pragma unroll
;                 for (int i = 0; i < 2; ++i) { if constexpr (Sched::GATHER) vA2[h][i] = (last && has_next) ? voffAn[h][i] : voffA[h][i]; else vA2[h][i] = voffA[h][i]; }
;             PG8_LDB(B0, 0, 0); PG8_LDB(B1, 0, 1); PG8_SCHED; PG8_LDA(At, 0, 0); PG8_STAGE(PG8_SA(1, 1), a1, voffA[1]);
;             PG8_WAIT_V(8); PG8_WAIT_L(0); PG8_BAR; PG8_MMA(0, 0, At, B0); PG8_MMA(0, 1, At, B1); PG8_BAR; PG8_SCHED;
;             PG8_LDA(At, 0, 1); PG8_STAGE(PG8_SB(0, 0), b2, voffB[0]); PG8_STAGE(PG8_SB(0, 1), b2, voffB[1]); PG8_STAGE(PG8_SA(0, 0), a2, vA2[0]);
;             PG8_WAIT_V(8); PG8_WAIT_L(0); PG8_BAR; PG8_MMA(1, 0, At, B0); PG8_MMA(1, 1, At, B1); PG8_BAR; PG8_SCHED;
;             PG8_LDB(B0, 1, 0); PG8_LDB(B1, 1, 1); PG8_SCHED; PG8_LDA(At, 1, 0); PG8_STAGE(PG8_SA(0, 1), a2, vA2[1]);
;             PG8_WAIT_V(8); PG8_WAIT_L(0); PG8_BAR; PG8_MMA(0, 0, At, B0); PG8_MMA(0, 1, At, B1); PG8_BAR; PG8_SCHED;
;             PG8_LDA(At, 1, 1); PG8_STAGE(PG8_SB(1, 0), b3, voffB[0]); PG8_STAGE(PG8_SB(1, 1), b3, voffB[1]); PG8_STAGE(PG8_SA(1, 0), a3, vA2[0]);
;             PG8_WAIT_V(8); PG8_WAIT_L(0); PG8_BAR; PG8_MMA(1, 0, At, B0); PG8_MMA(1, 1, At, B1); PG8_BAR; PG8_SCHED;
;         }
	s_setprio 2
	v_mfma_f32_16x16x128_f8f6f4 v[74:77], v[2:9], v[210:217], v[74:77]
	v_mfma_f32_16x16x128_f8f6f4 v[70:73], v[142:149], v[210:217], v[70:73]
	v_mfma_f32_16x16x128_f8f6f4 v[66:69], v[2:9], v[218:225], v[66:69]
	v_mfma_f32_16x16x128_f8f6f4 v[62:65], v[142:149], v[218:225], v[62:65]
	v_mfma_f32_16x16x128_f8f6f4 v[58:61], v[2:9], v[226:233], v[58:61]
	v_mfma_f32_16x16x128_f8f6f4 v[54:57], v[142:149], v[226:233], v[54:57]
	v_mfma_f32_16x16x128_f8f6f4 v[50:53], v[2:9], v[234:241], v[50:53]
	v_mfma_f32_16x16x128_f8f6f4 v[46:49], v[142:149], v[234:241], v[46:49]
	s_setprio 0
	s_setprio 2
	v_mfma_f32_16x16x128_f8f6f4 v[42:45], v[150:157], v[210:217], v[42:45]
	v_mfma_f32_16x16x128_f8f6f4 v[38:41], v[202:209], v[210:217], v[38:41]
	v_mfma_f32_16x16x128_f8f6f4 v[34:37], v[150:157], v[218:225], v[34:37]
	v_mfma_f32_16x16x128_f8f6f4 v[30:33], v[202:209], v[218:225], v[30:33]
	v_mfma_f32_16x16x128_f8f6f4 v[26:29], v[150:157], v[226:233], v[26:29]
	v_mfma_f32_16x16x128_f8f6f4 v[22:25], v[202:209], v[226:233], v[22:25]
	v_mfma_f32_16x16x128_f8f6f4 v[18:21], v[150:157], v[234:241], v[18:21]
	v_mfma_f32_16x16x128_f8f6f4 v[14:17], v[202:209], v[234:241], v[14:17]
	s_setprio 0
	s_add_i32 s78, 0, 0x18000
	s_add_i32 s79, 0, 0x1c000
	v_add_u32_e32 v2, s78, v190
	v_add_u32_e32 v10, s79, v190
	ds_read_b128 v[142:145], v2
	ds_read_b128 v[146:149], v2 offset:1024
	ds_read_b128 v[150:153], v2 offset:2048
	ds_read_b128 v[154:157], v2 offset:3072
	ds_read_b128 v[2:5], v10
	ds_read_b128 v[6:9], v10 offset:1024
	ds_read_b128 v[202:205], v10 offset:2048
	ds_read_b128 v[206:209], v10 offset:3072
	s_mov_b32 m0, s47
	ds_read_b128 v[210:213], v198 offset:32768
	ds_read_b128 v[214:217], v198 offset:33792
	ds_read_b128 v[218:221], v198 offset:34816
	ds_read_b128 v[222:225], v198 offset:35840
	ds_read_b128 v[226:229], v198 offset:36864
	ds_read_b128 v[230:233], v198 offset:37888
	ds_read_b128 v[234:237], v198 offset:38912
	ds_read_b128 v[238:241], v198 offset:39936
	global_load_lds_dwordx4 v166, s[30:31]
	s_mov_b32 m0, s48
	s_nop 0
	global_load_lds_dwordx4 v168, s[30:31]
	s_waitcnt vmcnt(8)
	s_waitcnt lgkmcnt(0)
	s_barrier
	s_setprio 2
	v_mfma_f32_16x16x128_f8f6f4 v[138:141], v[142:149], v[210:217], v[138:141]
	v_mfma_f32_16x16x128_f8f6f4 v[134:137], v[150:157], v[210:217], v[134:137]
	v_mfma_f32_16x16x128_f8f6f4 v[130:133], v[142:149], v[218:225], v[130:133]
	v_mfma_f32_16x16x128_f8f6f4 v[126:129], v[150:157], v[218:225], v[126:129]
	v_mfma_f32_16x16x128_f8f6f4 v[122:125], v[142:149], v[226:233], v[122:125]
	v_mfma_f32_16x16x128_f8f6f4 v[118:121], v[150:157], v[226:233], v[118:121]
	v_mfma_f32_16x16x128_f8f6f4 v[114:117], v[142:149], v[234:241], v[114:117]
	v_mfma_f32_16x16x128_f8f6f4 v[110:113], v[150:157], v[234:241], v[110:113]
	s_setprio 0
	s_setprio 2
	v_mfma_f32_16x16x128_f8f6f4 v[106:109], v[2:9], v[210:217], v[106:109]
	v_mfma_f32_16x16x128_f8f6f4 v[102:105], v[202:209], v[210:217], v[102:105]
	v_mfma_f32_16x16x128_f8f6f4 v[98:101], v[2:9], v[218:225], v[98:101]
	v_mfma_f32_16x16x128_f8f6f4 v[94:97], v[202:209], v[218:225], v[94:97]
	v_mfma_f32_16x16x128_f8f6f4 v[90:93], v[2:9], v[226:233], v[90:93]
	v_mfma_f32_16x16x128_f8f6f4 v[86:89], v[202:209], v[226:233], v[86:89]
	v_mfma_f32_16x16x128_f8f6f4 v[82:85], v[2:9], v[234:241], v[82:85]
	v_mfma_f32_16x16x128_f8f6f4 v[78:81], v[202:209], v[234:241], v[78:81]
	s_setprio 0
	s_add_u32 s28, s28, 0x8000
	s_addc_u32 s29, s29, 0
	s_add_i32 s30, s78, s44
	s_mov_b32 m0, s30
	ds_read_b128 v[210:213], v198 offset:49152
	ds_read_b128 v[214:217], v198 offset:50176
	ds_read_b128 v[218:221], v198 offset:51200
	ds_read_b128 v[222:225], v198 offset:52224
	ds_read_b128 v[226:229], v198 offset:53248
	ds_read_b128 v[230:233], v198 offset:54272
	ds_read_b128 v[234:237], v198 offset:55296
	ds_read_b128 v[238:241], v198 offset:56320
	global_load_lds_dwordx4 v158, s[28:29]
	s_add_i32 m0, s30, 0x2000
	s_add_i32 s30, s79, s44
	global_load_lds_dwordx4 v160, s[28:29]
	s_mov_b32 m0, s30
	s_nop 0
	global_load_lds_dwordx4 v172, s[28:29]
	s_add_i32 m0, s30, 0x2000
	s_nop 0
	global_load_lds_dwordx4 v174, s[28:29]
	s_mov_b32 m0, s50
	s_nop 0
	global_load_lds_dwordx4 v162, s[26:27]
	s_mov_b32 m0, s51
	s_nop 0
	global_load_lds_dwordx4 v164, s[26:27]
	s_waitcnt vmcnt(8)
	s_waitcnt lgkmcnt(0)
	s_barrier
	s_setprio 2
	v_mfma_f32_16x16x128_f8f6f4 v[74:77], v[142:149], v[210:217], v[74:77]
	v_mfma_f32_16x16x128_f8f6f4 v[70:73], v[150:157], v[210:217], v[70:73]
	v_mfma_f32_16x16x128_f8f6f4 v[66:69], v[142:149], v[218:225], v[66:69]
	v_mfma_f32_16x16x128_f8f6f4 v[62:65], v[150:157], v[218:225], v[62:65]
	v_mfma_f32_16x16x128_f8f6f4 v[58:61], v[142:149], v[226:233], v[58:61]
	v_mfma_f32_16x16x128_f8f6f4 v[54:57], v[150:157], v[226:233], v[54:57]
	v_mfma_f32_16x16x128_f8f6f4 v[50:53], v[142:149], v[234:241], v[50:53]
	v_mfma_f32_16x16x128_f8f6f4 v[46:49], v[150:157], v[234:241], v[46:49]
	s_setprio 0
	s_setprio 2
	v_mfma_f32_16x16x128_f8f6f4 v[42:45], v[2:9], v[210:217], v[42:45]
	v_mfma_f32_16x16x128_f8f6f4 v[38:41], v[202:209], v[210:217], v[38:41]
	v_mfma_f32_16x16x128_f8f6f4 v[34:37], v[2:9], v[218:225], v[34:37]
	v_mfma_f32_16x16x128_f8f6f4 v[30:33], v[202:209], v[218:225], v[30:33]
	v_mfma_f32_16x16x128_f8f6f4 v[26:29], v[2:9], v[226:233], v[26:29]
	v_mfma_f32_16x16x128_f8f6f4 v[22:25], v[202:209], v[226:233], v[22:25]
	v_mfma_f32_16x16x128_f8f6f4 v[18:21], v[2:9], v[234:241], v[18:21]
	v_mfma_f32_16x16x128_f8f6f4 v[14:17], v[202:209], v[234:241], v[14:17]
	s_setprio 0
	s_add_u32 s75, s75, 0x10000
	s_addc_u32 s76, s76, 0
	s_add_u32 s24, s24, 0x10000
	s_addc_u32 s25, s25, 0
	s_cmp_ge_i32 s77, s72
	s_mov_b32 s26, s77
	s_cbranch_scc0 .Lh1_834

; #define PG8_STAGE(bufoff, gbase, voff) do { _Pragma("unroll") for (int _i = 0; _i < 2; ++_i) \
;         __builtin_amdgcn_global_load_lds((const unsigned*)((const char*)(gbase) + (voff)[_i]), (PG8_LAS unsigned*)(lds + (bufoff) + ldsw + _i * 8192), 16, 0, 0); } while (0)
; #define PG8_WAIT_V(n) asm volatile("s_waitcnt vmcnt(" #n ")" ::: "memory")
; #define PG8_WAIT_L(n) asm volatile("s_waitcnt lgkmcnt(" #n ")" ::: "memory")
; #define PG8_BAR __builtin_amdgcn_s_barrier()
; #define PG8_SCHED __builtin_amdgcn_sched_barrier(0)
; template <class Epi, class Sched, bool ALIGN_EPI = true, bool F8 = false>
; __device__ __forceinline__ void gemm_phase(PG8_LAS unsigned char* lds, const Sched& S, const Epi& E) {
;     ...
;     f32x4 acc[2][2][4][2];
; #pragma unroll
;     for (int a = 0; a < 2; ++a)
; #pragma unroll
;         for (int b = 0; b < 2; ++b)
; #pragma unroll
;             for (int m = 0; m < 4; ++m)
; #pragma unroll
;                 for (int n = 0; n < 2; ++n) acc[a][b][m][n] = (f32x4){0.f, 0.f, 0.f, 0.f};
;     ...
;             PG8_LDB(B0, 0, 0); PG8_LDB(B1, 0, 1); PG8_SCHED; PG8_LDA(At, 0, 0); PG8_STAGE(PG8_SA(1, 1), a1, voffA[1]);
;             PG8_WAIT_V(8); PG8_WAIT_L(0); PG8_BAR; PG8_MMA(0, 0, At, B0); PG8_MMA(0, 1, At, B1); PG8_BAR; PG8_SCHED;
;             PG8_LDA(At, 0, 1); PG8_STAGE(PG8_SB(0, 0), b2, voffB[0]); PG8_STAGE(PG8_SB(0, 1), b2, voffB[1]); PG8_STAGE(PG8_SA(0, 0), a2, vA2[0]);
;             PG8_WAIT_V(8); PG8_WAIT_L(0); PG8_BAR; PG8_MMA(1, 0, At, B0); PG8_MMA(1, 1, At, B1); PG8_BAR; PG8_SCHED;
;             PG8_LDB(B0, 1, 0); PG8_LDB(B1, 1, 1); PG8_SCHED; PG8_LDA(At, 1, 0); PG8_STAGE(PG8_SA(0, 1), a2, vA2[1]);
;             PG8_WAIT_V(8); PG8_WAIT_L(0); PG8_BAR; PG8_MMA(0, 0, At, B0); PG8_MMA(0, 1, At, B1); PG8_BAR; PG8_SCHED;
;             PG8_LDA(At, 1, 1); PG8_STAGE(PG8_SB(1, 0), b3, voffB[0]); PG8_STAGE(PG8_SB(1, 1), b3, voffB[1]); PG8_STAGE(PG8_SA(1, 0), a3, vA2[0]);
;             PG8_WAIT_V(8); PG8_WAIT_L(0); PG8_BAR; PG8_MMA(1, 0, At, B0); PG8_MMA(1, 1, At, B1); PG8_BAR; PG8_SCHED;
.Lpk0_911:
	ds_read_b128 v[18:21], v191
	ds_read_b128 v[22:25], v191 offset:1024
	ds_read_b128 v[26:29], v191 offset:2048
	ds_read_b128 v[30:33], v191 offset:3072
	ds_read_b128 v[2:5], v192
	ds_read_b128 v[6:9], v192 offset:1024
	ds_read_b128 v[10:13], v192 offset:2048
	ds_read_b128 v[14:17], v192 offset:3072
	s_add_u32 s30, s28, 0x8000
	s_addc_u32 s31, s29, 0
	s_cmp_eq_u32 s65, 12
	s_cselect_b32 s42, s22, s30
	s_cselect_b32 s43, s23, s31
	s_cselect_b32 s40, s24, s19
	s_cselect_b32 s41, s25, s21
	s_add_u32 s30, s42, 0x8000
	s_addc_u32 s31, s43, 0
	s_add_i32 m0, s27, 0xc000
	ds_read_b128 v[196:199], v193
	ds_read_b128 v[200:203], v193 offset:1024
	ds_read_b128 v[204:207], v193 offset:2048
	ds_read_b128 v[208:211], v193 offset:3072
	ds_read_b128 v[212:215], v193 offset:4096
	ds_read_b128 v[216:219], v193 offset:5120
	ds_read_b128 v[220:223], v193 offset:6144
	ds_read_b128 v[224:227], v193 offset:7168
	global_load_lds_dwordx4 v182, s[28:29]
	s_add_i32 m0, s27, 0xe000
	s_nop 0
	global_load_lds_dwordx4 v180, s[28:29]
	s_waitcnt vmcnt(8)
	s_waitcnt lgkmcnt(0)
	s_setprio 1
	v_mfma_f32_16x16x128_f8f6f4 v[158:161], v[18:25], v[196:203], 0
	v_mfma_f32_16x16x128_f8f6f4 v[154:157], v[26:33], v[196:203], 0
	v_mfma_f32_16x16x128_f8f6f4 v[150:153], v[18:25], v[204:211], 0
	v_mfma_f32_16x16x128_f8f6f4 v[146:149], v[26:33], v[204:211], 0
	v_mfma_f32_16x16x128_f8f6f4 v[130:133], v[18:25], v[212:219], 0
	v_mfma_f32_16x16x128_f8f6f4 v[122:125], v[26:33], v[212:219], 0
	v_mfma_f32_16x16x128_f8f6f4 v[114:117], v[18:25], v[220:227], 0
	v_mfma_f32_16x16x128_f8f6f4 v[106:109], v[26:33], v[220:227], 0
	s_setprio 0
	s_setprio 1
	v_mfma_f32_16x16x128_f8f6f4 v[142:145], v[2:9], v[196:203], 0
	v_mfma_f32_16x16x128_f8f6f4 v[138:141], v[10:17], v[196:203], 0
	v_mfma_f32_16x16x128_f8f6f4 v[134:137], v[2:9], v[204:211], 0
	v_mfma_f32_16x16x128_f8f6f4 v[126:129], v[10:17], v[204:211], 0
	v_mfma_f32_16x16x128_f8f6f4 v[118:121], v[2:9], v[212:219], 0
	v_mfma_f32_16x16x128_f8f6f4 v[110:113], v[10:17], v[212:219], 0
	v_mfma_f32_16x16x128_f8f6f4 v[102:105], v[2:9], v[220:227], 0
	v_mfma_f32_16x16x128_f8f6f4 v[98:101], v[10:17], v[220:227], 0
	s_setprio 0
	s_barrier
	s_add_i32 s66, s60, s48
	s_mov_b32 m0, s66
	ds_read_b128 v[196:199], v193 offset:16384
	ds_read_b128 v[200:203], v193 offset:17408
	ds_read_b128 v[204:207], v193 offset:18432
	ds_read_b128 v[208:211], v193 offset:19456
	ds_read_b128 v[212:215], v193 offset:20480
	ds_read_b128 v[216:219], v193 offset:21504
	ds_read_b128 v[220:223], v193 offset:22528
	ds_read_b128 v[224:227], v193 offset:23552
	global_load_lds_dwordx4 v162, s[40:41]
	s_add_i32 m0, s66, 0x2000
	s_add_i32 s66, s61, s48
	global_load_lds_dwordx4 v164, s[40:41]
	s_add_u32 s98, s40, s6
	s_addc_u32 s99, s41, s7
	s_mov_b32 m0, s66
	s_nop 0
	global_load_lds_dwordx4 v162, s[98:99]
	s_add_u32 s100, s40, s6
	s_addc_u32 s101, s41, s7
	s_add_i32 m0, s66, 0x2000
	s_nop 0
	global_load_lds_dwordx4 v164, s[100:101]
	s_mov_b32 m0, s27
	s_nop 0
	global_load_lds_dwordx4 v166, s[42:43]
	s_mov_b32 m0, s49
	s_nop 0
	global_load_lds_dwordx4 v168, s[42:43]
	s_waitcnt vmcnt(8)
	s_waitcnt lgkmcnt(0)
	s_setprio 1
	v_mfma_f32_16x16x128_f8f6f4 v[94:97], v[18:25], v[196:203], 0
	v_mfma_f32_16x16x128_f8f6f4 v[90:93], v[26:33], v[196:203], 0
	v_mfma_f32_16x16x128_f8f6f4 v[82:85], v[18:25], v[204:211], 0
	v_mfma_f32_16x16x128_f8f6f4 v[74:77], v[26:33], v[204:211], 0
	v_mfma_f32_16x16x128_f8f6f4 v[66:69], v[18:25], v[212:219], 0
	v_mfma_f32_16x16x128_f8f6f4 v[58:61], v[26:33], v[212:219], 0
	v_mfma_f32_16x16x128_f8f6f4 v[50:53], v[18:25], v[220:227], 0
	v_mfma_f32_16x16x128_f8f6f4 v[42:45], v[26:33], v[220:227], 0
	s_setprio 0
	s_setprio 1
	v_mfma_f32_16x16x128_f8f6f4 v[86:89], v[2:9], v[196:203], 0
	v_mfma_f32_16x16x128_f8f6f4 v[78:81], v[10:17], v[196:203], 0
	v_mfma_f32_16x16x128_f8f6f4 v[70:73], v[2:9], v[204:211], 0
	v_mfma_f32_16x16x128_f8f6f4 v[62:65], v[10:17], v[204:211], 0
	v_mfma_f32_16x16x128_f8f6f4 v[54:57], v[2:9], v[212:219], 0
	v_mfma_f32_16x16x128_f8f6f4 v[46:49], v[10:17], v[212:219], 0
	v_mfma_f32_16x16x128_f8f6f4 v[38:41], v[2:9], v[220:227], 0
	v_mfma_f32_16x16x128_f8f6f4 v[34:37], v[10:17], v[220:227], 0
	s_setprio 0
	s_barrier
	s_add_i32 s66, 0, 0x18000
	s_add_i32 s67, 0, 0x1c000
	v_add_u32_e32 v14, s66, v189
	v_add_u32_e32 v30, s67, v189
	ds_read_b128 v[2:5], v14
	ds_read_b128 v[6:9], v14 offset:1024
	ds_read_b128 v[10:13], v14 offset:2048
	ds_read_b128 v[14:17], v14 offset:3072
	ds_read_b128 v[18:21], v30
	ds_read_b128 v[22:25], v30 offset:1024
	ds_read_b128 v[26:29], v30 offset:2048
	ds_read_b128 v[30:33], v30 offset:3072
	s_mov_b32 m0, s50
	ds_read_b128 v[196:199], v193 offset:32768
	ds_read_b128 v[200:203], v193 offset:33792
	ds_read_b128 v[204:207], v193 offset:34816
	ds_read_b128 v[208:211], v193 offset:35840
	ds_read_b128 v[212:215], v193 offset:36864
	ds_read_b128 v[216:219], v193 offset:37888
	ds_read_b128 v[220:223], v193 offset:38912
	ds_read_b128 v[224:227], v193 offset:39936
	global_load_lds_dwordx4 v172, s[42:43]
	s_mov_b32 m0, s51
	s_nop 0
	global_load_lds_dwordx4 v174, s[42:43]
	s_waitcnt vmcnt(8)
	s_waitcnt lgkmcnt(0)
	s_setprio 1
	v_mfma_f32_16x16x128_f8f6f4 v[158:161], v[2:9], v[196:203], v[158:161]
	v_mfma_f32_16x16x128_f8f6f4 v[154:157], v[10:17], v[196:203], v[154:157]
	v_mfma_f32_16x16x128_f8f6f4 v[150:153], v[2:9], v[204:211], v[150:153]
	v_mfma_f32_16x16x128_f8f6f4 v[146:149], v[10:17], v[204:211], v[146:149]
	v_mfma_f32_16x16x128_f8f6f4 v[130:133], v[2:9], v[212:219], v[130:133]
	v_mfma_f32_16x16x128_f8f6f4 v[122:125], v[10:17], v[212:219], v[122:125]
	v_mfma_f32_16x16x128_f8f6f4 v[114:117], v[2:9], v[220:227], v[114:117]
	v_mfma_f32_16x16x128_f8f6f4 v[106:109], v[10:17], v[220:227], v[106:109]
	s_setprio 0
	s_setprio 1
	v_mfma_f32_16x16x128_f8f6f4 v[142:145], v[18:25], v[196:203], v[142:145]
	v_mfma_f32_16x16x128_f8f6f4 v[138:141], v[26:33], v[196:203], v[138:141]
	v_mfma_f32_16x16x128_f8f6f4 v[134:137], v[18:25], v[204:211], v[134:137]
	v_mfma_f32_16x16x128_f8f6f4 v[126:129], v[26:33], v[204:211], v[126:129]
	v_mfma_f32_16x16x128_f8f6f4 v[118:121], v[18:25], v[212:219], v[118:121]
	v_mfma_f32_16x16x128_f8f6f4 v[110:113], v[26:33], v[212:219], v[110:113]
	v_mfma_f32_16x16x128_f8f6f4 v[102:105], v[18:25], v[220:227], v[102:105]
	v_mfma_f32_16x16x128_f8f6f4 v[98:101], v[26:33], v[220:227], v[98:101]
	s_setprio 0
	s_barrier
; #define PG8_STAGE(bufoff, gbase, voff) do { _Pragma("unroll") for (int _i = 0; _i < 2; ++_i) \
;         __builtin_amdgcn_global_load_lds((const unsigned*)((const char*)(gbase) + (voff)[_i]), (PG8_LAS unsigned*)(lds + (bufoff) + ldsw + _i * 8192), 16, 0, 0); } while (0)
; #define PG8_WAIT_V(n) asm volatile("s_waitcnt vmcnt(" #n ")" ::: "memory")
; #define PG8_WAIT_L(n) asm volatile("s_waitcnt lgkmcnt(" #n ")" ::: "memory")
; #define PG8_BAR __builtin_amdgcn_s_barrier()
; #define PG8_SCHED __builtin_amdgcn_sched_barrier(0)
; template <class Epi, class Sched, bool ALIGN_EPI = true, bool F8 = false>
; __device__ __forceinline__ void gemm_phase(PG8_LAS unsigned char* lds, const Sched& S, const Epi& E) {
;     ...
;             PG8_LDB(B0, 0, 0); PG8_LDB(B1, 0, 1); PG8_SCHED; PG8_LDA(At, 0, 0); PG8_STAGE(PG8_SA(1, 1), a1, voffA[1]);
;             PG8_WAIT_V(8); PG8_WAIT_L(0); PG8_BAR; PG8_MMA(0, 0, At, B0); PG8_MMA(0, 1, At, B1); PG8_BAR; PG8_SCHED;
;             PG8_LDA(At, 0, 1); PG8_STAGE(PG8_SB(0, 0), b2, voffB[0]); PG8_STAGE(PG8_SB(0, 1), b2, voffB[1]); PG8_STAGE(PG8_SA(0, 0), a2, vA2[0]);
;             PG8_WAIT_V(8); PG8_WAIT_L(0); PG8_BAR; PG8_MMA(1, 0, At, B0); PG8_MMA(1, 1, At, B1); PG8_BAR; PG8_SCHED;
;             PG8_LDB(B0, 1, 0); PG8_LDB(B1, 1, 1); PG8_SCHED; PG8_LDA(At, 1, 0); PG8_STAGE(PG8_SA(0, 1), a2, vA2[1]);
;             PG8_WAIT_V(8); PG8_WAIT_L(0); PG8_BAR; PG8_MMA(0, 0, At, B0); PG8_MMA(0, 1, At, B1); PG8_BAR; PG8_SCHED;
;             PG8_LDA(At, 1, 1); PG8_STAGE(PG8_SB(1, 0), b3, voffB[0]); PG8_STAGE(PG8_SB(1, 1), b3, voffB[1]); PG8_STAGE(PG8_SA(1, 0), a3, vA2[0]);
;             PG8_WAIT_V(8); PG8_WAIT_L(0); PG8_BAR; PG8_MMA(1, 0, At, B0); PG8_MMA(1, 1, At, B1); PG8_BAR; PG8_SCHED;
	s_add_u32 s40, s40, 0x8000
	s_addc_u32 s41, s41, 0
	s_add_i32 s42, s66, s48
	s_mov_b32 m0, s42
	ds_read_b128 v[196:199], v193 offset:49152
	ds_read_b128 v[200:203], v193 offset:50176
	ds_read_b128 v[204:207], v193 offset:51200
	ds_read_b128 v[208:211], v193 offset:52224
	ds_read_b128 v[212:215], v193 offset:53248
	ds_read_b128 v[216:219], v193 offset:54272
	ds_read_b128 v[220:223], v193 offset:55296
	ds_read_b128 v[224:227], v193 offset:56320
	global_load_lds_dwordx4 v162, s[40:41]
	s_add_i32 m0, s42, 0x2000
	s_add_i32 s42, s67, s48
	global_load_lds_dwordx4 v164, s[40:41]
	s_mov_b32 m0, s42
	s_nop 0
	global_load_lds_dwordx4 v176, s[40:41]
	s_add_i32 m0, s42, 0x2000
	s_nop 0
	global_load_lds_dwordx4 v178, s[40:41]
	s_mov_b32 m0, s53
	s_nop 0
	global_load_lds_dwordx4 v166, s[30:31]
	s_mov_b32 m0, s58
	s_nop 0
	global_load_lds_dwordx4 v168, s[30:31]
	s_waitcnt vmcnt(8)
	s_waitcnt lgkmcnt(0)
	s_setprio 1
	v_mfma_f32_16x16x128_f8f6f4 v[94:97], v[2:9], v[196:203], v[94:97]
	v_mfma_f32_16x16x128_f8f6f4 v[90:93], v[10:17], v[196:203], v[90:93]
	v_mfma_f32_16x16x128_f8f6f4 v[82:85], v[2:9], v[204:211], v[82:85]
	v_mfma_f32_16x16x128_f8f6f4 v[74:77], v[10:17], v[204:211], v[74:77]
	v_mfma_f32_16x16x128_f8f6f4 v[66:69], v[2:9], v[212:219], v[66:69]
	v_mfma_f32_16x16x128_f8f6f4 v[58:61], v[10:17], v[212:219], v[58:61]
	v_mfma_f32_16x16x128_f8f6f4 v[50:53], v[2:9], v[220:227], v[50:53]
	v_mfma_f32_16x16x128_f8f6f4 v[42:45], v[10:17], v[220:227], v[42:45]
	s_setprio 0
	s_setprio 1
	v_mfma_f32_16x16x128_f8f6f4 v[86:89], v[18:25], v[196:203], v[86:89]
	v_mfma_f32_16x16x128_f8f6f4 v[78:81], v[26:33], v[196:203], v[78:81]
	v_mfma_f32_16x16x128_f8f6f4 v[70:73], v[18:25], v[204:211], v[70:73]
	v_mfma_f32_16x16x128_f8f6f4 v[62:65], v[26:33], v[204:211], v[62:65]
	v_mfma_f32_16x16x128_f8f6f4 v[54:57], v[18:25], v[212:219], v[54:57]
	v_mfma_f32_16x16x128_f8f6f4 v[46:49], v[26:33], v[212:219], v[46:49]
	v_mfma_f32_16x16x128_f8f6f4 v[38:41], v[18:25], v[220:227], v[38:41]
	v_mfma_f32_16x16x128_f8f6f4 v[34:37], v[26:33], v[220:227], v[34:37]
	s_setprio 0
	s_barrier
	s_add_i32 s65, s65, 2
	s_add_u32 s19, s19, 0x10000
	s_addc_u32 s21, s21, 0
	s_add_u32 s28, s28, 0x10000
	s_addc_u32 s29, s29, 0
	s_cmp_gt_u32 s65, 13
	s_cbranch_scc0 .LBB0_911
	s_branch .Lfx_26630
.LBB0_911:
	ds_read_b128 v[18:21], v191
	ds_read_b128 v[22:25], v191 offset:1024
	ds_read_b128 v[26:29], v191 offset:2048
	ds_read_b128 v[30:33], v191 offset:3072
	ds_read_b128 v[2:5], v192
	ds_read_b128 v[6:9], v192 offset:1024
	ds_read_b128 v[10:13], v192 offset:2048
	ds_read_b128 v[14:17], v192 offset:3072
	s_add_u32 s30, s28, 0x8000
	s_addc_u32 s31, s29, 0
	s_cmp_eq_u32 s65, 12
	s_cselect_b32 s42, s22, s30
	s_cselect_b32 s43, s23, s31
	s_cselect_b32 s40, s24, s19
	s_cselect_b32 s41, s25, s21
	s_add_u32 s30, s42, 0x8000
	s_addc_u32 s31, s43, 0
	s_add_i32 m0, s27, 0xc000
	ds_read_b128 v[196:199], v193
	ds_read_b128 v[200:203], v193 offset:1024
	ds_read_b128 v[204:207], v193 offset:2048
	ds_read_b128 v[208:211], v193 offset:3072
	ds_read_b128 v[212:215], v193 offset:4096
	ds_read_b128 v[216:219], v193 offset:5120
	ds_read_b128 v[220:223], v193 offset:6144
	ds_read_b128 v[224:227], v193 offset:7168
	global_load_lds_dwordx4 v182, s[28:29]
	s_add_i32 m0, s27, 0xe000
	s_nop 0
	global_load_lds_dwordx4 v180, s[28:29]
	s_waitcnt vmcnt(8)
	s_waitcnt lgkmcnt(0)
	s_setprio 1
	v_mfma_f32_16x16x128_f8f6f4 v[158:161], v[18:25], v[196:203], v[158:161]
	v_mfma_f32_16x16x128_f8f6f4 v[154:157], v[26:33], v[196:203], v[154:157]
	v_mfma_f32_16x16x128_f8f6f4 v[150:153], v[18:25], v[204:211], v[150:153]
	v_mfma_f32_16x16x128_f8f6f4 v[146:149], v[26:33], v[204:211], v[146:149]
	v_mfma_f32_16x16x128_f8f6f4 v[130:133], v[18:25], v[212:219], v[130:133]
	v_mfma_f32_16x16x128_f8f6f4 v[122:125], v[26:33], v[212:219], v[122:125]
	v_mfma_f32_16x16x128_f8f6f4 v[114:117], v[18:25], v[220:227], v[114:117]
	v_mfma_f32_16x16x128_f8f6f4 v[106:109], v[26:33], v[220:227], v[106:109]
	s_setprio 0
	s_setprio 1
	v_mfma_f32_16x16x128_f8f6f4 v[142:145], v[2:9], v[196:203], v[142:145]
	v_mfma_f32_16x16x128_f8f6f4 v[138:141], v[10:17], v[196:203], v[138:141]
	v_mfma_f32_16x16x128_f8f6f4 v[134:137], v[2:9], v[204:211], v[134:137]
	v_mfma_f32_16x16x128_f8f6f4 v[126:129], v[10:17], v[204:211], v[126:129]
	v_mfma_f32_16x16x128_f8f6f4 v[118:121], v[2:9], v[212:219], v[118:121]
	v_mfma_f32_16x16x128_f8f6f4 v[110:113], v[10:17], v[212:219], v[110:113]
	v_mfma_f32_16x16x128_f8f6f4 v[102:105], v[2:9], v[220:227], v[102:105]
	v_mfma_f32_16x16x128_f8f6f4 v[98:101], v[10:17], v[220:227], v[98:101]
	s_setprio 0
	s_barrier
; #define PG8_STAGE(bufoff, gbase, voff) do { _Pragma("unroll") for (int _i = 0; _i < 2; ++_i) \
;         __builtin_amdgcn_global_load_lds((const unsigned*)((const char*)(gbase) + (voff)[_i]), (PG8_LAS unsigned*)(lds + (bufoff) + ldsw + _i * 8192), 16, 0, 0); } while (0)
; #define PG8_WAIT_V(n) asm volatile("s_waitcnt vmcnt(" #n ")" ::: "memory")
; #define PG8_WAIT_L(n) asm volatile("s_waitcnt lgkmcnt(" #n ")" ::: "memory")
; #define PG8_BAR __builtin_amdgcn_s_barrier()
; #define PG8_SCHED __builtin_amdgcn_sched_barrier(0)
; template <class Epi, class Sched, bool ALIGN_EPI = true, bool F8 = false>
; __device__ __forceinline__ void gemm_phase(PG8_LAS unsigned char* lds, const Sched& S, const Epi& E) {
;     ...
;             PG8_LDB(B0, 0, 0); PG8_LDB(B1, 0, 1); PG8_SCHED; PG8_LDA(At, 0, 0); PG8_STAGE(PG8_SA(1, 1), a1, voffA[1]);
;             PG8_WAIT_V(8); PG8_WAIT_L(0); PG8_BAR; PG8_MMA(0, 0, At, B0); PG8_MMA(0, 1, At, B1); PG8_BAR; PG8_SCHED;
;             PG8_LDA(At, 0, 1); PG8_STAGE(PG8_SB(0, 0), b2, voffB[0]); PG8_STAGE(PG8_SB(0, 1), b2, voffB[1]); PG8_STAGE(PG8_SA(0, 0), a2, vA2[0]);
;             PG8_WAIT_V(8); PG8_WAIT_L(0); PG8_BAR; PG8_MMA(1, 0, At, B0); PG8_MMA(1, 1, At, B1); PG8_BAR; PG8_SCHED;
;             PG8_LDB(B0, 1, 0); PG8_LDB(B1, 1, 1); PG8_SCHED; PG8_LDA(At, 1, 0); PG8_STAGE(PG8_SA(0, 1), a2, vA2[1]);
;             PG8_WAIT_V(8); PG8_WAIT_L(0); PG8_BAR; PG8_MMA(0, 0, At, B0); PG8_MMA(0, 1, At, B1); PG8_BAR; PG8_SCHED;
;             PG8_LDA(At, 1, 1); PG8_STAGE(PG8_SB(1, 0), b3, voffB[0]); PG8_STAGE(PG8_SB(1, 1), b3, voffB[1]); PG8_STAGE(PG8_SA(1, 0), a3, vA2[0]);
;             PG8_WAIT_V(8); PG8_WAIT_L(0); PG8_BAR; PG8_MMA(1, 0, At, B0); PG8_MMA(1, 1, At, B1); PG8_BAR; PG8_SCHED;
	s_add_i32 s66, s60, s48
	s_mov_b32 m0, s66
	ds_read_b128 v[196:199], v193 offset:16384
	ds_read_b128 v[200:203], v193 offset:17408
	ds_read_b128 v[204:207], v193 offset:18432
	ds_read_b128 v[208:211], v193 offset:19456
	ds_read_b128 v[212:215], v193 offset:20480
	ds_read_b128 v[216:219], v193 offset:21504
	ds_read_b128 v[220:223], v193 offset:22528
	ds_read_b128 v[224:227], v193 offset:23552
	global_load_lds_dwordx4 v162, s[40:41]
	s_add_i32 m0, s66, 0x2000
	s_add_i32 s66, s61, s48
	global_load_lds_dwordx4 v164, s[40:41]
	s_add_u32 s98, s40, s6
	s_addc_u32 s99, s41, s7
	s_mov_b32 m0, s66
	s_nop 0
	global_load_lds_dwordx4 v162, s[98:99]
	s_add_u32 s100, s40, s6
	s_addc_u32 s101, s41, s7
	s_add_i32 m0, s66, 0x2000
	s_nop 0
	global_load_lds_dwordx4 v164, s[100:101]
	s_mov_b32 m0, s27
	s_nop 0
	global_load_lds_dwordx4 v166, s[42:43]
	s_mov_b32 m0, s49
	s_nop 0
	global_load_lds_dwordx4 v168, s[42:43]
	s_waitcnt vmcnt(8)
	s_waitcnt lgkmcnt(0)
	s_setprio 1
	v_mfma_f32_16x16x128_f8f6f4 v[94:97], v[18:25], v[196:203], v[94:97]
	v_mfma_f32_16x16x128_f8f6f4 v[90:93], v[26:33], v[196:203], v[90:93]
	v_mfma_f32_16x16x128_f8f6f4 v[82:85], v[18:25], v[204:211], v[82:85]
	v_mfma_f32_16x16x128_f8f6f4 v[74:77], v[26:33], v[204:211], v[74:77]
	v_mfma_f32_16x16x128_f8f6f4 v[66:69], v[18:25], v[212:219], v[66:69]
	v_mfma_f32_16x16x128_f8f6f4 v[58:61], v[26:33], v[212:219], v[58:61]
	v_mfma_f32_16x16x128_f8f6f4 v[50:53], v[18:25], v[220:227], v[50:53]
	v_mfma_f32_16x16x128_f8f6f4 v[42:45], v[26:33], v[220:227], v[42:45]
	s_setprio 0
	s_setprio 1
	v_mfma_f32_16x16x128_f8f6f4 v[86:89], v[2:9], v[196:203], v[86:89]
	v_mfma_f32_16x16x128_f8f6f4 v[78:81], v[10:17], v[196:203], v[78:81]
	v_mfma_f32_16x16x128_f8f6f4 v[70:73], v[2:9], v[204:211], v[70:73]
	v_mfma_f32_16x16x128_f8f6f4 v[62:65], v[10:17], v[204:211], v[62:65]
	v_mfma_f32_16x16x128_f8f6f4 v[54:57], v[2:9], v[212:219], v[54:57]
	v_mfma_f32_16x16x128_f8f6f4 v[46:49], v[10:17], v[212:219], v[46:49]
	v_mfma_f32_16x16x128_f8f6f4 v[38:41], v[2:9], v[220:227], v[38:41]
	v_mfma_f32_16x16x128_f8f6f4 v[34:37], v[10:17], v[220:227], v[34:37]
	s_setprio 0
	s_barrier
	s_add_i32 s66, 0, 0x18000
	s_add_i32 s67, 0, 0x1c000
	v_add_u32_e32 v14, s66, v189
	v_add_u32_e32 v30, s67, v189
	ds_read_b128 v[2:5], v14
	ds_read_b128 v[6:9], v14 offset:1024
	ds_read_b128 v[10:13], v14 offset:2048
	ds_read_b128 v[14:17], v14 offset:3072
	ds_read_b128 v[18:21], v30
	ds_read_b128 v[22:25], v30 offset:1024
	ds_read_b128 v[26:29], v30 offset:2048
	ds_read_b128 v[30:33], v30 offset:3072
	s_mov_b32 m0, s50
	ds_read_b128 v[196:199], v193 offset:32768
	ds_read_b128 v[200:203], v193 offset:33792
	ds_read_b128 v[204:207], v193 offset:34816
	ds_read_b128 v[208:211], v193 offset:35840
	ds_read_b128 v[212:215], v193 offset:36864
	ds_read_b128 v[216:219], v193 offset:37888
	ds_read_b128 v[220:223], v193 offset:38912
	ds_read_b128 v[224:227], v193 offset:39936
	global_load_lds_dwordx4 v172, s[42:43]
	s_mov_b32 m0, s51
	s_nop 0
	global_load_lds_dwordx4 v174, s[42:43]
	s_waitcnt vmcnt(8)
	s_waitcnt lgkmcnt(0)
	s_setprio 1
	v_mfma_f32_16x16x128_f8f6f4 v[158:161], v[2:9], v[196:203], v[158:161]
	v_mfma_f32_16x16x128_f8f6f4 v[154:157], v[10:17], v[196:203], v[154:157]
	v_mfma_f32_16x16x128_f8f6f4 v[150:153], v[2:9], v[204:211], v[150:153]
	v_mfma_f32_16x16x128_f8f6f4 v[146:149], v[10:17], v[204:211], v[146:149]
	v_mfma_f32_16x16x128_f8f6f4 v[130:133], v[2:9], v[212:219], v[130:133]
	v_mfma_f32_16x16x128_f8f6f4 v[122:125], v[10:17], v[212:219], v[122:125]
	v_mfma_f32_16x16x128_f8f6f4 v[114:117], v[2:9], v[220:227], v[114:117]
	v_mfma_f32_16x16x128_f8f6f4 v[106:109], v[10:17], v[220:227], v[106:109]
	s_setprio 0
	s_setprio 1
	v_mfma_f32_16x16x128_f8f6f4 v[142:145], v[18:25], v[196:203], v[142:145]
	v_mfma_f32_16x16x128_f8f6f4 v[138:141], v[26:33], v[196:203], v[138:141]
	v_mfma_f32_16x16x128_f8f6f4 v[134:137], v[18:25], v[204:211], v[134:137]
	v_mfma_f32_16x16x128_f8f6f4 v[126:129], v[26:33], v[204:211], v[126:129]
	v_mfma_f32_16x16x128_f8f6f4 v[118:121], v[18:25], v[212:219], v[118:121]
	v_mfma_f32_16x16x128_f8f6f4 v[110:113], v[26:33], v[212:219], v[110:113]
	v_mfma_f32_16x16x128_f8f6f4 v[102:105], v[18:25], v[220:227], v[102:105]
	v_mfma_f32_16x16x128_f8f6f4 v[98:101], v[26:33], v[220:227], v[98:101]
	s_setprio 0
	s_barrier
	s_add_u32 s40, s40, 0x8000
	s_addc_u32 s41, s41, 0
	s_add_i32 s42, s66, s48
	s_mov_b32 m0, s42
	ds_read_b128 v[196:199], v193 offset:49152
	ds_read_b128 v[200:203], v193 offset:50176
	ds_read_b128 v[204:207], v193 offset:51200
	ds_read_b128 v[208:211], v193 offset:52224
	ds_read_b128 v[212:215], v193 offset:53248
	ds_read_b128 v[216:219], v193 offset:54272
	ds_read_b128 v[220:223], v193 offset:55296
	ds_read_b128 v[224:227], v193 offset:56320
	global_load_lds_dwordx4 v162, s[40:41]
	s_add_i32 m0, s42, 0x2000
	s_add_i32 s42, s67, s48
	global_load_lds_dwordx4 v164, s[40:41]
	s_mov_b32 m0, s42
	s_nop 0
	global_load_lds_dwordx4 v176, s[40:41]
	s_add_i32 m0, s42, 0x2000
	s_nop 0
	global_load_lds_dwordx4 v178, s[40:41]
	s_mov_b32 m0, s53
	s_nop 0
	global_load_lds_dwordx4 v166, s[30:31]
	s_mov_b32 m0, s58
	s_nop 0
	global_load_lds_dwordx4 v168, s[30:31]
	s_waitcnt vmcnt(8)
	s_waitcnt lgkmcnt(0)
	s_setprio 1
	v_mfma_f32_16x16x128_f8f6f4 v[94:97], v[2:9], v[196:203], v[94:97]
	v_mfma_f32_16x16x128_f8f6f4 v[90:93], v[10:17], v[196:203], v[90:93]
	v_mfma_f32_16x16x128_f8f6f4 v[82:85], v[2:9], v[204:211], v[82:85]
	v_mfma_f32_16x16x128_f8f6f4 v[74:77], v[10:17], v[204:211], v[74:77]
	v_mfma_f32_16x16x128_f8f6f4 v[66:69], v[2:9], v[212:219], v[66:69]
	v_mfma_f32_16x16x128_f8f6f4 v[58:61], v[10:17], v[212:219], v[58:61]
	v_mfma_f32_16x16x128_f8f6f4 v[50:53], v[2:9], v[220:227], v[50:53]
	v_mfma_f32_16x16x128_f8f6f4 v[42:45], v[10:17], v[220:227], v[42:45]
	s_setprio 0
	s_setprio 1
	v_mfma_f32_16x16x128_f8f6f4 v[86:89], v[18:25], v[196:203], v[86:89]
	v_mfma_f32_16x16x128_f8f6f4 v[78:81], v[26:33], v[196:203], v[78:81]
	v_mfma_f32_16x16x128_f8f6f4 v[70:73], v[18:25], v[204:211], v[70:73]
	v_mfma_f32_16x16x128_f8f6f4 v[62:65], v[26:33], v[204:211], v[62:65]
	v_mfma_f32_16x16x128_f8f6f4 v[54:57], v[18:25], v[212:219], v[54:57]
	v_mfma_f32_16x16x128_f8f6f4 v[46:49], v[26:33], v[212:219], v[46:49]
	v_mfma_f32_16x16x128_f8f6f4 v[38:41], v[18:25], v[220:227], v[38:41]
	v_mfma_f32_16x16x128_f8f6f4 v[34:37], v[26:33], v[220:227], v[34:37]
	s_setprio 0
	s_barrier
	s_add_i32 s65, s65, 2
	s_add_u32 s19, s19, 0x10000
	s_addc_u32 s21, s21, 0
	s_add_u32 s28, s28, 0x10000
	s_addc_u32 s29, s29, 0
	s_cmp_gt_u32 s65, 13
	s_cbranch_scc0 .LBB0_911
	s_branch .Lfx_26630
; #define PG8_STAGE(bufoff, gbase, voff) do { _Pragma("unroll") for (int _i = 0; _i < 2; ++_i) \
;         __builtin_amdgcn_global_load_lds((const unsigned*)((const char*)(gbase) + (voff)[_i]), (PG8_LAS unsigned*)(lds + (bufoff) + ldsw + _i * 8192), 16, 0, 0); } while (0)
; #define PG8_WAIT_V(n) asm volatile("s_waitcnt vmcnt(" #n ")" ::: "memory")
; #define PG8_WAIT_L(n) asm volatile("s_waitcnt lgkmcnt(" #n ")" ::: "memory")
; #define PG8_BAR __builtin_amdgcn_s_barrier()
; #define PG8_SCHED __builtin_amdgcn_sched_barrier(0)
; template <class Epi, class Sched, bool ALIGN_EPI = true, bool F8 = false>
; __device__ __forceinline__ void gemm_phase(PG8_LAS unsigned char* lds, const Sched& S, const Epi& E) {
;     ...
;     f32x4 acc[2][2][4][2];
; #pragma unroll
;     for (int a = 0; a < 2; ++a)
; #pragma unroll
;         for (int b = 0; b < 2; ++b)
; #pragma unroll
;             for (int m = 0; m < 4; ++m)
; #pragma unroll
;                 for (int n = 0; n < 2; ++n) acc[a][b][m][n] = (f32x4){0.f, 0.f, 0.f, 0.f};
;     ...
;             PG8_LDB(B0, 0, 0); PG8_LDB(B1, 0, 1); PG8_SCHED; PG8_LDA(At, 0, 0); PG8_STAGE(PG8_SA(1, 1), a1, voffA[1]);
;             PG8_WAIT_V(8); PG8_WAIT_L(0); PG8_BAR; PG8_MMA(0, 0, At, B0); PG8_MMA(0, 1, At, B1); PG8_BAR; PG8_SCHED;
;             PG8_LDA(At, 0, 1); PG8_STAGE(PG8_SB(0, 0), b2, voffB[0]); PG8_STAGE(PG8_SB(0, 1), b2, voffB[1]); PG8_STAGE(PG8_SA(0, 0), a2, vA2[0]);
;             PG8_WAIT_V(8); PG8_WAIT_L(0); PG8_BAR; PG8_MMA(1, 0, At, B0); PG8_MMA(1, 1, At, B1); PG8_BAR; PG8_SCHED;
;             PG8_LDB(B0, 1, 0); PG8_LDB(B1, 1, 1); PG8_SCHED; PG8_LDA(At, 1, 0); PG8_STAGE(PG8_SA(0, 1), a2, vA2[1]);
;             PG8_WAIT_V(8); PG8_WAIT_L(0); PG8_BAR; PG8_MMA(0, 0, At, B0); PG8_MMA(0, 1, At, B1); PG8_BAR; PG8_SCHED;
;             PG8_LDA(At, 1, 1); PG8_STAGE(PG8_SB(1, 0), b3, voffB[0]); PG8_STAGE(PG8_SB(1, 1), b3, voffB[1]); PG8_STAGE(PG8_SA(1, 0), a3, vA2[0]);
;             PG8_WAIT_V(8); PG8_WAIT_L(0); PG8_BAR; PG8_MMA(1, 0, At, B0); PG8_MMA(1, 1, At, B1); PG8_BAR; PG8_SCHED;
.Lh1e_26630:
.Lpk1_911:
	ds_read_b128 v[18:21], v191
	ds_read_b128 v[22:25], v191 offset:1024
	ds_read_b128 v[26:29], v191 offset:2048
	ds_read_b128 v[30:33], v191 offset:3072
	ds_read_b128 v[2:5], v192
	ds_read_b128 v[6:9], v192 offset:1024
	ds_read_b128 v[10:13], v192 offset:2048
	ds_read_b128 v[14:17], v192 offset:3072
	s_add_u32 s30, s28, 0x8000
	s_addc_u32 s31, s29, 0
	s_cmp_eq_u32 s65, 12
	s_cselect_b32 s42, s22, s30
	s_cselect_b32 s43, s23, s31
	s_cselect_b32 s40, s24, s19
	s_cselect_b32 s41, s25, s21
	s_add_u32 s30, s42, 0x8000
	s_addc_u32 s31, s43, 0
	s_add_i32 m0, s27, 0xc000
	ds_read_b128 v[196:199], v193
	ds_read_b128 v[200:203], v193 offset:1024
	ds_read_b128 v[204:207], v193 offset:2048
	ds_read_b128 v[208:211], v193 offset:3072
	ds_read_b128 v[212:215], v193 offset:4096
	ds_read_b128 v[216:219], v193 offset:5120
	ds_read_b128 v[220:223], v193 offset:6144
	ds_read_b128 v[224:227], v193 offset:7168
	global_load_lds_dwordx4 v182, s[28:29]
	s_add_i32 m0, s27, 0xe000
	s_nop 0
	global_load_lds_dwordx4 v180, s[28:29]
	s_waitcnt vmcnt(8)
	s_waitcnt lgkmcnt(0)
	s_barrier
	s_setprio 2
	v_mfma_f32_16x16x128_f8f6f4 v[158:161], v[18:25], v[196:203], 0
	v_mfma_f32_16x16x128_f8f6f4 v[154:157], v[26:33], v[196:203], 0
	v_mfma_f32_16x16x128_f8f6f4 v[150:153], v[18:25], v[204:211], 0
	v_mfma_f32_16x16x128_f8f6f4 v[146:149], v[26:33], v[204:211], 0
	v_mfma_f32_16x16x128_f8f6f4 v[130:133], v[18:25], v[212:219], 0
	v_mfma_f32_16x16x128_f8f6f4 v[122:125], v[26:33], v[212:219], 0
	v_mfma_f32_16x16x128_f8f6f4 v[114:117], v[18:25], v[220:227], 0
	v_mfma_f32_16x16x128_f8f6f4 v[106:109], v[26:33], v[220:227], 0
	s_setprio 0
	s_setprio 2
	v_mfma_f32_16x16x128_f8f6f4 v[142:145], v[2:9], v[196:203], 0
	v_mfma_f32_16x16x128_f8f6f4 v[138:141], v[10:17], v[196:203], 0
	v_mfma_f32_16x16x128_f8f6f4 v[134:137], v[2:9], v[204:211], 0
	v_mfma_f32_16x16x128_f8f6f4 v[126:129], v[10:17], v[204:211], 0
	v_mfma_f32_16x16x128_f8f6f4 v[118:121], v[2:9], v[212:219], 0
	v_mfma_f32_16x16x128_f8f6f4 v[110:113], v[10:17], v[212:219], 0
	v_mfma_f32_16x16x128_f8f6f4 v[102:105], v[2:9], v[220:227], 0
	v_mfma_f32_16x16x128_f8f6f4 v[98:101], v[10:17], v[220:227], 0
	s_setprio 0
	s_add_i32 s66, s60, s48
	s_mov_b32 m0, s66
	ds_read_b128 v[196:199], v193 offset:16384
	ds_read_b128 v[200:203], v193 offset:17408
	ds_read_b128 v[204:207], v193 offset:18432
	ds_read_b128 v[208:211], v193 offset:19456
	ds_read_b128 v[212:215], v193 offset:20480
	ds_read_b128 v[216:219], v193 offset:21504
	ds_read_b128 v[220:223], v193 offset:22528
	ds_read_b128 v[224:227], v193 offset:23552
	global_load_lds_dwordx4 v162, s[40:41]
	s_add_i32 m0, s66, 0x2000
	s_add_i32 s66, s61, s48
	global_load_lds_dwordx4 v164, s[40:41]
	s_add_u32 s98, s40, s6
	s_addc_u32 s99, s41, s7
	s_mov_b32 m0, s66
	s_nop 0
	global_load_lds_dwordx4 v162, s[98:99]
	s_add_u32 s100, s40, s6
	s_addc_u32 s101, s41, s7
	s_add_i32 m0, s66, 0x2000
	s_nop 0
	global_load_lds_dwordx4 v164, s[100:101]
	s_mov_b32 m0, s27
	s_nop 0
	global_load_lds_dwordx4 v166, s[42:43]
	s_mov_b32 m0, s49
	s_nop 0
	global_load_lds_dwordx4 v168, s[42:43]
	s_waitcnt vmcnt(8)
	s_waitcnt lgkmcnt(0)
	s_barrier
	s_setprio 2
	v_mfma_f32_16x16x128_f8f6f4 v[94:97], v[18:25], v[196:203], 0
	v_mfma_f32_16x16x128_f8f6f4 v[90:93], v[26:33], v[196:203], 0
	v_mfma_f32_16x16x128_f8f6f4 v[82:85], v[18:25], v[204:211], 0
	v_mfma_f32_16x16x128_f8f6f4 v[74:77], v[26:33], v[204:211], 0
	v_mfma_f32_16x16x128_f8f6f4 v[66:69], v[18:25], v[212:219], 0
	v_mfma_f32_16x16x128_f8f6f4 v[58:61], v[26:33], v[212:219], 0
	v_mfma_f32_16x16x128_f8f6f4 v[50:53], v[18:25], v[220:227], 0
	v_mfma_f32_16x16x128_f8f6f4 v[42:45], v[26:33], v[220:227], 0
	s_setprio 0
	s_setprio 2
	v_mfma_f32_16x16x128_f8f6f4 v[86:89], v[2:9], v[196:203], 0
	v_mfma_f32_16x16x128_f8f6f4 v[78:81], v[10:17], v[196:203], 0
	v_mfma_f32_16x16x128_f8f6f4 v[70:73], v[2:9], v[204:211], 0
	v_mfma_f32_16x16x128_f8f6f4 v[62:65], v[10:17], v[204:211], 0
	v_mfma_f32_16x16x128_f8f6f4 v[54:57], v[2:9], v[212:219], 0
	v_mfma_f32_16x16x128_f8f6f4 v[46:49], v[10:17], v[212:219], 0
	v_mfma_f32_16x16x128_f8f6f4 v[38:41], v[2:9], v[220:227], 0
	v_mfma_f32_16x16x128_f8f6f4 v[34:37], v[10:17], v[220:227], 0
	s_setprio 0
	s_add_i32 s66, 0, 0x18000
	s_add_i32 s67, 0, 0x1c000
	v_add_u32_e32 v14, s66, v189
	v_add_u32_e32 v30, s67, v189
	ds_read_b128 v[2:5], v14
	ds_read_b128 v[6:9], v14 offset:1024
	ds_read_b128 v[10:13], v14 offset:2048
	ds_read_b128 v[14:17], v14 offset:3072
	ds_read_b128 v[18:21], v30
	ds_read_b128 v[22:25], v30 offset:1024
	ds_read_b128 v[26:29], v30 offset:2048
	ds_read_b128 v[30:33], v30 offset:3072
	s_mov_b32 m0, s50
	ds_read_b128 v[196:199], v193 offset:32768
	ds_read_b128 v[200:203], v193 offset:33792
	ds_read_b128 v[204:207], v193 offset:34816
	ds_read_b128 v[208:211], v193 offset:35840
	ds_read_b128 v[212:215], v193 offset:36864
	ds_read_b128 v[216:219], v193 offset:37888
	ds_read_b128 v[220:223], v193 offset:38912
	ds_read_b128 v[224:227], v193 offset:39936
	global_load_lds_dwordx4 v172, s[42:43]
	s_mov_b32 m0, s51
	s_nop 0
	global_load_lds_dwordx4 v174, s[42:43]
	s_waitcnt vmcnt(8)
	s_waitcnt lgkmcnt(0)
	s_barrier
; #define PG8_STAGE(bufoff, gbase, voff) do { _Pragma("unroll") for (int _i = 0; _i < 2; ++_i) \
;         __builtin_amdgcn_global_load_lds((const unsigned*)((const char*)(gbase) + (voff)[_i]), (PG8_LAS unsigned*)(lds + (bufoff) + ldsw + _i * 8192), 16, 0, 0); } while (0)
; #define PG8_WAIT_V(n) asm volatile("s_waitcnt vmcnt(" #n ")" ::: "memory")
; #define PG8_WAIT_L(n) asm volatile("s_waitcnt lgkmcnt(" #n ")" ::: "memory")
; #define PG8_BAR __builtin_amdgcn_s_barrier()
; #define PG8_SCHED __builtin_amdgcn_sched_barrier(0)
; template <class Epi, class Sched, bool ALIGN_EPI = true, bool F8 = false>
; __device__ __forceinline__ void gemm_phase(PG8_LAS unsigned char* lds, const Sched& S, const Epi& E) {
;     ...
;             PG8_LDB(B0, 0, 0); PG8_LDB(B1, 0, 1); PG8_SCHED; PG8_LDA(At, 0, 0); PG8_STAGE(PG8_SA(1, 1), a1, voffA[1]);
;             PG8_WAIT_V(8); PG8_WAIT_L(0); PG8_BAR; PG8_MMA(0, 0, At, B0); PG8_MMA(0, 1, At, B1); PG8_BAR; PG8_SCHED;
;             PG8_LDA(At, 0, 1); PG8_STAGE(PG8_SB(0, 0), b2, voffB[0]); PG8_STAGE(PG8_SB(0, 1), b2, voffB[1]); PG8_STAGE(PG8_SA(0, 0), a2, vA2[0]);
;             PG8_WAIT_V(8); PG8_WAIT_L(0); PG8_BAR; PG8_MMA(1, 0, At, B0); PG8_MMA(1, 1, At, B1); PG8_BAR; PG8_SCHED;
;             PG8_LDB(B0, 1, 0); PG8_LDB(B1, 1, 1); PG8_SCHED; PG8_LDA(At, 1, 0); PG8_STAGE(PG8_SA(0, 1), a2, vA2[1]);
;             PG8_WAIT_V(8); PG8_WAIT_L(0); PG8_BAR; PG8_MMA(0, 0, At, B0); PG8_MMA(0, 1, At, B1); PG8_BAR; PG8_SCHED;
;             PG8_LDA(At, 1, 1); PG8_STAGE(PG8_SB(1, 0), b3, voffB[0]); PG8_STAGE(PG8_SB(1, 1), b3, voffB[1]); PG8_STAGE(PG8_SA(1, 0), a3, vA2[0]);
;             PG8_WAIT_V(8); PG8_WAIT_L(0); PG8_BAR; PG8_MMA(1, 0, At, B0); PG8_MMA(1, 1, At, B1); PG8_BAR; PG8_SCHED;
	s_setprio 2
	v_mfma_f32_16x16x128_f8f6f4 v[158:161], v[2:9], v[196:203], v[158:161]
	v_mfma_f32_16x16x128_f8f6f4 v[154:157], v[10:17], v[196:203], v[154:157]
	v_mfma_f32_16x16x128_f8f6f4 v[150:153], v[2:9], v[204:211], v[150:153]
	v_mfma_f32_16x16x128_f8f6f4 v[146:149], v[10:17], v[204:211], v[146:149]
	v_mfma_f32_16x16x128_f8f6f4 v[130:133], v[2:9], v[212:219], v[130:133]
	v_mfma_f32_16x16x128_f8f6f4 v[122:125], v[10:17], v[212:219], v[122:125]
	v_mfma_f32_16x16x128_f8f6f4 v[114:117], v[2:9], v[220:227], v[114:117]
	v_mfma_f32_16x16x128_f8f6f4 v[106:109], v[10:17], v[220:227], v[106:109]
	s_setprio 0
	s_setprio 2
	v_mfma_f32_16x16x128_f8f6f4 v[142:145], v[18:25], v[196:203], v[142:145]
	v_mfma_f32_16x16x128_f8f6f4 v[138:141], v[26:33], v[196:203], v[138:141]
	v_mfma_f32_16x16x128_f8f6f4 v[134:137], v[18:25], v[204:211], v[134:137]
	v_mfma_f32_16x16x128_f8f6f4 v[126:129], v[26:33], v[204:211], v[126:129]
	v_mfma_f32_16x16x128_f8f6f4 v[118:121], v[18:25], v[212:219], v[118:121]
	v_mfma_f32_16x16x128_f8f6f4 v[110:113], v[26:33], v[212:219], v[110:113]
	v_mfma_f32_16x16x128_f8f6f4 v[102:105], v[18:25], v[220:227], v[102:105]
	v_mfma_f32_16x16x128_f8f6f4 v[98:101], v[26:33], v[220:227], v[98:101]
	s_setprio 0
	s_add_u32 s40, s40, 0x8000
	s_addc_u32 s41, s41, 0
	s_add_i32 s42, s66, s48
	s_mov_b32 m0, s42
	ds_read_b128 v[196:199], v193 offset:49152
	ds_read_b128 v[200:203], v193 offset:50176
	ds_read_b128 v[204:207], v193 offset:51200
	ds_read_b128 v[208:211], v193 offset:52224
	ds_read_b128 v[212:215], v193 offset:53248
	ds_read_b128 v[216:219], v193 offset:54272
	ds_read_b128 v[220:223], v193 offset:55296
	ds_read_b128 v[224:227], v193 offset:56320
	global_load_lds_dwordx4 v162, s[40:41]
	s_add_i32 m0, s42, 0x2000
	s_add_i32 s42, s67, s48
	global_load_lds_dwordx4 v164, s[40:41]
	s_mov_b32 m0, s42
	s_nop 0
	global_load_lds_dwordx4 v176, s[40:41]
	s_add_i32 m0, s42, 0x2000
	s_nop 0
	global_load_lds_dwordx4 v178, s[40:41]
	s_mov_b32 m0, s53
	s_nop 0
	global_load_lds_dwordx4 v166, s[30:31]
	s_mov_b32 m0, s58
	s_nop 0
	global_load_lds_dwordx4 v168, s[30:31]
	s_waitcnt vmcnt(8)
	s_waitcnt lgkmcnt(0)
	s_barrier
	s_setprio 2
	v_mfma_f32_16x16x128_f8f6f4 v[94:97], v[2:9], v[196:203], v[94:97]
	v_mfma_f32_16x16x128_f8f6f4 v[90:93], v[10:17], v[196:203], v[90:93]
	v_mfma_f32_16x16x128_f8f6f4 v[82:85], v[2:9], v[204:211], v[82:85]
	v_mfma_f32_16x16x128_f8f6f4 v[74:77], v[10:17], v[204:211], v[74:77]
	v_mfma_f32_16x16x128_f8f6f4 v[66:69], v[2:9], v[212:219], v[66:69]
	v_mfma_f32_16x16x128_f8f6f4 v[58:61], v[10:17], v[212:219], v[58:61]
	v_mfma_f32_16x16x128_f8f6f4 v[50:53], v[2:9], v[220:227], v[50:53]
	v_mfma_f32_16x16x128_f8f6f4 v[42:45], v[10:17], v[220:227], v[42:45]
	s_setprio 0
	s_setprio 2
	v_mfma_f32_16x16x128_f8f6f4 v[86:89], v[18:25], v[196:203], v[86:89]
	v_mfma_f32_16x16x128_f8f6f4 v[78:81], v[26:33], v[196:203], v[78:81]
	v_mfma_f32_16x16x128_f8f6f4 v[70:73], v[18:25], v[204:211], v[70:73]
	v_mfma_f32_16x16x128_f8f6f4 v[62:65], v[26:33], v[204:211], v[62:65]
	v_mfma_f32_16x16x128_f8f6f4 v[54:57], v[18:25], v[212:219], v[54:57]
	v_mfma_f32_16x16x128_f8f6f4 v[46:49], v[26:33], v[212:219], v[46:49]
	v_mfma_f32_16x16x128_f8f6f4 v[38:41], v[18:25], v[220:227], v[38:41]
	v_mfma_f32_16x16x128_f8f6f4 v[34:37], v[26:33], v[220:227], v[34:37]
	s_setprio 0
	s_add_i32 s65, s65, 2
	s_add_u32 s19, s19, 0x10000
	s_addc_u32 s21, s21, 0
	s_add_u32 s28, s28, 0x10000
	s_addc_u32 s29, s29, 0
	s_cmp_gt_u32 s65, 13
	s_cbranch_scc0 .Lh1_911
	s_branch .Lfx_26630
.Lh1_911:
	ds_read_b128 v[18:21], v191
	ds_read_b128 v[22:25], v191 offset:1024
	ds_read_b128 v[26:29], v191 offset:2048
	ds_read_b128 v[30:33], v191 offset:3072
	ds_read_b128 v[2:5], v192
	ds_read_b128 v[6:9], v192 offset:1024
	ds_read_b128 v[10:13], v192 offset:2048
	ds_read_b128 v[14:17], v192 offset:3072
	s_add_u32 s30, s28, 0x8000
	s_addc_u32 s31, s29, 0
	s_cmp_eq_u32 s65, 12
	s_cselect_b32 s42, s22, s30
	s_cselect_b32 s43, s23, s31
	s_cselect_b32 s40, s24, s19
	s_cselect_b32 s41, s25, s21
	s_add_u32 s30, s42, 0x8000
	s_addc_u32 s31, s43, 0
	s_add_i32 m0, s27, 0xc000
	ds_read_b128 v[196:199], v193
	ds_read_b128 v[200:203], v193 offset:1024
	ds_read_b128 v[204:207], v193 offset:2048
	ds_read_b128 v[208:211], v193 offset:3072
	ds_read_b128 v[212:215], v193 offset:4096
	ds_read_b128 v[216:219], v193 offset:5120
	ds_read_b128 v[220:223], v193 offset:6144
	ds_read_b128 v[224:227], v193 offset:7168
	global_load_lds_dwordx4 v182, s[28:29]
	s_add_i32 m0, s27, 0xe000
	s_nop 0
	global_load_lds_dwordx4 v180, s[28:29]
	s_waitcnt vmcnt(8)
	s_waitcnt lgkmcnt(0)
	s_barrier
; #define PG8_STAGE(bufoff, gbase, voff) do { _Pragma("unroll") for (int _i = 0; _i < 2; ++_i) \
;         __builtin_amdgcn_global_load_lds((const unsigned*)((const char*)(gbase) + (voff)[_i]), (PG8_LAS unsigned*)(lds + (bufoff) + ldsw + _i * 8192), 16, 0, 0); } while (0)
; #define PG8_WAIT_V(n) asm volatile("s_waitcnt vmcnt(" #n ")" ::: "memory")
; #define PG8_WAIT_L(n) asm volatile("s_waitcnt lgkmcnt(" #n ")" ::: "memory")
; #define PG8_BAR __builtin_amdgcn_s_barrier()
; #define PG8_SCHED __builtin_amdgcn_sched_barrier(0)
; template <class Epi, class Sched, bool ALIGN_EPI = true, bool F8 = false>
; __device__ __forceinline__ void gemm_phase(PG8_LAS unsigned char* lds, const Sched& S, const Epi& E) {
;     ...
;             PG8_LDB(B0, 0, 0); PG8_LDB(B1, 0, 1); PG8_SCHED; PG8_LDA(At, 0, 0); PG8_STAGE(PG8_SA(1, 1), a1, voffA[1]);
;             PG8_WAIT_V(8); PG8_WAIT_L(0); PG8_BAR; PG8_MMA(0, 0, At, B0); PG8_MMA(0, 1, At, B1); PG8_BAR; PG8_SCHED;
;             PG8_LDA(At, 0, 1); PG8_STAGE(PG8_SB(0, 0), b2, voffB[0]); PG8_STAGE(PG8_SB(0, 1), b2, voffB[1]); PG8_STAGE(PG8_SA(0, 0), a2, vA2[0]);
;             PG8_WAIT_V(8); PG8_WAIT_L(0); PG8_BAR; PG8_MMA(1, 0, At, B0); PG8_MMA(1, 1, At, B1); PG8_BAR; PG8_SCHED;
;             PG8_LDB(B0, 1, 0); PG8_LDB(B1, 1, 1); PG8_SCHED; PG8_LDA(At, 1, 0); PG8_STAGE(PG8_SA(0, 1), a2, vA2[1]);
;             PG8_WAIT_V(8); PG8_WAIT_L(0); PG8_BAR; PG8_MMA(0, 0, At, B0); PG8_MMA(0, 1, At, B1); PG8_BAR; PG8_SCHED;
;             PG8_LDA(At, 1, 1); PG8_STAGE(PG8_SB(1, 0), b3, voffB[0]); PG8_STAGE(PG8_SB(1, 1), b3, voffB[1]); PG8_STAGE(PG8_SA(1, 0), a3, vA2[0]);
;             PG8_WAIT_V(8); PG8_WAIT_L(0); PG8_BAR; PG8_MMA(1, 0, At, B0); PG8_MMA(1, 1, At, B1); PG8_BAR; PG8_SCHED;
	s_setprio 2
	v_mfma_f32_16x16x128_f8f6f4 v[158:161], v[18:25], v[196:203], v[158:161]
	v_mfma_f32_16x16x128_f8f6f4 v[154:157], v[26:33], v[196:203], v[154:157]
	v_mfma_f32_16x16x128_f8f6f4 v[150:153], v[18:25], v[204:211], v[150:153]
	v_mfma_f32_16x16x128_f8f6f4 v[146:149], v[26:33], v[204:211], v[146:149]
	v_mfma_f32_16x16x128_f8f6f4 v[130:133], v[18:25], v[212:219], v[130:133]
	v_mfma_f32_16x16x128_f8f6f4 v[122:125], v[26:33], v[212:219], v[122:125]
	v_mfma_f32_16x16x128_f8f6f4 v[114:117], v[18:25], v[220:227], v[114:117]
	v_mfma_f32_16x16x128_f8f6f4 v[106:109], v[26:33], v[220:227], v[106:109]
	s_setprio 0
	s_setprio 2
	v_mfma_f32_16x16x128_f8f6f4 v[142:145], v[2:9], v[196:203], v[142:145]
	v_mfma_f32_16x16x128_f8f6f4 v[138:141], v[10:17], v[196:203], v[138:141]
	v_mfma_f32_16x16x128_f8f6f4 v[134:137], v[2:9], v[204:211], v[134:137]
	v_mfma_f32_16x16x128_f8f6f4 v[126:129], v[10:17], v[204:211], v[126:129]
	v_mfma_f32_16x16x128_f8f6f4 v[118:121], v[2:9], v[212:219], v[118:121]
	v_mfma_f32_16x16x128_f8f6f4 v[110:113], v[10:17], v[212:219], v[110:113]
	v_mfma_f32_16x16x128_f8f6f4 v[102:105], v[2:9], v[220:227], v[102:105]
	v_mfma_f32_16x16x128_f8f6f4 v[98:101], v[10:17], v[220:227], v[98:101]
	s_setprio 0
	s_add_i32 s66, s60, s48
	s_mov_b32 m0, s66
	ds_read_b128 v[196:199], v193 offset:16384
	ds_read_b128 v[200:203], v193 offset:17408
	ds_read_b128 v[204:207], v193 offset:18432
	ds_read_b128 v[208:211], v193 offset:19456
	ds_read_b128 v[212:215], v193 offset:20480
	ds_read_b128 v[216:219], v193 offset:21504
	ds_read_b128 v[220:223], v193 offset:22528
	ds_read_b128 v[224:227], v193 offset:23552
	global_load_lds_dwordx4 v162, s[40:41]
	s_add_i32 m0, s66, 0x2000
	s_add_i32 s66, s61, s48
	global_load_lds_dwordx4 v164, s[40:41]
	s_add_u32 s98, s40, s6
	s_addc_u32 s99, s41, s7
	s_mov_b32 m0, s66
	s_nop 0
	global_load_lds_dwordx4 v162, s[98:99]
	s_add_u32 s100, s40, s6
	s_addc_u32 s101, s41, s7
	s_add_i32 m0, s66, 0x2000
	s_nop 0
	global_load_lds_dwordx4 v164, s[100:101]
	s_mov_b32 m0, s27
	s_nop 0
	global_load_lds_dwordx4 v166, s[42:43]
	s_mov_b32 m0, s49
	s_nop 0
	global_load_lds_dwordx4 v168, s[42:43]
	s_waitcnt vmcnt(8)
	s_waitcnt lgkmcnt(0)
	s_barrier
	s_setprio 2
	v_mfma_f32_16x16x128_f8f6f4 v[94:97], v[18:25], v[196:203], v[94:97]
	v_mfma_f32_16x16x128_f8f6f4 v[90:93], v[26:33], v[196:203], v[90:93]
	v_mfma_f32_16x16x128_f8f6f4 v[82:85], v[18:25], v[204:211], v[82:85]
	v_mfma_f32_16x16x128_f8f6f4 v[74:77], v[26:33], v[204:211], v[74:77]
	v_mfma_f32_16x16x128_f8f6f4 v[66:69], v[18:25], v[212:219], v[66:69]
	v_mfma_f32_16x16x128_f8f6f4 v[58:61], v[26:33], v[212:219], v[58:61]
	v_mfma_f32_16x16x128_f8f6f4 v[50:53], v[18:25], v[220:227], v[50:53]
	v_mfma_f32_16x16x128_f8f6f4 v[42:45], v[26:33], v[220:227], v[42:45]
	s_setprio 0
	s_setprio 2
	v_mfma_f32_16x16x128_f8f6f4 v[86:89], v[2:9], v[196:203], v[86:89]
	v_mfma_f32_16x16x128_f8f6f4 v[78:81], v[10:17], v[196:203], v[78:81]
	v_mfma_f32_16x16x128_f8f6f4 v[70:73], v[2:9], v[204:211], v[70:73]
	v_mfma_f32_16x16x128_f8f6f4 v[62:65], v[10:17], v[204:211], v[62:65]
	v_mfma_f32_16x16x128_f8f6f4 v[54:57], v[2:9], v[212:219], v[54:57]
	v_mfma_f32_16x16x128_f8f6f4 v[46:49], v[10:17], v[212:219], v[46:49]
	v_mfma_f32_16x16x128_f8f6f4 v[38:41], v[2:9], v[220:227], v[38:41]
	v_mfma_f32_16x16x128_f8f6f4 v[34:37], v[10:17], v[220:227], v[34:37]
	s_setprio 0
	s_add_i32 s66, 0, 0x18000
	s_add_i32 s67, 0, 0x1c000
	v_add_u32_e32 v14, s66, v189
	v_add_u32_e32 v30, s67, v189
	ds_read_b128 v[2:5], v14
	ds_read_b128 v[6:9], v14 offset:1024
	ds_read_b128 v[10:13], v14 offset:2048
	ds_read_b128 v[14:17], v14 offset:3072
	ds_read_b128 v[18:21], v30
	ds_read_b128 v[22:25], v30 offset:1024
	ds_read_b128 v[26:29], v30 offset:2048
	ds_read_b128 v[30:33], v30 offset:3072
	s_mov_b32 m0, s50
	ds_read_b128 v[196:199], v193 offset:32768
	ds_read_b128 v[200:203], v193 offset:33792
	ds_read_b128 v[204:207], v193 offset:34816
	ds_read_b128 v[208:211], v193 offset:35840
	ds_read_b128 v[212:215], v193 offset:36864
	ds_read_b128 v[216:219], v193 offset:37888
	ds_read_b128 v[220:223], v193 offset:38912
	ds_read_b128 v[224:227], v193 offset:39936
	global_load_lds_dwordx4 v172, s[42:43]
	s_mov_b32 m0, s51
	s_nop 0
	global_load_lds_dwordx4 v174, s[42:43]
	s_waitcnt vmcnt(8)
	s_waitcnt lgkmcnt(0)
	s_barrier
; #define PG8_STAGE(bufoff, gbase, voff) do { _Pragma("unroll") for (int _i = 0; _i < 2; ++_i) \
;         __builtin_amdgcn_global_load_lds((const unsigned*)((const char*)(gbase) + (voff)[_i]), (PG8_LAS unsigned*)(lds + (bufoff) + ldsw + _i * 8192), 16, 0, 0); } while (0)
; #define PG8_WAIT_V(n) asm volatile("s_waitcnt vmcnt(" #n ")" ::: "memory")
; #define PG8_WAIT_L(n) asm volatile("s_waitcnt lgkmcnt(" #n ")" ::: "memory")
; #define PG8_BAR __builtin_amdgcn_s_barrier()
; #define PG8_SCHED __builtin_amdgcn_sched_barrier(0)
; template <class Epi, class Sched, bool ALIGN_EPI = true, bool F8 = false>
; __device__ __forceinline__ void gemm_phase(PG8_LAS unsigned char* lds, const Sched& S, const Epi& E) {
;     ...
;             PG8_LDB(B0, 0, 0); PG8_LDB(B1, 0, 1); PG8_SCHED; PG8_LDA(At, 0, 0); PG8_STAGE(PG8_SA(1, 1), a1, voffA[1]);
;             PG8_WAIT_V(8); PG8_WAIT_L(0); PG8_BAR; PG8_MMA(0, 0, At, B0); PG8_MMA(0, 1, At, B1); PG8_BAR; PG8_SCHED;
;             PG8_LDA(At, 0, 1); PG8_STAGE(PG8_SB(0, 0), b2, voffB[0]); PG8_STAGE(PG8_SB(0, 1), b2, voffB[1]); PG8_STAGE(PG8_SA(0, 0), a2, vA2[0]);
;             PG8_WAIT_V(8); PG8_WAIT_L(0); PG8_BAR; PG8_MMA(1, 0, At, B0); PG8_MMA(1, 1, At, B1); PG8_BAR; PG8_SCHED;
;             PG8_LDB(B0, 1, 0); PG8_LDB(B1, 1, 1); PG8_SCHED; PG8_LDA(At, 1, 0); PG8_STAGE(PG8_SA(0, 1), a2, vA2[1]);
;             PG8_WAIT_V(8); PG8_WAIT_L(0); PG8_BAR; PG8_MMA(0, 0, At, B0); PG8_MMA(0, 1, At, B1); PG8_BAR; PG8_SCHED;
;             PG8_LDA(At, 1, 1); PG8_STAGE(PG8_SB(1, 0), b3, voffB[0]); PG8_STAGE(PG8_SB(1, 1), b3, voffB[1]); PG8_STAGE(PG8_SA(1, 0), a3, vA2[0]);
;             PG8_WAIT_V(8); PG8_WAIT_L(0); PG8_BAR; PG8_MMA(1, 0, At, B0); PG8_MMA(1, 1, At, B1); PG8_BAR; PG8_SCHED;
	s_setprio 2
	v_mfma_f32_16x16x128_f8f6f4 v[158:161], v[2:9], v[196:203], v[158:161]
	v_mfma_f32_16x16x128_f8f6f4 v[154:157], v[10:17], v[196:203], v[154:157]
	v_mfma_f32_16x16x128_f8f6f4 v[150:153], v[2:9], v[204:211], v[150:153]
	v_mfma_f32_16x16x128_f8f6f4 v[146:149], v[10:17], v[204:211], v[146:149]
	v_mfma_f32_16x16x128_f8f6f4 v[130:133], v[2:9], v[212:219], v[130:133]
	v_mfma_f32_16x16x128_f8f6f4 v[122:125], v[10:17], v[212:219], v[122:125]
	v_mfma_f32_16x16x128_f8f6f4 v[114:117], v[2:9], v[220:227], v[114:117]
	v_mfma_f32_16x16x128_f8f6f4 v[106:109], v[10:17], v[220:227], v[106:109]
	s_setprio 0
	s_setprio 2
	v_mfma_f32_16x16x128_f8f6f4 v[142:145], v[18:25], v[196:203], v[142:145]
	v_mfma_f32_16x16x128_f8f6f4 v[138:141], v[26:33], v[196:203], v[138:141]
	v_mfma_f32_16x16x128_f8f6f4 v[134:137], v[18:25], v[204:211], v[134:137]
	v_mfma_f32_16x16x128_f8f6f4 v[126:129], v[26:33], v[204:211], v[126:129]
	v_mfma_f32_16x16x128_f8f6f4 v[118:121], v[18:25], v[212:219], v[118:121]
	v_mfma_f32_16x16x128_f8f6f4 v[110:113], v[26:33], v[212:219], v[110:113]
	v_mfma_f32_16x16x128_f8f6f4 v[102:105], v[18:25], v[220:227], v[102:105]
	v_mfma_f32_16x16x128_f8f6f4 v[98:101], v[26:33], v[220:227], v[98:101]
	s_setprio 0
	s_add_u32 s40, s40, 0x8000
	s_addc_u32 s41, s41, 0
	s_add_i32 s42, s66, s48
	s_mov_b32 m0, s42
	ds_read_b128 v[196:199], v193 offset:49152
	ds_read_b128 v[200:203], v193 offset:50176
	ds_read_b128 v[204:207], v193 offset:51200
	ds_read_b128 v[208:211], v193 offset:52224
	ds_read_b128 v[212:215], v193 offset:53248
	ds_read_b128 v[216:219], v193 offset:54272
	ds_read_b128 v[220:223], v193 offset:55296
	ds_read_b128 v[224:227], v193 offset:56320
	global_load_lds_dwordx4 v162, s[40:41]
	s_add_i32 m0, s42, 0x2000
	s_add_i32 s42, s67, s48
	global_load_lds_dwordx4 v164, s[40:41]
	s_mov_b32 m0, s42
	s_nop 0
	global_load_lds_dwordx4 v176, s[40:41]
	s_add_i32 m0, s42, 0x2000
	s_nop 0
	global_load_lds_dwordx4 v178, s[40:41]
	s_mov_b32 m0, s53
	s_nop 0
	global_load_lds_dwordx4 v166, s[30:31]
	s_mov_b32 m0, s58
	s_nop 0
	global_load_lds_dwordx4 v168, s[30:31]
	s_waitcnt vmcnt(8)
	s_waitcnt lgkmcnt(0)
	s_barrier
	s_setprio 2
	v_mfma_f32_16x16x128_f8f6f4 v[94:97], v[2:9], v[196:203], v[94:97]
	v_mfma_f32_16x16x128_f8f6f4 v[90:93], v[10:17], v[196:203], v[90:93]
	v_mfma_f32_16x16x128_f8f6f4 v[82:85], v[2:9], v[204:211], v[82:85]
	v_mfma_f32_16x16x128_f8f6f4 v[74:77], v[10:17], v[204:211], v[74:77]
	v_mfma_f32_16x16x128_f8f6f4 v[66:69], v[2:9], v[212:219], v[66:69]
	v_mfma_f32_16x16x128_f8f6f4 v[58:61], v[10:17], v[212:219], v[58:61]
	v_mfma_f32_16x16x128_f8f6f4 v[50:53], v[2:9], v[220:227], v[50:53]
	v_mfma_f32_16x16x128_f8f6f4 v[42:45], v[10:17], v[220:227], v[42:45]
	s_setprio 0
	s_setprio 2
	v_mfma_f32_16x16x128_f8f6f4 v[86:89], v[18:25], v[196:203], v[86:89]
	v_mfma_f32_16x16x128_f8f6f4 v[78:81], v[26:33], v[196:203], v[78:81]
	v_mfma_f32_16x16x128_f8f6f4 v[70:73], v[18:25], v[204:211], v[70:73]
	v_mfma_f32_16x16x128_f8f6f4 v[62:65], v[26:33], v[204:211], v[62:65]
	v_mfma_f32_16x16x128_f8f6f4 v[54:57], v[18:25], v[212:219], v[54:57]
	v_mfma_f32_16x16x128_f8f6f4 v[46:49], v[26:33], v[212:219], v[46:49]
	v_mfma_f32_16x16x128_f8f6f4 v[38:41], v[18:25], v[220:227], v[38:41]
	v_mfma_f32_16x16x128_f8f6f4 v[34:37], v[26:33], v[220:227], v[34:37]
	s_setprio 0
	s_add_i32 s65, s65, 2
	s_add_u32 s19, s19, 0x10000
	s_addc_u32 s21, s21, 0
	s_add_u32 s28, s28, 0x10000
	s_addc_u32 s29, s29, 0
	s_cmp_gt_u32 s65, 13
	s_cbranch_scc0 .Lh1_911

; #define PG8_STAGE(bufoff, gbase, voff) do { _Pragma("unroll") for (int _i = 0; _i < 2; ++_i) \
;         __builtin_amdgcn_global_load_lds((const unsigned*)((const char*)(gbase) + (voff)[_i]), (PG8_LAS unsigned*)(lds + (bufoff) + ldsw + _i * 8192), 16, 0, 0); } while (0)
; #define PG8_WAIT_V(n) asm volatile("s_waitcnt vmcnt(" #n ")" ::: "memory")
; #define PG8_WAIT_L(n) asm volatile("s_waitcnt lgkmcnt(" #n ")" ::: "memory")
; #define PG8_BAR __builtin_amdgcn_s_barrier()
; #define PG8_SCHED __builtin_amdgcn_sched_barrier(0)
; template <class Epi, class Sched, bool ALIGN_EPI = true, bool F8 = false>
; __device__ __forceinline__ void gemm_phase(PG8_LAS unsigned char* lds, const Sched& S, const Epi& E) {
;     ...
;             if constexpr (Sched::GATHER) { if (last && has_next) S.a_off(nxt, Rs, Cs, voffAn); }
;             const char* a1 = cA + (size_t)(t + 1) * kstep;
;             const char* a2 = last ? nA : cA + (size_t)(t + 2) * kstep; const char* b2 = last ? nB : cB + (size_t)(t + 2) * kstepB;
;             const char* a3 = a2 + kstep; const char* b3 = b2 + kstepB;
;             unsigned vA2[2][2];
; #pragma unroll
;             for (int h = 0; h < 2; ++h)
; #pragma unroll
;                 for (int i = 0; i < 2; ++i) { if constexpr (Sched::GATHER) vA2[h][i] = (last && has_next) ? voffAn[h][i] : voffA[h][i]; else vA2[h][i] = voffA[h][i]; }
;             PG8_LDB(B0, 0, 0); PG8_LDB(B1, 0, 1); PG8_SCHED; PG8_LDA(At, 0, 0); PG8_STAGE(PG8_SA(1, 1), a1, voffA[1]);
;             PG8_WAIT_V(8); PG8_WAIT_L(0); PG8_BAR; PG8_MMA(0, 0, At, B0); PG8_MMA(0, 1, At, B1); PG8_BAR; PG8_SCHED;
;             PG8_LDA(At, 0, 1); PG8_STAGE(PG8_SB(0, 0), b2, voffB[0]); PG8_STAGE(PG8_SB(0, 1), b2, voffB[1]); PG8_STAGE(PG8_SA(0, 0), a2, vA2[0]);
;             PG8_WAIT_V(8); PG8_WAIT_L(0); PG8_BAR; PG8_MMA(1, 0, At, B0); PG8_MMA(1, 1, At, B1); PG8_BAR; PG8_SCHED;
;             PG8_LDB(B0, 1, 0); PG8_LDB(B1, 1, 1); PG8_SCHED; PG8_LDA(At, 1, 0); PG8_STAGE(PG8_SA(0, 1), a2, vA2[1]);
;             PG8_WAIT_V(8); PG8_WAIT_L(0); PG8_BAR; PG8_MMA(0, 0, At, B0); PG8_MMA(0, 1, At, B1); PG8_BAR; PG8_SCHED;
;             PG8_LDA(At, 1, 1); PG8_STAGE(PG8_SB(1, 0), b3, voffB[0]); PG8_STAGE(PG8_SB(1, 1), b3, voffB[1]); PG8_STAGE(PG8_SA(1, 0), a3, vA2[0]);
;             PG8_WAIT_V(8); PG8_WAIT_L(0); PG8_BAR; PG8_MMA(1, 0, At, B0); PG8_MMA(1, 1, At, B1); PG8_BAR; PG8_SCHED;
.Lpk0_1060:
	v_add_u32_e32 v2, s12, v210
	v_add_u32_e32 v14, s62, v210
	s_add_u32 s28, s30, 0x100
	ds_read_b128 v[18:21], v2
	ds_read_b128 v[22:25], v2 offset:1024
	ds_read_b128 v[26:29], v2 offset:2048
	ds_read_b128 v[30:33], v2 offset:3072
	ds_read_b128 v[2:5], v14
	ds_read_b128 v[6:9], v14 offset:1024
	ds_read_b128 v[10:13], v14 offset:2048
	ds_read_b128 v[14:17], v14 offset:3072
	s_addc_u32 s29, s31, 0
	s_and_b64 s[42:43], s[40:41], exec
	s_cselect_b32 s42, 0, s28
	s_cselect_b32 s43, 0, s29
	s_add_u32 s42, s6, s42
	s_addc_u32 s43, s7, s43
	s_and_b64 s[40:41], s[40:41], exec
	s_cselect_b32 s41, s25, s68
	s_cselect_b32 s40, s24, s21
	v_lshl_add_u64 v[204:205], v[196:197], 0, s[30:31]
	s_add_i32 m0, s52, 0xc000
	ds_read_b128 v[222:225], v213
	ds_read_b128 v[226:229], v213 offset:1024
	ds_read_b128 v[230:233], v213 offset:2048
	ds_read_b128 v[234:237], v213 offset:3072
	ds_read_b128 v[238:241], v213 offset:4096
	ds_read_b128 v[242:245], v213 offset:5120
	ds_read_b128 v[246:249], v213 offset:6144
	ds_read_b128 v[250:253], v213 offset:7168
	global_load_lds_dwordx4 v[204:205], off
	v_lshl_add_u64 v[204:205], v[194:195], 0, s[30:31]
	s_add_i32 m0, s52, 0xe000
	s_nop 0
	global_load_lds_dwordx4 v[204:205], off
	s_waitcnt vmcnt(8)
	s_waitcnt lgkmcnt(0)
	s_setprio 1
	v_mfma_f32_16x16x128_f8f6f4 v[142:145], v[18:25], v[222:229], 0
	v_mfma_f32_16x16x128_f8f6f4 v[138:141], v[26:33], v[222:229], 0
	v_mfma_f32_16x16x128_f8f6f4 v[134:137], v[18:25], v[230:237], 0
	v_mfma_f32_16x16x128_f8f6f4 v[130:133], v[26:33], v[230:237], 0
	v_mfma_f32_16x16x128_f8f6f4 v[126:129], v[18:25], v[238:245], 0
	v_mfma_f32_16x16x128_f8f6f4 v[122:125], v[26:33], v[238:245], 0
	v_mfma_f32_16x16x128_f8f6f4 v[118:121], v[18:25], v[246:253], 0
	v_mfma_f32_16x16x128_f8f6f4 v[114:117], v[26:33], v[246:253], 0
	s_setprio 0
	s_setprio 1
	v_mfma_f32_16x16x128_f8f6f4 v[110:113], v[2:9], v[222:229], 0
	v_mfma_f32_16x16x128_f8f6f4 v[106:109], v[10:17], v[222:229], 0
	v_mfma_f32_16x16x128_f8f6f4 v[102:105], v[2:9], v[230:237], 0
	v_mfma_f32_16x16x128_f8f6f4 v[98:101], v[10:17], v[230:237], 0
	v_mfma_f32_16x16x128_f8f6f4 v[94:97], v[2:9], v[238:245], 0
	v_mfma_f32_16x16x128_f8f6f4 v[90:93], v[10:17], v[238:245], 0
	v_mfma_f32_16x16x128_f8f6f4 v[86:89], v[2:9], v[246:253], 0
	v_mfma_f32_16x16x128_f8f6f4 v[82:85], v[10:17], v[246:253], 0
	s_setprio 0
	s_barrier
	s_add_i32 s30, s12, s48
	v_lshl_add_u64 v[204:205], s[40:41], 0, v[162:163]
	s_mov_b32 m0, s30
	ds_read_b128 v[222:225], v213 offset:16384
	ds_read_b128 v[226:229], v213 offset:17408
	ds_read_b128 v[230:233], v213 offset:18432
	ds_read_b128 v[234:237], v213 offset:19456
	ds_read_b128 v[238:241], v213 offset:20480
	ds_read_b128 v[242:245], v213 offset:21504
	ds_read_b128 v[246:249], v213 offset:22528
	ds_read_b128 v[250:253], v213 offset:23552
	global_load_lds_dwordx4 v[204:205], off
	v_lshl_add_u64 v[204:205], s[40:41], 0, v[164:165]
	s_add_i32 m0, s30, 0x2000
	s_add_i32 s30, s62, s48
	global_load_lds_dwordx4 v[204:205], off
	v_lshl_add_u64 v[204:205], s[40:41], 0, v[166:167]
	s_mov_b32 m0, s30
	v_mov_b32_e32 v203, v171
	global_load_lds_dwordx4 v[204:205], off
	v_lshl_add_u64 v[204:205], s[40:41], 0, v[168:169]
	s_add_i32 m0, s30, 0x2000
	s_nop 0
	global_load_lds_dwordx4 v[204:205], off
	s_mov_b32 m0, s52
	v_lshl_add_u64 v[204:205], s[42:43], 0, v[170:171]
	global_load_lds_dwordx4 v170, s[42:43]
	s_mov_b32 m0, s53
	s_nop 0
	global_load_lds_dwordx4 v202, s[42:43]
	s_waitcnt vmcnt(8)
	s_waitcnt lgkmcnt(0)
	v_lshl_add_u64 v[202:203], s[42:43], 0, v[202:203]
	s_setprio 1
	v_mfma_f32_16x16x128_f8f6f4 v[78:81], v[18:25], v[222:229], 0
	v_mfma_f32_16x16x128_f8f6f4 v[74:77], v[26:33], v[222:229], 0
	v_mfma_f32_16x16x128_f8f6f4 v[70:73], v[18:25], v[230:237], 0
	v_mfma_f32_16x16x128_f8f6f4 v[66:69], v[26:33], v[230:237], 0
	v_mfma_f32_16x16x128_f8f6f4 v[62:65], v[18:25], v[238:245], 0
	v_mfma_f32_16x16x128_f8f6f4 v[58:61], v[26:33], v[238:245], 0
	v_mfma_f32_16x16x128_f8f6f4 v[54:57], v[18:25], v[246:253], 0
	v_mfma_f32_16x16x128_f8f6f4 v[50:53], v[26:33], v[246:253], 0
	s_setprio 0
	s_setprio 1
	v_mfma_f32_16x16x128_f8f6f4 v[46:49], v[2:9], v[222:229], 0
	v_mfma_f32_16x16x128_f8f6f4 v[42:45], v[10:17], v[222:229], 0
	v_mfma_f32_16x16x128_f8f6f4 v[38:41], v[2:9], v[230:237], 0
	v_mfma_f32_16x16x128_f8f6f4 v[34:37], v[10:17], v[230:237], 0
	v_mfma_f32_16x16x128_f8f6f4 v[146:149], v[2:9], v[238:245], 0
	v_mfma_f32_16x16x128_f8f6f4 v[150:153], v[10:17], v[238:245], 0
	v_mfma_f32_16x16x128_f8f6f4 v[154:157], v[2:9], v[246:253], 0
	v_mfma_f32_16x16x128_f8f6f4 v[158:161], v[10:17], v[246:253], 0
	s_setprio 0
	s_barrier
; #define PG8_STAGE(bufoff, gbase, voff) do { _Pragma("unroll") for (int _i = 0; _i < 2; ++_i) \
;         __builtin_amdgcn_global_load_lds((const unsigned*)((const char*)(gbase) + (voff)[_i]), (PG8_LAS unsigned*)(lds + (bufoff) + ldsw + _i * 8192), 16, 0, 0); } while (0)
; #define PG8_WAIT_V(n) asm volatile("s_waitcnt vmcnt(" #n ")" ::: "memory")
; #define PG8_WAIT_L(n) asm volatile("s_waitcnt lgkmcnt(" #n ")" ::: "memory")
; #define PG8_BAR __builtin_amdgcn_s_barrier()
; #define PG8_SCHED __builtin_amdgcn_sched_barrier(0)
; template <class Epi, class Sched, bool ALIGN_EPI = true, bool F8 = false>
; __device__ __forceinline__ void gemm_phase(PG8_LAS unsigned char* lds, const Sched& S, const Epi& E) {
;     ...
;             PG8_LDB(B0, 0, 0); PG8_LDB(B1, 0, 1); PG8_SCHED; PG8_LDA(At, 0, 0); PG8_STAGE(PG8_SA(1, 1), a1, voffA[1]);
;             PG8_WAIT_V(8); PG8_WAIT_L(0); PG8_BAR; PG8_MMA(0, 0, At, B0); PG8_MMA(0, 1, At, B1); PG8_BAR; PG8_SCHED;
;             PG8_LDA(At, 0, 1); PG8_STAGE(PG8_SB(0, 0), b2, voffB[0]); PG8_STAGE(PG8_SB(0, 1), b2, voffB[1]); PG8_STAGE(PG8_SA(0, 0), a2, vA2[0]);
;             PG8_WAIT_V(8); PG8_WAIT_L(0); PG8_BAR; PG8_MMA(1, 0, At, B0); PG8_MMA(1, 1, At, B1); PG8_BAR; PG8_SCHED;
;             PG8_LDB(B0, 1, 0); PG8_LDB(B1, 1, 1); PG8_SCHED; PG8_LDA(At, 1, 0); PG8_STAGE(PG8_SA(0, 1), a2, vA2[1]);
;             PG8_WAIT_V(8); PG8_WAIT_L(0); PG8_BAR; PG8_MMA(0, 0, At, B0); PG8_MMA(0, 1, At, B1); PG8_BAR; PG8_SCHED;
;             PG8_LDA(At, 1, 1); PG8_STAGE(PG8_SB(1, 0), b3, voffB[0]); PG8_STAGE(PG8_SB(1, 1), b3, voffB[1]); PG8_STAGE(PG8_SA(1, 0), a3, vA2[0]);
;             PG8_WAIT_V(8); PG8_WAIT_L(0); PG8_BAR; PG8_MMA(1, 0, At, B0); PG8_MMA(1, 1, At, B1); PG8_BAR; PG8_SCHED;
	s_add_i32 s70, 0, 0x18000
	s_add_i32 s71, 0, 0x1c000
	v_add_u32_e32 v14, s70, v210
	v_add_u32_e32 v30, s71, v210
	ds_read_b128 v[2:5], v14
	ds_read_b128 v[6:9], v14 offset:1024
	ds_read_b128 v[10:13], v14 offset:2048
	ds_read_b128 v[14:17], v14 offset:3072
	ds_read_b128 v[18:21], v30
	ds_read_b128 v[22:25], v30 offset:1024
	ds_read_b128 v[26:29], v30 offset:2048
	ds_read_b128 v[30:33], v30 offset:3072
	s_mov_b32 m0, s58
	v_lshl_add_u64 v[200:201], s[42:43], 0, v[200:201]
	ds_read_b128 v[222:225], v213 offset:32768
	ds_read_b128 v[226:229], v213 offset:33792
	ds_read_b128 v[230:233], v213 offset:34816
	ds_read_b128 v[234:237], v213 offset:35840
	ds_read_b128 v[238:241], v213 offset:36864
	ds_read_b128 v[242:245], v213 offset:37888
	ds_read_b128 v[246:249], v213 offset:38912
	ds_read_b128 v[250:253], v213 offset:39936
	global_load_lds_dwordx4 v[200:201], off
	v_lshl_add_u64 v[198:199], s[42:43], 0, v[198:199]
	s_mov_b32 m0, s59
	s_nop 0
	global_load_lds_dwordx4 v[198:199], off
	s_waitcnt vmcnt(8)
	s_waitcnt lgkmcnt(0)
	s_setprio 1
	v_mfma_f32_16x16x128_f8f6f4 v[142:145], v[2:9], v[222:229], v[142:145]
	v_mfma_f32_16x16x128_f8f6f4 v[138:141], v[10:17], v[222:229], v[138:141]
	v_mfma_f32_16x16x128_f8f6f4 v[134:137], v[2:9], v[230:237], v[134:137]
	v_mfma_f32_16x16x128_f8f6f4 v[130:133], v[10:17], v[230:237], v[130:133]
	v_mfma_f32_16x16x128_f8f6f4 v[126:129], v[2:9], v[238:245], v[126:129]
	v_mfma_f32_16x16x128_f8f6f4 v[122:125], v[10:17], v[238:245], v[122:125]
	v_mfma_f32_16x16x128_f8f6f4 v[118:121], v[2:9], v[246:253], v[118:121]
	v_mfma_f32_16x16x128_f8f6f4 v[114:117], v[10:17], v[246:253], v[114:117]
	s_setprio 0
	s_setprio 1
	v_mfma_f32_16x16x128_f8f6f4 v[110:113], v[18:25], v[222:229], v[110:113]
	v_mfma_f32_16x16x128_f8f6f4 v[106:109], v[26:33], v[222:229], v[106:109]
	v_mfma_f32_16x16x128_f8f6f4 v[102:105], v[18:25], v[230:237], v[102:105]
	v_mfma_f32_16x16x128_f8f6f4 v[98:101], v[26:33], v[230:237], v[98:101]
	v_mfma_f32_16x16x128_f8f6f4 v[94:97], v[18:25], v[238:245], v[94:97]
	v_mfma_f32_16x16x128_f8f6f4 v[90:93], v[26:33], v[238:245], v[90:93]
	v_mfma_f32_16x16x128_f8f6f4 v[86:89], v[18:25], v[246:253], v[86:89]
	v_mfma_f32_16x16x128_f8f6f4 v[82:85], v[26:33], v[246:253], v[82:85]
	s_setprio 0
	s_barrier
	s_add_u32 s30, s40, 0x8000
	s_addc_u32 s31, s41, 0
	s_add_i32 s40, s70, s48
	v_lshl_add_u64 v[198:199], s[30:31], 0, v[162:163]
	s_mov_b32 m0, s40
	ds_read_b128 v[222:225], v213 offset:49152
	ds_read_b128 v[226:229], v213 offset:50176
	ds_read_b128 v[230:233], v213 offset:51200
	ds_read_b128 v[234:237], v213 offset:52224
	ds_read_b128 v[238:241], v213 offset:53248
	ds_read_b128 v[242:245], v213 offset:54272
	ds_read_b128 v[246:249], v213 offset:55296
	ds_read_b128 v[250:253], v213 offset:56320
	global_load_lds_dwordx4 v[198:199], off
	v_lshl_add_u64 v[198:199], s[30:31], 0, v[164:165]
	s_add_i32 m0, s40, 0x2000
	s_add_i32 s40, s71, s48
	global_load_lds_dwordx4 v[198:199], off
	v_lshl_add_u64 v[198:199], s[30:31], 0, v[166:167]
	s_mov_b32 m0, s40
	s_nop 0
	global_load_lds_dwordx4 v[198:199], off
	v_lshl_add_u64 v[198:199], s[30:31], 0, v[168:169]
	s_add_i32 m0, s40, 0x2000
	s_nop 0
	global_load_lds_dwordx4 v[198:199], off
	v_lshl_add_u64 v[198:199], v[204:205], 0, s[18:19]
	s_mov_b32 m0, s60
	s_nop 0
	global_load_lds_dwordx4 v[198:199], off
	v_lshl_add_u64 v[198:199], v[202:203], 0, s[18:19]
	s_mov_b32 m0, s61
	s_nop 0
	global_load_lds_dwordx4 v[198:199], off
	s_waitcnt vmcnt(8)
	s_waitcnt lgkmcnt(0)
	s_setprio 1
	v_mfma_f32_16x16x128_f8f6f4 v[78:81], v[2:9], v[222:229], v[78:81]
	v_mfma_f32_16x16x128_f8f6f4 v[74:77], v[10:17], v[222:229], v[74:77]
	v_mfma_f32_16x16x128_f8f6f4 v[70:73], v[2:9], v[230:237], v[70:73]
	v_mfma_f32_16x16x128_f8f6f4 v[66:69], v[10:17], v[230:237], v[66:69]
	v_mfma_f32_16x16x128_f8f6f4 v[62:65], v[2:9], v[238:245], v[62:65]
	v_mfma_f32_16x16x128_f8f6f4 v[58:61], v[10:17], v[238:245], v[58:61]
	v_mfma_f32_16x16x128_f8f6f4 v[54:57], v[2:9], v[246:253], v[54:57]
	v_mfma_f32_16x16x128_f8f6f4 v[50:53], v[10:17], v[246:253], v[50:53]
	s_setprio 0
	s_setprio 1
	v_mfma_f32_16x16x128_f8f6f4 v[46:49], v[18:25], v[222:229], v[46:49]
	v_mfma_f32_16x16x128_f8f6f4 v[42:45], v[26:33], v[222:229], v[42:45]
	v_mfma_f32_16x16x128_f8f6f4 v[38:41], v[18:25], v[230:237], v[38:41]
	v_mfma_f32_16x16x128_f8f6f4 v[34:37], v[26:33], v[230:237], v[34:37]
	v_mfma_f32_16x16x128_f8f6f4 v[146:149], v[18:25], v[238:245], v[146:149]
	v_mfma_f32_16x16x128_f8f6f4 v[150:153], v[26:33], v[238:245], v[150:153]
	v_mfma_f32_16x16x128_f8f6f4 v[154:157], v[18:25], v[246:253], v[154:157]
	v_mfma_f32_16x16x128_f8f6f4 v[158:161], v[26:33], v[246:253], v[158:161]
	s_setprio 0
	s_barrier
	s_add_i32 s69, s69, 2
	s_add_u32 s21, s21, 0x10000
	s_addc_u32 s68, s68, 0
	s_cmp_gt_u32 s69, 13
	s_cbranch_scc1 .LBB0_1062
	s_mov_b64 s[30:31], s[28:29]
	s_branch .LBB0_1058

; #define PG8_STAGE(bufoff, gbase, voff) do { _Pragma("unroll") for (int _i = 0; _i < 2; ++_i) \
;         __builtin_amdgcn_global_load_lds((const unsigned*)((const char*)(gbase) + (voff)[_i]), (PG8_LAS unsigned*)(lds + (bufoff) + ldsw + _i * 8192), 16, 0, 0); } while (0)
; #define PG8_WAIT_V(n) asm volatile("s_waitcnt vmcnt(" #n ")" ::: "memory")
; #define PG8_WAIT_L(n) asm volatile("s_waitcnt lgkmcnt(" #n ")" ::: "memory")
; #define PG8_BAR __builtin_amdgcn_s_barrier()
; #define PG8_SCHED __builtin_amdgcn_sched_barrier(0)
; template <class Epi, class Sched, bool ALIGN_EPI = true, bool F8 = false>
; __device__ __forceinline__ void gemm_phase(PG8_LAS unsigned char* lds, const Sched& S, const Epi& E) {
;     ...
;             if constexpr (Sched::GATHER) { if (last && has_next) S.a_off(nxt, Rs, Cs, voffAn); }
;             const char* a1 = cA + (size_t)(t + 1) * kstep;
;             const char* a2 = last ? nA : cA + (size_t)(t + 2) * kstep; const char* b2 = last ? nB : cB + (size_t)(t + 2) * kstepB;
;             const char* a3 = a2 + kstep; const char* b3 = b2 + kstepB;
;             unsigned vA2[2][2];
; #pragma unroll
;             for (int h = 0; h < 2; ++h)
; #pragma unroll
;                 for (int i = 0; i < 2; ++i) { if constexpr (Sched::GATHER) vA2[h][i] = (last && has_next) ? voffAn[h][i] : voffA[h][i]; else vA2[h][i] = voffA[h][i]; }
;             PG8_LDB(B0, 0, 0); PG8_LDB(B1, 0, 1); PG8_SCHED; PG8_LDA(At, 0, 0); PG8_STAGE(PG8_SA(1, 1), a1, voffA[1]);
;             PG8_WAIT_V(8); PG8_WAIT_L(0); PG8_BAR; PG8_MMA(0, 0, At, B0); PG8_MMA(0, 1, At, B1); PG8_BAR; PG8_SCHED;
;             PG8_LDA(At, 0, 1); PG8_STAGE(PG8_SB(0, 0), b2, voffB[0]); PG8_STAGE(PG8_SB(0, 1), b2, voffB[1]); PG8_STAGE(PG8_SA(0, 0), a2, vA2[0]);
;             PG8_WAIT_V(8); PG8_WAIT_L(0); PG8_BAR; PG8_MMA(1, 0, At, B0); PG8_MMA(1, 1, At, B1); PG8_BAR; PG8_SCHED;
;             PG8_LDB(B0, 1, 0); PG8_LDB(B1, 1, 1); PG8_SCHED; PG8_LDA(At, 1, 0); PG8_STAGE(PG8_SA(0, 1), a2, vA2[1]);
;             PG8_WAIT_V(8); PG8_WAIT_L(0); PG8_BAR; PG8_MMA(0, 0, At, B0); PG8_MMA(0, 1, At, B1); PG8_BAR; PG8_SCHED;
;             PG8_LDA(At, 1, 1); PG8_STAGE(PG8_SB(1, 0), b3, voffB[0]); PG8_STAGE(PG8_SB(1, 1), b3, voffB[1]); PG8_STAGE(PG8_SA(1, 0), a3, vA2[0]);
;             PG8_WAIT_V(8); PG8_WAIT_L(0); PG8_BAR; PG8_MMA(1, 0, At, B0); PG8_MMA(1, 1, At, B1); PG8_BAR; PG8_SCHED;
.LBB0_1060:
	v_add_u32_e32 v2, s12, v210
	v_add_u32_e32 v14, s62, v210
	s_add_u32 s28, s30, 0x100
	ds_read_b128 v[18:21], v2
	ds_read_b128 v[22:25], v2 offset:1024
	ds_read_b128 v[26:29], v2 offset:2048
	ds_read_b128 v[30:33], v2 offset:3072
	ds_read_b128 v[2:5], v14
	ds_read_b128 v[6:9], v14 offset:1024
	ds_read_b128 v[10:13], v14 offset:2048
	ds_read_b128 v[14:17], v14 offset:3072
	s_addc_u32 s29, s31, 0
	s_and_b64 s[42:43], s[40:41], exec
	s_cselect_b32 s42, 0, s28
	s_cselect_b32 s43, 0, s29
	s_add_u32 s42, s6, s42
	s_addc_u32 s43, s7, s43
	s_and_b64 s[40:41], s[40:41], exec
	s_cselect_b32 s41, s25, s68
	s_cselect_b32 s40, s24, s21
	v_lshl_add_u64 v[204:205], v[196:197], 0, s[30:31]
	s_add_i32 m0, s52, 0xc000
	ds_read_b128 v[222:225], v213
	ds_read_b128 v[226:229], v213 offset:1024
	ds_read_b128 v[230:233], v213 offset:2048
	ds_read_b128 v[234:237], v213 offset:3072
	ds_read_b128 v[238:241], v213 offset:4096
	ds_read_b128 v[242:245], v213 offset:5120
	ds_read_b128 v[246:249], v213 offset:6144
	ds_read_b128 v[250:253], v213 offset:7168
	global_load_lds_dwordx4 v[204:205], off
	v_lshl_add_u64 v[204:205], v[194:195], 0, s[30:31]
	s_add_i32 m0, s52, 0xe000
	s_nop 0
	global_load_lds_dwordx4 v[204:205], off
	s_waitcnt vmcnt(8)
	s_waitcnt lgkmcnt(0)
	s_setprio 1
	v_mfma_f32_16x16x128_f8f6f4 v[142:145], v[18:25], v[222:229], v[142:145]
	v_mfma_f32_16x16x128_f8f6f4 v[138:141], v[26:33], v[222:229], v[138:141]
	v_mfma_f32_16x16x128_f8f6f4 v[134:137], v[18:25], v[230:237], v[134:137]
	v_mfma_f32_16x16x128_f8f6f4 v[130:133], v[26:33], v[230:237], v[130:133]
	v_mfma_f32_16x16x128_f8f6f4 v[126:129], v[18:25], v[238:245], v[126:129]
	v_mfma_f32_16x16x128_f8f6f4 v[122:125], v[26:33], v[238:245], v[122:125]
	v_mfma_f32_16x16x128_f8f6f4 v[118:121], v[18:25], v[246:253], v[118:121]
	v_mfma_f32_16x16x128_f8f6f4 v[114:117], v[26:33], v[246:253], v[114:117]
	s_setprio 0
	s_setprio 1
	v_mfma_f32_16x16x128_f8f6f4 v[110:113], v[2:9], v[222:229], v[110:113]
	v_mfma_f32_16x16x128_f8f6f4 v[106:109], v[10:17], v[222:229], v[106:109]
	v_mfma_f32_16x16x128_f8f6f4 v[102:105], v[2:9], v[230:237], v[102:105]
	v_mfma_f32_16x16x128_f8f6f4 v[98:101], v[10:17], v[230:237], v[98:101]
	v_mfma_f32_16x16x128_f8f6f4 v[94:97], v[2:9], v[238:245], v[94:97]
	v_mfma_f32_16x16x128_f8f6f4 v[90:93], v[10:17], v[238:245], v[90:93]
	v_mfma_f32_16x16x128_f8f6f4 v[86:89], v[2:9], v[246:253], v[86:89]
	v_mfma_f32_16x16x128_f8f6f4 v[82:85], v[10:17], v[246:253], v[82:85]
	s_setprio 0
	s_barrier
	s_add_i32 s30, s12, s48
	v_lshl_add_u64 v[204:205], s[40:41], 0, v[162:163]
	s_mov_b32 m0, s30
	ds_read_b128 v[222:225], v213 offset:16384
	ds_read_b128 v[226:229], v213 offset:17408
	ds_read_b128 v[230:233], v213 offset:18432
	ds_read_b128 v[234:237], v213 offset:19456
	ds_read_b128 v[238:241], v213 offset:20480
	ds_read_b128 v[242:245], v213 offset:21504
	ds_read_b128 v[246:249], v213 offset:22528
	ds_read_b128 v[250:253], v213 offset:23552
	global_load_lds_dwordx4 v[204:205], off
	v_lshl_add_u64 v[204:205], s[40:41], 0, v[164:165]
	s_add_i32 m0, s30, 0x2000
	s_add_i32 s30, s62, s48
	global_load_lds_dwordx4 v[204:205], off
	v_lshl_add_u64 v[204:205], s[40:41], 0, v[166:167]
	s_mov_b32 m0, s30
	v_mov_b32_e32 v203, v171
	global_load_lds_dwordx4 v[204:205], off
	v_lshl_add_u64 v[204:205], s[40:41], 0, v[168:169]
	s_add_i32 m0, s30, 0x2000
	s_nop 0
	global_load_lds_dwordx4 v[204:205], off
	s_mov_b32 m0, s52
	v_lshl_add_u64 v[204:205], s[42:43], 0, v[170:171]
	global_load_lds_dwordx4 v170, s[42:43]
	s_mov_b32 m0, s53
	s_nop 0
	global_load_lds_dwordx4 v202, s[42:43]
	s_waitcnt vmcnt(8)
	s_waitcnt lgkmcnt(0)
	v_lshl_add_u64 v[202:203], s[42:43], 0, v[202:203]
	s_setprio 1
	v_mfma_f32_16x16x128_f8f6f4 v[78:81], v[18:25], v[222:229], v[78:81]
	v_mfma_f32_16x16x128_f8f6f4 v[74:77], v[26:33], v[222:229], v[74:77]
	v_mfma_f32_16x16x128_f8f6f4 v[70:73], v[18:25], v[230:237], v[70:73]
	v_mfma_f32_16x16x128_f8f6f4 v[66:69], v[26:33], v[230:237], v[66:69]
	v_mfma_f32_16x16x128_f8f6f4 v[62:65], v[18:25], v[238:245], v[62:65]
	v_mfma_f32_16x16x128_f8f6f4 v[58:61], v[26:33], v[238:245], v[58:61]
	v_mfma_f32_16x16x128_f8f6f4 v[54:57], v[18:25], v[246:253], v[54:57]
	v_mfma_f32_16x16x128_f8f6f4 v[50:53], v[26:33], v[246:253], v[50:53]
	s_setprio 0
	s_setprio 1
	v_mfma_f32_16x16x128_f8f6f4 v[46:49], v[2:9], v[222:229], v[46:49]
	v_mfma_f32_16x16x128_f8f6f4 v[42:45], v[10:17], v[222:229], v[42:45]
	v_mfma_f32_16x16x128_f8f6f4 v[38:41], v[2:9], v[230:237], v[38:41]
	v_mfma_f32_16x16x128_f8f6f4 v[34:37], v[10:17], v[230:237], v[34:37]
	v_mfma_f32_16x16x128_f8f6f4 v[146:149], v[2:9], v[238:245], v[146:149]
	v_mfma_f32_16x16x128_f8f6f4 v[150:153], v[10:17], v[238:245], v[150:153]
	v_mfma_f32_16x16x128_f8f6f4 v[154:157], v[2:9], v[246:253], v[154:157]
	v_mfma_f32_16x16x128_f8f6f4 v[158:161], v[10:17], v[246:253], v[158:161]
	s_setprio 0
	s_barrier
; #define PG8_STAGE(bufoff, gbase, voff) do { _Pragma("unroll") for (int _i = 0; _i < 2; ++_i) \
;         __builtin_amdgcn_global_load_lds((const unsigned*)((const char*)(gbase) + (voff)[_i]), (PG8_LAS unsigned*)(lds + (bufoff) + ldsw + _i * 8192), 16, 0, 0); } while (0)
; #define PG8_WAIT_V(n) asm volatile("s_waitcnt vmcnt(" #n ")" ::: "memory")
; #define PG8_WAIT_L(n) asm volatile("s_waitcnt lgkmcnt(" #n ")" ::: "memory")
; #define PG8_BAR __builtin_amdgcn_s_barrier()
; #define PG8_SCHED __builtin_amdgcn_sched_barrier(0)
; template <class Epi, class Sched, bool ALIGN_EPI = true, bool F8 = false>
; __device__ __forceinline__ void gemm_phase(PG8_LAS unsigned char* lds, const Sched& S, const Epi& E) {
;     ...
;             PG8_LDB(B0, 0, 0); PG8_LDB(B1, 0, 1); PG8_SCHED; PG8_LDA(At, 0, 0); PG8_STAGE(PG8_SA(1, 1), a1, voffA[1]);
;             PG8_WAIT_V(8); PG8_WAIT_L(0); PG8_BAR; PG8_MMA(0, 0, At, B0); PG8_MMA(0, 1, At, B1); PG8_BAR; PG8_SCHED;
;             PG8_LDA(At, 0, 1); PG8_STAGE(PG8_SB(0, 0), b2, voffB[0]); PG8_STAGE(PG8_SB(0, 1), b2, voffB[1]); PG8_STAGE(PG8_SA(0, 0), a2, vA2[0]);
;             PG8_WAIT_V(8); PG8_WAIT_L(0); PG8_BAR; PG8_MMA(1, 0, At, B0); PG8_MMA(1, 1, At, B1); PG8_BAR; PG8_SCHED;
;             PG8_LDB(B0, 1, 0); PG8_LDB(B1, 1, 1); PG8_SCHED; PG8_LDA(At, 1, 0); PG8_STAGE(PG8_SA(0, 1), a2, vA2[1]);
;             PG8_WAIT_V(8); PG8_WAIT_L(0); PG8_BAR; PG8_MMA(0, 0, At, B0); PG8_MMA(0, 1, At, B1); PG8_BAR; PG8_SCHED;
;             PG8_LDA(At, 1, 1); PG8_STAGE(PG8_SB(1, 0), b3, voffB[0]); PG8_STAGE(PG8_SB(1, 1), b3, voffB[1]); PG8_STAGE(PG8_SA(1, 0), a3, vA2[0]);
;             PG8_WAIT_V(8); PG8_WAIT_L(0); PG8_BAR; PG8_MMA(1, 0, At, B0); PG8_MMA(1, 1, At, B1); PG8_BAR; PG8_SCHED;
	s_add_i32 s70, 0, 0x18000
	s_add_i32 s71, 0, 0x1c000
	v_add_u32_e32 v14, s70, v210
	v_add_u32_e32 v30, s71, v210
	ds_read_b128 v[2:5], v14
	ds_read_b128 v[6:9], v14 offset:1024
	ds_read_b128 v[10:13], v14 offset:2048
	ds_read_b128 v[14:17], v14 offset:3072
	ds_read_b128 v[18:21], v30
	ds_read_b128 v[22:25], v30 offset:1024
	ds_read_b128 v[26:29], v30 offset:2048
	ds_read_b128 v[30:33], v30 offset:3072
	s_mov_b32 m0, s58
	v_lshl_add_u64 v[200:201], s[42:43], 0, v[200:201]
	ds_read_b128 v[222:225], v213 offset:32768
	ds_read_b128 v[226:229], v213 offset:33792
	ds_read_b128 v[230:233], v213 offset:34816
	ds_read_b128 v[234:237], v213 offset:35840
	ds_read_b128 v[238:241], v213 offset:36864
	ds_read_b128 v[242:245], v213 offset:37888
	ds_read_b128 v[246:249], v213 offset:38912
	ds_read_b128 v[250:253], v213 offset:39936
	global_load_lds_dwordx4 v[200:201], off
	v_lshl_add_u64 v[198:199], s[42:43], 0, v[198:199]
	s_mov_b32 m0, s59
	s_nop 0
	global_load_lds_dwordx4 v[198:199], off
	s_waitcnt vmcnt(8)
	s_waitcnt lgkmcnt(0)
	s_setprio 1
	v_mfma_f32_16x16x128_f8f6f4 v[142:145], v[2:9], v[222:229], v[142:145]
	v_mfma_f32_16x16x128_f8f6f4 v[138:141], v[10:17], v[222:229], v[138:141]
	v_mfma_f32_16x16x128_f8f6f4 v[134:137], v[2:9], v[230:237], v[134:137]
	v_mfma_f32_16x16x128_f8f6f4 v[130:133], v[10:17], v[230:237], v[130:133]
	v_mfma_f32_16x16x128_f8f6f4 v[126:129], v[2:9], v[238:245], v[126:129]
	v_mfma_f32_16x16x128_f8f6f4 v[122:125], v[10:17], v[238:245], v[122:125]
	v_mfma_f32_16x16x128_f8f6f4 v[118:121], v[2:9], v[246:253], v[118:121]
	v_mfma_f32_16x16x128_f8f6f4 v[114:117], v[10:17], v[246:253], v[114:117]
	s_setprio 0
	s_setprio 1
	v_mfma_f32_16x16x128_f8f6f4 v[110:113], v[18:25], v[222:229], v[110:113]
	v_mfma_f32_16x16x128_f8f6f4 v[106:109], v[26:33], v[222:229], v[106:109]
	v_mfma_f32_16x16x128_f8f6f4 v[102:105], v[18:25], v[230:237], v[102:105]
	v_mfma_f32_16x16x128_f8f6f4 v[98:101], v[26:33], v[230:237], v[98:101]
	v_mfma_f32_16x16x128_f8f6f4 v[94:97], v[18:25], v[238:245], v[94:97]
	v_mfma_f32_16x16x128_f8f6f4 v[90:93], v[26:33], v[238:245], v[90:93]
	v_mfma_f32_16x16x128_f8f6f4 v[86:89], v[18:25], v[246:253], v[86:89]
	v_mfma_f32_16x16x128_f8f6f4 v[82:85], v[26:33], v[246:253], v[82:85]
	s_setprio 0
	s_barrier
	s_add_u32 s30, s40, 0x8000
	s_addc_u32 s31, s41, 0
	s_add_i32 s40, s70, s48
	v_lshl_add_u64 v[198:199], s[30:31], 0, v[162:163]
	s_mov_b32 m0, s40
	ds_read_b128 v[222:225], v213 offset:49152
	ds_read_b128 v[226:229], v213 offset:50176
	ds_read_b128 v[230:233], v213 offset:51200
	ds_read_b128 v[234:237], v213 offset:52224
	ds_read_b128 v[238:241], v213 offset:53248
	ds_read_b128 v[242:245], v213 offset:54272
	ds_read_b128 v[246:249], v213 offset:55296
	ds_read_b128 v[250:253], v213 offset:56320
	global_load_lds_dwordx4 v[198:199], off
	v_lshl_add_u64 v[198:199], s[30:31], 0, v[164:165]
	s_add_i32 m0, s40, 0x2000
	s_add_i32 s40, s71, s48
	global_load_lds_dwordx4 v[198:199], off
	v_lshl_add_u64 v[198:199], s[30:31], 0, v[166:167]
	s_mov_b32 m0, s40
	s_nop 0
	global_load_lds_dwordx4 v[198:199], off
	v_lshl_add_u64 v[198:199], s[30:31], 0, v[168:169]
	s_add_i32 m0, s40, 0x2000
	s_nop 0
	global_load_lds_dwordx4 v[198:199], off
	v_lshl_add_u64 v[198:199], v[204:205], 0, s[18:19]
	s_mov_b32 m0, s60
	s_nop 0
	global_load_lds_dwordx4 v[198:199], off
	v_lshl_add_u64 v[198:199], v[202:203], 0, s[18:19]
	s_mov_b32 m0, s61
	s_nop 0
	global_load_lds_dwordx4 v[198:199], off
	s_waitcnt vmcnt(8)
	s_waitcnt lgkmcnt(0)
	s_setprio 1
	v_mfma_f32_16x16x128_f8f6f4 v[78:81], v[2:9], v[222:229], v[78:81]
	v_mfma_f32_16x16x128_f8f6f4 v[74:77], v[10:17], v[222:229], v[74:77]
	v_mfma_f32_16x16x128_f8f6f4 v[70:73], v[2:9], v[230:237], v[70:73]
	v_mfma_f32_16x16x128_f8f6f4 v[66:69], v[10:17], v[230:237], v[66:69]
	v_mfma_f32_16x16x128_f8f6f4 v[62:65], v[2:9], v[238:245], v[62:65]
	v_mfma_f32_16x16x128_f8f6f4 v[58:61], v[10:17], v[238:245], v[58:61]
	v_mfma_f32_16x16x128_f8f6f4 v[54:57], v[2:9], v[246:253], v[54:57]
	v_mfma_f32_16x16x128_f8f6f4 v[50:53], v[10:17], v[246:253], v[50:53]
	s_setprio 0
	s_setprio 1
	v_mfma_f32_16x16x128_f8f6f4 v[46:49], v[18:25], v[222:229], v[46:49]
	v_mfma_f32_16x16x128_f8f6f4 v[42:45], v[26:33], v[222:229], v[42:45]
	v_mfma_f32_16x16x128_f8f6f4 v[38:41], v[18:25], v[230:237], v[38:41]
	v_mfma_f32_16x16x128_f8f6f4 v[34:37], v[26:33], v[230:237], v[34:37]
	v_mfma_f32_16x16x128_f8f6f4 v[146:149], v[18:25], v[238:245], v[146:149]
	v_mfma_f32_16x16x128_f8f6f4 v[150:153], v[26:33], v[238:245], v[150:153]
	v_mfma_f32_16x16x128_f8f6f4 v[154:157], v[18:25], v[246:253], v[154:157]
	v_mfma_f32_16x16x128_f8f6f4 v[158:161], v[26:33], v[246:253], v[158:161]
	s_setprio 0
	s_barrier
	s_add_i32 s69, s69, 2
	s_add_u32 s21, s21, 0x10000
	s_addc_u32 s68, s68, 0
	s_cmp_gt_u32 s69, 13
	s_cbranch_scc1 .LBB0_1062
	s_mov_b64 s[30:31], s[28:29]
	s_branch .LBB0_1058

; #define PG8_STAGE(bufoff, gbase, voff) do { _Pragma("unroll") for (int _i = 0; _i < 2; ++_i) \
;         __builtin_amdgcn_global_load_lds((const unsigned*)((const char*)(gbase) + (voff)[_i]), (PG8_LAS unsigned*)(lds + (bufoff) + ldsw + _i * 8192), 16, 0, 0); } while (0)
; #define PG8_WAIT_V(n) asm volatile("s_waitcnt vmcnt(" #n ")" ::: "memory")
; #define PG8_WAIT_L(n) asm volatile("s_waitcnt lgkmcnt(" #n ")" ::: "memory")
; #define PG8_BAR __builtin_amdgcn_s_barrier()
; #define PG8_SCHED __builtin_amdgcn_sched_barrier(0)
; template <class Epi, class Sched, bool ALIGN_EPI = true, bool F8 = false>
; __device__ __forceinline__ void gemm_phase(PG8_LAS unsigned char* lds, const Sched& S, const Epi& E) {
;     ...
;     f32x4 acc[2][2][4][2];
; #pragma unroll
;     for (int a = 0; a < 2; ++a)
; #pragma unroll
;         for (int b = 0; b < 2; ++b)
; #pragma unroll
;             for (int m = 0; m < 4; ++m)
; #pragma unroll
;                 for (int n = 0; n < 2; ++n) acc[a][b][m][n] = (f32x4){0.f, 0.f, 0.f, 0.f};
;     ...
;             PG8_LDB(B0, 0, 0); PG8_LDB(B1, 0, 1); PG8_SCHED; PG8_LDA(At, 0, 0); PG8_STAGE(PG8_SA(1, 1), a1, voffA[1]);
;             PG8_WAIT_V(8); PG8_WAIT_L(0); PG8_BAR; PG8_MMA(0, 0, At, B0); PG8_MMA(0, 1, At, B1); PG8_BAR; PG8_SCHED;
;             PG8_LDA(At, 0, 1); PG8_STAGE(PG8_SB(0, 0), b2, voffB[0]); PG8_STAGE(PG8_SB(0, 1), b2, voffB[1]); PG8_STAGE(PG8_SA(0, 0), a2, vA2[0]);
;             PG8_WAIT_V(8); PG8_WAIT_L(0); PG8_BAR; PG8_MMA(1, 0, At, B0); PG8_MMA(1, 1, At, B1); PG8_BAR; PG8_SCHED;
;             PG8_LDB(B0, 1, 0); PG8_LDB(B1, 1, 1); PG8_SCHED; PG8_LDA(At, 1, 0); PG8_STAGE(PG8_SA(0, 1), a2, vA2[1]);
;             PG8_WAIT_V(8); PG8_WAIT_L(0); PG8_BAR; PG8_MMA(0, 0, At, B0); PG8_MMA(0, 1, At, B1); PG8_BAR; PG8_SCHED;
;             PG8_LDA(At, 1, 1); PG8_STAGE(PG8_SB(1, 0), b3, voffB[0]); PG8_STAGE(PG8_SB(1, 1), b3, voffB[1]); PG8_STAGE(PG8_SA(1, 0), a3, vA2[0]);
;             PG8_WAIT_V(8); PG8_WAIT_L(0); PG8_BAR; PG8_MMA(1, 0, At, B0); PG8_MMA(1, 1, At, B1); PG8_BAR; PG8_SCHED;
.Lpk1_1060:
	v_add_u32_e32 v2, s12, v210
	v_add_u32_e32 v14, s62, v210
	s_add_u32 s28, s30, 0x100
	ds_read_b128 v[18:21], v2
	ds_read_b128 v[22:25], v2 offset:1024
	ds_read_b128 v[26:29], v2 offset:2048
	ds_read_b128 v[30:33], v2 offset:3072
	ds_read_b128 v[2:5], v14
	ds_read_b128 v[6:9], v14 offset:1024
	ds_read_b128 v[10:13], v14 offset:2048
	ds_read_b128 v[14:17], v14 offset:3072
	s_addc_u32 s29, s31, 0
	s_and_b64 s[42:43], s[40:41], exec
	s_cselect_b32 s42, 0, s28
	s_cselect_b32 s43, 0, s29
	s_add_u32 s42, s6, s42
	s_addc_u32 s43, s7, s43
	s_and_b64 s[40:41], s[40:41], exec
	s_cselect_b32 s41, s25, s68
	s_cselect_b32 s40, s24, s21
	v_lshl_add_u64 v[204:205], v[196:197], 0, s[30:31]
	s_add_i32 m0, s52, 0xc000
	ds_read_b128 v[222:225], v213
	ds_read_b128 v[226:229], v213 offset:1024
	ds_read_b128 v[230:233], v213 offset:2048
	ds_read_b128 v[234:237], v213 offset:3072
	ds_read_b128 v[238:241], v213 offset:4096
	ds_read_b128 v[242:245], v213 offset:5120
	ds_read_b128 v[246:249], v213 offset:6144
	ds_read_b128 v[250:253], v213 offset:7168
	global_load_lds_dwordx4 v[204:205], off
	v_lshl_add_u64 v[204:205], v[194:195], 0, s[30:31]
	s_add_i32 m0, s52, 0xe000
	s_nop 0
	global_load_lds_dwordx4 v[204:205], off
	s_waitcnt vmcnt(8)
	s_waitcnt lgkmcnt(0)
	s_barrier
	s_setprio 2
	v_mfma_f32_16x16x128_f8f6f4 v[142:145], v[18:25], v[222:229], 0
	v_mfma_f32_16x16x128_f8f6f4 v[138:141], v[26:33], v[222:229], 0
	v_mfma_f32_16x16x128_f8f6f4 v[134:137], v[18:25], v[230:237], 0
	v_mfma_f32_16x16x128_f8f6f4 v[130:133], v[26:33], v[230:237], 0
	v_mfma_f32_16x16x128_f8f6f4 v[126:129], v[18:25], v[238:245], 0
	v_mfma_f32_16x16x128_f8f6f4 v[122:125], v[26:33], v[238:245], 0
	v_mfma_f32_16x16x128_f8f6f4 v[118:121], v[18:25], v[246:253], 0
	v_mfma_f32_16x16x128_f8f6f4 v[114:117], v[26:33], v[246:253], 0
	s_setprio 0
	s_setprio 2
	v_mfma_f32_16x16x128_f8f6f4 v[110:113], v[2:9], v[222:229], 0
	v_mfma_f32_16x16x128_f8f6f4 v[106:109], v[10:17], v[222:229], 0
	v_mfma_f32_16x16x128_f8f6f4 v[102:105], v[2:9], v[230:237], 0
	v_mfma_f32_16x16x128_f8f6f4 v[98:101], v[10:17], v[230:237], 0
	v_mfma_f32_16x16x128_f8f6f4 v[94:97], v[2:9], v[238:245], 0
	v_mfma_f32_16x16x128_f8f6f4 v[90:93], v[10:17], v[238:245], 0
	v_mfma_f32_16x16x128_f8f6f4 v[86:89], v[2:9], v[246:253], 0
	v_mfma_f32_16x16x128_f8f6f4 v[82:85], v[10:17], v[246:253], 0
	s_setprio 0
	s_add_i32 s30, s12, s48
	v_lshl_add_u64 v[204:205], s[40:41], 0, v[162:163]
	s_mov_b32 m0, s30
	ds_read_b128 v[222:225], v213 offset:16384
	ds_read_b128 v[226:229], v213 offset:17408
	ds_read_b128 v[230:233], v213 offset:18432
	ds_read_b128 v[234:237], v213 offset:19456
	ds_read_b128 v[238:241], v213 offset:20480
	ds_read_b128 v[242:245], v213 offset:21504
	ds_read_b128 v[246:249], v213 offset:22528
	ds_read_b128 v[250:253], v213 offset:23552
	global_load_lds_dwordx4 v[204:205], off
	v_lshl_add_u64 v[204:205], s[40:41], 0, v[164:165]
	s_add_i32 m0, s30, 0x2000
	s_add_i32 s30, s62, s48
	global_load_lds_dwordx4 v[204:205], off
	v_lshl_add_u64 v[204:205], s[40:41], 0, v[166:167]
	s_mov_b32 m0, s30
	v_mov_b32_e32 v203, v171
	global_load_lds_dwordx4 v[204:205], off
	v_lshl_add_u64 v[204:205], s[40:41], 0, v[168:169]
	s_add_i32 m0, s30, 0x2000
	s_nop 0
	global_load_lds_dwordx4 v[204:205], off
	s_mov_b32 m0, s52
	v_lshl_add_u64 v[204:205], s[42:43], 0, v[170:171]
	global_load_lds_dwordx4 v170, s[42:43]
	s_mov_b32 m0, s53
	s_nop 0
	global_load_lds_dwordx4 v202, s[42:43]
	s_waitcnt vmcnt(8)
	s_waitcnt lgkmcnt(0)
	v_lshl_add_u64 v[202:203], s[42:43], 0, v[202:203]
	s_barrier
	s_setprio 2
	v_mfma_f32_16x16x128_f8f6f4 v[78:81], v[18:25], v[222:229], 0
	v_mfma_f32_16x16x128_f8f6f4 v[74:77], v[26:33], v[222:229], 0
	v_mfma_f32_16x16x128_f8f6f4 v[70:73], v[18:25], v[230:237], 0
	v_mfma_f32_16x16x128_f8f6f4 v[66:69], v[26:33], v[230:237], 0
	v_mfma_f32_16x16x128_f8f6f4 v[62:65], v[18:25], v[238:245], 0
	v_mfma_f32_16x16x128_f8f6f4 v[58:61], v[26:33], v[238:245], 0
	v_mfma_f32_16x16x128_f8f6f4 v[54:57], v[18:25], v[246:253], 0
	v_mfma_f32_16x16x128_f8f6f4 v[50:53], v[26:33], v[246:253], 0
	s_setprio 0
	s_setprio 2
	v_mfma_f32_16x16x128_f8f6f4 v[46:49], v[2:9], v[222:229], 0
	v_mfma_f32_16x16x128_f8f6f4 v[42:45], v[10:17], v[222:229], 0
	v_mfma_f32_16x16x128_f8f6f4 v[38:41], v[2:9], v[230:237], 0
	v_mfma_f32_16x16x128_f8f6f4 v[34:37], v[10:17], v[230:237], 0
	v_mfma_f32_16x16x128_f8f6f4 v[146:149], v[2:9], v[238:245], 0
	v_mfma_f32_16x16x128_f8f6f4 v[150:153], v[10:17], v[238:245], 0
	v_mfma_f32_16x16x128_f8f6f4 v[154:157], v[2:9], v[246:253], 0
	v_mfma_f32_16x16x128_f8f6f4 v[158:161], v[10:17], v[246:253], 0
	s_setprio 0
	s_add_i32 s70, 0, 0x18000
	s_add_i32 s71, 0, 0x1c000
	v_add_u32_e32 v14, s70, v210
	v_add_u32_e32 v30, s71, v210
	ds_read_b128 v[2:5], v14
	ds_read_b128 v[6:9], v14 offset:1024
	ds_read_b128 v[10:13], v14 offset:2048
	ds_read_b128 v[14:17], v14 offset:3072
	ds_read_b128 v[18:21], v30
	ds_read_b128 v[22:25], v30 offset:1024
	ds_read_b128 v[26:29], v30 offset:2048
	ds_read_b128 v[30:33], v30 offset:3072
	s_mov_b32 m0, s58
	v_lshl_add_u64 v[200:201], s[42:43], 0, v[200:201]
	ds_read_b128 v[222:225], v213 offset:32768
	ds_read_b128 v[226:229], v213 offset:33792
	ds_read_b128 v[230:233], v213 offset:34816
	ds_read_b128 v[234:237], v213 offset:35840
	ds_read_b128 v[238:241], v213 offset:36864
	ds_read_b128 v[242:245], v213 offset:37888
	ds_read_b128 v[246:249], v213 offset:38912
	ds_read_b128 v[250:253], v213 offset:39936
	global_load_lds_dwordx4 v[200:201], off
	v_lshl_add_u64 v[198:199], s[42:43], 0, v[198:199]
	s_mov_b32 m0, s59
	s_nop 0
	global_load_lds_dwordx4 v[198:199], off
	s_waitcnt vmcnt(8)
	s_waitcnt lgkmcnt(0)
	s_barrier
; #define PG8_STAGE(bufoff, gbase, voff) do { _Pragma("unroll") for (int _i = 0; _i < 2; ++_i) \
;         __builtin_amdgcn_global_load_lds((const unsigned*)((const char*)(gbase) + (voff)[_i]), (PG8_LAS unsigned*)(lds + (bufoff) + ldsw + _i * 8192), 16, 0, 0); } while (0)
; #define PG8_WAIT_V(n) asm volatile("s_waitcnt vmcnt(" #n ")" ::: "memory")
; #define PG8_WAIT_L(n) asm volatile("s_waitcnt lgkmcnt(" #n ")" ::: "memory")
; #define PG8_BAR __builtin_amdgcn_s_barrier()
; #define PG8_SCHED __builtin_amdgcn_sched_barrier(0)
; template <class Epi, class Sched, bool ALIGN_EPI = true, bool F8 = false>
; __device__ __forceinline__ void gemm_phase(PG8_LAS unsigned char* lds, const Sched& S, const Epi& E) {
;     ...
;             PG8_LDB(B0, 0, 0); PG8_LDB(B1, 0, 1); PG8_SCHED; PG8_LDA(At, 0, 0); PG8_STAGE(PG8_SA(1, 1), a1, voffA[1]);
;             PG8_WAIT_V(8); PG8_WAIT_L(0); PG8_BAR; PG8_MMA(0, 0, At, B0); PG8_MMA(0, 1, At, B1); PG8_BAR; PG8_SCHED;
;             PG8_LDA(At, 0, 1); PG8_STAGE(PG8_SB(0, 0), b2, voffB[0]); PG8_STAGE(PG8_SB(0, 1), b2, voffB[1]); PG8_STAGE(PG8_SA(0, 0), a2, vA2[0]);
;             PG8_WAIT_V(8); PG8_WAIT_L(0); PG8_BAR; PG8_MMA(1, 0, At, B0); PG8_MMA(1, 1, At, B1); PG8_BAR; PG8_SCHED;
;             PG8_LDB(B0, 1, 0); PG8_LDB(B1, 1, 1); PG8_SCHED; PG8_LDA(At, 1, 0); PG8_STAGE(PG8_SA(0, 1), a2, vA2[1]);
;             PG8_WAIT_V(8); PG8_WAIT_L(0); PG8_BAR; PG8_MMA(0, 0, At, B0); PG8_MMA(0, 1, At, B1); PG8_BAR; PG8_SCHED;
;             PG8_LDA(At, 1, 1); PG8_STAGE(PG8_SB(1, 0), b3, voffB[0]); PG8_STAGE(PG8_SB(1, 1), b3, voffB[1]); PG8_STAGE(PG8_SA(1, 0), a3, vA2[0]);
;             PG8_WAIT_V(8); PG8_WAIT_L(0); PG8_BAR; PG8_MMA(1, 0, At, B0); PG8_MMA(1, 1, At, B1); PG8_BAR; PG8_SCHED;
	s_setprio 2
	v_mfma_f32_16x16x128_f8f6f4 v[142:145], v[2:9], v[222:229], v[142:145]
	v_mfma_f32_16x16x128_f8f6f4 v[138:141], v[10:17], v[222:229], v[138:141]
	v_mfma_f32_16x16x128_f8f6f4 v[134:137], v[2:9], v[230:237], v[134:137]
	v_mfma_f32_16x16x128_f8f6f4 v[130:133], v[10:17], v[230:237], v[130:133]
	v_mfma_f32_16x16x128_f8f6f4 v[126:129], v[2:9], v[238:245], v[126:129]
	v_mfma_f32_16x16x128_f8f6f4 v[122:125], v[10:17], v[238:245], v[122:125]
	v_mfma_f32_16x16x128_f8f6f4 v[118:121], v[2:9], v[246:253], v[118:121]
	v_mfma_f32_16x16x128_f8f6f4 v[114:117], v[10:17], v[246:253], v[114:117]
	s_setprio 0
	s_setprio 2
	v_mfma_f32_16x16x128_f8f6f4 v[110:113], v[18:25], v[222:229], v[110:113]
	v_mfma_f32_16x16x128_f8f6f4 v[106:109], v[26:33], v[222:229], v[106:109]
	v_mfma_f32_16x16x128_f8f6f4 v[102:105], v[18:25], v[230:237], v[102:105]
	v_mfma_f32_16x16x128_f8f6f4 v[98:101], v[26:33], v[230:237], v[98:101]
	v_mfma_f32_16x16x128_f8f6f4 v[94:97], v[18:25], v[238:245], v[94:97]
	v_mfma_f32_16x16x128_f8f6f4 v[90:93], v[26:33], v[238:245], v[90:93]
	v_mfma_f32_16x16x128_f8f6f4 v[86:89], v[18:25], v[246:253], v[86:89]
	v_mfma_f32_16x16x128_f8f6f4 v[82:85], v[26:33], v[246:253], v[82:85]
	s_setprio 0
	s_add_u32 s30, s40, 0x8000
	s_addc_u32 s31, s41, 0
	s_add_i32 s40, s70, s48
	v_lshl_add_u64 v[198:199], s[30:31], 0, v[162:163]
	s_mov_b32 m0, s40
	ds_read_b128 v[222:225], v213 offset:49152
	ds_read_b128 v[226:229], v213 offset:50176
	ds_read_b128 v[230:233], v213 offset:51200
	ds_read_b128 v[234:237], v213 offset:52224
	ds_read_b128 v[238:241], v213 offset:53248
	ds_read_b128 v[242:245], v213 offset:54272
	ds_read_b128 v[246:249], v213 offset:55296
	ds_read_b128 v[250:253], v213 offset:56320
	global_load_lds_dwordx4 v[198:199], off
	v_lshl_add_u64 v[198:199], s[30:31], 0, v[164:165]
	s_add_i32 m0, s40, 0x2000
	s_add_i32 s40, s71, s48
	global_load_lds_dwordx4 v[198:199], off
	v_lshl_add_u64 v[198:199], s[30:31], 0, v[166:167]
	s_mov_b32 m0, s40
	s_nop 0
	global_load_lds_dwordx4 v[198:199], off
	v_lshl_add_u64 v[198:199], s[30:31], 0, v[168:169]
	s_add_i32 m0, s40, 0x2000
	s_nop 0
	global_load_lds_dwordx4 v[198:199], off
	v_lshl_add_u64 v[198:199], v[204:205], 0, s[18:19]
	s_mov_b32 m0, s60
	s_nop 0
	global_load_lds_dwordx4 v[198:199], off
	v_lshl_add_u64 v[198:199], v[202:203], 0, s[18:19]
	s_mov_b32 m0, s61
	s_nop 0
	global_load_lds_dwordx4 v[198:199], off
	s_waitcnt vmcnt(8)
	s_waitcnt lgkmcnt(0)
	s_barrier
	s_setprio 2
	v_mfma_f32_16x16x128_f8f6f4 v[78:81], v[2:9], v[222:229], v[78:81]
	v_mfma_f32_16x16x128_f8f6f4 v[74:77], v[10:17], v[222:229], v[74:77]
	v_mfma_f32_16x16x128_f8f6f4 v[70:73], v[2:9], v[230:237], v[70:73]
	v_mfma_f32_16x16x128_f8f6f4 v[66:69], v[10:17], v[230:237], v[66:69]
	v_mfma_f32_16x16x128_f8f6f4 v[62:65], v[2:9], v[238:245], v[62:65]
	v_mfma_f32_16x16x128_f8f6f4 v[58:61], v[10:17], v[238:245], v[58:61]
	v_mfma_f32_16x16x128_f8f6f4 v[54:57], v[2:9], v[246:253], v[54:57]
	v_mfma_f32_16x16x128_f8f6f4 v[50:53], v[10:17], v[246:253], v[50:53]
	s_setprio 0
	s_setprio 2
	v_mfma_f32_16x16x128_f8f6f4 v[46:49], v[18:25], v[222:229], v[46:49]
	v_mfma_f32_16x16x128_f8f6f4 v[42:45], v[26:33], v[222:229], v[42:45]
	v_mfma_f32_16x16x128_f8f6f4 v[38:41], v[18:25], v[230:237], v[38:41]
	v_mfma_f32_16x16x128_f8f6f4 v[34:37], v[26:33], v[230:237], v[34:37]
	v_mfma_f32_16x16x128_f8f6f4 v[146:149], v[18:25], v[238:245], v[146:149]
	v_mfma_f32_16x16x128_f8f6f4 v[150:153], v[26:33], v[238:245], v[150:153]
	v_mfma_f32_16x16x128_f8f6f4 v[154:157], v[18:25], v[246:253], v[154:157]
	v_mfma_f32_16x16x128_f8f6f4 v[158:161], v[26:33], v[246:253], v[158:161]
	s_setprio 0
	s_add_i32 s69, s69, 2
	s_add_u32 s21, s21, 0x10000
	s_addc_u32 s68, s68, 0
	s_cmp_gt_u32 s69, 13
	s_cbranch_scc1 .LBB0_1062
	s_mov_b64 s[30:31], s[28:29]
	s_branch .Lh1_1058

; #define PG8_STAGE(bufoff, gbase, voff) do { _Pragma("unroll") for (int _i = 0; _i < 2; ++_i) \
;         __builtin_amdgcn_global_load_lds((const unsigned*)((const char*)(gbase) + (voff)[_i]), (PG8_LAS unsigned*)(lds + (bufoff) + ldsw + _i * 8192), 16, 0, 0); } while (0)
; #define PG8_WAIT_V(n) asm volatile("s_waitcnt vmcnt(" #n ")" ::: "memory")
; #define PG8_WAIT_L(n) asm volatile("s_waitcnt lgkmcnt(" #n ")" ::: "memory")
; #define PG8_BAR __builtin_amdgcn_s_barrier()
; #define PG8_SCHED __builtin_amdgcn_sched_barrier(0)
; template <class Epi, class Sched, bool ALIGN_EPI = true, bool F8 = false>
; __device__ __forceinline__ void gemm_phase(PG8_LAS unsigned char* lds, const Sched& S, const Epi& E) {
;     ...
;             if constexpr (Sched::GATHER) { if (last && has_next) S.a_off(nxt, Rs, Cs, voffAn); }
;             const char* a1 = cA + (size_t)(t + 1) * kstep;
;             const char* a2 = last ? nA : cA + (size_t)(t + 2) * kstep; const char* b2 = last ? nB : cB + (size_t)(t + 2) * kstepB;
;             const char* a3 = a2 + kstep; const char* b3 = b2 + kstepB;
;             unsigned vA2[2][2];
; #pragma unroll
;             for (int h = 0; h < 2; ++h)
; #pragma unroll
;                 for (int i = 0; i < 2; ++i) { if constexpr (Sched::GATHER) vA2[h][i] = (last && has_next) ? voffAn[h][i] : voffA[h][i]; else vA2[h][i] = voffA[h][i]; }
;             PG8_LDB(B0, 0, 0); PG8_LDB(B1, 0, 1); PG8_SCHED; PG8_LDA(At, 0, 0); PG8_STAGE(PG8_SA(1, 1), a1, voffA[1]);
;             PG8_WAIT_V(8); PG8_WAIT_L(0); PG8_BAR; PG8_MMA(0, 0, At, B0); PG8_MMA(0, 1, At, B1); PG8_BAR; PG8_SCHED;
;             PG8_LDA(At, 0, 1); PG8_STAGE(PG8_SB(0, 0), b2, voffB[0]); PG8_STAGE(PG8_SB(0, 1), b2, voffB[1]); PG8_STAGE(PG8_SA(0, 0), a2, vA2[0]);
;             PG8_WAIT_V(8); PG8_WAIT_L(0); PG8_BAR; PG8_MMA(1, 0, At, B0); PG8_MMA(1, 1, At, B1); PG8_BAR; PG8_SCHED;
;             PG8_LDB(B0, 1, 0); PG8_LDB(B1, 1, 1); PG8_SCHED; PG8_LDA(At, 1, 0); PG8_STAGE(PG8_SA(0, 1), a2, vA2[1]);
;             PG8_WAIT_V(8); PG8_WAIT_L(0); PG8_BAR; PG8_MMA(0, 0, At, B0); PG8_MMA(0, 1, At, B1); PG8_BAR; PG8_SCHED;
;             PG8_LDA(At, 1, 1); PG8_STAGE(PG8_SB(1, 0), b3, voffB[0]); PG8_STAGE(PG8_SB(1, 1), b3, voffB[1]); PG8_STAGE(PG8_SA(1, 0), a3, vA2[0]);
;             PG8_WAIT_V(8); PG8_WAIT_L(0); PG8_BAR; PG8_MMA(1, 0, At, B0); PG8_MMA(1, 1, At, B1); PG8_BAR; PG8_SCHED;
.Lh1_1060:
	v_add_u32_e32 v2, s12, v210
	v_add_u32_e32 v14, s62, v210
	s_add_u32 s28, s30, 0x100
	ds_read_b128 v[18:21], v2
	ds_read_b128 v[22:25], v2 offset:1024
	ds_read_b128 v[26:29], v2 offset:2048
	ds_read_b128 v[30:33], v2 offset:3072
	ds_read_b128 v[2:5], v14
	ds_read_b128 v[6:9], v14 offset:1024
	ds_read_b128 v[10:13], v14 offset:2048
	ds_read_b128 v[14:17], v14 offset:3072
	s_addc_u32 s29, s31, 0
	s_and_b64 s[42:43], s[40:41], exec
	s_cselect_b32 s42, 0, s28
	s_cselect_b32 s43, 0, s29
	s_add_u32 s42, s6, s42
	s_addc_u32 s43, s7, s43
	s_and_b64 s[40:41], s[40:41], exec
	s_cselect_b32 s41, s25, s68
	s_cselect_b32 s40, s24, s21
	v_lshl_add_u64 v[204:205], v[196:197], 0, s[30:31]
	s_add_i32 m0, s52, 0xc000
	ds_read_b128 v[222:225], v213
	ds_read_b128 v[226:229], v213 offset:1024
	ds_read_b128 v[230:233], v213 offset:2048
	ds_read_b128 v[234:237], v213 offset:3072
	ds_read_b128 v[238:241], v213 offset:4096
	ds_read_b128 v[242:245], v213 offset:5120
	ds_read_b128 v[246:249], v213 offset:6144
	ds_read_b128 v[250:253], v213 offset:7168
	global_load_lds_dwordx4 v[204:205], off
	v_lshl_add_u64 v[204:205], v[194:195], 0, s[30:31]
	s_add_i32 m0, s52, 0xe000
	s_nop 0
	global_load_lds_dwordx4 v[204:205], off
	s_waitcnt vmcnt(8)
	s_waitcnt lgkmcnt(0)
	s_barrier
	s_setprio 2
	v_mfma_f32_16x16x128_f8f6f4 v[142:145], v[18:25], v[222:229], v[142:145]
	v_mfma_f32_16x16x128_f8f6f4 v[138:141], v[26:33], v[222:229], v[138:141]
	v_mfma_f32_16x16x128_f8f6f4 v[134:137], v[18:25], v[230:237], v[134:137]
	v_mfma_f32_16x16x128_f8f6f4 v[130:133], v[26:33], v[230:237], v[130:133]
	v_mfma_f32_16x16x128_f8f6f4 v[126:129], v[18:25], v[238:245], v[126:129]
	v_mfma_f32_16x16x128_f8f6f4 v[122:125], v[26:33], v[238:245], v[122:125]
	v_mfma_f32_16x16x128_f8f6f4 v[118:121], v[18:25], v[246:253], v[118:121]
	v_mfma_f32_16x16x128_f8f6f4 v[114:117], v[26:33], v[246:253], v[114:117]
	s_setprio 0
	s_setprio 2
	v_mfma_f32_16x16x128_f8f6f4 v[110:113], v[2:9], v[222:229], v[110:113]
	v_mfma_f32_16x16x128_f8f6f4 v[106:109], v[10:17], v[222:229], v[106:109]
	v_mfma_f32_16x16x128_f8f6f4 v[102:105], v[2:9], v[230:237], v[102:105]
	v_mfma_f32_16x16x128_f8f6f4 v[98:101], v[10:17], v[230:237], v[98:101]
	v_mfma_f32_16x16x128_f8f6f4 v[94:97], v[2:9], v[238:245], v[94:97]
	v_mfma_f32_16x16x128_f8f6f4 v[90:93], v[10:17], v[238:245], v[90:93]
	v_mfma_f32_16x16x128_f8f6f4 v[86:89], v[2:9], v[246:253], v[86:89]
	v_mfma_f32_16x16x128_f8f6f4 v[82:85], v[10:17], v[246:253], v[82:85]
	s_setprio 0
	s_add_i32 s30, s12, s48
	v_lshl_add_u64 v[204:205], s[40:41], 0, v[162:163]
	s_mov_b32 m0, s30
	ds_read_b128 v[222:225], v213 offset:16384
	ds_read_b128 v[226:229], v213 offset:17408
	ds_read_b128 v[230:233], v213 offset:18432
	ds_read_b128 v[234:237], v213 offset:19456
	ds_read_b128 v[238:241], v213 offset:20480
	ds_read_b128 v[242:245], v213 offset:21504
	ds_read_b128 v[246:249], v213 offset:22528
	ds_read_b128 v[250:253], v213 offset:23552
	global_load_lds_dwordx4 v[204:205], off
	v_lshl_add_u64 v[204:205], s[40:41], 0, v[164:165]
	s_add_i32 m0, s30, 0x2000
	s_add_i32 s30, s62, s48
	global_load_lds_dwordx4 v[204:205], off
	v_lshl_add_u64 v[204:205], s[40:41], 0, v[166:167]
	s_mov_b32 m0, s30
	v_mov_b32_e32 v203, v171
	global_load_lds_dwordx4 v[204:205], off
	v_lshl_add_u64 v[204:205], s[40:41], 0, v[168:169]
	s_add_i32 m0, s30, 0x2000
	s_nop 0
	global_load_lds_dwordx4 v[204:205], off
	s_mov_b32 m0, s52
	v_lshl_add_u64 v[204:205], s[42:43], 0, v[170:171]
	global_load_lds_dwordx4 v170, s[42:43]
	s_mov_b32 m0, s53
	s_nop 0
	global_load_lds_dwordx4 v202, s[42:43]
	s_waitcnt vmcnt(8)
	s_waitcnt lgkmcnt(0)
	v_lshl_add_u64 v[202:203], s[42:43], 0, v[202:203]
	s_barrier
	s_setprio 2
	v_mfma_f32_16x16x128_f8f6f4 v[78:81], v[18:25], v[222:229], v[78:81]
	v_mfma_f32_16x16x128_f8f6f4 v[74:77], v[26:33], v[222:229], v[74:77]
	v_mfma_f32_16x16x128_f8f6f4 v[70:73], v[18:25], v[230:237], v[70:73]
	v_mfma_f32_16x16x128_f8f6f4 v[66:69], v[26:33], v[230:237], v[66:69]
	v_mfma_f32_16x16x128_f8f6f4 v[62:65], v[18:25], v[238:245], v[62:65]
	v_mfma_f32_16x16x128_f8f6f4 v[58:61], v[26:33], v[238:245], v[58:61]
	v_mfma_f32_16x16x128_f8f6f4 v[54:57], v[18:25], v[246:253], v[54:57]
	v_mfma_f32_16x16x128_f8f6f4 v[50:53], v[26:33], v[246:253], v[50:53]
	s_setprio 0
	s_setprio 2
	v_mfma_f32_16x16x128_f8f6f4 v[46:49], v[2:9], v[222:229], v[46:49]
	v_mfma_f32_16x16x128_f8f6f4 v[42:45], v[10:17], v[222:229], v[42:45]
	v_mfma_f32_16x16x128_f8f6f4 v[38:41], v[2:9], v[230:237], v[38:41]
	v_mfma_f32_16x16x128_f8f6f4 v[34:37], v[10:17], v[230:237], v[34:37]
	v_mfma_f32_16x16x128_f8f6f4 v[146:149], v[2:9], v[238:245], v[146:149]
	v_mfma_f32_16x16x128_f8f6f4 v[150:153], v[10:17], v[238:245], v[150:153]
	v_mfma_f32_16x16x128_f8f6f4 v[154:157], v[2:9], v[246:253], v[154:157]
	v_mfma_f32_16x16x128_f8f6f4 v[158:161], v[10:17], v[246:253], v[158:161]
	s_setprio 0
	s_add_i32 s70, 0, 0x18000
	s_add_i32 s71, 0, 0x1c000
	v_add_u32_e32 v14, s70, v210
	v_add_u32_e32 v30, s71, v210
	ds_read_b128 v[2:5], v14
	ds_read_b128 v[6:9], v14 offset:1024
	ds_read_b128 v[10:13], v14 offset:2048
	ds_read_b128 v[14:17], v14 offset:3072
	ds_read_b128 v[18:21], v30
	ds_read_b128 v[22:25], v30 offset:1024
	ds_read_b128 v[26:29], v30 offset:2048
	ds_read_b128 v[30:33], v30 offset:3072
	s_mov_b32 m0, s58
	v_lshl_add_u64 v[200:201], s[42:43], 0, v[200:201]
	ds_read_b128 v[222:225], v213 offset:32768
	ds_read_b128 v[226:229], v213 offset:33792
	ds_read_b128 v[230:233], v213 offset:34816
	ds_read_b128 v[234:237], v213 offset:35840
	ds_read_b128 v[238:241], v213 offset:36864
	ds_read_b128 v[242:245], v213 offset:37888
	ds_read_b128 v[246:249], v213 offset:38912
	ds_read_b128 v[250:253], v213 offset:39936
	global_load_lds_dwordx4 v[200:201], off
	v_lshl_add_u64 v[198:199], s[42:43], 0, v[198:199]
	s_mov_b32 m0, s59
	s_nop 0
	global_load_lds_dwordx4 v[198:199], off
	s_waitcnt vmcnt(8)
	s_waitcnt lgkmcnt(0)
	s_barrier
; #define PG8_STAGE(bufoff, gbase, voff) do { _Pragma("unroll") for (int _i = 0; _i < 2; ++_i) \
;         __builtin_amdgcn_global_load_lds((const unsigned*)((const char*)(gbase) + (voff)[_i]), (PG8_LAS unsigned*)(lds + (bufoff) + ldsw + _i * 8192), 16, 0, 0); } while (0)
; #define PG8_WAIT_V(n) asm volatile("s_waitcnt vmcnt(" #n ")" ::: "memory")
; #define PG8_WAIT_L(n) asm volatile("s_waitcnt lgkmcnt(" #n ")" ::: "memory")
; #define PG8_BAR __builtin_amdgcn_s_barrier()
; #define PG8_SCHED __builtin_amdgcn_sched_barrier(0)
; template <class Epi, class Sched, bool ALIGN_EPI = true, bool F8 = false>
; __device__ __forceinline__ void gemm_phase(PG8_LAS unsigned char* lds, const Sched& S, const Epi& E) {
;     ...
;             PG8_LDB(B0, 0, 0); PG8_LDB(B1, 0, 1); PG8_SCHED; PG8_LDA(At, 0, 0); PG8_STAGE(PG8_SA(1, 1), a1, voffA[1]);
;             PG8_WAIT_V(8); PG8_WAIT_L(0); PG8_BAR; PG8_MMA(0, 0, At, B0); PG8_MMA(0, 1, At, B1); PG8_BAR; PG8_SCHED;
;             PG8_LDA(At, 0, 1); PG8_STAGE(PG8_SB(0, 0), b2, voffB[0]); PG8_STAGE(PG8_SB(0, 1), b2, voffB[1]); PG8_STAGE(PG8_SA(0, 0), a2, vA2[0]);
;             PG8_WAIT_V(8); PG8_WAIT_L(0); PG8_BAR; PG8_MMA(1, 0, At, B0); PG8_MMA(1, 1, At, B1); PG8_BAR; PG8_SCHED;
;             PG8_LDB(B0, 1, 0); PG8_LDB(B1, 1, 1); PG8_SCHED; PG8_LDA(At, 1, 0); PG8_STAGE(PG8_SA(0, 1), a2, vA2[1]);
;             PG8_WAIT_V(8); PG8_WAIT_L(0); PG8_BAR; PG8_MMA(0, 0, At, B0); PG8_MMA(0, 1, At, B1); PG8_BAR; PG8_SCHED;
;             PG8_LDA(At, 1, 1); PG8_STAGE(PG8_SB(1, 0), b3, voffB[0]); PG8_STAGE(PG8_SB(1, 1), b3, voffB[1]); PG8_STAGE(PG8_SA(1, 0), a3, vA2[0]);
;             PG8_WAIT_V(8); PG8_WAIT_L(0); PG8_BAR; PG8_MMA(1, 0, At, B0); PG8_MMA(1, 1, At, B1); PG8_BAR; PG8_SCHED;
	s_setprio 2
	v_mfma_f32_16x16x128_f8f6f4 v[142:145], v[2:9], v[222:229], v[142:145]
	v_mfma_f32_16x16x128_f8f6f4 v[138:141], v[10:17], v[222:229], v[138:141]
	v_mfma_f32_16x16x128_f8f6f4 v[134:137], v[2:9], v[230:237], v[134:137]
	v_mfma_f32_16x16x128_f8f6f4 v[130:133], v[10:17], v[230:237], v[130:133]
	v_mfma_f32_16x16x128_f8f6f4 v[126:129], v[2:9], v[238:245], v[126:129]
	v_mfma_f32_16x16x128_f8f6f4 v[122:125], v[10:17], v[238:245], v[122:125]
	v_mfma_f32_16x16x128_f8f6f4 v[118:121], v[2:9], v[246:253], v[118:121]
	v_mfma_f32_16x16x128_f8f6f4 v[114:117], v[10:17], v[246:253], v[114:117]
	s_setprio 0
	s_setprio 2
	v_mfma_f32_16x16x128_f8f6f4 v[110:113], v[18:25], v[222:229], v[110:113]
	v_mfma_f32_16x16x128_f8f6f4 v[106:109], v[26:33], v[222:229], v[106:109]
	v_mfma_f32_16x16x128_f8f6f4 v[102:105], v[18:25], v[230:237], v[102:105]
	v_mfma_f32_16x16x128_f8f6f4 v[98:101], v[26:33], v[230:237], v[98:101]
	v_mfma_f32_16x16x128_f8f6f4 v[94:97], v[18:25], v[238:245], v[94:97]
	v_mfma_f32_16x16x128_f8f6f4 v[90:93], v[26:33], v[238:245], v[90:93]
	v_mfma_f32_16x16x128_f8f6f4 v[86:89], v[18:25], v[246:253], v[86:89]
	v_mfma_f32_16x16x128_f8f6f4 v[82:85], v[26:33], v[246:253], v[82:85]
	s_setprio 0
	s_add_u32 s30, s40, 0x8000
	s_addc_u32 s31, s41, 0
	s_add_i32 s40, s70, s48
	v_lshl_add_u64 v[198:199], s[30:31], 0, v[162:163]
	s_mov_b32 m0, s40
	ds_read_b128 v[222:225], v213 offset:49152
	ds_read_b128 v[226:229], v213 offset:50176
	ds_read_b128 v[230:233], v213 offset:51200
	ds_read_b128 v[234:237], v213 offset:52224
	ds_read_b128 v[238:241], v213 offset:53248
	ds_read_b128 v[242:245], v213 offset:54272
	ds_read_b128 v[246:249], v213 offset:55296
	ds_read_b128 v[250:253], v213 offset:56320
	global_load_lds_dwordx4 v[198:199], off
	v_lshl_add_u64 v[198:199], s[30:31], 0, v[164:165]
	s_add_i32 m0, s40, 0x2000
	s_add_i32 s40, s71, s48
	global_load_lds_dwordx4 v[198:199], off
	v_lshl_add_u64 v[198:199], s[30:31], 0, v[166:167]
	s_mov_b32 m0, s40
	s_nop 0
	global_load_lds_dwordx4 v[198:199], off
	v_lshl_add_u64 v[198:199], s[30:31], 0, v[168:169]
	s_add_i32 m0, s40, 0x2000
	s_nop 0
	global_load_lds_dwordx4 v[198:199], off
	v_lshl_add_u64 v[198:199], v[204:205], 0, s[18:19]
	s_mov_b32 m0, s60
	s_nop 0
	global_load_lds_dwordx4 v[198:199], off
	v_lshl_add_u64 v[198:199], v[202:203], 0, s[18:19]
	s_mov_b32 m0, s61
	s_nop 0
	global_load_lds_dwordx4 v[198:199], off
	s_waitcnt vmcnt(8)
	s_waitcnt lgkmcnt(0)
	s_barrier
	s_setprio 2
	v_mfma_f32_16x16x128_f8f6f4 v[78:81], v[2:9], v[222:229], v[78:81]
	v_mfma_f32_16x16x128_f8f6f4 v[74:77], v[10:17], v[222:229], v[74:77]
	v_mfma_f32_16x16x128_f8f6f4 v[70:73], v[2:9], v[230:237], v[70:73]
	v_mfma_f32_16x16x128_f8f6f4 v[66:69], v[10:17], v[230:237], v[66:69]
	v_mfma_f32_16x16x128_f8f6f4 v[62:65], v[2:9], v[238:245], v[62:65]
	v_mfma_f32_16x16x128_f8f6f4 v[58:61], v[10:17], v[238:245], v[58:61]
	v_mfma_f32_16x16x128_f8f6f4 v[54:57], v[2:9], v[246:253], v[54:57]
	v_mfma_f32_16x16x128_f8f6f4 v[50:53], v[10:17], v[246:253], v[50:53]
	s_setprio 0
	s_setprio 2
	v_mfma_f32_16x16x128_f8f6f4 v[46:49], v[18:25], v[222:229], v[46:49]
	v_mfma_f32_16x16x128_f8f6f4 v[42:45], v[26:33], v[222:229], v[42:45]
	v_mfma_f32_16x16x128_f8f6f4 v[38:41], v[18:25], v[230:237], v[38:41]
	v_mfma_f32_16x16x128_f8f6f4 v[34:37], v[26:33], v[230:237], v[34:37]
	v_mfma_f32_16x16x128_f8f6f4 v[146:149], v[18:25], v[238:245], v[146:149]
	v_mfma_f32_16x16x128_f8f6f4 v[150:153], v[26:33], v[238:245], v[150:153]
	v_mfma_f32_16x16x128_f8f6f4 v[154:157], v[18:25], v[246:253], v[154:157]
	v_mfma_f32_16x16x128_f8f6f4 v[158:161], v[26:33], v[246:253], v[158:161]
	s_setprio 0
	s_add_i32 s69, s69, 2
	s_add_u32 s21, s21, 0x10000
	s_addc_u32 s68, s68, 0
	s_cmp_gt_u32 s69, 13
	s_cbranch_scc1 .LBB0_1062
	s_mov_b64 s[30:31], s[28:29]
	s_branch .Lh1_1058

; #define PG8_STAGE(bufoff, gbase, voff) do { _Pragma("unroll") for (int _i = 0; _i < 2; ++_i) \
;         __builtin_amdgcn_global_load_lds((const unsigned*)((const char*)(gbase) + (voff)[_i]), (PG8_LAS unsigned*)(lds + (bufoff) + ldsw + _i * 8192), 16, 0, 0); } while (0)
; #define PG8_WAIT_V(n) asm volatile("s_waitcnt vmcnt(" #n ")" ::: "memory")
; #define PG8_WAIT_L(n) asm volatile("s_waitcnt lgkmcnt(" #n ")" ::: "memory")
; #define PG8_BAR __builtin_amdgcn_s_barrier()
; #define PG8_SCHED __builtin_amdgcn_sched_barrier(0)
; template <class Epi, class Sched, bool ALIGN_EPI = true, bool F8 = false>
; __device__ __forceinline__ void gemm_phase(PG8_LAS unsigned char* lds, const Sched& S, const Epi& E) {
;     ...
;     f32x4 acc[2][2][4][2];
; #pragma unroll
;     for (int a = 0; a < 2; ++a)
; #pragma unroll
;         for (int b = 0; b < 2; ++b)
; #pragma unroll
;             for (int m = 0; m < 4; ++m)
; #pragma unroll
;                 for (int n = 0; n < 2; ++n) acc[a][b][m][n] = (f32x4){0.f, 0.f, 0.f, 0.f};
;     ...
;             PG8_LDB(B0, 0, 0); PG8_LDB(B1, 0, 1); PG8_SCHED; PG8_LDA(At, 0, 0); PG8_STAGE(PG8_SA(1, 1), a1, voffA[1]);
;             PG8_WAIT_V(8); PG8_WAIT_L(0); PG8_BAR; PG8_MMA(0, 0, At, B0); PG8_MMA(0, 1, At, B1); PG8_BAR; PG8_SCHED;
;             PG8_LDA(At, 0, 1); PG8_STAGE(PG8_SB(0, 0), b2, voffB[0]); PG8_STAGE(PG8_SB(0, 1), b2, voffB[1]); PG8_STAGE(PG8_SA(0, 0), a2, vA2[0]);
;             PG8_WAIT_V(8); PG8_WAIT_L(0); PG8_BAR; PG8_MMA(1, 0, At, B0); PG8_MMA(1, 1, At, B1); PG8_BAR; PG8_SCHED;
;             PG8_LDB(B0, 1, 0); PG8_LDB(B1, 1, 1); PG8_SCHED; PG8_LDA(At, 1, 0); PG8_STAGE(PG8_SA(0, 1), a2, vA2[1]);
;             PG8_WAIT_V(8); PG8_WAIT_L(0); PG8_BAR; PG8_MMA(0, 0, At, B0); PG8_MMA(0, 1, At, B1); PG8_BAR; PG8_SCHED;
;             PG8_LDA(At, 1, 1); PG8_STAGE(PG8_SB(1, 0), b3, voffB[0]); PG8_STAGE(PG8_SB(1, 1), b3, voffB[1]); PG8_STAGE(PG8_SA(1, 0), a3, vA2[0]);
;             PG8_WAIT_V(8); PG8_WAIT_L(0); PG8_BAR; PG8_MMA(1, 0, At, B0); PG8_MMA(1, 1, At, B1); PG8_BAR; PG8_SCHED;
.Lpk0_1138:
	ds_read_b128 v[18:21], v189
	ds_read_b128 v[22:25], v189 offset:1024
	ds_read_b128 v[26:29], v189 offset:2048
	ds_read_b128 v[30:33], v189 offset:3072
	ds_read_b128 v[2:5], v190
	ds_read_b128 v[6:9], v190 offset:1024
	ds_read_b128 v[10:13], v190 offset:2048
	ds_read_b128 v[14:17], v190 offset:3072
	s_add_u32 s26, s24, 0x8000
	s_addc_u32 s27, s25, 0
	s_cmp_eq_u32 s68, 4
	s_cselect_b32 s30, s16, s26
	s_cselect_b32 s31, s17, s27
	s_cselect_b32 s28, s18, s23
	s_cselect_b32 s29, s19, s67
	s_add_u32 s26, s30, 0x8000
	s_addc_u32 s27, s31, 0
	s_add_i32 m0, s44, 0xc000
	ds_read_b128 v[194:197], v191
	ds_read_b128 v[198:201], v191 offset:1024
	ds_read_b128 v[202:205], v191 offset:2048
	ds_read_b128 v[206:209], v191 offset:3072
	ds_read_b128 v[210:213], v191 offset:4096
	ds_read_b128 v[214:217], v191 offset:5120
	ds_read_b128 v[218:221], v191 offset:6144
	ds_read_b128 v[222:225], v191 offset:7168
	global_load_lds_dwordx4 v184, s[24:25]
	s_add_i32 m0, s44, 0xe000
	s_nop 0
	global_load_lds_dwordx4 v182, s[24:25]
	s_waitcnt vmcnt(8)
	s_waitcnt lgkmcnt(0)
	s_setprio 1
	v_mfma_f32_16x16x128_f8f6f4 v[158:161], v[18:25], v[194:201], 0
	v_mfma_f32_16x16x128_f8f6f4 v[154:157], v[26:33], v[194:201], 0
	v_mfma_f32_16x16x128_f8f6f4 v[142:145], v[18:25], v[202:209], 0
	v_mfma_f32_16x16x128_f8f6f4 v[138:141], v[26:33], v[202:209], 0
	v_mfma_f32_16x16x128_f8f6f4 v[126:129], v[18:25], v[210:217], 0
	v_mfma_f32_16x16x128_f8f6f4 v[122:125], v[26:33], v[210:217], 0
	v_mfma_f32_16x16x128_f8f6f4 v[110:113], v[18:25], v[218:225], 0
	v_mfma_f32_16x16x128_f8f6f4 v[106:109], v[26:33], v[218:225], 0
	s_setprio 0
	s_setprio 1
	v_mfma_f32_16x16x128_f8f6f4 v[150:153], v[2:9], v[194:201], 0
	v_mfma_f32_16x16x128_f8f6f4 v[146:149], v[10:17], v[194:201], 0
	v_mfma_f32_16x16x128_f8f6f4 v[134:137], v[2:9], v[202:209], 0
	v_mfma_f32_16x16x128_f8f6f4 v[130:133], v[10:17], v[202:209], 0
	v_mfma_f32_16x16x128_f8f6f4 v[118:121], v[2:9], v[210:217], 0
	v_mfma_f32_16x16x128_f8f6f4 v[114:117], v[10:17], v[210:217], 0
	v_mfma_f32_16x16x128_f8f6f4 v[102:105], v[2:9], v[218:225], 0
	v_mfma_f32_16x16x128_f8f6f4 v[98:101], v[10:17], v[218:225], 0
	s_setprio 0
	s_barrier
	s_add_i32 s69, s53, s43
	s_mov_b32 m0, s69
	ds_read_b128 v[194:197], v191 offset:16384
	ds_read_b128 v[198:201], v191 offset:17408
	ds_read_b128 v[202:205], v191 offset:18432
	ds_read_b128 v[206:209], v191 offset:19456
	ds_read_b128 v[210:213], v191 offset:20480
	ds_read_b128 v[214:217], v191 offset:21504
	ds_read_b128 v[218:221], v191 offset:22528
	ds_read_b128 v[222:225], v191 offset:23552
	global_load_lds_dwordx4 v164, s[28:29]
	s_add_i32 m0, s69, 0x2000
	s_add_i32 s69, s58, s43
	global_load_lds_dwordx4 v166, s[28:29]
	s_add_u32 s98, s28, s4
	s_addc_u32 s99, s29, s5
	s_mov_b32 m0, s69
	s_nop 0
	global_load_lds_dwordx4 v164, s[98:99]
	s_add_u32 s100, s28, s4
	s_addc_u32 s101, s29, s5
	s_add_i32 m0, s69, 0x2000
	s_nop 0
	global_load_lds_dwordx4 v166, s[100:101]
	s_mov_b32 m0, s44
	s_nop 0
	global_load_lds_dwordx4 v168, s[30:31]
	s_mov_b32 m0, s45
	s_nop 0
	global_load_lds_dwordx4 v170, s[30:31]
	s_waitcnt vmcnt(8)
	s_waitcnt lgkmcnt(0)
	s_setprio 1
	v_mfma_f32_16x16x128_f8f6f4 v[94:97], v[18:25], v[194:201], 0
	v_mfma_f32_16x16x128_f8f6f4 v[90:93], v[26:33], v[194:201], 0
	v_mfma_f32_16x16x128_f8f6f4 v[78:81], v[18:25], v[202:209], 0
	v_mfma_f32_16x16x128_f8f6f4 v[74:77], v[26:33], v[202:209], 0
	v_mfma_f32_16x16x128_f8f6f4 v[62:65], v[18:25], v[210:217], 0
	v_mfma_f32_16x16x128_f8f6f4 v[58:61], v[26:33], v[210:217], 0
	v_mfma_f32_16x16x128_f8f6f4 v[46:49], v[18:25], v[218:225], 0
	v_mfma_f32_16x16x128_f8f6f4 v[42:45], v[26:33], v[218:225], 0
	s_setprio 0
	s_setprio 1
	v_mfma_f32_16x16x128_f8f6f4 v[86:89], v[2:9], v[194:201], 0
	v_mfma_f32_16x16x128_f8f6f4 v[82:85], v[10:17], v[194:201], 0
	v_mfma_f32_16x16x128_f8f6f4 v[70:73], v[2:9], v[202:209], 0
	v_mfma_f32_16x16x128_f8f6f4 v[66:69], v[10:17], v[202:209], 0
	v_mfma_f32_16x16x128_f8f6f4 v[54:57], v[2:9], v[210:217], 0
	v_mfma_f32_16x16x128_f8f6f4 v[50:53], v[10:17], v[210:217], 0
	v_mfma_f32_16x16x128_f8f6f4 v[38:41], v[2:9], v[218:225], 0
	v_mfma_f32_16x16x128_f8f6f4 v[34:37], v[10:17], v[218:225], 0
	s_setprio 0
	s_barrier
	s_add_i32 s69, 0, 0x18000
	s_add_i32 s70, 0, 0x1c000
	v_add_u32_e32 v14, s69, v187
	v_add_u32_e32 v30, s70, v187
	ds_read_b128 v[2:5], v14
	ds_read_b128 v[6:9], v14 offset:1024
	ds_read_b128 v[10:13], v14 offset:2048
	ds_read_b128 v[14:17], v14 offset:3072
	ds_read_b128 v[18:21], v30
	ds_read_b128 v[22:25], v30 offset:1024
	ds_read_b128 v[26:29], v30 offset:2048
	ds_read_b128 v[30:33], v30 offset:3072
	s_mov_b32 m0, s46
	ds_read_b128 v[194:197], v191 offset:32768
	ds_read_b128 v[198:201], v191 offset:33792
	ds_read_b128 v[202:205], v191 offset:34816
	ds_read_b128 v[206:209], v191 offset:35840
	ds_read_b128 v[210:213], v191 offset:36864
	ds_read_b128 v[214:217], v191 offset:37888
	ds_read_b128 v[218:221], v191 offset:38912
	ds_read_b128 v[222:225], v191 offset:39936
	global_load_lds_dwordx4 v172, s[30:31]
	s_mov_b32 m0, s47
	s_nop 0
	global_load_lds_dwordx4 v174, s[30:31]
	s_waitcnt vmcnt(8)
	s_waitcnt lgkmcnt(0)
	s_setprio 1
	v_mfma_f32_16x16x128_f8f6f4 v[158:161], v[2:9], v[194:201], v[158:161]
	v_mfma_f32_16x16x128_f8f6f4 v[154:157], v[10:17], v[194:201], v[154:157]
	v_mfma_f32_16x16x128_f8f6f4 v[142:145], v[2:9], v[202:209], v[142:145]
	v_mfma_f32_16x16x128_f8f6f4 v[138:141], v[10:17], v[202:209], v[138:141]
	v_mfma_f32_16x16x128_f8f6f4 v[126:129], v[2:9], v[210:217], v[126:129]
	v_mfma_f32_16x16x128_f8f6f4 v[122:125], v[10:17], v[210:217], v[122:125]
	v_mfma_f32_16x16x128_f8f6f4 v[110:113], v[2:9], v[218:225], v[110:113]
	v_mfma_f32_16x16x128_f8f6f4 v[106:109], v[10:17], v[218:225], v[106:109]
	s_setprio 0
	s_setprio 1
	v_mfma_f32_16x16x128_f8f6f4 v[150:153], v[18:25], v[194:201], v[150:153]
	v_mfma_f32_16x16x128_f8f6f4 v[146:149], v[26:33], v[194:201], v[146:149]
	v_mfma_f32_16x16x128_f8f6f4 v[134:137], v[18:25], v[202:209], v[134:137]
	v_mfma_f32_16x16x128_f8f6f4 v[130:133], v[26:33], v[202:209], v[130:133]
	v_mfma_f32_16x16x128_f8f6f4 v[118:121], v[18:25], v[210:217], v[118:121]
	v_mfma_f32_16x16x128_f8f6f4 v[114:117], v[26:33], v[210:217], v[114:117]
	v_mfma_f32_16x16x128_f8f6f4 v[102:105], v[18:25], v[218:225], v[102:105]
	v_mfma_f32_16x16x128_f8f6f4 v[98:101], v[26:33], v[218:225], v[98:101]
	s_setprio 0
	s_barrier
; #define PG8_STAGE(bufoff, gbase, voff) do { _Pragma("unroll") for (int _i = 0; _i < 2; ++_i) \
;         __builtin_amdgcn_global_load_lds((const unsigned*)((const char*)(gbase) + (voff)[_i]), (PG8_LAS unsigned*)(lds + (bufoff) + ldsw + _i * 8192), 16, 0, 0); } while (0)
; #define PG8_WAIT_V(n) asm volatile("s_waitcnt vmcnt(" #n ")" ::: "memory")
; #define PG8_WAIT_L(n) asm volatile("s_waitcnt lgkmcnt(" #n ")" ::: "memory")
; #define PG8_BAR __builtin_amdgcn_s_barrier()
; #define PG8_SCHED __builtin_amdgcn_sched_barrier(0)
; template <class Epi, class Sched, bool ALIGN_EPI = true, bool F8 = false>
; __device__ __forceinline__ void gemm_phase(PG8_LAS unsigned char* lds, const Sched& S, const Epi& E) {
;     ...
;             PG8_LDB(B0, 0, 0); PG8_LDB(B1, 0, 1); PG8_SCHED; PG8_LDA(At, 0, 0); PG8_STAGE(PG8_SA(1, 1), a1, voffA[1]);
;             PG8_WAIT_V(8); PG8_WAIT_L(0); PG8_BAR; PG8_MMA(0, 0, At, B0); PG8_MMA(0, 1, At, B1); PG8_BAR; PG8_SCHED;
;             PG8_LDA(At, 0, 1); PG8_STAGE(PG8_SB(0, 0), b2, voffB[0]); PG8_STAGE(PG8_SB(0, 1), b2, voffB[1]); PG8_STAGE(PG8_SA(0, 0), a2, vA2[0]);
;             PG8_WAIT_V(8); PG8_WAIT_L(0); PG8_BAR; PG8_MMA(1, 0, At, B0); PG8_MMA(1, 1, At, B1); PG8_BAR; PG8_SCHED;
;             PG8_LDB(B0, 1, 0); PG8_LDB(B1, 1, 1); PG8_SCHED; PG8_LDA(At, 1, 0); PG8_STAGE(PG8_SA(0, 1), a2, vA2[1]);
;             PG8_WAIT_V(8); PG8_WAIT_L(0); PG8_BAR; PG8_MMA(0, 0, At, B0); PG8_MMA(0, 1, At, B1); PG8_BAR; PG8_SCHED;
;             PG8_LDA(At, 1, 1); PG8_STAGE(PG8_SB(1, 0), b3, voffB[0]); PG8_STAGE(PG8_SB(1, 1), b3, voffB[1]); PG8_STAGE(PG8_SA(1, 0), a3, vA2[0]);
;             PG8_WAIT_V(8); PG8_WAIT_L(0); PG8_BAR; PG8_MMA(1, 0, At, B0); PG8_MMA(1, 1, At, B1); PG8_BAR; PG8_SCHED;
	s_add_u32 s28, s28, 0x8000
	s_addc_u32 s29, s29, 0
	s_add_i32 s30, s69, s43
	s_mov_b32 m0, s30
	ds_read_b128 v[194:197], v191 offset:49152
	ds_read_b128 v[198:201], v191 offset:50176
	ds_read_b128 v[202:205], v191 offset:51200
	ds_read_b128 v[206:209], v191 offset:52224
	ds_read_b128 v[210:213], v191 offset:53248
	ds_read_b128 v[214:217], v191 offset:54272
	ds_read_b128 v[218:221], v191 offset:55296
	ds_read_b128 v[222:225], v191 offset:56320
	global_load_lds_dwordx4 v164, s[28:29]
	s_add_i32 m0, s30, 0x2000
	s_add_i32 s30, s70, s43
	global_load_lds_dwordx4 v166, s[28:29]
	s_mov_b32 m0, s30
	s_nop 0
	global_load_lds_dwordx4 v178, s[28:29]
	s_add_i32 m0, s30, 0x2000
	s_nop 0
	global_load_lds_dwordx4 v180, s[28:29]
	s_mov_b32 m0, s51
	s_nop 0
	global_load_lds_dwordx4 v168, s[26:27]
	s_mov_b32 m0, s52
	s_nop 0
	global_load_lds_dwordx4 v170, s[26:27]
	s_waitcnt vmcnt(8)
	s_waitcnt lgkmcnt(0)
	s_setprio 1
	v_mfma_f32_16x16x128_f8f6f4 v[94:97], v[2:9], v[194:201], v[94:97]
	v_mfma_f32_16x16x128_f8f6f4 v[90:93], v[10:17], v[194:201], v[90:93]
	v_mfma_f32_16x16x128_f8f6f4 v[78:81], v[2:9], v[202:209], v[78:81]
	v_mfma_f32_16x16x128_f8f6f4 v[74:77], v[10:17], v[202:209], v[74:77]
	v_mfma_f32_16x16x128_f8f6f4 v[62:65], v[2:9], v[210:217], v[62:65]
	v_mfma_f32_16x16x128_f8f6f4 v[58:61], v[10:17], v[210:217], v[58:61]
	v_mfma_f32_16x16x128_f8f6f4 v[46:49], v[2:9], v[218:225], v[46:49]
	v_mfma_f32_16x16x128_f8f6f4 v[42:45], v[10:17], v[218:225], v[42:45]
	s_setprio 0
	s_setprio 1
	v_mfma_f32_16x16x128_f8f6f4 v[86:89], v[18:25], v[194:201], v[86:89]
	v_mfma_f32_16x16x128_f8f6f4 v[82:85], v[26:33], v[194:201], v[82:85]
	v_mfma_f32_16x16x128_f8f6f4 v[70:73], v[18:25], v[202:209], v[70:73]
	v_mfma_f32_16x16x128_f8f6f4 v[66:69], v[26:33], v[202:209], v[66:69]
	v_mfma_f32_16x16x128_f8f6f4 v[54:57], v[18:25], v[210:217], v[54:57]
	v_mfma_f32_16x16x128_f8f6f4 v[50:53], v[26:33], v[210:217], v[50:53]
	v_mfma_f32_16x16x128_f8f6f4 v[38:41], v[18:25], v[218:225], v[38:41]
	v_mfma_f32_16x16x128_f8f6f4 v[34:37], v[26:33], v[218:225], v[34:37]
	s_setprio 0
	s_barrier
	s_add_i32 s68, s68, 2
	s_add_u32 s23, s23, 0x10000
	s_addc_u32 s67, s67, 0
	s_add_u32 s24, s24, 0x10000
	s_addc_u32 s25, s25, 0
	s_cmp_gt_u32 s68, 5
	s_cbranch_scc0 .LBB0_1138
	s_branch .Lfx_33571
.LBB0_1138:
	ds_read_b128 v[18:21], v189
	ds_read_b128 v[22:25], v189 offset:1024
	ds_read_b128 v[26:29], v189 offset:2048
	ds_read_b128 v[30:33], v189 offset:3072
	ds_read_b128 v[2:5], v190
	ds_read_b128 v[6:9], v190 offset:1024
	ds_read_b128 v[10:13], v190 offset:2048
	ds_read_b128 v[14:17], v190 offset:3072
	s_add_u32 s26, s24, 0x8000
	s_addc_u32 s27, s25, 0
	s_cmp_eq_u32 s68, 4
	s_cselect_b32 s30, s16, s26
	s_cselect_b32 s31, s17, s27
	s_cselect_b32 s28, s18, s23
	s_cselect_b32 s29, s19, s67
	s_add_u32 s26, s30, 0x8000
	s_addc_u32 s27, s31, 0
	s_add_i32 m0, s44, 0xc000
	ds_read_b128 v[194:197], v191
	ds_read_b128 v[198:201], v191 offset:1024
	ds_read_b128 v[202:205], v191 offset:2048
	ds_read_b128 v[206:209], v191 offset:3072
	ds_read_b128 v[210:213], v191 offset:4096
	ds_read_b128 v[214:217], v191 offset:5120
	ds_read_b128 v[218:221], v191 offset:6144
	ds_read_b128 v[222:225], v191 offset:7168
	global_load_lds_dwordx4 v184, s[24:25]
	s_add_i32 m0, s44, 0xe000
	s_nop 0
	global_load_lds_dwordx4 v182, s[24:25]
	s_waitcnt vmcnt(8)
	s_waitcnt lgkmcnt(0)
	s_setprio 1
	v_mfma_f32_16x16x128_f8f6f4 v[158:161], v[18:25], v[194:201], v[158:161]
	v_mfma_f32_16x16x128_f8f6f4 v[154:157], v[26:33], v[194:201], v[154:157]
	v_mfma_f32_16x16x128_f8f6f4 v[142:145], v[18:25], v[202:209], v[142:145]
	v_mfma_f32_16x16x128_f8f6f4 v[138:141], v[26:33], v[202:209], v[138:141]
	v_mfma_f32_16x16x128_f8f6f4 v[126:129], v[18:25], v[210:217], v[126:129]
	v_mfma_f32_16x16x128_f8f6f4 v[122:125], v[26:33], v[210:217], v[122:125]
	v_mfma_f32_16x16x128_f8f6f4 v[110:113], v[18:25], v[218:225], v[110:113]
	v_mfma_f32_16x16x128_f8f6f4 v[106:109], v[26:33], v[218:225], v[106:109]
	s_setprio 0
	s_setprio 1
	v_mfma_f32_16x16x128_f8f6f4 v[150:153], v[2:9], v[194:201], v[150:153]
	v_mfma_f32_16x16x128_f8f6f4 v[146:149], v[10:17], v[194:201], v[146:149]
	v_mfma_f32_16x16x128_f8f6f4 v[134:137], v[2:9], v[202:209], v[134:137]
	v_mfma_f32_16x16x128_f8f6f4 v[130:133], v[10:17], v[202:209], v[130:133]
	v_mfma_f32_16x16x128_f8f6f4 v[118:121], v[2:9], v[210:217], v[118:121]
	v_mfma_f32_16x16x128_f8f6f4 v[114:117], v[10:17], v[210:217], v[114:117]
	v_mfma_f32_16x16x128_f8f6f4 v[102:105], v[2:9], v[218:225], v[102:105]
	v_mfma_f32_16x16x128_f8f6f4 v[98:101], v[10:17], v[218:225], v[98:101]
	s_setprio 0
	s_barrier
; #define PG8_STAGE(bufoff, gbase, voff) do { _Pragma("unroll") for (int _i = 0; _i < 2; ++_i) \
;         __builtin_amdgcn_global_load_lds((const unsigned*)((const char*)(gbase) + (voff)[_i]), (PG8_LAS unsigned*)(lds + (bufoff) + ldsw + _i * 8192), 16, 0, 0); } while (0)
; #define PG8_WAIT_V(n) asm volatile("s_waitcnt vmcnt(" #n ")" ::: "memory")
; #define PG8_WAIT_L(n) asm volatile("s_waitcnt lgkmcnt(" #n ")" ::: "memory")
; #define PG8_BAR __builtin_amdgcn_s_barrier()
; #define PG8_SCHED __builtin_amdgcn_sched_barrier(0)
; template <class Epi, class Sched, bool ALIGN_EPI = true, bool F8 = false>
; __device__ __forceinline__ void gemm_phase(PG8_LAS unsigned char* lds, const Sched& S, const Epi& E) {
;     ...
;             PG8_LDB(B0, 0, 0); PG8_LDB(B1, 0, 1); PG8_SCHED; PG8_LDA(At, 0, 0); PG8_STAGE(PG8_SA(1, 1), a1, voffA[1]);
;             PG8_WAIT_V(8); PG8_WAIT_L(0); PG8_BAR; PG8_MMA(0, 0, At, B0); PG8_MMA(0, 1, At, B1); PG8_BAR; PG8_SCHED;
;             PG8_LDA(At, 0, 1); PG8_STAGE(PG8_SB(0, 0), b2, voffB[0]); PG8_STAGE(PG8_SB(0, 1), b2, voffB[1]); PG8_STAGE(PG8_SA(0, 0), a2, vA2[0]);
;             PG8_WAIT_V(8); PG8_WAIT_L(0); PG8_BAR; PG8_MMA(1, 0, At, B0); PG8_MMA(1, 1, At, B1); PG8_BAR; PG8_SCHED;
;             PG8_LDB(B0, 1, 0); PG8_LDB(B1, 1, 1); PG8_SCHED; PG8_LDA(At, 1, 0); PG8_STAGE(PG8_SA(0, 1), a2, vA2[1]);
;             PG8_WAIT_V(8); PG8_WAIT_L(0); PG8_BAR; PG8_MMA(0, 0, At, B0); PG8_MMA(0, 1, At, B1); PG8_BAR; PG8_SCHED;
;             PG8_LDA(At, 1, 1); PG8_STAGE(PG8_SB(1, 0), b3, voffB[0]); PG8_STAGE(PG8_SB(1, 1), b3, voffB[1]); PG8_STAGE(PG8_SA(1, 0), a3, vA2[0]);
;             PG8_WAIT_V(8); PG8_WAIT_L(0); PG8_BAR; PG8_MMA(1, 0, At, B0); PG8_MMA(1, 1, At, B1); PG8_BAR; PG8_SCHED;
	s_add_i32 s69, s53, s43
	s_mov_b32 m0, s69
	ds_read_b128 v[194:197], v191 offset:16384
	ds_read_b128 v[198:201], v191 offset:17408
	ds_read_b128 v[202:205], v191 offset:18432
	ds_read_b128 v[206:209], v191 offset:19456
	ds_read_b128 v[210:213], v191 offset:20480
	ds_read_b128 v[214:217], v191 offset:21504
	ds_read_b128 v[218:221], v191 offset:22528
	ds_read_b128 v[222:225], v191 offset:23552
	global_load_lds_dwordx4 v164, s[28:29]
	s_add_i32 m0, s69, 0x2000
	s_add_i32 s69, s58, s43
	global_load_lds_dwordx4 v166, s[28:29]
	s_add_u32 s98, s28, s4
	s_addc_u32 s99, s29, s5
	s_mov_b32 m0, s69
	s_nop 0
	global_load_lds_dwordx4 v164, s[98:99]
	s_add_u32 s100, s28, s4
	s_addc_u32 s101, s29, s5
	s_add_i32 m0, s69, 0x2000
	s_nop 0
	global_load_lds_dwordx4 v166, s[100:101]
	s_mov_b32 m0, s44
	s_nop 0
	global_load_lds_dwordx4 v168, s[30:31]
	s_mov_b32 m0, s45
	s_nop 0
	global_load_lds_dwordx4 v170, s[30:31]
	s_waitcnt vmcnt(8)
	s_waitcnt lgkmcnt(0)
	s_setprio 1
	v_mfma_f32_16x16x128_f8f6f4 v[94:97], v[18:25], v[194:201], v[94:97]
	v_mfma_f32_16x16x128_f8f6f4 v[90:93], v[26:33], v[194:201], v[90:93]
	v_mfma_f32_16x16x128_f8f6f4 v[78:81], v[18:25], v[202:209], v[78:81]
	v_mfma_f32_16x16x128_f8f6f4 v[74:77], v[26:33], v[202:209], v[74:77]
	v_mfma_f32_16x16x128_f8f6f4 v[62:65], v[18:25], v[210:217], v[62:65]
	v_mfma_f32_16x16x128_f8f6f4 v[58:61], v[26:33], v[210:217], v[58:61]
	v_mfma_f32_16x16x128_f8f6f4 v[46:49], v[18:25], v[218:225], v[46:49]
	v_mfma_f32_16x16x128_f8f6f4 v[42:45], v[26:33], v[218:225], v[42:45]
	s_setprio 0
	s_setprio 1
	v_mfma_f32_16x16x128_f8f6f4 v[86:89], v[2:9], v[194:201], v[86:89]
	v_mfma_f32_16x16x128_f8f6f4 v[82:85], v[10:17], v[194:201], v[82:85]
	v_mfma_f32_16x16x128_f8f6f4 v[70:73], v[2:9], v[202:209], v[70:73]
	v_mfma_f32_16x16x128_f8f6f4 v[66:69], v[10:17], v[202:209], v[66:69]
	v_mfma_f32_16x16x128_f8f6f4 v[54:57], v[2:9], v[210:217], v[54:57]
	v_mfma_f32_16x16x128_f8f6f4 v[50:53], v[10:17], v[210:217], v[50:53]
	v_mfma_f32_16x16x128_f8f6f4 v[38:41], v[2:9], v[218:225], v[38:41]
	v_mfma_f32_16x16x128_f8f6f4 v[34:37], v[10:17], v[218:225], v[34:37]
	s_setprio 0
	s_barrier
	s_add_i32 s69, 0, 0x18000
	s_add_i32 s70, 0, 0x1c000
	v_add_u32_e32 v14, s69, v187
	v_add_u32_e32 v30, s70, v187
	ds_read_b128 v[2:5], v14
	ds_read_b128 v[6:9], v14 offset:1024
	ds_read_b128 v[10:13], v14 offset:2048
	ds_read_b128 v[14:17], v14 offset:3072
	ds_read_b128 v[18:21], v30
	ds_read_b128 v[22:25], v30 offset:1024
	ds_read_b128 v[26:29], v30 offset:2048
	ds_read_b128 v[30:33], v30 offset:3072
	s_mov_b32 m0, s46
	ds_read_b128 v[194:197], v191 offset:32768
	ds_read_b128 v[198:201], v191 offset:33792
	ds_read_b128 v[202:205], v191 offset:34816
	ds_read_b128 v[206:209], v191 offset:35840
	ds_read_b128 v[210:213], v191 offset:36864
	ds_read_b128 v[214:217], v191 offset:37888
	ds_read_b128 v[218:221], v191 offset:38912
	ds_read_b128 v[222:225], v191 offset:39936
	global_load_lds_dwordx4 v172, s[30:31]
	s_mov_b32 m0, s47
	s_nop 0
	global_load_lds_dwordx4 v174, s[30:31]
	s_waitcnt vmcnt(8)
	s_waitcnt lgkmcnt(0)
	s_setprio 1
	v_mfma_f32_16x16x128_f8f6f4 v[158:161], v[2:9], v[194:201], v[158:161]
	v_mfma_f32_16x16x128_f8f6f4 v[154:157], v[10:17], v[194:201], v[154:157]
	v_mfma_f32_16x16x128_f8f6f4 v[142:145], v[2:9], v[202:209], v[142:145]
	v_mfma_f32_16x16x128_f8f6f4 v[138:141], v[10:17], v[202:209], v[138:141]
	v_mfma_f32_16x16x128_f8f6f4 v[126:129], v[2:9], v[210:217], v[126:129]
	v_mfma_f32_16x16x128_f8f6f4 v[122:125], v[10:17], v[210:217], v[122:125]
	v_mfma_f32_16x16x128_f8f6f4 v[110:113], v[2:9], v[218:225], v[110:113]
	v_mfma_f32_16x16x128_f8f6f4 v[106:109], v[10:17], v[218:225], v[106:109]
	s_setprio 0
	s_setprio 1
	v_mfma_f32_16x16x128_f8f6f4 v[150:153], v[18:25], v[194:201], v[150:153]
	v_mfma_f32_16x16x128_f8f6f4 v[146:149], v[26:33], v[194:201], v[146:149]
	v_mfma_f32_16x16x128_f8f6f4 v[134:137], v[18:25], v[202:209], v[134:137]
	v_mfma_f32_16x16x128_f8f6f4 v[130:133], v[26:33], v[202:209], v[130:133]
	v_mfma_f32_16x16x128_f8f6f4 v[118:121], v[18:25], v[210:217], v[118:121]
	v_mfma_f32_16x16x128_f8f6f4 v[114:117], v[26:33], v[210:217], v[114:117]
	v_mfma_f32_16x16x128_f8f6f4 v[102:105], v[18:25], v[218:225], v[102:105]
	v_mfma_f32_16x16x128_f8f6f4 v[98:101], v[26:33], v[218:225], v[98:101]
	s_setprio 0
	s_barrier
	s_add_u32 s28, s28, 0x8000
	s_addc_u32 s29, s29, 0
	s_add_i32 s30, s69, s43
	s_mov_b32 m0, s30
	ds_read_b128 v[194:197], v191 offset:49152
	ds_read_b128 v[198:201], v191 offset:50176
	ds_read_b128 v[202:205], v191 offset:51200
	ds_read_b128 v[206:209], v191 offset:52224
	ds_read_b128 v[210:213], v191 offset:53248
	ds_read_b128 v[214:217], v191 offset:54272
	ds_read_b128 v[218:221], v191 offset:55296
	ds_read_b128 v[222:225], v191 offset:56320
	global_load_lds_dwordx4 v164, s[28:29]
	s_add_i32 m0, s30, 0x2000
	s_add_i32 s30, s70, s43
	global_load_lds_dwordx4 v166, s[28:29]
	s_mov_b32 m0, s30
	s_nop 0
	global_load_lds_dwordx4 v178, s[28:29]
	s_add_i32 m0, s30, 0x2000
	s_nop 0
	global_load_lds_dwordx4 v180, s[28:29]
	s_mov_b32 m0, s51
	s_nop 0
	global_load_lds_dwordx4 v168, s[26:27]
	s_mov_b32 m0, s52
	s_nop 0
	global_load_lds_dwordx4 v170, s[26:27]
	s_waitcnt vmcnt(8)
	s_waitcnt lgkmcnt(0)
	s_setprio 1
	v_mfma_f32_16x16x128_f8f6f4 v[94:97], v[2:9], v[194:201], v[94:97]
	v_mfma_f32_16x16x128_f8f6f4 v[90:93], v[10:17], v[194:201], v[90:93]
	v_mfma_f32_16x16x128_f8f6f4 v[78:81], v[2:9], v[202:209], v[78:81]
	v_mfma_f32_16x16x128_f8f6f4 v[74:77], v[10:17], v[202:209], v[74:77]
	v_mfma_f32_16x16x128_f8f6f4 v[62:65], v[2:9], v[210:217], v[62:65]
	v_mfma_f32_16x16x128_f8f6f4 v[58:61], v[10:17], v[210:217], v[58:61]
	v_mfma_f32_16x16x128_f8f6f4 v[46:49], v[2:9], v[218:225], v[46:49]
	v_mfma_f32_16x16x128_f8f6f4 v[42:45], v[10:17], v[218:225], v[42:45]
	s_setprio 0
	s_setprio 1
	v_mfma_f32_16x16x128_f8f6f4 v[86:89], v[18:25], v[194:201], v[86:89]
	v_mfma_f32_16x16x128_f8f6f4 v[82:85], v[26:33], v[194:201], v[82:85]
	v_mfma_f32_16x16x128_f8f6f4 v[70:73], v[18:25], v[202:209], v[70:73]
	v_mfma_f32_16x16x128_f8f6f4 v[66:69], v[26:33], v[202:209], v[66:69]
	v_mfma_f32_16x16x128_f8f6f4 v[54:57], v[18:25], v[210:217], v[54:57]
	v_mfma_f32_16x16x128_f8f6f4 v[50:53], v[26:33], v[210:217], v[50:53]
	v_mfma_f32_16x16x128_f8f6f4 v[38:41], v[18:25], v[218:225], v[38:41]
	v_mfma_f32_16x16x128_f8f6f4 v[34:37], v[26:33], v[218:225], v[34:37]
	s_setprio 0
	s_barrier
	s_add_i32 s68, s68, 2
	s_add_u32 s23, s23, 0x10000
	s_addc_u32 s67, s67, 0
	s_add_u32 s24, s24, 0x10000
	s_addc_u32 s25, s25, 0
	s_cmp_gt_u32 s68, 5
	s_cbranch_scc0 .LBB0_1138
	s_branch .Lfx_33571
; #define PG8_STAGE(bufoff, gbase, voff) do { _Pragma("unroll") for (int _i = 0; _i < 2; ++_i) \
;         __builtin_amdgcn_global_load_lds((const unsigned*)((const char*)(gbase) + (voff)[_i]), (PG8_LAS unsigned*)(lds + (bufoff) + ldsw + _i * 8192), 16, 0, 0); } while (0)
; #define PG8_WAIT_V(n) asm volatile("s_waitcnt vmcnt(" #n ")" ::: "memory")
; #define PG8_WAIT_L(n) asm volatile("s_waitcnt lgkmcnt(" #n ")" ::: "memory")
; #define PG8_BAR __builtin_amdgcn_s_barrier()
; #define PG8_SCHED __builtin_amdgcn_sched_barrier(0)
; template <class Epi, class Sched, bool ALIGN_EPI = true, bool F8 = false>
; __device__ __forceinline__ void gemm_phase(PG8_LAS unsigned char* lds, const Sched& S, const Epi& E) {
;     ...
;     f32x4 acc[2][2][4][2];
; #pragma unroll
;     for (int a = 0; a < 2; ++a)
; #pragma unroll
;         for (int b = 0; b < 2; ++b)
; #pragma unroll
;             for (int m = 0; m < 4; ++m)
; #pragma unroll
;                 for (int n = 0; n < 2; ++n) acc[a][b][m][n] = (f32x4){0.f, 0.f, 0.f, 0.f};
;     ...
;             PG8_LDB(B0, 0, 0); PG8_LDB(B1, 0, 1); PG8_SCHED; PG8_LDA(At, 0, 0); PG8_STAGE(PG8_SA(1, 1), a1, voffA[1]);
;             PG8_WAIT_V(8); PG8_WAIT_L(0); PG8_BAR; PG8_MMA(0, 0, At, B0); PG8_MMA(0, 1, At, B1); PG8_BAR; PG8_SCHED;
;             PG8_LDA(At, 0, 1); PG8_STAGE(PG8_SB(0, 0), b2, voffB[0]); PG8_STAGE(PG8_SB(0, 1), b2, voffB[1]); PG8_STAGE(PG8_SA(0, 0), a2, vA2[0]);
;             PG8_WAIT_V(8); PG8_WAIT_L(0); PG8_BAR; PG8_MMA(1, 0, At, B0); PG8_MMA(1, 1, At, B1); PG8_BAR; PG8_SCHED;
;             PG8_LDB(B0, 1, 0); PG8_LDB(B1, 1, 1); PG8_SCHED; PG8_LDA(At, 1, 0); PG8_STAGE(PG8_SA(0, 1), a2, vA2[1]);
;             PG8_WAIT_V(8); PG8_WAIT_L(0); PG8_BAR; PG8_MMA(0, 0, At, B0); PG8_MMA(0, 1, At, B1); PG8_BAR; PG8_SCHED;
;             PG8_LDA(At, 1, 1); PG8_STAGE(PG8_SB(1, 0), b3, voffB[0]); PG8_STAGE(PG8_SB(1, 1), b3, voffB[1]); PG8_STAGE(PG8_SA(1, 0), a3, vA2[0]);
;             PG8_WAIT_V(8); PG8_WAIT_L(0); PG8_BAR; PG8_MMA(1, 0, At, B0); PG8_MMA(1, 1, At, B1); PG8_BAR; PG8_SCHED;
.Lh1e_33571:
.Lpk1_1138:
	ds_read_b128 v[18:21], v189
	ds_read_b128 v[22:25], v189 offset:1024
	ds_read_b128 v[26:29], v189 offset:2048
	ds_read_b128 v[30:33], v189 offset:3072
	ds_read_b128 v[2:5], v190
	ds_read_b128 v[6:9], v190 offset:1024
	ds_read_b128 v[10:13], v190 offset:2048
	ds_read_b128 v[14:17], v190 offset:3072
	s_add_u32 s26, s24, 0x8000
	s_addc_u32 s27, s25, 0
	s_cmp_eq_u32 s68, 4
	s_cselect_b32 s30, s16, s26
	s_cselect_b32 s31, s17, s27
	s_cselect_b32 s28, s18, s23
	s_cselect_b32 s29, s19, s67
	s_add_u32 s26, s30, 0x8000
	s_addc_u32 s27, s31, 0
	s_add_i32 m0, s44, 0xc000
	ds_read_b128 v[194:197], v191
	ds_read_b128 v[198:201], v191 offset:1024
	ds_read_b128 v[202:205], v191 offset:2048
	ds_read_b128 v[206:209], v191 offset:3072
	ds_read_b128 v[210:213], v191 offset:4096
	ds_read_b128 v[214:217], v191 offset:5120
	ds_read_b128 v[218:221], v191 offset:6144
	ds_read_b128 v[222:225], v191 offset:7168
	global_load_lds_dwordx4 v184, s[24:25]
	s_add_i32 m0, s44, 0xe000
	s_nop 0
	global_load_lds_dwordx4 v182, s[24:25]
	s_waitcnt vmcnt(8)
	s_waitcnt lgkmcnt(0)
	s_barrier
	s_setprio 2
	v_mfma_f32_16x16x128_f8f6f4 v[158:161], v[18:25], v[194:201], 0
	v_mfma_f32_16x16x128_f8f6f4 v[154:157], v[26:33], v[194:201], 0
	v_mfma_f32_16x16x128_f8f6f4 v[142:145], v[18:25], v[202:209], 0
	v_mfma_f32_16x16x128_f8f6f4 v[138:141], v[26:33], v[202:209], 0
	v_mfma_f32_16x16x128_f8f6f4 v[126:129], v[18:25], v[210:217], 0
	v_mfma_f32_16x16x128_f8f6f4 v[122:125], v[26:33], v[210:217], 0
	v_mfma_f32_16x16x128_f8f6f4 v[110:113], v[18:25], v[218:225], 0
	v_mfma_f32_16x16x128_f8f6f4 v[106:109], v[26:33], v[218:225], 0
	s_setprio 0
	s_setprio 2
	v_mfma_f32_16x16x128_f8f6f4 v[150:153], v[2:9], v[194:201], 0
	v_mfma_f32_16x16x128_f8f6f4 v[146:149], v[10:17], v[194:201], 0
	v_mfma_f32_16x16x128_f8f6f4 v[134:137], v[2:9], v[202:209], 0
	v_mfma_f32_16x16x128_f8f6f4 v[130:133], v[10:17], v[202:209], 0
	v_mfma_f32_16x16x128_f8f6f4 v[118:121], v[2:9], v[210:217], 0
	v_mfma_f32_16x16x128_f8f6f4 v[114:117], v[10:17], v[210:217], 0
	v_mfma_f32_16x16x128_f8f6f4 v[102:105], v[2:9], v[218:225], 0
	v_mfma_f32_16x16x128_f8f6f4 v[98:101], v[10:17], v[218:225], 0
	s_setprio 0
	s_add_i32 s69, s53, s43
	s_mov_b32 m0, s69
	ds_read_b128 v[194:197], v191 offset:16384
	ds_read_b128 v[198:201], v191 offset:17408
	ds_read_b128 v[202:205], v191 offset:18432
	ds_read_b128 v[206:209], v191 offset:19456
	ds_read_b128 v[210:213], v191 offset:20480
	ds_read_b128 v[214:217], v191 offset:21504
	ds_read_b128 v[218:221], v191 offset:22528
	ds_read_b128 v[222:225], v191 offset:23552
	global_load_lds_dwordx4 v164, s[28:29]
	s_add_i32 m0, s69, 0x2000
	s_add_i32 s69, s58, s43
	global_load_lds_dwordx4 v166, s[28:29]
	s_add_u32 s98, s28, s4
	s_addc_u32 s99, s29, s5
	s_mov_b32 m0, s69
	s_nop 0
	global_load_lds_dwordx4 v164, s[98:99]
	s_add_u32 s100, s28, s4
	s_addc_u32 s101, s29, s5
	s_add_i32 m0, s69, 0x2000
	s_nop 0
	global_load_lds_dwordx4 v166, s[100:101]
	s_mov_b32 m0, s44
	s_nop 0
	global_load_lds_dwordx4 v168, s[30:31]
	s_mov_b32 m0, s45
	s_nop 0
	global_load_lds_dwordx4 v170, s[30:31]
	s_waitcnt vmcnt(8)
	s_waitcnt lgkmcnt(0)
	s_barrier
	s_setprio 2
	v_mfma_f32_16x16x128_f8f6f4 v[94:97], v[18:25], v[194:201], 0
	v_mfma_f32_16x16x128_f8f6f4 v[90:93], v[26:33], v[194:201], 0
	v_mfma_f32_16x16x128_f8f6f4 v[78:81], v[18:25], v[202:209], 0
	v_mfma_f32_16x16x128_f8f6f4 v[74:77], v[26:33], v[202:209], 0
	v_mfma_f32_16x16x128_f8f6f4 v[62:65], v[18:25], v[210:217], 0
	v_mfma_f32_16x16x128_f8f6f4 v[58:61], v[26:33], v[210:217], 0
	v_mfma_f32_16x16x128_f8f6f4 v[46:49], v[18:25], v[218:225], 0
	v_mfma_f32_16x16x128_f8f6f4 v[42:45], v[26:33], v[218:225], 0
	s_setprio 0
	s_setprio 2
	v_mfma_f32_16x16x128_f8f6f4 v[86:89], v[2:9], v[194:201], 0
	v_mfma_f32_16x16x128_f8f6f4 v[82:85], v[10:17], v[194:201], 0
	v_mfma_f32_16x16x128_f8f6f4 v[70:73], v[2:9], v[202:209], 0
	v_mfma_f32_16x16x128_f8f6f4 v[66:69], v[10:17], v[202:209], 0
	v_mfma_f32_16x16x128_f8f6f4 v[54:57], v[2:9], v[210:217], 0
	v_mfma_f32_16x16x128_f8f6f4 v[50:53], v[10:17], v[210:217], 0
	v_mfma_f32_16x16x128_f8f6f4 v[38:41], v[2:9], v[218:225], 0
	v_mfma_f32_16x16x128_f8f6f4 v[34:37], v[10:17], v[218:225], 0
	s_setprio 0
	s_add_i32 s69, 0, 0x18000
	s_add_i32 s70, 0, 0x1c000
	v_add_u32_e32 v14, s69, v187
	v_add_u32_e32 v30, s70, v187
	ds_read_b128 v[2:5], v14
	ds_read_b128 v[6:9], v14 offset:1024
	ds_read_b128 v[10:13], v14 offset:2048
	ds_read_b128 v[14:17], v14 offset:3072
	ds_read_b128 v[18:21], v30
	ds_read_b128 v[22:25], v30 offset:1024
	ds_read_b128 v[26:29], v30 offset:2048
	ds_read_b128 v[30:33], v30 offset:3072
	s_mov_b32 m0, s46
	ds_read_b128 v[194:197], v191 offset:32768
	ds_read_b128 v[198:201], v191 offset:33792
	ds_read_b128 v[202:205], v191 offset:34816
	ds_read_b128 v[206:209], v191 offset:35840
	ds_read_b128 v[210:213], v191 offset:36864
	ds_read_b128 v[214:217], v191 offset:37888
	ds_read_b128 v[218:221], v191 offset:38912
	ds_read_b128 v[222:225], v191 offset:39936
	global_load_lds_dwordx4 v172, s[30:31]
	s_mov_b32 m0, s47
	s_nop 0
	global_load_lds_dwordx4 v174, s[30:31]
	s_waitcnt vmcnt(8)
	s_waitcnt lgkmcnt(0)
	s_barrier
; #define PG8_STAGE(bufoff, gbase, voff) do { _Pragma("unroll") for (int _i = 0; _i < 2; ++_i) \
;         __builtin_amdgcn_global_load_lds((const unsigned*)((const char*)(gbase) + (voff)[_i]), (PG8_LAS unsigned*)(lds + (bufoff) + ldsw + _i * 8192), 16, 0, 0); } while (0)
; #define PG8_WAIT_V(n) asm volatile("s_waitcnt vmcnt(" #n ")" ::: "memory")
; #define PG8_WAIT_L(n) asm volatile("s_waitcnt lgkmcnt(" #n ")" ::: "memory")
; #define PG8_BAR __builtin_amdgcn_s_barrier()
; #define PG8_SCHED __builtin_amdgcn_sched_barrier(0)
; template <class Epi, class Sched, bool ALIGN_EPI = true, bool F8 = false>
; __device__ __forceinline__ void gemm_phase(PG8_LAS unsigned char* lds, const Sched& S, const Epi& E) {
;     ...
;             PG8_LDB(B0, 0, 0); PG8_LDB(B1, 0, 1); PG8_SCHED; PG8_LDA(At, 0, 0); PG8_STAGE(PG8_SA(1, 1), a1, voffA[1]);
;             PG8_WAIT_V(8); PG8_WAIT_L(0); PG8_BAR; PG8_MMA(0, 0, At, B0); PG8_MMA(0, 1, At, B1); PG8_BAR; PG8_SCHED;
;             PG8_LDA(At, 0, 1); PG8_STAGE(PG8_SB(0, 0), b2, voffB[0]); PG8_STAGE(PG8_SB(0, 1), b2, voffB[1]); PG8_STAGE(PG8_SA(0, 0), a2, vA2[0]);
;             PG8_WAIT_V(8); PG8_WAIT_L(0); PG8_BAR; PG8_MMA(1, 0, At, B0); PG8_MMA(1, 1, At, B1); PG8_BAR; PG8_SCHED;
;             PG8_LDB(B0, 1, 0); PG8_LDB(B1, 1, 1); PG8_SCHED; PG8_LDA(At, 1, 0); PG8_STAGE(PG8_SA(0, 1), a2, vA2[1]);
;             PG8_WAIT_V(8); PG8_WAIT_L(0); PG8_BAR; PG8_MMA(0, 0, At, B0); PG8_MMA(0, 1, At, B1); PG8_BAR; PG8_SCHED;
;             PG8_LDA(At, 1, 1); PG8_STAGE(PG8_SB(1, 0), b3, voffB[0]); PG8_STAGE(PG8_SB(1, 1), b3, voffB[1]); PG8_STAGE(PG8_SA(1, 0), a3, vA2[0]);
;             PG8_WAIT_V(8); PG8_WAIT_L(0); PG8_BAR; PG8_MMA(1, 0, At, B0); PG8_MMA(1, 1, At, B1); PG8_BAR; PG8_SCHED;
	s_setprio 2
	v_mfma_f32_16x16x128_f8f6f4 v[158:161], v[2:9], v[194:201], v[158:161]
	v_mfma_f32_16x16x128_f8f6f4 v[154:157], v[10:17], v[194:201], v[154:157]
	v_mfma_f32_16x16x128_f8f6f4 v[142:145], v[2:9], v[202:209], v[142:145]
	v_mfma_f32_16x16x128_f8f6f4 v[138:141], v[10:17], v[202:209], v[138:141]
	v_mfma_f32_16x16x128_f8f6f4 v[126:129], v[2:9], v[210:217], v[126:129]
	v_mfma_f32_16x16x128_f8f6f4 v[122:125], v[10:17], v[210:217], v[122:125]
	v_mfma_f32_16x16x128_f8f6f4 v[110:113], v[2:9], v[218:225], v[110:113]
	v_mfma_f32_16x16x128_f8f6f4 v[106:109], v[10:17], v[218:225], v[106:109]
	s_setprio 0
	s_setprio 2
	v_mfma_f32_16x16x128_f8f6f4 v[150:153], v[18:25], v[194:201], v[150:153]
	v_mfma_f32_16x16x128_f8f6f4 v[146:149], v[26:33], v[194:201], v[146:149]
	v_mfma_f32_16x16x128_f8f6f4 v[134:137], v[18:25], v[202:209], v[134:137]
	v_mfma_f32_16x16x128_f8f6f4 v[130:133], v[26:33], v[202:209], v[130:133]
	v_mfma_f32_16x16x128_f8f6f4 v[118:121], v[18:25], v[210:217], v[118:121]
	v_mfma_f32_16x16x128_f8f6f4 v[114:117], v[26:33], v[210:217], v[114:117]
	v_mfma_f32_16x16x128_f8f6f4 v[102:105], v[18:25], v[218:225], v[102:105]
	v_mfma_f32_16x16x128_f8f6f4 v[98:101], v[26:33], v[218:225], v[98:101]
	s_setprio 0
	s_add_u32 s28, s28, 0x8000
	s_addc_u32 s29, s29, 0
	s_add_i32 s30, s69, s43
	s_mov_b32 m0, s30
	ds_read_b128 v[194:197], v191 offset:49152
	ds_read_b128 v[198:201], v191 offset:50176
	ds_read_b128 v[202:205], v191 offset:51200
	ds_read_b128 v[206:209], v191 offset:52224
	ds_read_b128 v[210:213], v191 offset:53248
	ds_read_b128 v[214:217], v191 offset:54272
	ds_read_b128 v[218:221], v191 offset:55296
	ds_read_b128 v[222:225], v191 offset:56320
	global_load_lds_dwordx4 v164, s[28:29]
	s_add_i32 m0, s30, 0x2000
	s_add_i32 s30, s70, s43
	global_load_lds_dwordx4 v166, s[28:29]
	s_mov_b32 m0, s30
	s_nop 0
	global_load_lds_dwordx4 v178, s[28:29]
	s_add_i32 m0, s30, 0x2000
	s_nop 0
	global_load_lds_dwordx4 v180, s[28:29]
	s_mov_b32 m0, s51
	s_nop 0
	global_load_lds_dwordx4 v168, s[26:27]
	s_mov_b32 m0, s52
	s_nop 0
	global_load_lds_dwordx4 v170, s[26:27]
	s_waitcnt vmcnt(8)
	s_waitcnt lgkmcnt(0)
	s_barrier
	s_setprio 2
	v_mfma_f32_16x16x128_f8f6f4 v[94:97], v[2:9], v[194:201], v[94:97]
	v_mfma_f32_16x16x128_f8f6f4 v[90:93], v[10:17], v[194:201], v[90:93]
	v_mfma_f32_16x16x128_f8f6f4 v[78:81], v[2:9], v[202:209], v[78:81]
	v_mfma_f32_16x16x128_f8f6f4 v[74:77], v[10:17], v[202:209], v[74:77]
	v_mfma_f32_16x16x128_f8f6f4 v[62:65], v[2:9], v[210:217], v[62:65]
	v_mfma_f32_16x16x128_f8f6f4 v[58:61], v[10:17], v[210:217], v[58:61]
	v_mfma_f32_16x16x128_f8f6f4 v[46:49], v[2:9], v[218:225], v[46:49]
	v_mfma_f32_16x16x128_f8f6f4 v[42:45], v[10:17], v[218:225], v[42:45]
	s_setprio 0
	s_setprio 2
	v_mfma_f32_16x16x128_f8f6f4 v[86:89], v[18:25], v[194:201], v[86:89]
	v_mfma_f32_16x16x128_f8f6f4 v[82:85], v[26:33], v[194:201], v[82:85]
	v_mfma_f32_16x16x128_f8f6f4 v[70:73], v[18:25], v[202:209], v[70:73]
	v_mfma_f32_16x16x128_f8f6f4 v[66:69], v[26:33], v[202:209], v[66:69]
	v_mfma_f32_16x16x128_f8f6f4 v[54:57], v[18:25], v[210:217], v[54:57]
	v_mfma_f32_16x16x128_f8f6f4 v[50:53], v[26:33], v[210:217], v[50:53]
	v_mfma_f32_16x16x128_f8f6f4 v[38:41], v[18:25], v[218:225], v[38:41]
	v_mfma_f32_16x16x128_f8f6f4 v[34:37], v[26:33], v[218:225], v[34:37]
	s_setprio 0
	s_add_i32 s68, s68, 2
	s_add_u32 s23, s23, 0x10000
	s_addc_u32 s67, s67, 0
	s_add_u32 s24, s24, 0x10000
	s_addc_u32 s25, s25, 0
	s_cmp_gt_u32 s68, 5
	s_cbranch_scc0 .Lh1_1138
	s_branch .Lfx_33571
.Lh1_1138:
	ds_read_b128 v[18:21], v189
	ds_read_b128 v[22:25], v189 offset:1024
	ds_read_b128 v[26:29], v189 offset:2048
	ds_read_b128 v[30:33], v189 offset:3072
	ds_read_b128 v[2:5], v190
	ds_read_b128 v[6:9], v190 offset:1024
	ds_read_b128 v[10:13], v190 offset:2048
	ds_read_b128 v[14:17], v190 offset:3072
	s_add_u32 s26, s24, 0x8000
	s_addc_u32 s27, s25, 0
	s_cmp_eq_u32 s68, 4
	s_cselect_b32 s30, s16, s26
	s_cselect_b32 s31, s17, s27
	s_cselect_b32 s28, s18, s23
	s_cselect_b32 s29, s19, s67
	s_add_u32 s26, s30, 0x8000
	s_addc_u32 s27, s31, 0
	s_add_i32 m0, s44, 0xc000
	ds_read_b128 v[194:197], v191
	ds_read_b128 v[198:201], v191 offset:1024
	ds_read_b128 v[202:205], v191 offset:2048
	ds_read_b128 v[206:209], v191 offset:3072
	ds_read_b128 v[210:213], v191 offset:4096
	ds_read_b128 v[214:217], v191 offset:5120
	ds_read_b128 v[218:221], v191 offset:6144
	ds_read_b128 v[222:225], v191 offset:7168
	global_load_lds_dwordx4 v184, s[24:25]
	s_add_i32 m0, s44, 0xe000
	s_nop 0
	global_load_lds_dwordx4 v182, s[24:25]
	s_waitcnt vmcnt(8)
	s_waitcnt lgkmcnt(0)
	s_barrier
; #define PG8_STAGE(bufoff, gbase, voff) do { _Pragma("unroll") for (int _i = 0; _i < 2; ++_i) \
;         __builtin_amdgcn_global_load_lds((const unsigned*)((const char*)(gbase) + (voff)[_i]), (PG8_LAS unsigned*)(lds + (bufoff) + ldsw + _i * 8192), 16, 0, 0); } while (0)
; #define PG8_WAIT_V(n) asm volatile("s_waitcnt vmcnt(" #n ")" ::: "memory")
; #define PG8_WAIT_L(n) asm volatile("s_waitcnt lgkmcnt(" #n ")" ::: "memory")
; #define PG8_BAR __builtin_amdgcn_s_barrier()
; #define PG8_SCHED __builtin_amdgcn_sched_barrier(0)
; template <class Epi, class Sched, bool ALIGN_EPI = true, bool F8 = false>
; __device__ __forceinline__ void gemm_phase(PG8_LAS unsigned char* lds, const Sched& S, const Epi& E) {
;     ...
;             PG8_LDB(B0, 0, 0); PG8_LDB(B1, 0, 1); PG8_SCHED; PG8_LDA(At, 0, 0); PG8_STAGE(PG8_SA(1, 1), a1, voffA[1]);
;             PG8_WAIT_V(8); PG8_WAIT_L(0); PG8_BAR; PG8_MMA(0, 0, At, B0); PG8_MMA(0, 1, At, B1); PG8_BAR; PG8_SCHED;
;             PG8_LDA(At, 0, 1); PG8_STAGE(PG8_SB(0, 0), b2, voffB[0]); PG8_STAGE(PG8_SB(0, 1), b2, voffB[1]); PG8_STAGE(PG8_SA(0, 0), a2, vA2[0]);
;             PG8_WAIT_V(8); PG8_WAIT_L(0); PG8_BAR; PG8_MMA(1, 0, At, B0); PG8_MMA(1, 1, At, B1); PG8_BAR; PG8_SCHED;
;             PG8_LDB(B0, 1, 0); PG8_LDB(B1, 1, 1); PG8_SCHED; PG8_LDA(At, 1, 0); PG8_STAGE(PG8_SA(0, 1), a2, vA2[1]);
;             PG8_WAIT_V(8); PG8_WAIT_L(0); PG8_BAR; PG8_MMA(0, 0, At, B0); PG8_MMA(0, 1, At, B1); PG8_BAR; PG8_SCHED;
;             PG8_LDA(At, 1, 1); PG8_STAGE(PG8_SB(1, 0), b3, voffB[0]); PG8_STAGE(PG8_SB(1, 1), b3, voffB[1]); PG8_STAGE(PG8_SA(1, 0), a3, vA2[0]);
;             PG8_WAIT_V(8); PG8_WAIT_L(0); PG8_BAR; PG8_MMA(1, 0, At, B0); PG8_MMA(1, 1, At, B1); PG8_BAR; PG8_SCHED;
	s_setprio 2
	v_mfma_f32_16x16x128_f8f6f4 v[158:161], v[18:25], v[194:201], v[158:161]
	v_mfma_f32_16x16x128_f8f6f4 v[154:157], v[26:33], v[194:201], v[154:157]
	v_mfma_f32_16x16x128_f8f6f4 v[142:145], v[18:25], v[202:209], v[142:145]
	v_mfma_f32_16x16x128_f8f6f4 v[138:141], v[26:33], v[202:209], v[138:141]
	v_mfma_f32_16x16x128_f8f6f4 v[126:129], v[18:25], v[210:217], v[126:129]
	v_mfma_f32_16x16x128_f8f6f4 v[122:125], v[26:33], v[210:217], v[122:125]
	v_mfma_f32_16x16x128_f8f6f4 v[110:113], v[18:25], v[218:225], v[110:113]
	v_mfma_f32_16x16x128_f8f6f4 v[106:109], v[26:33], v[218:225], v[106:109]
	s_setprio 0
	s_setprio 2
	v_mfma_f32_16x16x128_f8f6f4 v[150:153], v[2:9], v[194:201], v[150:153]
	v_mfma_f32_16x16x128_f8f6f4 v[146:149], v[10:17], v[194:201], v[146:149]
	v_mfma_f32_16x16x128_f8f6f4 v[134:137], v[2:9], v[202:209], v[134:137]
	v_mfma_f32_16x16x128_f8f6f4 v[130:133], v[10:17], v[202:209], v[130:133]
	v_mfma_f32_16x16x128_f8f6f4 v[118:121], v[2:9], v[210:217], v[118:121]
	v_mfma_f32_16x16x128_f8f6f4 v[114:117], v[10:17], v[210:217], v[114:117]
	v_mfma_f32_16x16x128_f8f6f4 v[102:105], v[2:9], v[218:225], v[102:105]
	v_mfma_f32_16x16x128_f8f6f4 v[98:101], v[10:17], v[218:225], v[98:101]
	s_setprio 0
	s_add_i32 s69, s53, s43
	s_mov_b32 m0, s69
	ds_read_b128 v[194:197], v191 offset:16384
	ds_read_b128 v[198:201], v191 offset:17408
	ds_read_b128 v[202:205], v191 offset:18432
	ds_read_b128 v[206:209], v191 offset:19456
	ds_read_b128 v[210:213], v191 offset:20480
	ds_read_b128 v[214:217], v191 offset:21504
	ds_read_b128 v[218:221], v191 offset:22528
	ds_read_b128 v[222:225], v191 offset:23552
	global_load_lds_dwordx4 v164, s[28:29]
	s_add_i32 m0, s69, 0x2000
	s_add_i32 s69, s58, s43
	global_load_lds_dwordx4 v166, s[28:29]
	s_add_u32 s98, s28, s4
	s_addc_u32 s99, s29, s5
	s_mov_b32 m0, s69
	s_nop 0
	global_load_lds_dwordx4 v164, s[98:99]
	s_add_u32 s100, s28, s4
	s_addc_u32 s101, s29, s5
	s_add_i32 m0, s69, 0x2000
	s_nop 0
	global_load_lds_dwordx4 v166, s[100:101]
	s_mov_b32 m0, s44
	s_nop 0
	global_load_lds_dwordx4 v168, s[30:31]
	s_mov_b32 m0, s45
	s_nop 0
	global_load_lds_dwordx4 v170, s[30:31]
	s_waitcnt vmcnt(8)
	s_waitcnt lgkmcnt(0)
	s_barrier
	s_setprio 2
	v_mfma_f32_16x16x128_f8f6f4 v[94:97], v[18:25], v[194:201], v[94:97]
	v_mfma_f32_16x16x128_f8f6f4 v[90:93], v[26:33], v[194:201], v[90:93]
	v_mfma_f32_16x16x128_f8f6f4 v[78:81], v[18:25], v[202:209], v[78:81]
	v_mfma_f32_16x16x128_f8f6f4 v[74:77], v[26:33], v[202:209], v[74:77]
	v_mfma_f32_16x16x128_f8f6f4 v[62:65], v[18:25], v[210:217], v[62:65]
	v_mfma_f32_16x16x128_f8f6f4 v[58:61], v[26:33], v[210:217], v[58:61]
	v_mfma_f32_16x16x128_f8f6f4 v[46:49], v[18:25], v[218:225], v[46:49]
	v_mfma_f32_16x16x128_f8f6f4 v[42:45], v[26:33], v[218:225], v[42:45]
	s_setprio 0
	s_setprio 2
	v_mfma_f32_16x16x128_f8f6f4 v[86:89], v[2:9], v[194:201], v[86:89]
	v_mfma_f32_16x16x128_f8f6f4 v[82:85], v[10:17], v[194:201], v[82:85]
	v_mfma_f32_16x16x128_f8f6f4 v[70:73], v[2:9], v[202:209], v[70:73]
	v_mfma_f32_16x16x128_f8f6f4 v[66:69], v[10:17], v[202:209], v[66:69]
	v_mfma_f32_16x16x128_f8f6f4 v[54:57], v[2:9], v[210:217], v[54:57]
	v_mfma_f32_16x16x128_f8f6f4 v[50:53], v[10:17], v[210:217], v[50:53]
	v_mfma_f32_16x16x128_f8f6f4 v[38:41], v[2:9], v[218:225], v[38:41]
	v_mfma_f32_16x16x128_f8f6f4 v[34:37], v[10:17], v[218:225], v[34:37]
	s_setprio 0
	s_add_i32 s69, 0, 0x18000
	s_add_i32 s70, 0, 0x1c000
	v_add_u32_e32 v14, s69, v187
	v_add_u32_e32 v30, s70, v187
	ds_read_b128 v[2:5], v14
	ds_read_b128 v[6:9], v14 offset:1024
	ds_read_b128 v[10:13], v14 offset:2048
	ds_read_b128 v[14:17], v14 offset:3072
	ds_read_b128 v[18:21], v30
	ds_read_b128 v[22:25], v30 offset:1024
	ds_read_b128 v[26:29], v30 offset:2048
	ds_read_b128 v[30:33], v30 offset:3072
	s_mov_b32 m0, s46
	ds_read_b128 v[194:197], v191 offset:32768
	ds_read_b128 v[198:201], v191 offset:33792
	ds_read_b128 v[202:205], v191 offset:34816
	ds_read_b128 v[206:209], v191 offset:35840
	ds_read_b128 v[210:213], v191 offset:36864
	ds_read_b128 v[214:217], v191 offset:37888
	ds_read_b128 v[218:221], v191 offset:38912
	ds_read_b128 v[222:225], v191 offset:39936
	global_load_lds_dwordx4 v172, s[30:31]
	s_mov_b32 m0, s47
	s_nop 0
	global_load_lds_dwordx4 v174, s[30:31]
	s_waitcnt vmcnt(8)
	s_waitcnt lgkmcnt(0)
	s_barrier
; #define PG8_STAGE(bufoff, gbase, voff) do { _Pragma("unroll") for (int _i = 0; _i < 2; ++_i) \
;         __builtin_amdgcn_global_load_lds((const unsigned*)((const char*)(gbase) + (voff)[_i]), (PG8_LAS unsigned*)(lds + (bufoff) + ldsw + _i * 8192), 16, 0, 0); } while (0)
; #define PG8_WAIT_V(n) asm volatile("s_waitcnt vmcnt(" #n ")" ::: "memory")
; #define PG8_WAIT_L(n) asm volatile("s_waitcnt lgkmcnt(" #n ")" ::: "memory")
; #define PG8_BAR __builtin_amdgcn_s_barrier()
; #define PG8_SCHED __builtin_amdgcn_sched_barrier(0)
; template <class Epi, class Sched, bool ALIGN_EPI = true, bool F8 = false>
; __device__ __forceinline__ void gemm_phase(PG8_LAS unsigned char* lds, const Sched& S, const Epi& E) {
;     ...
;             PG8_LDB(B0, 0, 0); PG8_LDB(B1, 0, 1); PG8_SCHED; PG8_LDA(At, 0, 0); PG8_STAGE(PG8_SA(1, 1), a1, voffA[1]);
;             PG8_WAIT_V(8); PG8_WAIT_L(0); PG8_BAR; PG8_MMA(0, 0, At, B0); PG8_MMA(0, 1, At, B1); PG8_BAR; PG8_SCHED;
;             PG8_LDA(At, 0, 1); PG8_STAGE(PG8_SB(0, 0), b2, voffB[0]); PG8_STAGE(PG8_SB(0, 1), b2, voffB[1]); PG8_STAGE(PG8_SA(0, 0), a2, vA2[0]);
;             PG8_WAIT_V(8); PG8_WAIT_L(0); PG8_BAR; PG8_MMA(1, 0, At, B0); PG8_MMA(1, 1, At, B1); PG8_BAR; PG8_SCHED;
;             PG8_LDB(B0, 1, 0); PG8_LDB(B1, 1, 1); PG8_SCHED; PG8_LDA(At, 1, 0); PG8_STAGE(PG8_SA(0, 1), a2, vA2[1]);
;             PG8_WAIT_V(8); PG8_WAIT_L(0); PG8_BAR; PG8_MMA(0, 0, At, B0); PG8_MMA(0, 1, At, B1); PG8_BAR; PG8_SCHED;
;             PG8_LDA(At, 1, 1); PG8_STAGE(PG8_SB(1, 0), b3, voffB[0]); PG8_STAGE(PG8_SB(1, 1), b3, voffB[1]); PG8_STAGE(PG8_SA(1, 0), a3, vA2[0]);
;             PG8_WAIT_V(8); PG8_WAIT_L(0); PG8_BAR; PG8_MMA(1, 0, At, B0); PG8_MMA(1, 1, At, B1); PG8_BAR; PG8_SCHED;
	s_setprio 2
	v_mfma_f32_16x16x128_f8f6f4 v[158:161], v[2:9], v[194:201], v[158:161]
	v_mfma_f32_16x16x128_f8f6f4 v[154:157], v[10:17], v[194:201], v[154:157]
	v_mfma_f32_16x16x128_f8f6f4 v[142:145], v[2:9], v[202:209], v[142:145]
	v_mfma_f32_16x16x128_f8f6f4 v[138:141], v[10:17], v[202:209], v[138:141]
	v_mfma_f32_16x16x128_f8f6f4 v[126:129], v[2:9], v[210:217], v[126:129]
	v_mfma_f32_16x16x128_f8f6f4 v[122:125], v[10:17], v[210:217], v[122:125]
	v_mfma_f32_16x16x128_f8f6f4 v[110:113], v[2:9], v[218:225], v[110:113]
	v_mfma_f32_16x16x128_f8f6f4 v[106:109], v[10:17], v[218:225], v[106:109]
	s_setprio 0
	s_setprio 2
	v_mfma_f32_16x16x128_f8f6f4 v[150:153], v[18:25], v[194:201], v[150:153]
	v_mfma_f32_16x16x128_f8f6f4 v[146:149], v[26:33], v[194:201], v[146:149]
	v_mfma_f32_16x16x128_f8f6f4 v[134:137], v[18:25], v[202:209], v[134:137]
	v_mfma_f32_16x16x128_f8f6f4 v[130:133], v[26:33], v[202:209], v[130:133]
	v_mfma_f32_16x16x128_f8f6f4 v[118:121], v[18:25], v[210:217], v[118:121]
	v_mfma_f32_16x16x128_f8f6f4 v[114:117], v[26:33], v[210:217], v[114:117]
	v_mfma_f32_16x16x128_f8f6f4 v[102:105], v[18:25], v[218:225], v[102:105]
	v_mfma_f32_16x16x128_f8f6f4 v[98:101], v[26:33], v[218:225], v[98:101]
	s_setprio 0
	s_add_u32 s28, s28, 0x8000
	s_addc_u32 s29, s29, 0
	s_add_i32 s30, s69, s43
	s_mov_b32 m0, s30
	ds_read_b128 v[194:197], v191 offset:49152
	ds_read_b128 v[198:201], v191 offset:50176
	ds_read_b128 v[202:205], v191 offset:51200
	ds_read_b128 v[206:209], v191 offset:52224
	ds_read_b128 v[210:213], v191 offset:53248
	ds_read_b128 v[214:217], v191 offset:54272
	ds_read_b128 v[218:221], v191 offset:55296
	ds_read_b128 v[222:225], v191 offset:56320
	global_load_lds_dwordx4 v164, s[28:29]
	s_add_i32 m0, s30, 0x2000
	s_add_i32 s30, s70, s43
	global_load_lds_dwordx4 v166, s[28:29]
	s_mov_b32 m0, s30
	s_nop 0
	global_load_lds_dwordx4 v178, s[28:29]
	s_add_i32 m0, s30, 0x2000
	s_nop 0
	global_load_lds_dwordx4 v180, s[28:29]
	s_mov_b32 m0, s51
	s_nop 0
	global_load_lds_dwordx4 v168, s[26:27]
	s_mov_b32 m0, s52
	s_nop 0
	global_load_lds_dwordx4 v170, s[26:27]
	s_waitcnt vmcnt(8)
	s_waitcnt lgkmcnt(0)
	s_barrier
	s_setprio 2
	v_mfma_f32_16x16x128_f8f6f4 v[94:97], v[2:9], v[194:201], v[94:97]
	v_mfma_f32_16x16x128_f8f6f4 v[90:93], v[10:17], v[194:201], v[90:93]
	v_mfma_f32_16x16x128_f8f6f4 v[78:81], v[2:9], v[202:209], v[78:81]
	v_mfma_f32_16x16x128_f8f6f4 v[74:77], v[10:17], v[202:209], v[74:77]
	v_mfma_f32_16x16x128_f8f6f4 v[62:65], v[2:9], v[210:217], v[62:65]
	v_mfma_f32_16x16x128_f8f6f4 v[58:61], v[10:17], v[210:217], v[58:61]
	v_mfma_f32_16x16x128_f8f6f4 v[46:49], v[2:9], v[218:225], v[46:49]
	v_mfma_f32_16x16x128_f8f6f4 v[42:45], v[10:17], v[218:225], v[42:45]
	s_setprio 0
	s_setprio 2
	v_mfma_f32_16x16x128_f8f6f4 v[86:89], v[18:25], v[194:201], v[86:89]
	v_mfma_f32_16x16x128_f8f6f4 v[82:85], v[26:33], v[194:201], v[82:85]
	v_mfma_f32_16x16x128_f8f6f4 v[70:73], v[18:25], v[202:209], v[70:73]
	v_mfma_f32_16x16x128_f8f6f4 v[66:69], v[26:33], v[202:209], v[66:69]
	v_mfma_f32_16x16x128_f8f6f4 v[54:57], v[18:25], v[210:217], v[54:57]
	v_mfma_f32_16x16x128_f8f6f4 v[50:53], v[26:33], v[210:217], v[50:53]
	v_mfma_f32_16x16x128_f8f6f4 v[38:41], v[18:25], v[218:225], v[38:41]
	v_mfma_f32_16x16x128_f8f6f4 v[34:37], v[26:33], v[218:225], v[34:37]
	s_setprio 0
	s_add_i32 s68, s68, 2
	s_add_u32 s23, s23, 0x10000
	s_addc_u32 s67, s67, 0
	s_add_u32 s24, s24, 0x10000
	s_addc_u32 s25, s25, 0
	s_cmp_gt_u32 s68, 5
	s_cbranch_scc0 .Lh1_1138
